# stack4: stack3 minus out-proj prefetch, plus 8-row x 128-B full-cache-line LDS-DMA pieces with XOR-swizzled LDS image in all GEMM phases except uq/ukv
# speedup vs baseline: 1.0114x; 1.0101x over previous
; __device__ __forceinline__ int lane_id() { int l_; asm volatile("v_mbcnt_lo_u32_b32 %0, -1, 0\n\tv_mbcnt_hi_u32_b32 %0, -1, %0" : "=v"(l_)); return l_; }
; #define PG8_STAGE(bufoff, gbase, voff) do { _Pragma("unroll") for (int _i = 0; _i < 2; ++_i) \
;         glds16((const void*)(gbase), (voff)[_i], ldsbase + (unsigned)(bufoff) + ldsw + (unsigned)_i * 8192u); } while (0)
; #define PG8_WAIT_V(n) asm volatile("s_waitcnt vmcnt(" #n ")" ::: "memory")
; #define PG8_BAR __builtin_amdgcn_s_barrier()
;     ...
;     int tid = w0_ * 64 + lane_id(); asm volatile("" : "+v"(tid));
;     const int wid = __builtin_amdgcn_readfirstlane(tid >> 6), lane = tid & 63, wr = wid >> 2, wc = wid & 3, fr = lane & 15, fq = lane >> 4;
;     const int nt = nt_ ? nt_ : Kb / 128;
;     unsigned voffA[2], voffB[2];
; #pragma unroll
;     for (int i = 0; i < 2; ++i) { int R, C; stage_rc(tid * 16 + i * 8192, R, C); const int Rb = Epi::PERM ? ((R & ~31) + perm32(R & 31)) : R;
;         voffA[i] = (unsigned)(R * ldab + C * 2); voffB[i] = (unsigned)(Rb * Kb + C * 2); }
;     const size_t kstep = (size_t)(BK * 2);
;     const size_t hstepA = (size_t)HALF * ldab, hstepB = (size_t)HALF * Kb;
;     const unsigned ldsw = (unsigned)wid * 1024u, ldsbase = (unsigned)(size_t)lds;
;     const int aoff = lds_byte(wr * 64 + fr, fq * 8), boff = lds_byte(wc * 32 + fr, fq * 8);
;     ...
;     PG8_STAGE(PG8_SB(0, 0), cB, voffB); PG8_STAGE(PG8_SB(0, 1), cB + hstepB, voffB); PG8_STAGE(PG8_SA(0, 0), cA, voffA); PG8_STAGE(PG8_SA(0, 1), cA + hstepA, voffA);
;     if (wr == 1) PG8_BAR;
;     PG8_WAIT_V(2); PG8_BAR;
;     PG8_STAGE(PG8_SB(1, 0), cB + kstep, voffB); PG8_STAGE(PG8_SA(1, 0), cA + kstep, voffA); PG8_STAGE(PG8_SB(1, 1), cB + hstepB + kstep, voffB);
;     PG8_WAIT_V(6); PG8_BAR;
.LBB0_1941:
	s_and_b64 vcc, exec, s[2:3]
	s_cbranch_vccnz .LBB0_2045
	v_bfe_i32 v4, v0, 27, 1
	v_lshlrev_b32_e32 v2, 4, v0
	v_lshrrev_b32_e32 v4, 22, v4
	v_add_u32_e32 v4, v2, v4
	v_and_b32_e32 v4, 0xfffffc00, v4
	v_sub_u32_e32 v4, v2, v4
	v_ashrrev_i32_e32 v1, 31, v0
	v_lshrrev_b32_e32 v5, 4, v4
	v_lshrrev_b32_e32 v1, 26, v1
	v_bitop3_b32 v4, v5, v4, 32 bitop3:0x6c
	v_add_u32_e32 v1, v0, v1
	v_ashrrev_i32_e32 v6, 31, v4
	v_ashrrev_i32_e32 v1, 6, v1
	v_lshrrev_b32_e32 v6, 26, v6
	v_lshlrev_b32_e32 v5, 3, v1
	v_add_u32_e32 v6, v4, v6
	v_and_b32_e32 v5, -16, v5
	v_ashrrev_i32_e32 v7, 6, v6
	v_and_b32_e32 v6, 0xc0, v6
	v_add_u32_e32 v5, v7, v5
	v_sub_u32_e32 v4, v4, v6
	v_lshlrev_b32_e32 v1, 5, v1
	v_ashrrev_i16_sdwa v4, v188, sext(v4) dst_sel:DWORD dst_unused:UNUSED_PAD src0_sel:DWORD src1_sel:BYTE_0
	v_lshlrev_b32_e32 v6, 1, v5
	v_lshrrev_b32_e32 v8, 2, v5
	v_and_b32_e32 v7, 3, v7
	s_mov_b32 s3, 0x1fffe0
	v_and_b32_e32 v1, 32, v1
	v_bfe_i32 v4, v4, 0, 16
	v_and_b32_e32 v6, 24, v6
	v_and_b32_e32 v8, 4, v8
	v_and_or_b32 v7, v5, s3, v7
	v_or3_b32 v6, v7, v8, v6
	v_add_lshl_u32 v4, v1, v4, 1
	v_add_u32_e32 v2, 0x2000, v2
	v_lshl_add_u32 v1, v5, 11, v4
	v_lshl_add_u32 v180, v6, 11, v4
	v_ashrrev_i32_e32 v4, 31, v2
	v_lshrrev_b32_e32 v4, 22, v4
	v_add_u32_e32 v4, v2, v4
	v_ashrrev_i32_e32 v4, 10, v4
	v_mul_i32_i24_e32 v5, 0x400, v4
	v_sub_u32_e32 v2, v2, v5
	v_lshrrev_b32_e32 v5, 4, v2
	v_bitop3_b32 v2, v5, v2, 32 bitop3:0x6c
	v_ashrrev_i32_e32 v6, 31, v2
	v_lshrrev_b32_e32 v6, 26, v6
	v_lshlrev_b32_e32 v5, 3, v4
	v_add_u32_e32 v6, v2, v6
	v_and_b32_e32 v5, -16, v5
	v_ashrrev_i32_e32 v7, 6, v6
	v_and_b32_e32 v6, 0xc0, v6
	s_ashr_i32 s2, s14, 6
	v_add_u32_e32 v5, v7, v5
	v_sub_u32_e32 v2, v2, v6
	v_lshlrev_b32_e32 v4, 5, v4
	v_ashrrev_i16_sdwa v2, v188, sext(v2) dst_sel:DWORD dst_unused:UNUSED_PAD src0_sel:DWORD src1_sel:BYTE_0
	v_lshlrev_b32_e32 v6, 1, v5
	v_lshrrev_b32_e32 v8, 2, v5
	v_and_b32_e32 v7, 3, v7
	s_lshl_b32 s8, s2, 10
	v_and_b32_e32 v4, 32, v4
	v_bfe_i32 v2, v2, 0, 16
	v_and_b32_e32 v6, 24, v6
	v_and_b32_e32 v8, 4, v8
	v_and_or_b32 v7, v5, s3, v7
	s_add_i32 s37, s8, 0
	v_or3_b32 v6, v7, v8, v6
	v_add_lshl_u32 v2, v4, v2, 1
	s_add_i32 s38, s37, 0x10000
	s_nop 0
	v_readlane_b32 s70, v250, 60
	v_mbcnt_lo_u32_b32 v246, -1, 0
	v_mbcnt_hi_u32_b32 v246, -1, v246
	v_add_u32_e32 v246, s70, v246
	v_bfe_u32 v247, v246, 4, 2
	v_bfe_u32 v248, v246, 6, 1
	v_lshl_or_b32 v247, v248, 2, v247
	v_and_b32_e32 v248, 7, v246
	v_xor_b32_e32 v247, v247, v248
	v_lshlrev_b32_e32 v247, 4, v247
	v_lshrrev_b32_e32 v248, 3, v246
	v_lshl_add_u32 v238, v248, 11, v247
	v_add_u32_e32 v239, 0x20000, v238
	v_and_b32_e32 v249, 0x23, v248
	v_and_b32_e32 v244, 12, v248
	v_lshl_or_b32 v249, v244, 1, v249
	v_bfe_u32 v244, v248, 4, 1
	v_lshl_or_b32 v249, v244, 2, v249
	v_lshl_add_u32 v240, v249, 11, v247
	v_add_u32_e32 v241, 0x20000, v240
	v_bfe_u32 v247, v246, 4, 2
	v_bfe_u32 v248, v246, 1, 3
	v_xor_b32_e32 v247, v247, v248
	v_lshlrev_b32_e32 v247, 4, v247
	v_and_b32_e32 v248, 7, v246
	v_lshl_or_b32 v247, v248, 7, v247
	v_bfe_u32 v248, v246, 3, 1
	v_lshl_or_b32 v247, v248, 10, v247
	v_bfe_u32 v248, v246, 8, 1
	v_lshl_or_b32 v242, v248, 13, v247
	v_xor_b32_e32 v243, 64, v242
	v_bfe_u32 v248, v246, 6, 2
	v_lshl_or_b32 v244, v248, 12, v247
	v_xor_b32_e32 v245, 64, v244
	s_mov_b32 m0, s38
	s_nop 0
	global_load_lds_dwordx4 v240, s[24:25]
	v_lshl_add_u32 v182, v6, 11, v2
	s_ashr_i32 s3, s14, 8
	s_add_i32 s39, s37, 0x12000
	s_mov_b32 m0, s39
	s_nop 0
	global_load_lds_dwordx4 v241, s[24:25]
	s_add_u32 s8, s24, 0x40000
	s_addc_u32 s9, s25, 0
	s_add_i32 s40, s37, 0x14000
	s_mov_b32 m0, s40
	s_nop 0
	global_load_lds_dwordx4 v240, s[8:9]
	s_add_i32 s41, s37, 0x16000
	s_mov_b32 m0, s41
	s_nop 0
	global_load_lds_dwordx4 v241, s[8:9]
	s_mov_b32 m0, s37
	s_nop 0
	global_load_lds_dwordx4 v238, s[4:5]
	v_lshl_add_u32 v181, v5, 11, v2
	s_add_i32 s42, s37, 0x2000
	s_mov_b32 m0, s42
	s_nop 0
	global_load_lds_dwordx4 v239, s[4:5]
	s_add_u32 s8, s4, 0x40000
	s_addc_u32 s9, s5, 0
	s_add_i32 s43, s37, 0x4000
	s_mov_b32 m0, s43
	s_nop 0
	global_load_lds_dwordx4 v238, s[8:9]
	s_add_i32 s44, s37, 0x6000
	s_mov_b32 m0, s44
	s_nop 0
	global_load_lds_dwordx4 v239, s[8:9]
	s_cmp_eq_u32 s3, 1
	s_cselect_b64 s[8:9], -1, 0
	s_cmp_lg_u32 s3, 1
	s_cbranch_scc1 .LBB0_1944
	s_barrier
.LBB0_1944:
	s_add_u32 s10, s16, 0x41892000
	s_addc_u32 s11, s17, 0
	s_add_u32 s45, s16, 0x43892000
	s_addc_u32 s46, s17, 0
	s_add_u32 s12, s16, 0x32882000
	s_addc_u32 s13, s17, 0
	s_and_b64 s[6:7], s[6:7], exec
	v_bfe_u32 v4, v0, 4, 2
	s_movk_i32 s6, 0x7f
	v_and_b32_e32 v183, 15, v0
	v_lshlrev_b32_e32 v2, 4, v4
	v_lshlrev_b32_e32 v0, 2, v0
	s_cselect_b32 s47, 0x7c, s6
	s_and_b32 s18, s2, 3
	v_lshl_or_b32 v5, v183, 6, v2
	s_lshl_b32 s2, s3, 13
	v_and_b32_e32 v0, 32, v0
	s_lshl_b32 s48, s3, 6
	v_bitop3_b32 v7, v5, s2, v0 bitop3:0xde
	s_lshl_b32 s2, s18, 12
	s_add_u32 s6, s16, 0x3a892000
	s_addc_u32 s7, s17, 0
	v_bitop3_b32 v8, v5, s2, v0 bitop3:0xde
	s_add_u32 s2, s24, 0x80
	s_waitcnt vmcnt(2)
	s_barrier
	s_addc_u32 s3, s25, 0
	s_add_i32 s49, s37, 0x18000
	s_mov_b32 m0, s49
	s_nop 0
	global_load_lds_dwordx4 v240, s[2:3]
	s_add_i32 s50, s37, 0x1a000
	s_mov_b32 m0, s50
	s_nop 0
	global_load_lds_dwordx4 v241, s[2:3]
	s_add_u32 s2, s4, 0x80
	s_addc_u32 s3, s5, 0
	s_add_i32 s51, s37, 0x8000
	s_mov_b32 m0, s51
	s_nop 0
	global_load_lds_dwordx4 v238, s[2:3]
	s_add_i32 s52, s37, 0xa000
	s_mov_b32 m0, s52
	s_nop 0
	global_load_lds_dwordx4 v239, s[2:3]
	s_add_u32 s2, s24, 0x40080
	s_addc_u32 s3, s25, 0
	s_add_i32 s53, s37, 0x1c000
	s_mov_b32 m0, s53
	s_nop 0
	global_load_lds_dwordx4 v240, s[2:3]
	s_add_i32 s54, s37, 0x1e000
	s_add_i32 s55, s37, 0xc000
	s_mov_b32 m0, s54
	s_nop 0
	global_load_lds_dwordx4 v241, s[2:3]
	s_cmpk_lt_u32 s14, 0x100
	s_cselect_b64 s[14:15], -1, 0
	s_add_i32 s56, s37, 0xe000
	s_lshl_b32 s2, s18, 6
	v_lshlrev_b32_e32 v0, 2, v4
	s_add_u32 s2, s45, s2
	v_lshl_or_b32 v0, s18, 4, v0
	s_addc_u32 s3, s46, 0
	v_lshl_add_u64 v[164:165], s[2:3], 0, v[2:3]
	v_lshlrev_b32_e32 v2, 2, v0
	v_lshlrev_b32_e32 v6, 3, v4
	s_waitcnt vmcnt(6)
	v_lshl_add_u64 v[4:5], s[16:17], 0, v[2:3]
	s_mov_b64 s[2:3], 0x32500000
	v_lshl_add_u64 v[166:167], v[4:5], 0, s[2:3]
	s_mov_b64 s[2:3], 0x32580000
	v_lshl_or_b32 v2, s18, 5, v6
	v_lshl_add_u64 v[168:169], v[4:5], 0, s[2:3]
	s_mov_b32 s57, 0
	v_add_u32_e32 v184, 0, v8
	v_add_u32_e32 v185, 0, v7
	v_lshlrev_b32_e32 v205, 1, v2
	s_mov_b64 s[22:23], s[24:25]
	s_mov_b64 s[20:21], s[4:5]
	s_barrier
	s_branch .LBB0_1947

; #define PG8_STAGE(bufoff, gbase, voff) do { _Pragma("unroll") for (int _i = 0; _i < 2; ++_i) \
;         glds16((const void*)(gbase), (voff)[_i], ldsbase + (unsigned)(bufoff) + ldsw + (unsigned)_i * 8192u); } while (0)
; #define PG8_LDA(dst, b, h) do { _Pragma("unroll") for (int m = 0; m < 4; ++m) _Pragma("unroll") for (int k = 0; k < 2; ++k) dst[m][k] = *(const LAS bf16x8*)(lds + PG8_SA(b, h) + aoff + m * 2048 + k * 1024); } while (0)
; #define PG8_LDB(dst, b, h) do { _Pragma("unroll") for (int n = 0; n < 2; ++n) _Pragma("unroll") for (int k = 0; k < 2; ++k) dst[n][k] = *(const LAS bf16x8*)(lds + PG8_SB(b, h) + boff + n * 2048 + k * 1024); } while (0)
; #define PG8_WAIT_V(n) asm volatile("s_waitcnt vmcnt(" #n ")" ::: "memory")
; #define PG8_WAIT_L(n) asm volatile("s_waitcnt lgkmcnt(" #n ")" ::: "memory")
; #define PG8_BAR __builtin_amdgcn_s_barrier()
; #define PG8_SCHED __builtin_amdgcn_sched_barrier(0)
;     ...
;             PG8_LDB(B0, 0, 0); PG8_LDB(B1, 0, 1); PG8_SCHED; PG8_LDA(At, 0, 0); PG8_STAGE(PG8_SA(1, 1), a1 + hstepA, voffA);
;             PG8_WAIT_V(8); PG8_WAIT_L(0); PG8_BAR; PG8_MMA(0, 0, At, B0); PG8_MMA(0, 1, At, B1); PG8_BAR; PG8_SCHED;
;             PG8_LDA(At, 0, 1); PG8_STAGE(PG8_SB(0, 0), b2, voffB); PG8_STAGE(PG8_SB(0, 1), b2 + hstepB, voffB); PG8_STAGE(PG8_SA(0, 0), a2, voffA);
;             PG8_WAIT_V(8); PG8_WAIT_L(0); PG8_BAR; PG8_MMA(1, 0, At, B0); PG8_MMA(1, 1, At, B1); PG8_BAR; PG8_SCHED;
.LBB0_1950:
	v_add_u32_e32 v2, 0x10000, v244
	v_add_u32_e32 v246, 0x10000, v245
	ds_read_b128 v[28:31], v2
	ds_read_b128 v[32:35], v246
	ds_read_b128 v[20:23], v2 offset:2048
	ds_read_b128 v[24:27], v246 offset:2048
	v_add_u32_e32 v2, 0x14000, v244
	v_add_u32_e32 v246, 0x14000, v245
	s_waitcnt lgkmcnt(4)
	ds_read_b128 v[12:15], v2
	ds_read_b128 v[16:19], v246
	ds_read_b128 v[4:7], v2 offset:2048
	ds_read_b128 v[8:11], v246 offset:2048
	s_add_u32 s24, s4, 0xfffc0080
	s_addc_u32 s25, s5, -1
	s_cmp_eq_u32 s31, 12
	s_cselect_b32 s28, s20, s24
	s_cselect_b32 s29, s21, s25
	s_cselect_b32 s26, s22, s17
	s_cselect_b32 s27, s23, s19
	s_add_u32 s24, s28, 0x80
	s_addc_u32 s25, s29, 0
	ds_read_b128 v[206:209], v242
	ds_read_b128 v[210:213], v243
	ds_read_b128 v[214:217], v242 offset:2048
	ds_read_b128 v[218:221], v243 offset:2048
	ds_read_b128 v[222:225], v242 offset:4096
	ds_read_b128 v[226:229], v243 offset:4096
	ds_read_b128 v[230:233], v242 offset:6144
	ds_read_b128 v[234:237], v243 offset:6144
	s_mov_b32 m0, s55
	s_nop 0
	global_load_lds_dwordx4 v238, s[4:5]
	s_nop 0
	s_mov_b32 m0, s56
	s_nop 0
	global_load_lds_dwordx4 v239, s[4:5]
	s_waitcnt vmcnt(8)
	s_waitcnt lgkmcnt(0)
	s_barrier
	s_setprio 1
	v_mov_b32_e32 v2, s47
	s_waitcnt lgkmcnt(6)
	v_mfma_scale_f32_16x16x128_f8f6f4 v[160:163], v[28:35], v[206:213], v[160:163], v189, v2 op_sel_hi:[0,0,0]
	v_mfma_scale_f32_16x16x128_f8f6f4 v[156:159], v[20:27], v[206:213], v[156:159], v189, v2 op_sel_hi:[0,0,0]
	s_waitcnt lgkmcnt(4)
	v_mfma_scale_f32_16x16x128_f8f6f4 v[148:151], v[28:35], v[214:221], v[148:151], v189, v2 op_sel_hi:[0,0,0]
	v_mfma_scale_f32_16x16x128_f8f6f4 v[140:143], v[20:27], v[214:221], v[140:143], v189, v2 op_sel_hi:[0,0,0]
	s_waitcnt lgkmcnt(2)
	v_mfma_scale_f32_16x16x128_f8f6f4 v[132:135], v[28:35], v[222:229], v[132:135], v189, v2 op_sel_hi:[0,0,0]
	v_mfma_scale_f32_16x16x128_f8f6f4 v[124:127], v[20:27], v[222:229], v[124:127], v189, v2 op_sel_hi:[0,0,0]
	s_waitcnt lgkmcnt(0)
	v_mfma_scale_f32_16x16x128_f8f6f4 v[116:119], v[28:35], v[230:237], v[116:119], v189, v2 op_sel_hi:[0,0,0]
	v_mfma_scale_f32_16x16x128_f8f6f4 v[108:111], v[20:27], v[230:237], v[108:111], v189, v2 op_sel_hi:[0,0,0]
	s_setprio 0
	s_setprio 1
	v_mfma_scale_f32_16x16x128_f8f6f4 v[152:155], v[12:19], v[206:213], v[152:155], v189, v2 op_sel_hi:[0,0,0]
	v_mfma_scale_f32_16x16x128_f8f6f4 v[144:147], v[4:11], v[206:213], v[144:147], v189, v2 op_sel_hi:[0,0,0]
	v_mfma_scale_f32_16x16x128_f8f6f4 v[136:139], v[12:19], v[214:221], v[136:139], v189, v2 op_sel_hi:[0,0,0]
	v_mfma_scale_f32_16x16x128_f8f6f4 v[128:131], v[4:11], v[214:221], v[128:131], v189, v2 op_sel_hi:[0,0,0]
	v_mfma_scale_f32_16x16x128_f8f6f4 v[120:123], v[12:19], v[222:229], v[120:123], v189, v2 op_sel_hi:[0,0,0]
	v_mfma_scale_f32_16x16x128_f8f6f4 v[112:115], v[4:11], v[222:229], v[112:115], v189, v2 op_sel_hi:[0,0,0]
	v_mfma_scale_f32_16x16x128_f8f6f4 v[104:107], v[12:19], v[230:237], v[104:107], v189, v2 op_sel_hi:[0,0,0]
	v_mfma_scale_f32_16x16x128_f8f6f4 v[100:103], v[4:11], v[230:237], v[100:103], v189, v2 op_sel_hi:[0,0,0]
	s_setprio 0
	s_barrier
	ds_read_b128 v[206:209], v242 offset:16384
	ds_read_b128 v[210:213], v243 offset:16384
	ds_read_b128 v[214:217], v242 offset:18432
	ds_read_b128 v[218:221], v243 offset:18432
	ds_read_b128 v[222:225], v242 offset:20480
	ds_read_b128 v[226:229], v243 offset:20480
	ds_read_b128 v[230:233], v242 offset:22528
	ds_read_b128 v[234:237], v243 offset:22528
	s_mov_b32 m0, s38
	s_nop 0
	global_load_lds_dwordx4 v240, s[26:27]
	s_add_u32 s60, s26, 0x40000
	s_mov_b32 m0, s39
	s_nop 0
	global_load_lds_dwordx4 v241, s[26:27]
	s_addc_u32 s61, s27, 0
	s_mov_b32 m0, s40
	s_nop 0
	global_load_lds_dwordx4 v240, s[60:61]
	s_nop 0
	s_mov_b32 m0, s41
	s_nop 0
	global_load_lds_dwordx4 v241, s[60:61]
	s_nop 0
	s_mov_b32 m0, s37
	s_nop 0
	global_load_lds_dwordx4 v238, s[28:29]
	s_nop 0
	s_mov_b32 m0, s42
	s_nop 0
	global_load_lds_dwordx4 v239, s[28:29]
	s_waitcnt vmcnt(8)
	s_waitcnt lgkmcnt(0)
	s_barrier
	s_setprio 1
	s_waitcnt lgkmcnt(6)
	v_mfma_scale_f32_16x16x128_f8f6f4 v[96:99], v[28:35], v[206:213], v[96:99], v189, v2 op_sel_hi:[0,0,0]
	v_mfma_scale_f32_16x16x128_f8f6f4 v[92:95], v[20:27], v[206:213], v[92:95], v189, v2 op_sel_hi:[0,0,0]
	s_waitcnt lgkmcnt(4)
	v_mfma_scale_f32_16x16x128_f8f6f4 v[84:87], v[28:35], v[214:221], v[84:87], v189, v2 op_sel_hi:[0,0,0]
	v_mfma_scale_f32_16x16x128_f8f6f4 v[76:79], v[20:27], v[214:221], v[76:79], v189, v2 op_sel_hi:[0,0,0]
	s_waitcnt lgkmcnt(2)
	v_mfma_scale_f32_16x16x128_f8f6f4 v[68:71], v[28:35], v[222:229], v[68:71], v189, v2 op_sel_hi:[0,0,0]
	v_mfma_scale_f32_16x16x128_f8f6f4 v[60:63], v[20:27], v[222:229], v[60:63], v189, v2 op_sel_hi:[0,0,0]
	s_waitcnt lgkmcnt(0)
	v_mfma_scale_f32_16x16x128_f8f6f4 v[52:55], v[28:35], v[230:237], v[52:55], v189, v2 op_sel_hi:[0,0,0]
	v_mfma_scale_f32_16x16x128_f8f6f4 v[44:47], v[20:27], v[230:237], v[44:47], v189, v2 op_sel_hi:[0,0,0]
	s_setprio 0
	s_setprio 1
	v_mfma_scale_f32_16x16x128_f8f6f4 v[88:91], v[12:19], v[206:213], v[88:91], v189, v2 op_sel_hi:[0,0,0]
	v_mfma_scale_f32_16x16x128_f8f6f4 v[80:83], v[4:11], v[206:213], v[80:83], v189, v2 op_sel_hi:[0,0,0]
	v_mfma_scale_f32_16x16x128_f8f6f4 v[72:75], v[12:19], v[214:221], v[72:75], v189, v2 op_sel_hi:[0,0,0]
	v_mfma_scale_f32_16x16x128_f8f6f4 v[64:67], v[4:11], v[214:221], v[64:67], v189, v2 op_sel_hi:[0,0,0]
	v_mfma_scale_f32_16x16x128_f8f6f4 v[56:59], v[12:19], v[222:229], v[56:59], v189, v2 op_sel_hi:[0,0,0]
	v_mfma_scale_f32_16x16x128_f8f6f4 v[48:51], v[4:11], v[222:229], v[48:51], v189, v2 op_sel_hi:[0,0,0]
	v_mfma_scale_f32_16x16x128_f8f6f4 v[40:43], v[12:19], v[230:237], v[40:43], v189, v2 op_sel_hi:[0,0,0]
	v_mfma_scale_f32_16x16x128_f8f6f4 v[36:39], v[4:11], v[230:237], v[36:39], v189, v2 op_sel_hi:[0,0,0]
	s_setprio 0
	s_barrier
; #define PG8_STAGE(bufoff, gbase, voff) do { _Pragma("unroll") for (int _i = 0; _i < 2; ++_i) \
;         glds16((const void*)(gbase), (voff)[_i], ldsbase + (unsigned)(bufoff) + ldsw + (unsigned)_i * 8192u); } while (0)
; #define PG8_LDA(dst, b, h) do { _Pragma("unroll") for (int m = 0; m < 4; ++m) _Pragma("unroll") for (int k = 0; k < 2; ++k) dst[m][k] = *(const LAS bf16x8*)(lds + PG8_SA(b, h) + aoff + m * 2048 + k * 1024); } while (0)
; #define PG8_LDB(dst, b, h) do { _Pragma("unroll") for (int n = 0; n < 2; ++n) _Pragma("unroll") for (int k = 0; k < 2; ++k) dst[n][k] = *(const LAS bf16x8*)(lds + PG8_SB(b, h) + boff + n * 2048 + k * 1024); } while (0)
; #define PG8_WAIT_V(n) asm volatile("s_waitcnt vmcnt(" #n ")" ::: "memory")
; #define PG8_WAIT_L(n) asm volatile("s_waitcnt lgkmcnt(" #n ")" ::: "memory")
; #define PG8_BAR __builtin_amdgcn_s_barrier()
; #define PG8_SCHED __builtin_amdgcn_sched_barrier(0)
;     ...
;             PG8_LDB(B0, 1, 0); PG8_LDB(B1, 1, 1); PG8_SCHED; PG8_LDA(At, 1, 0); PG8_STAGE(PG8_SA(0, 1), a2 + hstepA, voffA);
;             PG8_WAIT_V(8); PG8_WAIT_L(0); PG8_BAR; PG8_MMA(0, 0, At, B0); PG8_MMA(0, 1, At, B1); PG8_BAR; PG8_SCHED;
;             PG8_LDA(At, 1, 1); PG8_STAGE(PG8_SB(1, 0), b3, voffB); PG8_STAGE(PG8_SB(1, 1), b3 + hstepB, voffB); PG8_STAGE(PG8_SA(1, 0), a3, voffA);
;             PG8_WAIT_V(8); PG8_WAIT_L(0); PG8_BAR; PG8_MMA(1, 0, At, B0); PG8_MMA(1, 1, At, B1); PG8_BAR; PG8_SCHED;
;         }
	v_add_u32_e32 v4, 0x18000, v244
	v_add_u32_e32 v247, 0x18000, v245
	v_add_u32_e32 v8, 0x1c000, v244
	v_add_u32_e32 v248, 0x1c000, v245
	ds_read_b128 v[20:23], v4
	ds_read_b128 v[24:27], v247
	ds_read_b128 v[28:31], v4 offset:2048
	ds_read_b128 v[32:35], v247 offset:2048
	ds_read_b128 v[12:15], v8
	ds_read_b128 v[16:19], v248
	ds_read_b128 v[4:7], v8 offset:2048
	ds_read_b128 v[8:11], v248 offset:2048
	ds_read_b128 v[206:209], v242 offset:32768
	ds_read_b128 v[210:213], v243 offset:32768
	ds_read_b128 v[214:217], v242 offset:34816
	ds_read_b128 v[218:221], v243 offset:34816
	ds_read_b128 v[222:225], v242 offset:36864
	ds_read_b128 v[226:229], v243 offset:36864
	ds_read_b128 v[230:233], v242 offset:38912
	ds_read_b128 v[234:237], v243 offset:38912
	s_add_u32 s28, s28, 0x40000
	s_addc_u32 s29, s29, 0
	s_mov_b32 m0, s43
	s_nop 0
	global_load_lds_dwordx4 v238, s[28:29]
	s_nop 0
	s_mov_b32 m0, s44
	s_nop 0
	global_load_lds_dwordx4 v239, s[28:29]
	s_waitcnt vmcnt(8)
	s_waitcnt lgkmcnt(0)
	s_barrier
	s_setprio 1
	s_waitcnt lgkmcnt(6)
	v_mfma_scale_f32_16x16x128_f8f6f4 v[160:163], v[20:27], v[206:213], v[160:163], v189, v2 op_sel_hi:[0,0,0]
	v_mfma_scale_f32_16x16x128_f8f6f4 v[156:159], v[28:35], v[206:213], v[156:159], v189, v2 op_sel_hi:[0,0,0]
	s_waitcnt lgkmcnt(4)
	v_mfma_scale_f32_16x16x128_f8f6f4 v[148:151], v[20:27], v[214:221], v[148:151], v189, v2 op_sel_hi:[0,0,0]
	v_mfma_scale_f32_16x16x128_f8f6f4 v[140:143], v[28:35], v[214:221], v[140:143], v189, v2 op_sel_hi:[0,0,0]
	s_waitcnt lgkmcnt(2)
	v_mfma_scale_f32_16x16x128_f8f6f4 v[132:135], v[20:27], v[222:229], v[132:135], v189, v2 op_sel_hi:[0,0,0]
	v_mfma_scale_f32_16x16x128_f8f6f4 v[124:127], v[28:35], v[222:229], v[124:127], v189, v2 op_sel_hi:[0,0,0]
	s_waitcnt lgkmcnt(0)
	v_mfma_scale_f32_16x16x128_f8f6f4 v[116:119], v[20:27], v[230:237], v[116:119], v189, v2 op_sel_hi:[0,0,0]
	v_mfma_scale_f32_16x16x128_f8f6f4 v[108:111], v[28:35], v[230:237], v[108:111], v189, v2 op_sel_hi:[0,0,0]
	s_setprio 0
	s_setprio 1
	v_mfma_scale_f32_16x16x128_f8f6f4 v[152:155], v[12:19], v[206:213], v[152:155], v189, v2 op_sel_hi:[0,0,0]
	v_mfma_scale_f32_16x16x128_f8f6f4 v[144:147], v[4:11], v[206:213], v[144:147], v189, v2 op_sel_hi:[0,0,0]
	v_mfma_scale_f32_16x16x128_f8f6f4 v[136:139], v[12:19], v[214:221], v[136:139], v189, v2 op_sel_hi:[0,0,0]
	v_mfma_scale_f32_16x16x128_f8f6f4 v[128:131], v[4:11], v[214:221], v[128:131], v189, v2 op_sel_hi:[0,0,0]
	v_mfma_scale_f32_16x16x128_f8f6f4 v[120:123], v[12:19], v[222:229], v[120:123], v189, v2 op_sel_hi:[0,0,0]
	v_mfma_scale_f32_16x16x128_f8f6f4 v[112:115], v[4:11], v[222:229], v[112:115], v189, v2 op_sel_hi:[0,0,0]
	v_mfma_scale_f32_16x16x128_f8f6f4 v[104:107], v[12:19], v[230:237], v[104:107], v189, v2 op_sel_hi:[0,0,0]
	v_mfma_scale_f32_16x16x128_f8f6f4 v[100:103], v[4:11], v[230:237], v[100:103], v189, v2 op_sel_hi:[0,0,0]
	s_setprio 0
	s_barrier
	ds_read_b128 v[206:209], v242 offset:49152
	ds_read_b128 v[210:213], v243 offset:49152
	ds_read_b128 v[214:217], v242 offset:51200
	ds_read_b128 v[218:221], v243 offset:51200
	ds_read_b128 v[222:225], v242 offset:53248
	ds_read_b128 v[226:229], v243 offset:53248
	ds_read_b128 v[230:233], v242 offset:55296
	ds_read_b128 v[234:237], v243 offset:55296
	s_add_u32 s28, s26, 0x80
	s_addc_u32 s29, s27, 0
	s_mov_b32 m0, s49
	s_nop 0
	global_load_lds_dwordx4 v240, s[28:29]
	s_add_u32 s26, s26, 0x40080
	s_mov_b32 m0, s50
	s_nop 0
	global_load_lds_dwordx4 v241, s[28:29]
	s_addc_u32 s27, s27, 0
	s_mov_b32 m0, s53
	s_nop 0
	global_load_lds_dwordx4 v240, s[26:27]
	s_nop 0
	s_mov_b32 m0, s54
	s_nop 0
	global_load_lds_dwordx4 v241, s[26:27]
	s_mov_b32 m0, s51
	s_nop 0
	global_load_lds_dwordx4 v238, s[24:25]
	s_nop 0
	s_mov_b32 m0, s52
	s_nop 0
	global_load_lds_dwordx4 v239, s[24:25]
	s_waitcnt vmcnt(8)
	s_waitcnt lgkmcnt(0)
	s_barrier
	s_setprio 1
	s_waitcnt lgkmcnt(6)
	v_mfma_scale_f32_16x16x128_f8f6f4 v[96:99], v[20:27], v[206:213], v[96:99], v189, v2 op_sel_hi:[0,0,0]
	v_mfma_scale_f32_16x16x128_f8f6f4 v[92:95], v[28:35], v[206:213], v[92:95], v189, v2 op_sel_hi:[0,0,0]
	s_waitcnt lgkmcnt(4)
	v_mfma_scale_f32_16x16x128_f8f6f4 v[84:87], v[20:27], v[214:221], v[84:87], v189, v2 op_sel_hi:[0,0,0]
	v_mfma_scale_f32_16x16x128_f8f6f4 v[76:79], v[28:35], v[214:221], v[76:79], v189, v2 op_sel_hi:[0,0,0]
	s_waitcnt lgkmcnt(2)
	v_mfma_scale_f32_16x16x128_f8f6f4 v[68:71], v[20:27], v[222:229], v[68:71], v189, v2 op_sel_hi:[0,0,0]
	v_mfma_scale_f32_16x16x128_f8f6f4 v[60:63], v[28:35], v[222:229], v[60:63], v189, v2 op_sel_hi:[0,0,0]
	s_waitcnt lgkmcnt(0)
	v_mfma_scale_f32_16x16x128_f8f6f4 v[52:55], v[20:27], v[230:237], v[52:55], v189, v2 op_sel_hi:[0,0,0]
	v_mfma_scale_f32_16x16x128_f8f6f4 v[44:47], v[28:35], v[230:237], v[44:47], v189, v2 op_sel_hi:[0,0,0]
	s_setprio 0
	s_setprio 1
	v_mfma_scale_f32_16x16x128_f8f6f4 v[88:91], v[12:19], v[206:213], v[88:91], v189, v2 op_sel_hi:[0,0,0]
	v_mfma_scale_f32_16x16x128_f8f6f4 v[80:83], v[4:11], v[206:213], v[80:83], v189, v2 op_sel_hi:[0,0,0]
	v_mfma_scale_f32_16x16x128_f8f6f4 v[72:75], v[12:19], v[214:221], v[72:75], v189, v2 op_sel_hi:[0,0,0]
	v_mfma_scale_f32_16x16x128_f8f6f4 v[64:67], v[4:11], v[214:221], v[64:67], v189, v2 op_sel_hi:[0,0,0]
	v_mfma_scale_f32_16x16x128_f8f6f4 v[56:59], v[12:19], v[222:229], v[56:59], v189, v2 op_sel_hi:[0,0,0]
	v_mfma_scale_f32_16x16x128_f8f6f4 v[48:51], v[4:11], v[222:229], v[48:51], v189, v2 op_sel_hi:[0,0,0]
	v_mfma_scale_f32_16x16x128_f8f6f4 v[40:43], v[12:19], v[230:237], v[40:43], v189, v2 op_sel_hi:[0,0,0]
	v_mfma_scale_f32_16x16x128_f8f6f4 v[36:39], v[4:11], v[230:237], v[36:39], v189, v2 op_sel_hi:[0,0,0]
	s_setprio 0
	s_barrier
	s_add_i32 s31, s31, 2
	s_add_u32 s17, s17, 0x100
	s_addc_u32 s19, s19, 0
	s_add_u32 s4, s4, 0x100
	s_addc_u32 s5, s5, 0
	s_cmp_gt_u32 s31, 13
	s_cbranch_scc0 .LBB0_1950
	s_and_b64 vcc, exec, s[14:15]
	s_cbranch_vccz .LBB0_1953
	s_barrier

; __device__ __forceinline__ unsigned cvtpk(float lo, float hi) { unsigned r; asm volatile("v_cvt_pk_bf16_f32 %0, %1, %2" : "=v"(r) : "v"(lo), "v"(hi)); return r; }
;     __device__ __forceinline__ void operator()(const f32x4 (&acc)[2][2][4][2], const Unit& u, int wr, int wc, int fr, int fq) const {
;     ...
;         } else {
;             const int uu = 4 * wc + fq; const bool isq = pn < 4; const float scale = isq ? 0.08838834764831845f : 1.0f;
; #pragma unroll
;             for (int ai = 0; ai < 2; ++ai)
; #pragma unroll
;                 for (int m = 0; m < 4; ++m) { const int t = row0 + ai * HALF + m * 16, b = t >> 11, s = t & 2047;
;                     const float rsc = scale * rr8[ai][m];
;                     const f32x4 c = *(const f32x4*)(cosN + s * 64 + 4 * uu) * rsc, sn = *(const f32x4*)(sinN + s * 64 + 4 * uu) * rsc;
; #pragma unroll
;                     for (int bj = 0; bj < 2; ++bj) { const f32x4 x1 = acc[ai][bj][m][0], x2 = acc[ai][bj][m][1];
;                         const f32x4 o1 = x1 * c - x2 * sn, o2 = x1 * sn + x2 * c;
;                         bf16_t* dst = isq ? (QN + (size_t)t * 1024 + (2 * pn + bj) * 128 + 4 * uu) : (KV6 + (size_t)(pn - 4) * kvstride + ((size_t)(b * 2 + bj) * 2048 + s) * 128 + 4 * uu);
;                         u32x2 w1, w2; w1.x = cvtpk(o1[0], o1[1]); w1.y = cvtpk(o1[2], o1[3]); w2.x = cvtpk(o2[0], o2[1]); w2.y = cvtpk(o2[2], o2[3]);
;                         *(u32x2*)dst = w1; *(u32x2*)(dst + 64) = w2; } }
.LBB0_1968:
	s_andn2_b64 vcc, exec, s[24:25]
	s_cbranch_vccnz .LBB0_2034
	v_and_b32_e32 v13, 0x7cf, v12
	v_lshlrev_b32_e32 v2, 8, v13
	v_lshl_add_u64 v[4:5], v[166:167], 0, v[2:3]
	v_lshl_add_u64 v[8:9], v[168:169], 0, v[2:3]
	global_load_dwordx4 v[4:7], v[4:5], off
	v_lshlrev_b32_e32 v2, 7, v13
	global_load_dwordx4 v[8:11], v[8:9], off
	v_lshlrev_b32_e32 v248, 8, v13
	v_mov_b32_e32 v249, v3
	v_lshl_add_u64 v[246:247], v[166:167], 0, v[248:249]
	v_lshl_add_u64 v[248:249], v[168:169], 0, v[248:249]
	s_mov_b64 s[66:67], 0x1000
	v_lshl_add_u64 v[198:199], s[66:67], 0, v[246:247]
	global_load_dwordx4 v[210:213], v[198:199], off
	v_lshl_add_u64 v[198:199], s[66:67], 0, v[248:249]
	global_load_dwordx4 v[206:209], v[198:199], off
	s_mov_b64 s[66:67], 0x2000
	v_lshl_add_u64 v[198:199], s[66:67], 0, v[246:247]
	global_load_dwordx4 v[218:221], v[198:199], off
	v_lshl_add_u64 v[198:199], s[66:67], 0, v[248:249]
	global_load_dwordx4 v[214:217], v[198:199], off
	s_mov_b64 s[66:67], 0x3000
	v_lshl_add_u64 v[198:199], s[66:67], 0, v[246:247]
	global_load_dwordx4 v[226:229], v[198:199], off
	v_lshl_add_u64 v[198:199], s[66:67], 0, v[248:249]
	global_load_dwordx4 v[222:225], v[198:199], off
	s_mov_b64 s[66:67], 0x8000
	v_lshl_add_u64 v[198:199], s[66:67], 0, v[246:247]
	global_load_dwordx4 v[234:237], v[198:199], off
	v_lshl_add_u64 v[198:199], s[66:67], 0, v[248:249]
	global_load_dwordx4 v[230:233], v[198:199], off
	s_mov_b64 s[30:31], -1
	s_and_b64 vcc, exec, s[28:29]
	s_mul_hi_u32 s17, s19, 0x802000
	s_mul_i32 s19, s19, 0x802000
	v_lshlrev_b32_e32 v170, 1, v2
	s_cbranch_vccz .LBB0_1971
	s_add_u32 s30, s45, s19
	s_addc_u32 s31, s46, s17
	s_ashr_i32 s27, s26, 31
	s_lshl_b64 s[24:25], s[26:27], 19
	s_add_u32 s24, s30, s24
	s_addc_u32 s25, s31, s25
	v_mov_b32_e32 v171, v3
	v_lshl_add_u64 v[178:179], s[24:25], 0, v[170:171]
	s_mov_b64 s[30:31], 0

; __device__ __forceinline__ unsigned cvtpk(float lo, float hi) { unsigned r; asm volatile("v_cvt_pk_bf16_f32 %0, %1, %2" : "=v"(r) : "v"(lo), "v"(hi)); return r; }
;     __device__ __forceinline__ void operator()(const f32x4 (&acc)[2][2][4][2], const Unit& u, int wr, int wc, int fr, int fq) const {
;     ...
;                 for (int m = 0; m < 4; ++m) { const int t = row0 + ai * HALF + m * 16, b = t >> 11, s = t & 2047;
;                     const float rsc = scale * rr8[ai][m];
;                     const f32x4 c = *(const f32x4*)(cosN + s * 64 + 4 * uu) * rsc, sn = *(const f32x4*)(sinN + s * 64 + 4 * uu) * rsc;
; #pragma unroll
;                     for (int bj = 0; bj < 2; ++bj) { const f32x4 x1 = acc[ai][bj][m][0], x2 = acc[ai][bj][m][1];
;                         const f32x4 o1 = x1 * c - x2 * sn, o2 = x1 * sn + x2 * c;
;                         bf16_t* dst = isq ? (QN + (size_t)t * 1024 + (2 * pn + bj) * 128 + 4 * uu) : (KV6 + (size_t)(pn - 4) * kvstride + ((size_t)(b * 2 + bj) * 2048 + s) * 128 + 4 * uu);
;                         u32x2 w1, w2; w1.x = cvtpk(o1[0], o1[1]); w1.y = cvtpk(o1[2], o1[3]); w2.x = cvtpk(o2[0], o2[1]); w2.y = cvtpk(o2[2], o2[3]);
;                         *(u32x2*)dst = w1; *(u32x2*)(dst + 64) = w2; } }
.LBB0_1973:
	v_mov_b32_e32 v2, 0x3db504f3
	v_cndmask_b32_e64 v13, 1.0, v2, s[4:5]
	s_waitcnt vmcnt(10)
	v_mul_f32_e32 v2, v13, v30
	s_waitcnt vmcnt(8)
	v_pk_mul_f32 v[8:9], v[2:3], v[8:9] op_sel_hi:[0,1]
	v_pk_mul_f32 v[4:5], v[2:3], v[4:5] op_sel_hi:[0,1]
	v_pk_mul_f32 v[10:11], v[2:3], v[10:11] op_sel_hi:[0,1]
	v_pk_mul_f32 v[172:173], v[156:157], v[8:9]
	v_pk_mul_f32 v[6:7], v[2:3], v[6:7] op_sel_hi:[0,1]
	v_pk_mul_f32 v[174:175], v[158:159], v[10:11]
	v_pk_fma_f32 v[172:173], v[160:161], v[4:5], v[172:173] neg_lo:[0,0,1] neg_hi:[0,0,1]
	v_lshlrev_b32_e32 v2, 1, v0
	v_cndmask_b32_e64 v15, 0, 1, s[28:29]
	v_pk_fma_f32 v[174:175], v[162:163], v[6:7], v[174:175] neg_lo:[0,0,1] neg_hi:[0,0,1]
	v_pk_mul_f32 v[186:187], v[160:161], v[8:9]
	v_pk_mul_f32 v[196:197], v[162:163], v[10:11]
	v_lshl_add_u64 v[178:179], v[178:179], 0, v[2:3]
	v_cvt_pk_bf16_f32 v172, v172, v173
	v_cvt_pk_bf16_f32 v173, v174, v175
	v_cmp_ne_u32_e64 s[4:5], 1, v15
	s_andn2_b64 vcc, exec, s[28:29]
	s_mov_b64 s[28:29], -1
	v_pk_fma_f32 v[196:197], v[158:159], v[6:7], v[196:197]
	v_pk_fma_f32 v[186:187], v[156:157], v[4:5], v[186:187]
	s_nop 0
	v_cvt_pk_bf16_f32 v174, v186, v187
	v_cvt_pk_bf16_f32 v175, v196, v197
	global_store_dwordx2 v[178:179], v[172:173], off
	global_store_dwordx2 v[178:179], v[174:175], off offset:128
	s_cbranch_vccnz .LBB0_1975
	s_add_u32 s25, s45, s19
	s_addc_u32 s27, s46, s17
	s_or_b32 s28, s59, 1
	s_ashr_i32 s29, s28, 31
	s_lshl_b64 s[28:29], s[28:29], 19
	s_add_u32 s28, s25, s28
	s_addc_u32 s29, s27, s29
	v_mov_b32_e32 v171, v3
	v_lshl_add_u64 v[178:179], s[28:29], 0, v[170:171]
	s_mov_b64 s[28:29], 0

; __device__ __forceinline__ unsigned cvtpk(float lo, float hi) { unsigned r; asm volatile("v_cvt_pk_bf16_f32 %0, %1, %2" : "=v"(r) : "v"(lo), "v"(hi)); return r; }
;     __device__ __forceinline__ void operator()(const f32x4 (&acc)[2][2][4][2], const Unit& u, int wr, int wc, int fr, int fq) const {
;     ...
;             const int uu = 4 * wc + fq; const bool isq = pn < 4; const float scale = isq ? 0.08838834764831845f : 1.0f;
; #pragma unroll
;             for (int ai = 0; ai < 2; ++ai)
; #pragma unroll
;                 for (int m = 0; m < 4; ++m) { const int t = row0 + ai * HALF + m * 16, b = t >> 11, s = t & 2047;
;                     const float rsc = scale * rr8[ai][m];
;                     const f32x4 c = *(const f32x4*)(cosN + s * 64 + 4 * uu) * rsc, sn = *(const f32x4*)(sinN + s * 64 + 4 * uu) * rsc;
; #pragma unroll
;                     for (int bj = 0; bj < 2; ++bj) { const f32x4 x1 = acc[ai][bj][m][0], x2 = acc[ai][bj][m][1];
;                         const f32x4 o1 = x1 * c - x2 * sn, o2 = x1 * sn + x2 * c;
;                         bf16_t* dst = isq ? (QN + (size_t)t * 1024 + (2 * pn + bj) * 128 + 4 * uu) : (KV6 + (size_t)(pn - 4) * kvstride + ((size_t)(b * 2 + bj) * 2048 + s) * 128 + 4 * uu);
;                         u32x2 w1, w2; w1.x = cvtpk(o1[0], o1[1]); w1.y = cvtpk(o1[2], o1[3]); w2.x = cvtpk(o2[0], o2[1]); w2.y = cvtpk(o2[2], o2[3]);
;                         *(u32x2*)dst = w1; *(u32x2*)(dst + 64) = w2; } }
.LBB0_1981:
	v_mul_f32_e32 v172, v13, v28
	s_waitcnt vmcnt(10)
	v_pk_mul_f32 v[206:207], v[172:173], v[206:207] op_sel_hi:[0,1]
	v_pk_mul_f32 v[210:211], v[172:173], v[210:211] op_sel_hi:[0,1]
	v_pk_mul_f32 v[208:209], v[172:173], v[208:209] op_sel_hi:[0,1]
	v_pk_mul_f32 v[174:175], v[140:141], v[206:207]
	v_pk_mul_f32 v[212:213], v[172:173], v[212:213] op_sel_hi:[0,1]
	v_pk_mul_f32 v[172:173], v[142:143], v[208:209]
	v_pk_fma_f32 v[174:175], v[148:149], v[210:211], v[174:175] neg_lo:[0,0,1] neg_hi:[0,0,1]
	v_pk_fma_f32 v[172:173], v[150:151], v[212:213], v[172:173] neg_lo:[0,0,1] neg_hi:[0,0,1]
	v_pk_mul_f32 v[186:187], v[150:151], v[208:209]
	v_pk_mul_f32 v[196:197], v[148:149], v[206:207]
	v_lshl_add_u64 v[178:179], v[178:179], 0, v[2:3]
	v_cvt_pk_bf16_f32 v174, v174, v175
	v_cvt_pk_bf16_f32 v175, v172, v173
	s_and_b64 vcc, exec, s[4:5]
	s_mov_b64 s[28:29], -1
	v_pk_fma_f32 v[186:187], v[142:143], v[212:213], v[186:187]
	v_pk_fma_f32 v[196:197], v[140:141], v[210:211], v[196:197]
	s_nop 0
	v_cvt_pk_bf16_f32 v172, v196, v197
	v_cvt_pk_bf16_f32 v173, v186, v187
	global_store_dwordx2 v[178:179], v[174:175], off
	global_store_dwordx2 v[178:179], v[172:173], off offset:128
	s_cbranch_vccnz .LBB0_1983
	s_add_u32 s25, s45, s19
	s_addc_u32 s27, s46, s17
	s_or_b32 s28, s59, 1
	s_ashr_i32 s29, s28, 31
	s_lshl_b64 s[28:29], s[28:29], 19
	s_add_u32 s28, s25, s28
	s_addc_u32 s29, s27, s29
	v_mov_b32_e32 v171, v3
	v_lshl_add_u64 v[178:179], s[28:29], 0, v[170:171]
	s_mov_b64 s[28:29], 0

; __device__ __forceinline__ unsigned cvtpk(float lo, float hi) { unsigned r; asm volatile("v_cvt_pk_bf16_f32 %0, %1, %2" : "=v"(r) : "v"(lo), "v"(hi)); return r; }
;     __device__ __forceinline__ void operator()(const f32x4 (&acc)[2][2][4][2], const Unit& u, int wr, int wc, int fr, int fq) const {
;     ...
;             const int uu = 4 * wc + fq; const bool isq = pn < 4; const float scale = isq ? 0.08838834764831845f : 1.0f;
; #pragma unroll
;             for (int ai = 0; ai < 2; ++ai)
; #pragma unroll
;                 for (int m = 0; m < 4; ++m) { const int t = row0 + ai * HALF + m * 16, b = t >> 11, s = t & 2047;
;                     const float rsc = scale * rr8[ai][m];
;                     const f32x4 c = *(const f32x4*)(cosN + s * 64 + 4 * uu) * rsc, sn = *(const f32x4*)(sinN + s * 64 + 4 * uu) * rsc;
; #pragma unroll
;                     for (int bj = 0; bj < 2; ++bj) { const f32x4 x1 = acc[ai][bj][m][0], x2 = acc[ai][bj][m][1];
;                         const f32x4 o1 = x1 * c - x2 * sn, o2 = x1 * sn + x2 * c;
;                         bf16_t* dst = isq ? (QN + (size_t)t * 1024 + (2 * pn + bj) * 128 + 4 * uu) : (KV6 + (size_t)(pn - 4) * kvstride + ((size_t)(b * 2 + bj) * 2048 + s) * 128 + 4 * uu);
;                         u32x2 w1, w2; w1.x = cvtpk(o1[0], o1[1]); w1.y = cvtpk(o1[2], o1[3]); w2.x = cvtpk(o2[0], o2[1]); w2.y = cvtpk(o2[2], o2[3]);
;                         *(u32x2*)dst = w1; *(u32x2*)(dst + 64) = w2; } }
.LBB0_1985:
	v_pk_mul_f32 v[172:173], v[128:129], v[206:207]
	v_pk_mul_f32 v[206:207], v[136:137], v[206:207]
	v_pk_mul_f32 v[170:171], v[130:131], v[208:209]
	v_pk_mul_f32 v[208:209], v[138:139], v[208:209]
	v_pk_fma_f32 v[206:207], v[128:129], v[210:211], v[206:207]
	s_movk_i32 s25, 0x7ef
	v_pk_fma_f32 v[170:171], v[138:139], v[212:213], v[170:171] neg_lo:[0,0,1] neg_hi:[0,0,1]
	v_pk_fma_f32 v[172:173], v[136:137], v[210:211], v[172:173] neg_lo:[0,0,1] neg_hi:[0,0,1]
	v_pk_fma_f32 v[208:209], v[130:131], v[212:213], v[208:209]
	v_lshl_add_u64 v[210:211], v[178:179], 0, v[2:3]
	v_cvt_pk_bf16_f32 v212, v172, v173
	v_cvt_pk_bf16_f32 v213, v170, v171
	v_cvt_pk_bf16_f32 v206, v206, v207
	v_cvt_pk_bf16_f32 v207, v208, v209
	v_bitop3_b32 v15, v12, s25, 32 bitop3:0xc8
	global_store_dwordx2 v[210:211], v[212:213], off
	global_store_dwordx2 v[210:211], v[206:207], off offset:128
	s_mov_b64 s[66:67], 0x9000
	v_lshl_add_u64 v[198:199], s[66:67], 0, v[246:247]
	global_load_dwordx4 v[210:213], v[198:199], off
	v_lshl_add_u64 v[198:199], s[66:67], 0, v[248:249]
	global_load_dwordx4 v[206:209], v[198:199], off
	v_lshlrev_b32_e32 v4, 8, v15
	v_mov_b32_e32 v5, v3
	v_lshl_add_u64 v[6:7], v[166:167], 0, v[4:5]
	v_lshl_add_u64 v[4:5], v[168:169], 0, v[4:5]
	s_nop 0
	v_lshlrev_b32_e32 v15, 7, v15
	s_mov_b64 s[28:29], -1
	s_and_b64 vcc, exec, s[4:5]
	v_lshlrev_b32_e32 v170, 1, v15
	s_cbranch_vccnz .LBB0_1987
	s_add_u32 s25, s45, s19
	s_addc_u32 s30, s46, s17
	s_ashr_i32 s27, s26, 31
	s_lshl_b64 s[28:29], s[26:27], 19
	s_add_u32 s28, s25, s28
	s_addc_u32 s29, s30, s29
	v_mov_b32_e32 v171, v3
	v_lshl_add_u64 v[178:179], s[28:29], 0, v[170:171]
	s_mov_b64 s[28:29], 0

; __device__ __forceinline__ unsigned cvtpk(float lo, float hi) { unsigned r; asm volatile("v_cvt_pk_bf16_f32 %0, %1, %2" : "=v"(r) : "v"(lo), "v"(hi)); return r; }
;     __device__ __forceinline__ void operator()(const f32x4 (&acc)[2][2][4][2], const Unit& u, int wr, int wc, int fr, int fq) const {
;     ...
;             const int uu = 4 * wc + fq; const bool isq = pn < 4; const float scale = isq ? 0.08838834764831845f : 1.0f;
; #pragma unroll
;             for (int ai = 0; ai < 2; ++ai)
; #pragma unroll
;                 for (int m = 0; m < 4; ++m) { const int t = row0 + ai * HALF + m * 16, b = t >> 11, s = t & 2047;
;                     const float rsc = scale * rr8[ai][m];
;                     const f32x4 c = *(const f32x4*)(cosN + s * 64 + 4 * uu) * rsc, sn = *(const f32x4*)(sinN + s * 64 + 4 * uu) * rsc;
; #pragma unroll
;                     for (int bj = 0; bj < 2; ++bj) { const f32x4 x1 = acc[ai][bj][m][0], x2 = acc[ai][bj][m][1];
;                         const f32x4 o1 = x1 * c - x2 * sn, o2 = x1 * sn + x2 * c;
;                         bf16_t* dst = isq ? (QN + (size_t)t * 1024 + (2 * pn + bj) * 128 + 4 * uu) : (KV6 + (size_t)(pn - 4) * kvstride + ((size_t)(b * 2 + bj) * 2048 + s) * 128 + 4 * uu);
;                         u32x2 w1, w2; w1.x = cvtpk(o1[0], o1[1]); w1.y = cvtpk(o1[2], o1[3]); w2.x = cvtpk(o2[0], o2[1]); w2.y = cvtpk(o2[2], o2[3]);
;                         *(u32x2*)dst = w1; *(u32x2*)(dst + 64) = w2; } }
.LBB0_1989:
	v_mul_f32_e32 v172, v13, v26
	s_waitcnt vmcnt(14)
	v_pk_mul_f32 v[214:215], v[172:173], v[214:215] op_sel_hi:[0,1]
	v_pk_mul_f32 v[218:219], v[172:173], v[218:219] op_sel_hi:[0,1]
	v_pk_mul_f32 v[216:217], v[172:173], v[216:217] op_sel_hi:[0,1]
	v_pk_mul_f32 v[174:175], v[124:125], v[214:215]
	v_pk_mul_f32 v[220:221], v[172:173], v[220:221] op_sel_hi:[0,1]
	v_pk_mul_f32 v[172:173], v[126:127], v[216:217]
	v_pk_fma_f32 v[174:175], v[132:133], v[218:219], v[174:175] neg_lo:[0,0,1] neg_hi:[0,0,1]
	v_pk_fma_f32 v[172:173], v[134:135], v[220:221], v[172:173] neg_lo:[0,0,1] neg_hi:[0,0,1]
	v_pk_mul_f32 v[186:187], v[134:135], v[216:217]
	v_pk_mul_f32 v[196:197], v[132:133], v[214:215]
	v_lshl_add_u64 v[178:179], v[178:179], 0, v[2:3]
	v_cvt_pk_bf16_f32 v174, v174, v175
	v_cvt_pk_bf16_f32 v175, v172, v173
	s_and_b64 vcc, exec, s[4:5]
	s_mov_b64 s[28:29], -1
	v_pk_fma_f32 v[186:187], v[126:127], v[220:221], v[186:187]
	v_pk_fma_f32 v[196:197], v[124:125], v[218:219], v[196:197]
	s_nop 0
	v_cvt_pk_bf16_f32 v172, v196, v197
	v_cvt_pk_bf16_f32 v173, v186, v187
	global_store_dwordx2 v[178:179], v[174:175], off
	global_store_dwordx2 v[178:179], v[172:173], off offset:128
	s_cbranch_vccnz .LBB0_1991
	s_add_u32 s25, s45, s19
	s_addc_u32 s27, s46, s17
	s_or_b32 s28, s59, 1
	s_ashr_i32 s29, s28, 31
	s_lshl_b64 s[28:29], s[28:29], 19
	s_add_u32 s28, s25, s28
	s_addc_u32 s29, s27, s29
	v_mov_b32_e32 v171, v3
	v_lshl_add_u64 v[178:179], s[28:29], 0, v[170:171]
	s_mov_b64 s[28:29], 0

; __device__ __forceinline__ unsigned cvtpk(float lo, float hi) { unsigned r; asm volatile("v_cvt_pk_bf16_f32 %0, %1, %2" : "=v"(r) : "v"(lo), "v"(hi)); return r; }
;     __device__ __forceinline__ void operator()(const f32x4 (&acc)[2][2][4][2], const Unit& u, int wr, int wc, int fr, int fq) const {
;     ...
;             const int uu = 4 * wc + fq; const bool isq = pn < 4; const float scale = isq ? 0.08838834764831845f : 1.0f;
; #pragma unroll
;             for (int ai = 0; ai < 2; ++ai)
; #pragma unroll
;                 for (int m = 0; m < 4; ++m) { const int t = row0 + ai * HALF + m * 16, b = t >> 11, s = t & 2047;
;                     const float rsc = scale * rr8[ai][m];
;                     const f32x4 c = *(const f32x4*)(cosN + s * 64 + 4 * uu) * rsc, sn = *(const f32x4*)(sinN + s * 64 + 4 * uu) * rsc;
; #pragma unroll
;                     for (int bj = 0; bj < 2; ++bj) { const f32x4 x1 = acc[ai][bj][m][0], x2 = acc[ai][bj][m][1];
;                         const f32x4 o1 = x1 * c - x2 * sn, o2 = x1 * sn + x2 * c;
;                         bf16_t* dst = isq ? (QN + (size_t)t * 1024 + (2 * pn + bj) * 128 + 4 * uu) : (KV6 + (size_t)(pn - 4) * kvstride + ((size_t)(b * 2 + bj) * 2048 + s) * 128 + 4 * uu);
;                         u32x2 w1, w2; w1.x = cvtpk(o1[0], o1[1]); w1.y = cvtpk(o1[2], o1[3]); w2.x = cvtpk(o2[0], o2[1]); w2.y = cvtpk(o2[2], o2[3]);
;                         *(u32x2*)dst = w1; *(u32x2*)(dst + 64) = w2; } }
.LBB0_1993:
	v_pk_mul_f32 v[172:173], v[112:113], v[214:215]
	v_pk_mul_f32 v[214:215], v[120:121], v[214:215]
	v_pk_mul_f32 v[170:171], v[114:115], v[216:217]
	v_pk_mul_f32 v[216:217], v[122:123], v[216:217]
	v_pk_fma_f32 v[214:215], v[112:113], v[218:219], v[214:215]
	s_movk_i32 s25, 0x7ff
	v_pk_fma_f32 v[170:171], v[122:123], v[220:221], v[170:171] neg_lo:[0,0,1] neg_hi:[0,0,1]
	v_pk_fma_f32 v[172:173], v[120:121], v[218:219], v[172:173] neg_lo:[0,0,1] neg_hi:[0,0,1]
	v_pk_fma_f32 v[216:217], v[114:115], v[220:221], v[216:217]
	v_lshl_add_u64 v[218:219], v[178:179], 0, v[2:3]
	v_cvt_pk_bf16_f32 v220, v172, v173
	v_cvt_pk_bf16_f32 v221, v170, v171
	v_cvt_pk_bf16_f32 v214, v214, v215
	v_cvt_pk_bf16_f32 v215, v216, v217
	v_bitop3_b32 v15, v12, s25, 48 bitop3:0xc8
	global_store_dwordx2 v[218:219], v[220:221], off
	global_store_dwordx2 v[218:219], v[214:215], off offset:128
	s_mov_b64 s[66:67], 0xa000
	v_lshl_add_u64 v[198:199], s[66:67], 0, v[246:247]
	global_load_dwordx4 v[218:221], v[198:199], off
	v_lshl_add_u64 v[198:199], s[66:67], 0, v[248:249]
	global_load_dwordx4 v[214:217], v[198:199], off
	v_lshlrev_b32_e32 v4, 8, v15
	v_mov_b32_e32 v5, v3
	v_lshl_add_u64 v[6:7], v[166:167], 0, v[4:5]
	v_lshl_add_u64 v[4:5], v[168:169], 0, v[4:5]
	s_nop 0
	v_lshlrev_b32_e32 v15, 7, v15
	s_mov_b64 s[28:29], -1
	s_and_b64 vcc, exec, s[4:5]
	v_lshlrev_b32_e32 v170, 1, v15
	s_cbranch_vccnz .LBB0_1995
	s_add_u32 s25, s45, s19
	s_addc_u32 s28, s46, s17
	s_ashr_i32 s27, s26, 31
	s_lshl_b64 s[26:27], s[26:27], 19
	s_add_u32 s26, s25, s26
	s_addc_u32 s27, s28, s27
	v_mov_b32_e32 v171, v3
	v_lshl_add_u64 v[178:179], s[26:27], 0, v[170:171]
	s_mov_b64 s[28:29], 0

; __device__ __forceinline__ unsigned cvtpk(float lo, float hi) { unsigned r; asm volatile("v_cvt_pk_bf16_f32 %0, %1, %2" : "=v"(r) : "v"(lo), "v"(hi)); return r; }
;     __device__ __forceinline__ void operator()(const f32x4 (&acc)[2][2][4][2], const Unit& u, int wr, int wc, int fr, int fq) const {
;     ...
;             const int uu = 4 * wc + fq; const bool isq = pn < 4; const float scale = isq ? 0.08838834764831845f : 1.0f;
; #pragma unroll
;             for (int ai = 0; ai < 2; ++ai)
; #pragma unroll
;                 for (int m = 0; m < 4; ++m) { const int t = row0 + ai * HALF + m * 16, b = t >> 11, s = t & 2047;
;                     const float rsc = scale * rr8[ai][m];
;                     const f32x4 c = *(const f32x4*)(cosN + s * 64 + 4 * uu) * rsc, sn = *(const f32x4*)(sinN + s * 64 + 4 * uu) * rsc;
; #pragma unroll
;                     for (int bj = 0; bj < 2; ++bj) { const f32x4 x1 = acc[ai][bj][m][0], x2 = acc[ai][bj][m][1];
;                         const f32x4 o1 = x1 * c - x2 * sn, o2 = x1 * sn + x2 * c;
;                         bf16_t* dst = isq ? (QN + (size_t)t * 1024 + (2 * pn + bj) * 128 + 4 * uu) : (KV6 + (size_t)(pn - 4) * kvstride + ((size_t)(b * 2 + bj) * 2048 + s) * 128 + 4 * uu);
;                         u32x2 w1, w2; w1.x = cvtpk(o1[0], o1[1]); w1.y = cvtpk(o1[2], o1[3]); w2.x = cvtpk(o2[0], o2[1]); w2.y = cvtpk(o2[2], o2[3]);
;                         *(u32x2*)dst = w1; *(u32x2*)(dst + 64) = w2; } }
.LBB0_1997:
	v_mul_f32_e32 v172, v13, v22
	s_waitcnt vmcnt(18)
	v_pk_mul_f32 v[222:223], v[172:173], v[222:223] op_sel_hi:[0,1]
	v_pk_mul_f32 v[226:227], v[172:173], v[226:227] op_sel_hi:[0,1]
	v_pk_mul_f32 v[224:225], v[172:173], v[224:225] op_sel_hi:[0,1]
	v_pk_mul_f32 v[174:175], v[108:109], v[222:223]
	v_pk_mul_f32 v[228:229], v[172:173], v[228:229] op_sel_hi:[0,1]
	v_pk_mul_f32 v[172:173], v[110:111], v[224:225]
	v_pk_fma_f32 v[174:175], v[116:117], v[226:227], v[174:175] neg_lo:[0,0,1] neg_hi:[0,0,1]
	v_pk_fma_f32 v[172:173], v[118:119], v[228:229], v[172:173] neg_lo:[0,0,1] neg_hi:[0,0,1]
	v_pk_mul_f32 v[186:187], v[118:119], v[224:225]
	v_pk_mul_f32 v[196:197], v[116:117], v[222:223]
	v_lshl_add_u64 v[178:179], v[178:179], 0, v[2:3]
	v_cvt_pk_bf16_f32 v174, v174, v175
	v_cvt_pk_bf16_f32 v175, v172, v173
	s_and_b64 vcc, exec, s[4:5]
	s_mov_b64 s[26:27], -1
	v_pk_fma_f32 v[186:187], v[110:111], v[228:229], v[186:187]
	v_pk_fma_f32 v[196:197], v[108:109], v[226:227], v[196:197]
	s_nop 0
	v_cvt_pk_bf16_f32 v172, v196, v197
	v_cvt_pk_bf16_f32 v173, v186, v187
	global_store_dwordx2 v[178:179], v[174:175], off
	global_store_dwordx2 v[178:179], v[172:173], off offset:128
	s_cbranch_vccnz .LBB0_1999
	s_add_u32 s25, s45, s19
	s_addc_u32 s28, s46, s17
	s_or_b32 s26, s59, 1
	s_ashr_i32 s27, s26, 31
	s_lshl_b64 s[26:27], s[26:27], 19
	s_add_u32 s26, s25, s26
	s_addc_u32 s27, s28, s27
	v_mov_b32_e32 v171, v3
	v_lshl_add_u64 v[178:179], s[26:27], 0, v[170:171]
	s_mov_b64 s[26:27], 0

; __device__ __forceinline__ unsigned cvtpk(float lo, float hi) { unsigned r; asm volatile("v_cvt_pk_bf16_f32 %0, %1, %2" : "=v"(r) : "v"(lo), "v"(hi)); return r; }
;     __device__ __forceinline__ void operator()(const f32x4 (&acc)[2][2][4][2], const Unit& u, int wr, int wc, int fr, int fq) const {
;     ...
;             const int uu = 4 * wc + fq; const bool isq = pn < 4; const float scale = isq ? 0.08838834764831845f : 1.0f;
; #pragma unroll
;             for (int ai = 0; ai < 2; ++ai)
; #pragma unroll
;                 for (int m = 0; m < 4; ++m) { const int t = row0 + ai * HALF + m * 16, b = t >> 11, s = t & 2047;
;                     const float rsc = scale * rr8[ai][m];
;                     const f32x4 c = *(const f32x4*)(cosN + s * 64 + 4 * uu) * rsc, sn = *(const f32x4*)(sinN + s * 64 + 4 * uu) * rsc;
; #pragma unroll
;                     for (int bj = 0; bj < 2; ++bj) { const f32x4 x1 = acc[ai][bj][m][0], x2 = acc[ai][bj][m][1];
;                         const f32x4 o1 = x1 * c - x2 * sn, o2 = x1 * sn + x2 * c;
;                         bf16_t* dst = isq ? (QN + (size_t)t * 1024 + (2 * pn + bj) * 128 + 4 * uu) : (KV6 + (size_t)(pn - 4) * kvstride + ((size_t)(b * 2 + bj) * 2048 + s) * 128 + 4 * uu);
;                         u32x2 w1, w2; w1.x = cvtpk(o1[0], o1[1]); w1.y = cvtpk(o1[2], o1[3]); w2.x = cvtpk(o2[0], o2[1]); w2.y = cvtpk(o2[2], o2[3]);
;                         *(u32x2*)dst = w1; *(u32x2*)(dst + 64) = w2; } }
.LBB0_2001:
	v_pk_mul_f32 v[172:173], v[100:101], v[222:223]
	v_pk_mul_f32 v[222:223], v[104:105], v[222:223]
	v_pk_mul_f32 v[170:171], v[102:103], v[224:225]
	v_pk_mul_f32 v[224:225], v[106:107], v[224:225]
	v_pk_fma_f32 v[222:223], v[100:101], v[226:227], v[222:223]
	v_pk_fma_f32 v[170:171], v[106:107], v[228:229], v[170:171] neg_lo:[0,0,1] neg_hi:[0,0,1]
	v_pk_fma_f32 v[172:173], v[104:105], v[226:227], v[172:173] neg_lo:[0,0,1] neg_hi:[0,0,1]
	v_pk_fma_f32 v[224:225], v[102:103], v[228:229], v[224:225]
	v_lshl_add_u64 v[226:227], v[178:179], 0, v[2:3]
	v_cvt_pk_bf16_f32 v228, v172, v173
	v_cvt_pk_bf16_f32 v229, v170, v171
	v_cvt_pk_bf16_f32 v222, v222, v223
	v_cvt_pk_bf16_f32 v223, v224, v225
	v_and_b32_e32 v15, 0x7cf, v24
	global_store_dwordx2 v[226:227], v[228:229], off
	global_store_dwordx2 v[226:227], v[222:223], off offset:128
	s_mov_b64 s[66:67], 0xb000
	v_lshl_add_u64 v[198:199], s[66:67], 0, v[246:247]
	global_load_dwordx4 v[226:229], v[198:199], off
	v_lshl_add_u64 v[198:199], s[66:67], 0, v[248:249]
	global_load_dwordx4 v[222:225], v[198:199], off
	v_lshlrev_b32_e32 v4, 8, v15
	v_mov_b32_e32 v5, v3
	v_lshl_add_u64 v[6:7], v[166:167], 0, v[4:5]
	v_lshl_add_u64 v[4:5], v[168:169], 0, v[4:5]
	s_nop 0
	v_lshlrev_b32_e32 v15, 7, v15
	s_mov_b64 s[26:27], -1
	s_and_b64 vcc, exec, s[4:5]
	v_ashrrev_i32_e32 v35, 31, v34
	v_lshlrev_b32_e32 v170, 1, v15
	s_cbranch_vccnz .LBB0_2003
	s_add_u32 s26, s45, s19
	s_addc_u32 s27, s46, s17
	v_lshlrev_b64 v[172:173], 19, v[34:35]
	v_lshl_add_u64 v[172:173], s[26:27], 0, v[172:173]
	v_mov_b32_e32 v171, v3
	v_lshl_add_u64 v[178:179], v[172:173], 0, v[170:171]
	s_mov_b64 s[26:27], 0

; __device__ __forceinline__ unsigned cvtpk(float lo, float hi) { unsigned r; asm volatile("v_cvt_pk_bf16_f32 %0, %1, %2" : "=v"(r) : "v"(lo), "v"(hi)); return r; }
;     __device__ __forceinline__ void operator()(const f32x4 (&acc)[2][2][4][2], const Unit& u, int wr, int wc, int fr, int fq) const {
;     ...
;             const int uu = 4 * wc + fq; const bool isq = pn < 4; const float scale = isq ? 0.08838834764831845f : 1.0f;
; #pragma unroll
;             for (int ai = 0; ai < 2; ++ai)
; #pragma unroll
;                 for (int m = 0; m < 4; ++m) { const int t = row0 + ai * HALF + m * 16, b = t >> 11, s = t & 2047;
;                     const float rsc = scale * rr8[ai][m];
;                     const f32x4 c = *(const f32x4*)(cosN + s * 64 + 4 * uu) * rsc, sn = *(const f32x4*)(sinN + s * 64 + 4 * uu) * rsc;
; #pragma unroll
;                     for (int bj = 0; bj < 2; ++bj) { const f32x4 x1 = acc[ai][bj][m][0], x2 = acc[ai][bj][m][1];
;                         const f32x4 o1 = x1 * c - x2 * sn, o2 = x1 * sn + x2 * c;
;                         bf16_t* dst = isq ? (QN + (size_t)t * 1024 + (2 * pn + bj) * 128 + 4 * uu) : (KV6 + (size_t)(pn - 4) * kvstride + ((size_t)(b * 2 + bj) * 2048 + s) * 128 + 4 * uu);
;                         u32x2 w1, w2; w1.x = cvtpk(o1[0], o1[1]); w1.y = cvtpk(o1[2], o1[3]); w2.x = cvtpk(o2[0], o2[1]); w2.y = cvtpk(o2[2], o2[3]);
;                         *(u32x2*)dst = w1; *(u32x2*)(dst + 64) = w2; } }
.LBB0_2013:
	v_mul_f32_e32 v172, v13, v18
	s_waitcnt vmcnt(16)
	v_pk_mul_f32 v[206:207], v[172:173], v[206:207] op_sel_hi:[0,1]
	v_pk_mul_f32 v[210:211], v[172:173], v[210:211] op_sel_hi:[0,1]
	v_pk_mul_f32 v[208:209], v[172:173], v[208:209] op_sel_hi:[0,1]
	v_pk_mul_f32 v[174:175], v[76:77], v[206:207]
	v_pk_mul_f32 v[212:213], v[172:173], v[212:213] op_sel_hi:[0,1]
	v_pk_mul_f32 v[172:173], v[78:79], v[208:209]
	v_pk_fma_f32 v[174:175], v[84:85], v[210:211], v[174:175] neg_lo:[0,0,1] neg_hi:[0,0,1]
	v_pk_fma_f32 v[172:173], v[86:87], v[212:213], v[172:173] neg_lo:[0,0,1] neg_hi:[0,0,1]
	v_pk_mul_f32 v[186:187], v[86:87], v[208:209]
	v_pk_mul_f32 v[196:197], v[84:85], v[206:207]
	v_lshl_add_u64 v[178:179], v[178:179], 0, v[2:3]
	v_cvt_pk_bf16_f32 v174, v174, v175
	v_cvt_pk_bf16_f32 v175, v172, v173
	s_and_b64 vcc, exec, s[4:5]
	s_mov_b64 s[26:27], -1
	v_pk_fma_f32 v[186:187], v[78:79], v[212:213], v[186:187]
	v_pk_fma_f32 v[196:197], v[76:77], v[210:211], v[196:197]
	s_nop 0
	v_cvt_pk_bf16_f32 v172, v196, v197
	v_cvt_pk_bf16_f32 v173, v186, v187
	global_store_dwordx2 v[178:179], v[174:175], off
	global_store_dwordx2 v[178:179], v[172:173], off offset:128
	s_cbranch_vccnz .LBB0_2015
	s_add_u32 s26, s45, s19
	s_addc_u32 s27, s46, s17
	v_lshlrev_b64 v[172:173], 19, v[32:33]
	v_lshl_add_u64 v[172:173], s[26:27], 0, v[172:173]
	v_mov_b32_e32 v171, v3
	v_lshl_add_u64 v[178:179], v[172:173], 0, v[170:171]
	s_mov_b64 s[26:27], 0

; __device__ __forceinline__ unsigned cvtpk(float lo, float hi) { unsigned r; asm volatile("v_cvt_pk_bf16_f32 %0, %1, %2" : "=v"(r) : "v"(lo), "v"(hi)); return r; }
;     __device__ __forceinline__ void operator()(const f32x4 (&acc)[2][2][4][2], const Unit& u, int wr, int wc, int fr, int fq) const {
;     ...
;             const int uu = 4 * wc + fq; const bool isq = pn < 4; const float scale = isq ? 0.08838834764831845f : 1.0f;
; #pragma unroll
;             for (int ai = 0; ai < 2; ++ai)
; #pragma unroll
;                 for (int m = 0; m < 4; ++m) { const int t = row0 + ai * HALF + m * 16, b = t >> 11, s = t & 2047;
;                     const float rsc = scale * rr8[ai][m];
;                     const f32x4 c = *(const f32x4*)(cosN + s * 64 + 4 * uu) * rsc, sn = *(const f32x4*)(sinN + s * 64 + 4 * uu) * rsc;
; #pragma unroll
;                     for (int bj = 0; bj < 2; ++bj) { const f32x4 x1 = acc[ai][bj][m][0], x2 = acc[ai][bj][m][1];
;                         const f32x4 o1 = x1 * c - x2 * sn, o2 = x1 * sn + x2 * c;
;                         bf16_t* dst = isq ? (QN + (size_t)t * 1024 + (2 * pn + bj) * 128 + 4 * uu) : (KV6 + (size_t)(pn - 4) * kvstride + ((size_t)(b * 2 + bj) * 2048 + s) * 128 + 4 * uu);
;                         u32x2 w1, w2; w1.x = cvtpk(o1[0], o1[1]); w1.y = cvtpk(o1[2], o1[3]); w2.x = cvtpk(o2[0], o2[1]); w2.y = cvtpk(o2[2], o2[3]);
;                         *(u32x2*)dst = w1; *(u32x2*)(dst + 64) = w2; } }
.LBB0_2017:
	v_pk_mul_f32 v[172:173], v[64:65], v[206:207]
	v_pk_mul_f32 v[206:207], v[72:73], v[206:207]
	v_pk_mul_f32 v[170:171], v[66:67], v[208:209]
	v_pk_mul_f32 v[208:209], v[74:75], v[208:209]
	v_pk_fma_f32 v[206:207], v[64:65], v[210:211], v[206:207]
	v_add_u32_e32 v176, 0xa0, v12
	v_pk_fma_f32 v[170:171], v[74:75], v[212:213], v[170:171] neg_lo:[0,0,1] neg_hi:[0,0,1]
	v_pk_fma_f32 v[172:173], v[72:73], v[210:211], v[172:173] neg_lo:[0,0,1] neg_hi:[0,0,1]
	v_pk_fma_f32 v[208:209], v[66:67], v[212:213], v[208:209]
	v_lshl_add_u64 v[210:211], v[178:179], 0, v[2:3]
	v_cvt_pk_bf16_f32 v212, v172, v173
	v_cvt_pk_bf16_f32 v213, v170, v171
	v_cvt_pk_bf16_f32 v206, v206, v207
	v_cvt_pk_bf16_f32 v207, v208, v209
	v_and_b32_e32 v15, 0x7ef, v176
	global_store_dwordx2 v[210:211], v[212:213], off
	global_store_dwordx2 v[210:211], v[206:207], off offset:128
	v_lshlrev_b32_e32 v4, 8, v15
	v_mov_b32_e32 v5, v3
	v_lshl_add_u64 v[6:7], v[166:167], 0, v[4:5]
	v_lshl_add_u64 v[4:5], v[168:169], 0, v[4:5]
	s_nop 0
	v_lshlrev_b32_e32 v15, 7, v15
	s_mov_b64 s[26:27], -1
	s_and_b64 vcc, exec, s[4:5]
	v_lshlrev_b32_e32 v170, 1, v15
	s_cbranch_vccnz .LBB0_2019
	s_add_u32 s26, s45, s19
	s_addc_u32 s27, s46, s17
	v_lshlrev_b64 v[172:173], 19, v[34:35]
	v_lshl_add_u64 v[172:173], s[26:27], 0, v[172:173]
	v_mov_b32_e32 v171, v3
	v_lshl_add_u64 v[178:179], v[172:173], 0, v[170:171]
	s_mov_b64 s[26:27], 0

; __device__ __forceinline__ unsigned cvtpk(float lo, float hi) { unsigned r; asm volatile("v_cvt_pk_bf16_f32 %0, %1, %2" : "=v"(r) : "v"(lo), "v"(hi)); return r; }
;     __device__ __forceinline__ void operator()(const f32x4 (&acc)[2][2][4][2], const Unit& u, int wr, int wc, int fr, int fq) const {
;     ...
;             const int uu = 4 * wc + fq; const bool isq = pn < 4; const float scale = isq ? 0.08838834764831845f : 1.0f;
; #pragma unroll
;             for (int ai = 0; ai < 2; ++ai)
; #pragma unroll
;                 for (int m = 0; m < 4; ++m) { const int t = row0 + ai * HALF + m * 16, b = t >> 11, s = t & 2047;
;                     const float rsc = scale * rr8[ai][m];
;                     const f32x4 c = *(const f32x4*)(cosN + s * 64 + 4 * uu) * rsc, sn = *(const f32x4*)(sinN + s * 64 + 4 * uu) * rsc;
; #pragma unroll
;                     for (int bj = 0; bj < 2; ++bj) { const f32x4 x1 = acc[ai][bj][m][0], x2 = acc[ai][bj][m][1];
;                         const f32x4 o1 = x1 * c - x2 * sn, o2 = x1 * sn + x2 * c;
;                         bf16_t* dst = isq ? (QN + (size_t)t * 1024 + (2 * pn + bj) * 128 + 4 * uu) : (KV6 + (size_t)(pn - 4) * kvstride + ((size_t)(b * 2 + bj) * 2048 + s) * 128 + 4 * uu);
;                         u32x2 w1, w2; w1.x = cvtpk(o1[0], o1[1]); w1.y = cvtpk(o1[2], o1[3]); w2.x = cvtpk(o2[0], o2[1]); w2.y = cvtpk(o2[2], o2[3]);
;                         *(u32x2*)dst = w1; *(u32x2*)(dst + 64) = w2; } }
.LBB0_2021:
	v_mul_f32_e32 v172, v13, v16
	s_waitcnt vmcnt(14)
	v_pk_mul_f32 v[214:215], v[172:173], v[214:215] op_sel_hi:[0,1]
	v_pk_mul_f32 v[218:219], v[172:173], v[218:219] op_sel_hi:[0,1]
	v_pk_mul_f32 v[216:217], v[172:173], v[216:217] op_sel_hi:[0,1]
	v_pk_mul_f32 v[174:175], v[60:61], v[214:215]
	v_pk_mul_f32 v[220:221], v[172:173], v[220:221] op_sel_hi:[0,1]
	v_pk_mul_f32 v[172:173], v[62:63], v[216:217]
	v_pk_fma_f32 v[174:175], v[68:69], v[218:219], v[174:175] neg_lo:[0,0,1] neg_hi:[0,0,1]
	v_pk_fma_f32 v[172:173], v[70:71], v[220:221], v[172:173] neg_lo:[0,0,1] neg_hi:[0,0,1]
	v_pk_mul_f32 v[186:187], v[70:71], v[216:217]
	v_pk_mul_f32 v[196:197], v[68:69], v[214:215]
	v_lshl_add_u64 v[178:179], v[178:179], 0, v[2:3]
	v_cvt_pk_bf16_f32 v174, v174, v175
	v_cvt_pk_bf16_f32 v175, v172, v173
	s_and_b64 vcc, exec, s[4:5]
	s_mov_b64 s[26:27], -1
	v_pk_fma_f32 v[186:187], v[62:63], v[220:221], v[186:187]
	v_pk_fma_f32 v[196:197], v[60:61], v[218:219], v[196:197]
	s_nop 0
	v_cvt_pk_bf16_f32 v172, v196, v197
	v_cvt_pk_bf16_f32 v173, v186, v187
	global_store_dwordx2 v[178:179], v[174:175], off
	global_store_dwordx2 v[178:179], v[172:173], off offset:128
	s_cbranch_vccnz .LBB0_2023
	s_add_u32 s26, s45, s19
	s_addc_u32 s27, s46, s17
	v_lshlrev_b64 v[172:173], 19, v[32:33]
	v_lshl_add_u64 v[172:173], s[26:27], 0, v[172:173]
	v_mov_b32_e32 v171, v3
	v_lshl_add_u64 v[178:179], v[172:173], 0, v[170:171]
	s_mov_b64 s[26:27], 0

; __device__ __forceinline__ unsigned cvtpk(float lo, float hi) { unsigned r; asm volatile("v_cvt_pk_bf16_f32 %0, %1, %2" : "=v"(r) : "v"(lo), "v"(hi)); return r; }
;     __device__ __forceinline__ void operator()(const f32x4 (&acc)[2][2][4][2], const Unit& u, int wr, int wc, int fr, int fq) const {
;     ...
;             const int uu = 4 * wc + fq; const bool isq = pn < 4; const float scale = isq ? 0.08838834764831845f : 1.0f;
; #pragma unroll
;             for (int ai = 0; ai < 2; ++ai)
; #pragma unroll
;                 for (int m = 0; m < 4; ++m) { const int t = row0 + ai * HALF + m * 16, b = t >> 11, s = t & 2047;
;                     const float rsc = scale * rr8[ai][m];
;                     const f32x4 c = *(const f32x4*)(cosN + s * 64 + 4 * uu) * rsc, sn = *(const f32x4*)(sinN + s * 64 + 4 * uu) * rsc;
; #pragma unroll
;                     for (int bj = 0; bj < 2; ++bj) { const f32x4 x1 = acc[ai][bj][m][0], x2 = acc[ai][bj][m][1];
;                         const f32x4 o1 = x1 * c - x2 * sn, o2 = x1 * sn + x2 * c;
;                         bf16_t* dst = isq ? (QN + (size_t)t * 1024 + (2 * pn + bj) * 128 + 4 * uu) : (KV6 + (size_t)(pn - 4) * kvstride + ((size_t)(b * 2 + bj) * 2048 + s) * 128 + 4 * uu);
;                         u32x2 w1, w2; w1.x = cvtpk(o1[0], o1[1]); w1.y = cvtpk(o1[2], o1[3]); w2.x = cvtpk(o2[0], o2[1]); w2.y = cvtpk(o2[2], o2[3]);
;                         *(u32x2*)dst = w1; *(u32x2*)(dst + 64) = w2; } }
.LBB0_2025:
	v_pk_mul_f32 v[172:173], v[48:49], v[214:215]
	v_pk_mul_f32 v[214:215], v[56:57], v[214:215]
	v_pk_mul_f32 v[170:171], v[50:51], v[216:217]
	v_pk_fma_f32 v[172:173], v[56:57], v[218:219], v[172:173] neg_lo:[0,0,1] neg_hi:[0,0,1]
	v_pk_mul_f32 v[216:217], v[58:59], v[216:217]
	v_pk_fma_f32 v[214:215], v[48:49], v[218:219], v[214:215]
	v_lshl_add_u64 v[218:219], v[178:179], 0, v[2:3]
	v_add_u32_e32 v178, 0xb0, v12
	v_pk_fma_f32 v[170:171], v[58:59], v[220:221], v[170:171] neg_lo:[0,0,1] neg_hi:[0,0,1]
	v_pk_fma_f32 v[216:217], v[50:51], v[220:221], v[216:217]
	v_cvt_pk_bf16_f32 v220, v172, v173
	v_cvt_pk_bf16_f32 v221, v170, v171
	v_cvt_pk_bf16_f32 v214, v214, v215
	v_and_b32_e32 v15, 0x7ff, v178
	v_cvt_pk_bf16_f32 v215, v216, v217
	global_store_dwordx2 v[218:219], v[220:221], off
	global_store_dwordx2 v[218:219], v[214:215], off offset:128
	v_lshlrev_b32_e32 v4, 8, v15
	v_mov_b32_e32 v5, v3
	v_lshl_add_u64 v[6:7], v[166:167], 0, v[4:5]
	v_lshl_add_u64 v[4:5], v[168:169], 0, v[4:5]
	s_nop 0
	v_lshlrev_b32_e32 v15, 7, v15
	s_mov_b64 s[26:27], -1
	s_and_b64 vcc, exec, s[4:5]
	v_lshlrev_b32_e32 v170, 1, v15
	s_cbranch_vccnz .LBB0_2027
	s_add_u32 s26, s45, s19
	s_addc_u32 s27, s46, s17
	v_lshlrev_b64 v[34:35], 19, v[34:35]
	v_lshl_add_u64 v[34:35], s[26:27], 0, v[34:35]
	v_mov_b32_e32 v171, v3
	v_lshl_add_u64 v[176:177], v[34:35], 0, v[170:171]
	s_mov_b64 s[26:27], 0

; __device__ __forceinline__ unsigned cvtpk(float lo, float hi) { unsigned r; asm volatile("v_cvt_pk_bf16_f32 %0, %1, %2" : "=v"(r) : "v"(lo), "v"(hi)); return r; }
;     __device__ __forceinline__ void operator()(const f32x4 (&acc)[2][2][4][2], const Unit& u, int wr, int wc, int fr, int fq) const {
;     ...
;             const int uu = 4 * wc + fq; const bool isq = pn < 4; const float scale = isq ? 0.08838834764831845f : 1.0f;
; #pragma unroll
;             for (int ai = 0; ai < 2; ++ai)
; #pragma unroll
;                 for (int m = 0; m < 4; ++m) { const int t = row0 + ai * HALF + m * 16, b = t >> 11, s = t & 2047;
;                     const float rsc = scale * rr8[ai][m];
;                     const f32x4 c = *(const f32x4*)(cosN + s * 64 + 4 * uu) * rsc, sn = *(const f32x4*)(sinN + s * 64 + 4 * uu) * rsc;
; #pragma unroll
;                     for (int bj = 0; bj < 2; ++bj) { const f32x4 x1 = acc[ai][bj][m][0], x2 = acc[ai][bj][m][1];
;                         const f32x4 o1 = x1 * c - x2 * sn, o2 = x1 * sn + x2 * c;
;                         bf16_t* dst = isq ? (QN + (size_t)t * 1024 + (2 * pn + bj) * 128 + 4 * uu) : (KV6 + (size_t)(pn - 4) * kvstride + ((size_t)(b * 2 + bj) * 2048 + s) * 128 + 4 * uu);
;                         u32x2 w1, w2; w1.x = cvtpk(o1[0], o1[1]); w1.y = cvtpk(o1[2], o1[3]); w2.x = cvtpk(o2[0], o2[1]); w2.y = cvtpk(o2[2], o2[3]);
;                         *(u32x2*)dst = w1; *(u32x2*)(dst + 64) = w2; } }
.LBB0_2029:
	v_mul_f32_e32 v172, v13, v14
	s_waitcnt vmcnt(12)
	v_pk_mul_f32 v[222:223], v[172:173], v[222:223] op_sel_hi:[0,1]
	v_pk_mul_f32 v[226:227], v[172:173], v[226:227] op_sel_hi:[0,1]
	v_pk_mul_f32 v[224:225], v[172:173], v[224:225] op_sel_hi:[0,1]
	v_pk_mul_f32 v[174:175], v[44:45], v[222:223]
	v_pk_mul_f32 v[228:229], v[172:173], v[228:229] op_sel_hi:[0,1]
	v_pk_mul_f32 v[172:173], v[46:47], v[224:225]
	v_pk_fma_f32 v[174:175], v[52:53], v[226:227], v[174:175] neg_lo:[0,0,1] neg_hi:[0,0,1]
	v_pk_fma_f32 v[172:173], v[54:55], v[228:229], v[172:173] neg_lo:[0,0,1] neg_hi:[0,0,1]
	v_pk_mul_f32 v[178:179], v[54:55], v[224:225]
	v_pk_mul_f32 v[186:187], v[52:53], v[222:223]
	v_lshl_add_u64 v[176:177], v[176:177], 0, v[2:3]
	v_cvt_pk_bf16_f32 v174, v174, v175
	v_cvt_pk_bf16_f32 v175, v172, v173
	s_and_b64 vcc, exec, s[4:5]
	s_mov_b64 s[4:5], -1
	v_pk_fma_f32 v[178:179], v[46:47], v[228:229], v[178:179]
	v_pk_fma_f32 v[186:187], v[44:45], v[226:227], v[186:187]
	s_nop 0
	v_cvt_pk_bf16_f32 v172, v186, v187
	v_cvt_pk_bf16_f32 v173, v178, v179
	global_store_dwordx2 v[176:177], v[174:175], off
	global_store_dwordx2 v[176:177], v[172:173], off offset:128
	s_cbranch_vccnz .LBB0_2031
	s_add_u32 s4, s45, s19
	s_addc_u32 s5, s46, s17
	v_lshlrev_b64 v[32:33], 19, v[32:33]
	v_lshl_add_u64 v[32:33], s[4:5], 0, v[32:33]
	v_mov_b32_e32 v171, v3
	v_lshl_add_u64 v[176:177], v[32:33], 0, v[170:171]
	s_mov_b64 s[4:5], 0

; __device__ __forceinline__ unsigned cvtpk(float lo, float hi) { unsigned r; asm volatile("v_cvt_pk_bf16_f32 %0, %1, %2" : "=v"(r) : "v"(lo), "v"(hi)); return r; }
;     __device__ __forceinline__ void operator()(const f32x4 (&acc)[2][2][4][2], const Unit& u, int wr, int wc, int fr, int fq) const {
;     ...
;             const int uu = 4 * wc + fq; const bool isq = pn < 4; const float scale = isq ? 0.08838834764831845f : 1.0f;
; #pragma unroll
;             for (int ai = 0; ai < 2; ++ai)
; #pragma unroll
;                 for (int m = 0; m < 4; ++m) { const int t = row0 + ai * HALF + m * 16, b = t >> 11, s = t & 2047;
;                     const float rsc = scale * rr8[ai][m];
;                     const f32x4 c = *(const f32x4*)(cosN + s * 64 + 4 * uu) * rsc, sn = *(const f32x4*)(sinN + s * 64 + 4 * uu) * rsc;
; #pragma unroll
;                     for (int bj = 0; bj < 2; ++bj) { const f32x4 x1 = acc[ai][bj][m][0], x2 = acc[ai][bj][m][1];
;                         const f32x4 o1 = x1 * c - x2 * sn, o2 = x1 * sn + x2 * c;
;                         bf16_t* dst = isq ? (QN + (size_t)t * 1024 + (2 * pn + bj) * 128 + 4 * uu) : (KV6 + (size_t)(pn - 4) * kvstride + ((size_t)(b * 2 + bj) * 2048 + s) * 128 + 4 * uu);
;                         u32x2 w1, w2; w1.x = cvtpk(o1[0], o1[1]); w1.y = cvtpk(o1[2], o1[3]); w2.x = cvtpk(o2[0], o2[1]); w2.y = cvtpk(o2[2], o2[3]);
;                         *(u32x2*)dst = w1; *(u32x2*)(dst + 64) = w2; } }
.LBB0_2033:
	v_pk_mul_f32 v[32:33], v[38:39], v[224:225]
	v_pk_mul_f32 v[34:35], v[36:37], v[222:223]
	v_pk_mul_f32 v[224:225], v[42:43], v[224:225]
	v_pk_mul_f32 v[222:223], v[40:41], v[222:223]
	v_pk_fma_f32 v[32:33], v[42:43], v[228:229], v[32:33] neg_lo:[0,0,1] neg_hi:[0,0,1]
	v_pk_fma_f32 v[34:35], v[40:41], v[226:227], v[34:35] neg_lo:[0,0,1] neg_hi:[0,0,1]
	v_pk_fma_f32 v[224:225], v[38:39], v[228:229], v[224:225]
	v_pk_fma_f32 v[222:223], v[36:37], v[226:227], v[222:223]
	v_lshl_add_u64 v[226:227], v[176:177], 0, v[2:3]
	v_cvt_pk_bf16_f32 v228, v34, v35
	v_cvt_pk_bf16_f32 v229, v32, v33
	v_cvt_pk_bf16_f32 v222, v222, v223
	v_cvt_pk_bf16_f32 v223, v224, v225
	global_store_dwordx2 v[226:227], v[228:229], off
	global_store_dwordx2 v[226:227], v[222:223], off offset:128

; __device__ __forceinline__ int lane_id() { int l_; asm volatile("v_mbcnt_lo_u32_b32 %0, -1, 0\n\tv_mbcnt_hi_u32_b32 %0, -1, %0" : "=v"(l_)); return l_; }
; #define PG8_STAGE(bufoff, gbase, voff) do { _Pragma("unroll") for (int _i = 0; _i < 2; ++_i) \
;         glds16((const void*)(gbase), (voff)[_i], ldsbase + (unsigned)(bufoff) + ldsw + (unsigned)_i * 8192u); } while (0)
; #define PG8_WAIT_V(n) asm volatile("s_waitcnt vmcnt(" #n ")" ::: "memory")
; #define PG8_BAR __builtin_amdgcn_s_barrier()
;     ...
;     int tid = w0_ * 64 + lane_id(); asm volatile("" : "+v"(tid));
;     const int wid = __builtin_amdgcn_readfirstlane(tid >> 6), lane = tid & 63, wr = wid >> 2, wc = wid & 3, fr = lane & 15, fq = lane >> 4;
;     const int nt = nt_ ? nt_ : Kb / 128;
;     unsigned voffA[2], voffB[2];
; #pragma unroll
;     for (int i = 0; i < 2; ++i) { int R, C; stage_rc(tid * 16 + i * 8192, R, C); const int Rb = Epi::PERM ? ((R & ~31) + perm32(R & 31)) : R;
;         voffA[i] = (unsigned)(R * ldab + C * 2); voffB[i] = (unsigned)(Rb * Kb + C * 2); }
;     const size_t kstep = (size_t)(BK * 2);
;     const size_t hstepA = (size_t)HALF * ldab, hstepB = (size_t)HALF * Kb;
;     const unsigned ldsw = (unsigned)wid * 1024u, ldsbase = (unsigned)(size_t)lds;
;     const int aoff = lds_byte(wr * 64 + fr, fq * 8), boff = lds_byte(wc * 32 + fr, fq * 8);
;     ...
;     Unit cur, nxt; int ui = 0;
;     if (!S.next(0, cur)) return;
;     f32x4 acc[2][2][4][2];
; #pragma unroll
;     for (int a = 0; a < 2; ++a)
; #pragma unroll
;         for (int b = 0; b < 2; ++b)
; #pragma unroll
;             for (int m = 0; m < 4; ++m)
; #pragma unroll
;                 for (int n = 0; n < 2; ++n) acc[a][b][m][n] = (f32x4){0.f, 0.f, 0.f, 0.f};
;     bf16x8 At[4][2], B0[2][2], B1[2][2];
;     const char* cA = uniform_ptr(cur.a); const char* cB = uniform_ptr(cur.b);
;     PG8_STAGE(PG8_SB(0, 0), cB, voffB); PG8_STAGE(PG8_SB(0, 1), cB + hstepB, voffB); PG8_STAGE(PG8_SA(0, 0), cA, voffA); PG8_STAGE(PG8_SA(0, 1), cA + hstepA, voffA);
;     if (wr == 1) PG8_BAR;
;     PG8_WAIT_V(2); PG8_BAR;
;     PG8_STAGE(PG8_SB(1, 0), cB + kstep, voffB); PG8_STAGE(PG8_SA(1, 0), cA + kstep, voffA); PG8_STAGE(PG8_SB(1, 1), cB + hstepB + kstep, voffB);
;     PG8_WAIT_V(6); PG8_BAR;
.LBB0_2099:
	s_andn2_b64 vcc, exec, s[2:3]
	s_cbranch_vccnz .LBB0_2205
	s_mov_b64 s[2:3], 0
	v_mbcnt_lo_u32_b32 v0, -1, 0
	v_mbcnt_hi_u32_b32 v0, -1, v0
	v_readlane_b32 s0, v250, 60
	v_readlane_b32 s4, v252, 30
	v_readlane_b32 s5, v252, 31
	v_add_u32_e32 v0, s0, v0
	s_andn2_b64 vcc, exec, s[4:5]
	v_mbcnt_lo_u32_b32 v0, -1, 0
	v_mbcnt_hi_u32_b32 v0, -1, v0
	s_nop 0
	v_add_u32_e32 v4, s0, v0
	s_nop 0
	v_readfirstlane_b32 s6, v4
	s_cbranch_vccnz .LBB0_2120
	s_waitcnt lgkmcnt(0)
	v_bfe_i32 v1, v4, 27, 1
	v_lshlrev_b32_e32 v2, 4, v4
	v_lshrrev_b32_e32 v1, 22, v1
	v_add_u32_e32 v1, v2, v1
	v_and_b32_e32 v1, 0xfffffc00, v1
	s_add_u32 s2, s80, s2
	v_sub_u32_e32 v1, v2, v1
	s_addc_u32 s3, s81, s3
	v_lshrrev_b32_e32 v5, 4, v1
	s_add_u32 s0, s2, 0x43892000
	v_bitop3_b32 v1, v5, v1, 32 bitop3:0x6c
	s_addc_u32 s24, s3, 0
	v_ashrrev_i32_e32 v0, 31, v4
	v_ashrrev_i32_e32 v6, 31, v1
	s_add_u32 s25, s2, 0x44094000
	v_lshrrev_b32_e32 v0, 26, v0
	v_lshrrev_b32_e32 v6, 26, v6
	s_addc_u32 s26, s3, 0
	s_lshl_b32 s4, s27, 23
	v_add_u32_e32 v0, v4, v0
	v_add_u32_e32 v6, v1, v6
	s_add_u32 s4, s2, s4
	v_ashrrev_i32_e32 v0, 6, v0
	v_lshrrev_b32_e32 v7, 6, v6
	v_and_b32_e32 v6, 0xc0, v6
	s_addc_u32 s5, s3, 0
	v_lshlrev_b32_e32 v5, 3, v0
	v_lshlrev_b32_e32 v0, 5, v0
	v_sub_u32_e32 v1, v1, v6
	s_add_u32 s27, s4, 0x2d00000
	v_and_b32_e32 v5, 0xffff0, v5
	v_and_b32_e32 v0, 32, v0
	v_ashrrev_i16_sdwa v1, v188, sext(v1) dst_sel:DWORD dst_unused:UNUSED_PAD src0_sel:DWORD src1_sel:BYTE_0
	v_add_u32_e32 v2, 0x2000, v2
	s_addc_u32 s28, s5, 0
	v_add_u32_sdwa v0, v0, sext(v1) dst_sel:DWORD dst_unused:UNUSED_PAD src0_sel:DWORD src1_sel:WORD_0
	v_add_lshl_u32 v1, v7, v5, 12
	v_ashrrev_i32_e32 v5, 31, v2
	s_ashr_i32 s8, s6, 6
	s_ashr_i32 s7, s6, 8
	v_lshrrev_b32_e32 v5, 22, v5
	s_lshl_b32 s9, s8, 10
	v_readlane_b32 s4, v253, 0
	v_add_u32_e32 v5, v2, v5
	v_readlane_b32 s5, v253, 1
	s_add_u32 s4, s27, s4
	v_ashrrev_i32_e32 v5, 10, v5
	s_addc_u32 s5, s28, s5
	v_readlane_b32 s10, v253, 3
	v_mul_i32_i24_e32 v6, 0x400, v5
	s_add_u32 s4, s4, s10
	v_sub_u32_e32 v2, v2, v6
	s_addc_u32 s5, s5, 0
	v_readlane_b32 s10, v253, 6
	v_lshrrev_b32_e32 v6, 4, v2
	v_readlane_b32 s11, v253, 7
	s_add_u32 s16, s4, s10
	v_bitop3_b32 v2, v6, v2, 32 bitop3:0x6c
	s_addc_u32 s17, s5, s11
	v_readlane_b32 s4, v253, 9
	v_ashrrev_i32_e32 v7, 31, v2
	v_readlane_b32 s5, v253, 10
	v_lshrrev_b32_e32 v7, 26, v7
	s_and_b64 s[4:5], s[4:5], exec
	v_add_u32_e32 v7, v2, v7
	s_cselect_b32 s5, s0, s25
	v_readlane_b32 s12, v253, 11
	v_lshrrev_b32_e32 v8, 6, v7
	v_and_b32_e32 v7, 0xc0, v7
	s_cselect_b32 s4, s24, s26
	s_add_u32 s5, s5, s12
	v_lshlrev_b32_e32 v6, 3, v5
	v_lshlrev_b32_e32 v5, 5, v5
	v_sub_u32_e32 v2, v2, v7
	s_addc_u32 s4, s4, 0
	v_and_b32_e32 v6, 0xffff0, v6
	v_and_b32_e32 v5, 32, v5
	v_ashrrev_i16_sdwa v2, v188, sext(v2) dst_sel:DWORD dst_unused:UNUSED_PAD src0_sel:DWORD src1_sel:BYTE_0
	s_add_u32 s18, s5, s10
	v_lshl_add_u32 v0, v0, 1, v1
	v_add_u32_sdwa v2, v5, sext(v2) dst_sel:DWORD dst_unused:UNUSED_PAD src0_sel:DWORD src1_sel:WORD_0
	v_add_lshl_u32 v5, v8, v6, 12
	s_addc_u32 s19, s4, s11
	s_add_i32 s29, s9, 0
	v_add_u32_e32 v1, v0, v1
	v_lshl_add_u32 v2, v2, 1, v5
	s_add_i32 s30, s29, 0x10000
	s_nop 0
	v_readlane_b32 s70, v250, 60
	v_mbcnt_lo_u32_b32 v246, -1, 0
	v_mbcnt_hi_u32_b32 v246, -1, v246
	v_add_u32_e32 v246, s70, v246
	v_bfe_u32 v247, v246, 4, 2
	v_bfe_u32 v248, v246, 6, 1
	v_lshl_or_b32 v247, v248, 2, v247
	v_and_b32_e32 v248, 7, v246
	v_xor_b32_e32 v247, v247, v248
	v_lshlrev_b32_e32 v247, 4, v247
	v_lshrrev_b32_e32 v248, 3, v246
	v_lshl_add_u32 v238, v248, 12, v247
	v_add_u32_e32 v239, 0x40000, v238
	v_lshl_add_u32 v240, v248, 13, v247
	v_add_u32_e32 v241, 0x80000, v240
	v_bfe_u32 v247, v246, 4, 2
	v_bfe_u32 v248, v246, 1, 3
	v_xor_b32_e32 v247, v247, v248
	v_lshlrev_b32_e32 v247, 4, v247
	v_and_b32_e32 v248, 7, v246
	v_lshl_or_b32 v247, v248, 7, v247
	v_bfe_u32 v248, v246, 3, 1
	v_lshl_or_b32 v247, v248, 10, v247
	v_bfe_u32 v248, v246, 8, 1
	v_lshl_or_b32 v242, v248, 13, v247
	v_xor_b32_e32 v243, 64, v242
	v_bfe_u32 v248, v246, 6, 2
	v_lshl_or_b32 v244, v248, 12, v247
	v_xor_b32_e32 v245, 64, v244
	s_mov_b32 m0, s30
	s_nop 0
	global_load_lds_dwordx4 v240, s[16:17]
	s_waitcnt vmcnt(0)
	v_add_u32_e32 v132, v2, v5
	s_add_i32 s31, s29, 0x12000
	s_mov_b32 m0, s31
	s_nop 0
	global_load_lds_dwordx4 v241, s[16:17]
	s_add_u32 s4, s16, 0x100000
	s_addc_u32 s5, s17, 0
	s_add_i32 s34, s29, 0x14000
	s_mov_b32 m0, s34
	s_nop 0
	global_load_lds_dwordx4 v240, s[4:5]
	s_add_i32 s35, s29, 0x16000
	s_mov_b32 m0, s35
	s_nop 0
	global_load_lds_dwordx4 v241, s[4:5]
	s_mov_b32 m0, s29
	s_nop 0
	global_load_lds_dwordx4 v238, s[18:19]
	s_add_i32 s36, s29, 0x2000
	s_mov_b32 m0, s36
	s_nop 0
	global_load_lds_dwordx4 v239, s[18:19]
	s_add_u32 s4, s18, 0x80000
	s_addc_u32 s5, s19, 0
	s_add_i32 s37, s29, 0x4000
	s_mov_b32 m0, s37
	s_nop 0
	global_load_lds_dwordx4 v238, s[4:5]
	s_add_i32 s38, s29, 0x6000
	s_mov_b32 m0, s38
	s_nop 0
	global_load_lds_dwordx4 v239, s[4:5]
	s_cmp_eq_u32 s7, 1
	s_cselect_b64 s[4:5], -1, 0
	s_cmp_lg_u32 s7, 1
	s_cbranch_scc1 .LBB0_2103
	s_barrier
.LBB0_2103:
	v_bfe_u32 v6, v4, 4, 2
	s_add_u32 s39, s2, 0x53a1e000
	v_and_b32_e32 v5, 15, v4
	v_lshlrev_b32_e32 v7, 4, v6
	v_lshlrev_b32_e32 v4, 2, v4
	s_addc_u32 s40, s3, 0
	v_lshl_or_b32 v133, s7, 6, v5
	v_lshl_or_b32 v5, v5, 6, v7
	s_lshl_b32 s2, s7, 13
	v_and_b32_e32 v4, 32, v4
	v_bitop3_b32 v7, v5, s2, v4 bitop3:0xde
	s_lshl_b32 s2, s8, 5
	s_and_b32 s8, s2, 0x60
	s_lshl_b32 s2, s8, 7
	v_bitop3_b32 v4, v5, s2, v4 bitop3:0xde
	s_add_u32 s2, s16, 0x80
	s_waitcnt vmcnt(2)
	s_barrier
	s_addc_u32 s3, s17, 0
	s_add_i32 s41, s29, 0x18000
	s_mov_b32 m0, s41
	s_nop 0
	global_load_lds_dwordx4 v240, s[2:3]
	s_add_i32 s42, s29, 0x1a000
	s_mov_b32 m0, s42
	s_nop 0
	global_load_lds_dwordx4 v241, s[2:3]
	s_add_u32 s2, s18, 0x80
	s_addc_u32 s3, s19, 0
	s_add_i32 s43, s29, 0x8000
	s_mov_b32 m0, s43
	s_nop 0
	global_load_lds_dwordx4 v238, s[2:3]
	s_add_i32 s44, s29, 0xa000
	s_mov_b32 m0, s44
	s_nop 0
	global_load_lds_dwordx4 v239, s[2:3]
	s_add_u32 s2, s16, 0x100080
	s_addc_u32 s3, s17, 0
	s_add_i32 s45, s29, 0x1c000
	s_mov_b32 m0, s45
	s_nop 0
	global_load_lds_dwordx4 v240, s[2:3]
	s_add_i32 s46, s29, 0x1e000
	s_mov_b32 m0, s46
	s_nop 0
	global_load_lds_dwordx4 v241, s[2:3]
	s_waitcnt vmcnt(6)
	s_add_i32 s47, s29, 0xc000
	v_readlane_b32 s14, v253, 4
	s_cmpk_lt_u32 s6, 0x100
	v_readlane_b32 s15, v253, 5
	s_cselect_b64 s[6:7], -1, 0
	s_add_i32 s48, s29, 0xe000
	v_lshl_or_b32 v134, v6, 2, s8
	s_mov_b32 s49, 0
	v_add_u32_e32 v135, 0, v4
	v_add_u32_e32 v136, 0, v7
	v_readlane_b32 s15, v253, 2
	v_readlane_b32 s52, v253, 8
	s_mov_b64 s[10:11], s[18:19]
	s_mov_b64 s[12:13], s[16:17]
	s_barrier
	s_branch .LBB0_2106

; #define PG8_STAGE(bufoff, gbase, voff) do { _Pragma("unroll") for (int _i = 0; _i < 2; ++_i) \
;         glds16((const void*)(gbase), (voff)[_i], ldsbase + (unsigned)(bufoff) + ldsw + (unsigned)_i * 8192u); } while (0)
; #define PG8_LDA(dst, b, h) do { _Pragma("unroll") for (int m = 0; m < 4; ++m) _Pragma("unroll") for (int k = 0; k < 2; ++k) dst[m][k] = *(const LAS bf16x8*)(lds + PG8_SA(b, h) + aoff + m * 2048 + k * 1024); } while (0)
; #define PG8_LDB(dst, b, h) do { _Pragma("unroll") for (int n = 0; n < 2; ++n) _Pragma("unroll") for (int k = 0; k < 2; ++k) dst[n][k] = *(const LAS bf16x8*)(lds + PG8_SB(b, h) + boff + n * 2048 + k * 1024); } while (0)
; #define PG8_WAIT_V(n) asm volatile("s_waitcnt vmcnt(" #n ")" ::: "memory")
; #define PG8_WAIT_L(n) asm volatile("s_waitcnt lgkmcnt(" #n ")" ::: "memory")
; #define PG8_BAR __builtin_amdgcn_s_barrier()
; #define PG8_SCHED __builtin_amdgcn_sched_barrier(0)
;     ...
;         for (int t = 0; t < nt; t += 2) {
;             const bool last = (t == nt - 2);
;             const char* a1 = cA + (size_t)(t + 1) * kstep;
;             const char* a2 = last ? nA : cA + (size_t)(t + 2) * kstep; const char* b2 = last ? nB : cB + (size_t)(t + 2) * kstep;
;             const char* a3 = a2 + kstep; const char* b3 = b2 + kstep;
;             PG8_LDB(B0, 0, 0); PG8_LDB(B1, 0, 1); PG8_SCHED; PG8_LDA(At, 0, 0); PG8_STAGE(PG8_SA(1, 1), a1 + hstepA, voffA);
;             PG8_WAIT_V(8); PG8_WAIT_L(0); PG8_BAR; PG8_MMA(0, 0, At, B0); PG8_MMA(0, 1, At, B1); PG8_BAR; PG8_SCHED;
;             PG8_LDA(At, 0, 1); PG8_STAGE(PG8_SB(0, 0), b2, voffB); PG8_STAGE(PG8_SB(0, 1), b2 + hstepB, voffB); PG8_STAGE(PG8_SA(0, 0), a2, voffA);
;             PG8_WAIT_V(8); PG8_WAIT_L(0); PG8_BAR; PG8_MMA(1, 0, At, B0); PG8_MMA(1, 1, At, B1); PG8_BAR; PG8_SCHED;
;             PG8_LDB(B0, 1, 0); PG8_LDB(B1, 1, 1); PG8_SCHED; PG8_LDA(At, 1, 0); PG8_STAGE(PG8_SA(0, 1), a2 + hstepA, voffA);
;             PG8_WAIT_V(8); PG8_WAIT_L(0); PG8_BAR; PG8_MMA(0, 0, At, B0); PG8_MMA(0, 1, At, B1); PG8_BAR; PG8_SCHED;
;             PG8_LDA(At, 1, 1); PG8_STAGE(PG8_SB(1, 0), b3, voffB); PG8_STAGE(PG8_SB(1, 1), b3 + hstepB, voffB); PG8_STAGE(PG8_SA(1, 0), a3, voffA);
;             PG8_WAIT_V(8); PG8_WAIT_L(0); PG8_BAR; PG8_MMA(1, 0, At, B0); PG8_MMA(1, 1, At, B1); PG8_BAR; PG8_SCHED;
;         }
.LBB0_2113:
	v_add_u32_e32 v137, 0x10000, v244
	v_add_u32_e32 v246, 0x10000, v245
	ds_read_b128 v[138:141], v137
	ds_read_b128 v[142:145], v246
	ds_read_b128 v[146:149], v137 offset:2048
	ds_read_b128 v[150:153], v246 offset:2048
	v_add_u32_e32 v137, 0x14000, v244
	v_add_u32_e32 v246, 0x14000, v245
	ds_read_b128 v[154:157], v137
	ds_read_b128 v[158:161], v246
	ds_read_b128 v[162:165], v137 offset:2048
	ds_read_b128 v[166:169], v246 offset:2048
	s_add_u32 s18, s16, 0xfff80080
	s_addc_u32 s19, s17, -1
	s_cmp_eq_u32 s54, 12
	s_cselect_b32 s22, s10, s18
	s_cselect_b32 s23, s11, s19
	s_cselect_b32 s20, s12, s9
	s_cselect_b32 s21, s13, s53
	s_add_u32 s18, s22, 0x80
	s_addc_u32 s19, s23, 0
	ds_read_b128 v[176:179], v242
	ds_read_b128 v[180:183], v243
	ds_read_b128 v[206:209], v242 offset:2048
	ds_read_b128 v[210:213], v243 offset:2048
	ds_read_b128 v[214:217], v242 offset:4096
	ds_read_b128 v[218:221], v243 offset:4096
	ds_read_b128 v[222:225], v242 offset:6144
	ds_read_b128 v[226:229], v243 offset:6144
	s_mov_b32 m0, s47
	s_nop 0
	global_load_lds_dwordx4 v238, s[16:17]
	s_nop 0
	s_mov_b32 m0, s48
	s_nop 0
	global_load_lds_dwordx4 v239, s[16:17]
	s_waitcnt vmcnt(8)
	s_waitcnt lgkmcnt(0)
	s_barrier
	s_setprio 1
	s_waitcnt lgkmcnt(7)
	v_mfma_f32_16x16x32_bf16 v[128:131], v[138:141], v[176:179], v[128:131]
	v_mfma_f32_16x16x32_bf16 v[124:127], v[146:149], v[176:179], v[124:127]
	s_waitcnt lgkmcnt(5)
	v_mfma_f32_16x16x32_bf16 v[120:123], v[138:141], v[206:209], v[120:123]
	v_mfma_f32_16x16x32_bf16 v[116:119], v[146:149], v[206:209], v[116:119]
	s_waitcnt lgkmcnt(3)
	v_mfma_f32_16x16x32_bf16 v[108:111], v[138:141], v[214:217], v[108:111]
	v_mfma_f32_16x16x32_bf16 v[100:103], v[146:149], v[214:217], v[100:103]
	s_waitcnt lgkmcnt(1)
	v_mfma_f32_16x16x32_bf16 v[92:95], v[138:141], v[222:225], v[92:95]
	v_mfma_f32_16x16x32_bf16 v[84:87], v[146:149], v[222:225], v[84:87]
	v_mfma_f32_16x16x32_bf16 v[128:131], v[142:145], v[180:183], v[128:131]
	v_mfma_f32_16x16x32_bf16 v[124:127], v[150:153], v[180:183], v[124:127]
	v_mfma_f32_16x16x32_bf16 v[120:123], v[142:145], v[210:213], v[120:123]
	v_mfma_f32_16x16x32_bf16 v[116:119], v[150:153], v[210:213], v[116:119]
	v_mfma_f32_16x16x32_bf16 v[108:111], v[142:145], v[218:221], v[108:111]
	v_mfma_f32_16x16x32_bf16 v[100:103], v[150:153], v[218:221], v[100:103]
	s_waitcnt lgkmcnt(0)
	v_mfma_f32_16x16x32_bf16 v[92:95], v[142:145], v[226:229], v[92:95]
	v_mfma_f32_16x16x32_bf16 v[84:87], v[150:153], v[226:229], v[84:87]
	s_setprio 0
	s_setprio 1
	v_mfma_f32_16x16x32_bf16 v[112:115], v[154:157], v[176:179], v[112:115]
	v_mfma_f32_16x16x32_bf16 v[104:107], v[162:165], v[176:179], v[104:107]
	v_mfma_f32_16x16x32_bf16 v[96:99], v[154:157], v[206:209], v[96:99]
	v_mfma_f32_16x16x32_bf16 v[88:91], v[162:165], v[206:209], v[88:91]
	v_mfma_f32_16x16x32_bf16 v[80:83], v[154:157], v[214:217], v[80:83]
	v_mfma_f32_16x16x32_bf16 v[76:79], v[162:165], v[214:217], v[76:79]
	v_mfma_f32_16x16x32_bf16 v[72:75], v[154:157], v[222:225], v[72:75]
	v_mfma_f32_16x16x32_bf16 v[68:71], v[162:165], v[222:225], v[68:71]
	v_mfma_f32_16x16x32_bf16 v[112:115], v[158:161], v[180:183], v[112:115]
	v_mfma_f32_16x16x32_bf16 v[104:107], v[166:169], v[180:183], v[104:107]
	v_mfma_f32_16x16x32_bf16 v[96:99], v[158:161], v[210:213], v[96:99]
	v_mfma_f32_16x16x32_bf16 v[88:91], v[166:169], v[210:213], v[88:91]
	v_mfma_f32_16x16x32_bf16 v[80:83], v[158:161], v[218:221], v[80:83]
	v_mfma_f32_16x16x32_bf16 v[76:79], v[166:169], v[218:221], v[76:79]
	v_mfma_f32_16x16x32_bf16 v[72:75], v[158:161], v[226:229], v[72:75]
	v_mfma_f32_16x16x32_bf16 v[68:71], v[166:169], v[226:229], v[68:71]
	s_setprio 0
	s_barrier
	ds_read_b128 v[176:179], v242 offset:16384
	ds_read_b128 v[180:183], v243 offset:16384
	ds_read_b128 v[206:209], v242 offset:18432
	ds_read_b128 v[210:213], v243 offset:18432
	ds_read_b128 v[214:217], v242 offset:20480
	ds_read_b128 v[218:221], v243 offset:20480
	ds_read_b128 v[222:225], v242 offset:22528
	ds_read_b128 v[226:229], v243 offset:22528
	s_mov_b32 m0, s30
	s_nop 0
	global_load_lds_dwordx4 v240, s[20:21]
	s_add_u32 s56, s20, 0x100000
	s_mov_b32 m0, s31
	s_nop 0
	global_load_lds_dwordx4 v241, s[20:21]
	s_addc_u32 s57, s21, 0
	s_mov_b32 m0, s34
	s_nop 0
	global_load_lds_dwordx4 v240, s[56:57]
	s_nop 0
	s_mov_b32 m0, s35
	s_nop 0
	global_load_lds_dwordx4 v241, s[56:57]
	s_nop 0
	s_mov_b32 m0, s29
	s_nop 0
	global_load_lds_dwordx4 v238, s[22:23]
	s_nop 0
	s_mov_b32 m0, s36
	s_nop 0
	global_load_lds_dwordx4 v239, s[22:23]
	s_waitcnt vmcnt(8)
	s_waitcnt lgkmcnt(0)
	s_barrier
; #define PG8_STAGE(bufoff, gbase, voff) do { _Pragma("unroll") for (int _i = 0; _i < 2; ++_i) \
;         glds16((const void*)(gbase), (voff)[_i], ldsbase + (unsigned)(bufoff) + ldsw + (unsigned)_i * 8192u); } while (0)
; #define PG8_LDA(dst, b, h) do { _Pragma("unroll") for (int m = 0; m < 4; ++m) _Pragma("unroll") for (int k = 0; k < 2; ++k) dst[m][k] = *(const LAS bf16x8*)(lds + PG8_SA(b, h) + aoff + m * 2048 + k * 1024); } while (0)
; #define PG8_LDB(dst, b, h) do { _Pragma("unroll") for (int n = 0; n < 2; ++n) _Pragma("unroll") for (int k = 0; k < 2; ++k) dst[n][k] = *(const LAS bf16x8*)(lds + PG8_SB(b, h) + boff + n * 2048 + k * 1024); } while (0)
; #define PG8_WAIT_V(n) asm volatile("s_waitcnt vmcnt(" #n ")" ::: "memory")
; #define PG8_WAIT_L(n) asm volatile("s_waitcnt lgkmcnt(" #n ")" ::: "memory")
; #define PG8_BAR __builtin_amdgcn_s_barrier()
; #define PG8_SCHED __builtin_amdgcn_sched_barrier(0)
;     ...
;         for (int t = 0; t < nt; t += 2) {
;             const bool last = (t == nt - 2);
;             const char* a1 = cA + (size_t)(t + 1) * kstep;
;             const char* a2 = last ? nA : cA + (size_t)(t + 2) * kstep; const char* b2 = last ? nB : cB + (size_t)(t + 2) * kstep;
;             const char* a3 = a2 + kstep; const char* b3 = b2 + kstep;
;             PG8_LDB(B0, 0, 0); PG8_LDB(B1, 0, 1); PG8_SCHED; PG8_LDA(At, 0, 0); PG8_STAGE(PG8_SA(1, 1), a1 + hstepA, voffA);
;             PG8_WAIT_V(8); PG8_WAIT_L(0); PG8_BAR; PG8_MMA(0, 0, At, B0); PG8_MMA(0, 1, At, B1); PG8_BAR; PG8_SCHED;
;             PG8_LDA(At, 0, 1); PG8_STAGE(PG8_SB(0, 0), b2, voffB); PG8_STAGE(PG8_SB(0, 1), b2 + hstepB, voffB); PG8_STAGE(PG8_SA(0, 0), a2, voffA);
;             PG8_WAIT_V(8); PG8_WAIT_L(0); PG8_BAR; PG8_MMA(1, 0, At, B0); PG8_MMA(1, 1, At, B1); PG8_BAR; PG8_SCHED;
;             PG8_LDB(B0, 1, 0); PG8_LDB(B1, 1, 1); PG8_SCHED; PG8_LDA(At, 1, 0); PG8_STAGE(PG8_SA(0, 1), a2 + hstepA, voffA);
;             PG8_WAIT_V(8); PG8_WAIT_L(0); PG8_BAR; PG8_MMA(0, 0, At, B0); PG8_MMA(0, 1, At, B1); PG8_BAR; PG8_SCHED;
;             PG8_LDA(At, 1, 1); PG8_STAGE(PG8_SB(1, 0), b3, voffB); PG8_STAGE(PG8_SB(1, 1), b3 + hstepB, voffB); PG8_STAGE(PG8_SA(1, 0), a3, voffA);
;             PG8_WAIT_V(8); PG8_WAIT_L(0); PG8_BAR; PG8_MMA(1, 0, At, B0); PG8_MMA(1, 1, At, B1); PG8_BAR; PG8_SCHED;
;         }
	s_setprio 1
	s_waitcnt lgkmcnt(7)
	v_mfma_f32_16x16x32_bf16 v[64:67], v[138:141], v[176:179], v[64:67]
	v_mfma_f32_16x16x32_bf16 v[60:63], v[146:149], v[176:179], v[60:63]
	s_waitcnt lgkmcnt(5)
	v_mfma_f32_16x16x32_bf16 v[56:59], v[138:141], v[206:209], v[56:59]
	v_mfma_f32_16x16x32_bf16 v[52:55], v[146:149], v[206:209], v[52:55]
	s_waitcnt lgkmcnt(3)
	v_mfma_f32_16x16x32_bf16 v[40:43], v[138:141], v[214:217], v[40:43]
	v_mfma_f32_16x16x32_bf16 v[36:39], v[146:149], v[214:217], v[36:39]
	s_waitcnt lgkmcnt(1)
	v_mfma_f32_16x16x32_bf16 v[24:27], v[138:141], v[222:225], v[24:27]
	v_mfma_f32_16x16x32_bf16 v[20:23], v[146:149], v[222:225], v[20:23]
	v_mfma_f32_16x16x32_bf16 v[64:67], v[142:145], v[180:183], v[64:67]
	v_mfma_f32_16x16x32_bf16 v[60:63], v[150:153], v[180:183], v[60:63]
	v_mfma_f32_16x16x32_bf16 v[56:59], v[142:145], v[210:213], v[56:59]
	v_mfma_f32_16x16x32_bf16 v[52:55], v[150:153], v[210:213], v[52:55]
	v_mfma_f32_16x16x32_bf16 v[40:43], v[142:145], v[218:221], v[40:43]
	v_mfma_f32_16x16x32_bf16 v[36:39], v[150:153], v[218:221], v[36:39]
	s_waitcnt lgkmcnt(0)
	v_mfma_f32_16x16x32_bf16 v[24:27], v[142:145], v[226:229], v[24:27]
	v_mfma_f32_16x16x32_bf16 v[20:23], v[150:153], v[226:229], v[20:23]
	s_setprio 0
	s_setprio 1
	v_mfma_f32_16x16x32_bf16 v[48:51], v[154:157], v[176:179], v[48:51]
	v_mfma_f32_16x16x32_bf16 v[44:47], v[162:165], v[176:179], v[44:47]
	v_mfma_f32_16x16x32_bf16 v[32:35], v[154:157], v[206:209], v[32:35]
	v_mfma_f32_16x16x32_bf16 v[28:31], v[162:165], v[206:209], v[28:31]
	v_mfma_f32_16x16x32_bf16 v[16:19], v[154:157], v[214:217], v[16:19]
	v_mfma_f32_16x16x32_bf16 v[12:15], v[162:165], v[214:217], v[12:15]
	v_mfma_f32_16x16x32_bf16 v[8:11], v[154:157], v[222:225], v[8:11]
	v_mfma_f32_16x16x32_bf16 v[4:7], v[162:165], v[222:225], v[4:7]
	v_mfma_f32_16x16x32_bf16 v[48:51], v[158:161], v[180:183], v[48:51]
	v_mfma_f32_16x16x32_bf16 v[44:47], v[166:169], v[180:183], v[44:47]
	v_mfma_f32_16x16x32_bf16 v[32:35], v[158:161], v[210:213], v[32:35]
	v_mfma_f32_16x16x32_bf16 v[28:31], v[166:169], v[210:213], v[28:31]
	v_mfma_f32_16x16x32_bf16 v[16:19], v[158:161], v[218:221], v[16:19]
	v_mfma_f32_16x16x32_bf16 v[12:15], v[166:169], v[218:221], v[12:15]
	v_mfma_f32_16x16x32_bf16 v[8:11], v[158:161], v[226:229], v[8:11]
	v_mfma_f32_16x16x32_bf16 v[4:7], v[166:169], v[226:229], v[4:7]
	s_setprio 0
	s_barrier
	v_add_u32_e32 v137, 0x18000, v244
	v_add_u32_e32 v246, 0x18000, v245
	ds_read_b128 v[138:141], v137
	ds_read_b128 v[142:145], v246
	ds_read_b128 v[146:149], v137 offset:2048
	ds_read_b128 v[150:153], v246 offset:2048
	v_add_u32_e32 v137, 0x1c000, v244
	v_add_u32_e32 v246, 0x1c000, v245
	ds_read_b128 v[154:157], v137
	ds_read_b128 v[158:161], v246
	ds_read_b128 v[162:165], v137 offset:2048
	ds_read_b128 v[166:169], v246 offset:2048
	ds_read_b128 v[176:179], v242 offset:32768
	ds_read_b128 v[180:183], v243 offset:32768
	ds_read_b128 v[206:209], v242 offset:34816
	ds_read_b128 v[210:213], v243 offset:34816
	ds_read_b128 v[214:217], v242 offset:36864
	ds_read_b128 v[218:221], v243 offset:36864
	ds_read_b128 v[222:225], v242 offset:38912
	ds_read_b128 v[226:229], v243 offset:38912
	s_add_u32 s22, s22, 0x80000
	s_addc_u32 s23, s23, 0
	s_mov_b32 m0, s37
	s_nop 0
	global_load_lds_dwordx4 v238, s[22:23]
	s_nop 0
	s_mov_b32 m0, s38
	s_nop 0
	global_load_lds_dwordx4 v239, s[22:23]
	s_waitcnt vmcnt(8)
	s_waitcnt lgkmcnt(0)
	s_barrier
	s_setprio 1
	s_waitcnt lgkmcnt(7)
	v_mfma_f32_16x16x32_bf16 v[128:131], v[138:141], v[176:179], v[128:131]
	v_mfma_f32_16x16x32_bf16 v[124:127], v[146:149], v[176:179], v[124:127]
	s_waitcnt lgkmcnt(5)
	v_mfma_f32_16x16x32_bf16 v[120:123], v[138:141], v[206:209], v[120:123]
	v_mfma_f32_16x16x32_bf16 v[116:119], v[146:149], v[206:209], v[116:119]
	s_waitcnt lgkmcnt(3)
	v_mfma_f32_16x16x32_bf16 v[108:111], v[138:141], v[214:217], v[108:111]
	v_mfma_f32_16x16x32_bf16 v[100:103], v[146:149], v[214:217], v[100:103]
	s_waitcnt lgkmcnt(1)
	v_mfma_f32_16x16x32_bf16 v[92:95], v[138:141], v[222:225], v[92:95]
	v_mfma_f32_16x16x32_bf16 v[84:87], v[146:149], v[222:225], v[84:87]
	v_mfma_f32_16x16x32_bf16 v[128:131], v[142:145], v[180:183], v[128:131]
	v_mfma_f32_16x16x32_bf16 v[124:127], v[150:153], v[180:183], v[124:127]
	v_mfma_f32_16x16x32_bf16 v[120:123], v[142:145], v[210:213], v[120:123]
	v_mfma_f32_16x16x32_bf16 v[116:119], v[150:153], v[210:213], v[116:119]
	v_mfma_f32_16x16x32_bf16 v[108:111], v[142:145], v[218:221], v[108:111]
	v_mfma_f32_16x16x32_bf16 v[100:103], v[150:153], v[218:221], v[100:103]
	s_waitcnt lgkmcnt(0)
	v_mfma_f32_16x16x32_bf16 v[92:95], v[142:145], v[226:229], v[92:95]
	v_mfma_f32_16x16x32_bf16 v[84:87], v[150:153], v[226:229], v[84:87]
	s_setprio 0
	s_setprio 1
	v_mfma_f32_16x16x32_bf16 v[112:115], v[154:157], v[176:179], v[112:115]
	v_mfma_f32_16x16x32_bf16 v[104:107], v[162:165], v[176:179], v[104:107]
	v_mfma_f32_16x16x32_bf16 v[96:99], v[154:157], v[206:209], v[96:99]
	v_mfma_f32_16x16x32_bf16 v[88:91], v[162:165], v[206:209], v[88:91]
	v_mfma_f32_16x16x32_bf16 v[80:83], v[154:157], v[214:217], v[80:83]
	v_mfma_f32_16x16x32_bf16 v[76:79], v[162:165], v[214:217], v[76:79]
	v_mfma_f32_16x16x32_bf16 v[72:75], v[154:157], v[222:225], v[72:75]
	v_mfma_f32_16x16x32_bf16 v[68:71], v[162:165], v[222:225], v[68:71]
	v_mfma_f32_16x16x32_bf16 v[112:115], v[158:161], v[180:183], v[112:115]
	v_mfma_f32_16x16x32_bf16 v[104:107], v[166:169], v[180:183], v[104:107]
	v_mfma_f32_16x16x32_bf16 v[96:99], v[158:161], v[210:213], v[96:99]
	v_mfma_f32_16x16x32_bf16 v[88:91], v[166:169], v[210:213], v[88:91]
	v_mfma_f32_16x16x32_bf16 v[80:83], v[158:161], v[218:221], v[80:83]
	v_mfma_f32_16x16x32_bf16 v[76:79], v[166:169], v[218:221], v[76:79]
	v_mfma_f32_16x16x32_bf16 v[72:75], v[158:161], v[226:229], v[72:75]
	v_mfma_f32_16x16x32_bf16 v[68:71], v[166:169], v[226:229], v[68:71]
	s_setprio 0
	s_barrier
; #define PG8_STAGE(bufoff, gbase, voff) do { _Pragma("unroll") for (int _i = 0; _i < 2; ++_i) \
;         glds16((const void*)(gbase), (voff)[_i], ldsbase + (unsigned)(bufoff) + ldsw + (unsigned)_i * 8192u); } while (0)
; #define PG8_LDA(dst, b, h) do { _Pragma("unroll") for (int m = 0; m < 4; ++m) _Pragma("unroll") for (int k = 0; k < 2; ++k) dst[m][k] = *(const LAS bf16x8*)(lds + PG8_SA(b, h) + aoff + m * 2048 + k * 1024); } while (0)
; #define PG8_LDB(dst, b, h) do { _Pragma("unroll") for (int n = 0; n < 2; ++n) _Pragma("unroll") for (int k = 0; k < 2; ++k) dst[n][k] = *(const LAS bf16x8*)(lds + PG8_SB(b, h) + boff + n * 2048 + k * 1024); } while (0)
; #define PG8_WAIT_V(n) asm volatile("s_waitcnt vmcnt(" #n ")" ::: "memory")
; #define PG8_WAIT_L(n) asm volatile("s_waitcnt lgkmcnt(" #n ")" ::: "memory")
; #define PG8_BAR __builtin_amdgcn_s_barrier()
; #define PG8_SCHED __builtin_amdgcn_sched_barrier(0)
;     ...
;         for (int t = 0; t < nt; t += 2) {
;             const bool last = (t == nt - 2);
;             const char* a1 = cA + (size_t)(t + 1) * kstep;
;             const char* a2 = last ? nA : cA + (size_t)(t + 2) * kstep; const char* b2 = last ? nB : cB + (size_t)(t + 2) * kstep;
;             const char* a3 = a2 + kstep; const char* b3 = b2 + kstep;
;             PG8_LDB(B0, 0, 0); PG8_LDB(B1, 0, 1); PG8_SCHED; PG8_LDA(At, 0, 0); PG8_STAGE(PG8_SA(1, 1), a1 + hstepA, voffA);
;             PG8_WAIT_V(8); PG8_WAIT_L(0); PG8_BAR; PG8_MMA(0, 0, At, B0); PG8_MMA(0, 1, At, B1); PG8_BAR; PG8_SCHED;
;             PG8_LDA(At, 0, 1); PG8_STAGE(PG8_SB(0, 0), b2, voffB); PG8_STAGE(PG8_SB(0, 1), b2 + hstepB, voffB); PG8_STAGE(PG8_SA(0, 0), a2, voffA);
;             PG8_WAIT_V(8); PG8_WAIT_L(0); PG8_BAR; PG8_MMA(1, 0, At, B0); PG8_MMA(1, 1, At, B1); PG8_BAR; PG8_SCHED;
;             PG8_LDB(B0, 1, 0); PG8_LDB(B1, 1, 1); PG8_SCHED; PG8_LDA(At, 1, 0); PG8_STAGE(PG8_SA(0, 1), a2 + hstepA, voffA);
;             PG8_WAIT_V(8); PG8_WAIT_L(0); PG8_BAR; PG8_MMA(0, 0, At, B0); PG8_MMA(0, 1, At, B1); PG8_BAR; PG8_SCHED;
;             PG8_LDA(At, 1, 1); PG8_STAGE(PG8_SB(1, 0), b3, voffB); PG8_STAGE(PG8_SB(1, 1), b3 + hstepB, voffB); PG8_STAGE(PG8_SA(1, 0), a3, voffA);
;             PG8_WAIT_V(8); PG8_WAIT_L(0); PG8_BAR; PG8_MMA(1, 0, At, B0); PG8_MMA(1, 1, At, B1); PG8_BAR; PG8_SCHED;
;         }
	ds_read_b128 v[176:179], v242 offset:49152
	ds_read_b128 v[180:183], v243 offset:49152
	ds_read_b128 v[206:209], v242 offset:51200
	ds_read_b128 v[210:213], v243 offset:51200
	ds_read_b128 v[214:217], v242 offset:53248
	ds_read_b128 v[218:221], v243 offset:53248
	ds_read_b128 v[222:225], v242 offset:55296
	ds_read_b128 v[226:229], v243 offset:55296
	s_add_u32 s22, s20, 0x80
	s_addc_u32 s23, s21, 0
	s_mov_b32 m0, s41
	s_nop 0
	global_load_lds_dwordx4 v240, s[22:23]
	s_add_u32 s20, s20, 0x100080
	s_mov_b32 m0, s42
	s_nop 0
	global_load_lds_dwordx4 v241, s[22:23]
	s_addc_u32 s21, s21, 0
	s_mov_b32 m0, s45
	s_nop 0
	global_load_lds_dwordx4 v240, s[20:21]
	s_nop 0
	s_mov_b32 m0, s46
	s_nop 0
	global_load_lds_dwordx4 v241, s[20:21]
	s_mov_b32 m0, s43
	s_nop 0
	global_load_lds_dwordx4 v238, s[18:19]
	s_nop 0
	s_mov_b32 m0, s44
	s_nop 0
	global_load_lds_dwordx4 v239, s[18:19]
	s_waitcnt vmcnt(8)
	s_waitcnt lgkmcnt(0)
	s_barrier
	s_setprio 1
	s_waitcnt lgkmcnt(7)
	v_mfma_f32_16x16x32_bf16 v[64:67], v[138:141], v[176:179], v[64:67]
	v_mfma_f32_16x16x32_bf16 v[60:63], v[146:149], v[176:179], v[60:63]
	s_waitcnt lgkmcnt(5)
	v_mfma_f32_16x16x32_bf16 v[56:59], v[138:141], v[206:209], v[56:59]
	v_mfma_f32_16x16x32_bf16 v[52:55], v[146:149], v[206:209], v[52:55]
	s_waitcnt lgkmcnt(3)
	v_mfma_f32_16x16x32_bf16 v[40:43], v[138:141], v[214:217], v[40:43]
	v_mfma_f32_16x16x32_bf16 v[36:39], v[146:149], v[214:217], v[36:39]
	s_waitcnt lgkmcnt(1)
	v_mfma_f32_16x16x32_bf16 v[24:27], v[138:141], v[222:225], v[24:27]
	v_mfma_f32_16x16x32_bf16 v[20:23], v[146:149], v[222:225], v[20:23]
	v_mfma_f32_16x16x32_bf16 v[64:67], v[142:145], v[180:183], v[64:67]
	v_mfma_f32_16x16x32_bf16 v[60:63], v[150:153], v[180:183], v[60:63]
	v_mfma_f32_16x16x32_bf16 v[56:59], v[142:145], v[210:213], v[56:59]
	v_mfma_f32_16x16x32_bf16 v[52:55], v[150:153], v[210:213], v[52:55]
	v_mfma_f32_16x16x32_bf16 v[40:43], v[142:145], v[218:221], v[40:43]
	v_mfma_f32_16x16x32_bf16 v[36:39], v[150:153], v[218:221], v[36:39]
	s_waitcnt lgkmcnt(0)
	v_mfma_f32_16x16x32_bf16 v[24:27], v[142:145], v[226:229], v[24:27]
	v_mfma_f32_16x16x32_bf16 v[20:23], v[150:153], v[226:229], v[20:23]
	s_setprio 0
	s_setprio 1
	v_mfma_f32_16x16x32_bf16 v[48:51], v[154:157], v[176:179], v[48:51]
	v_mfma_f32_16x16x32_bf16 v[44:47], v[162:165], v[176:179], v[44:47]
	v_mfma_f32_16x16x32_bf16 v[32:35], v[154:157], v[206:209], v[32:35]
	v_mfma_f32_16x16x32_bf16 v[28:31], v[162:165], v[206:209], v[28:31]
	v_mfma_f32_16x16x32_bf16 v[16:19], v[154:157], v[214:217], v[16:19]
	v_mfma_f32_16x16x32_bf16 v[12:15], v[162:165], v[214:217], v[12:15]
	v_mfma_f32_16x16x32_bf16 v[8:11], v[154:157], v[222:225], v[8:11]
	v_mfma_f32_16x16x32_bf16 v[4:7], v[162:165], v[222:225], v[4:7]
	v_mfma_f32_16x16x32_bf16 v[48:51], v[158:161], v[180:183], v[48:51]
	v_mfma_f32_16x16x32_bf16 v[44:47], v[166:169], v[180:183], v[44:47]
	v_mfma_f32_16x16x32_bf16 v[32:35], v[158:161], v[210:213], v[32:35]
	v_mfma_f32_16x16x32_bf16 v[28:31], v[166:169], v[210:213], v[28:31]
	v_mfma_f32_16x16x32_bf16 v[16:19], v[158:161], v[218:221], v[16:19]
	v_mfma_f32_16x16x32_bf16 v[12:15], v[166:169], v[218:221], v[12:15]
	v_mfma_f32_16x16x32_bf16 v[8:11], v[158:161], v[226:229], v[8:11]
	v_mfma_f32_16x16x32_bf16 v[4:7], v[166:169], v[226:229], v[4:7]
	s_setprio 0
	s_barrier
	s_add_i32 s54, s54, 2
	s_add_u32 s9, s9, 0x100
	s_addc_u32 s53, s53, 0
	s_add_u32 s16, s16, 0x100
	s_addc_u32 s17, s17, 0
	s_cmp_gt_u32 s54, 13
	s_cbranch_scc0 .LBB0_2113
	s_and_b64 vcc, exec, s[6:7]
	s_cbranch_vccz .LBB0_2116
	s_barrier

; __device__ __forceinline__ int lane_id() { int l_; asm volatile("v_mbcnt_lo_u32_b32 %0, -1, 0\n\tv_mbcnt_hi_u32_b32 %0, -1, %0" : "=v"(l_)); return l_; }
; #define PG8_STAGE(bufoff, gbase, voff) do { _Pragma("unroll") for (int _i = 0; _i < 2; ++_i) \
;         glds16((const void*)(gbase), (voff)[_i], ldsbase + (unsigned)(bufoff) + ldsw + (unsigned)_i * 8192u); } while (0)
; #define PG8_WAIT_V(n) asm volatile("s_waitcnt vmcnt(" #n ")" ::: "memory")
; #define PG8_BAR __builtin_amdgcn_s_barrier()
;     ...
;     int tid = w0_ * 64 + lane_id(); asm volatile("" : "+v"(tid));
;     const int wid = __builtin_amdgcn_readfirstlane(tid >> 6), lane = tid & 63, wr = wid >> 2, wc = wid & 3, fr = lane & 15, fq = lane >> 4;
;     const int nt = nt_ ? nt_ : Kb / 128;
;     unsigned voffA[2], voffB[2];
; #pragma unroll
;     for (int i = 0; i < 2; ++i) { int R, C; stage_rc(tid * 16 + i * 8192, R, C); const int Rb = Epi::PERM ? ((R & ~31) + perm32(R & 31)) : R;
;         voffA[i] = (unsigned)(R * ldab + C * 2); voffB[i] = (unsigned)(Rb * Kb + C * 2); }
;     const size_t kstep = (size_t)(BK * 2);
;     const size_t hstepA = (size_t)HALF * ldab, hstepB = (size_t)HALF * Kb;
;     const unsigned ldsw = (unsigned)wid * 1024u, ldsbase = (unsigned)(size_t)lds;
;     const int aoff = lds_byte(wr * 64 + fr, fq * 8), boff = lds_byte(wc * 32 + fr, fq * 8);
;     ...
;     Unit cur, nxt; int ui = 0;
;     if (!S.next(0, cur)) return;
;     f32x4 acc[2][2][4][2];
; #pragma unroll
;     for (int a = 0; a < 2; ++a)
; #pragma unroll
;         for (int b = 0; b < 2; ++b)
; #pragma unroll
;             for (int m = 0; m < 4; ++m)
; #pragma unroll
;                 for (int n = 0; n < 2; ++n) acc[a][b][m][n] = (f32x4){0.f, 0.f, 0.f, 0.f};
;     bf16x8 At[4][2], B0[2][2], B1[2][2];
;     const char* cA = uniform_ptr(cur.a); const char* cB = uniform_ptr(cur.b);
;     PG8_STAGE(PG8_SB(0, 0), cB, voffB); PG8_STAGE(PG8_SB(0, 1), cB + hstepB, voffB); PG8_STAGE(PG8_SA(0, 0), cA, voffA); PG8_STAGE(PG8_SA(0, 1), cA + hstepA, voffA);
;     if (wr == 1) PG8_BAR;
;     PG8_WAIT_V(2); PG8_BAR;
;     PG8_STAGE(PG8_SB(1, 0), cB + kstep, voffB); PG8_STAGE(PG8_SA(1, 0), cA + kstep, voffA); PG8_STAGE(PG8_SB(1, 1), cB + hstepB + kstep, voffB);
;     PG8_WAIT_V(6); PG8_BAR;
.LBB0_2263:
	v_mbcnt_lo_u32_b32 v0, -1, 0
	v_mbcnt_hi_u32_b32 v0, -1, v0
	v_readlane_b32 s0, v250, 60
	v_readlane_b32 s4, v252, 37
	v_readlane_b32 s5, v252, 38
	v_add_u32_e32 v0, s0, v0
	s_andn2_b64 vcc, exec, s[4:5]
	v_readfirstlane_b32 s8, v0
	s_cbranch_vccnz .LBB0_2283
	v_bfe_i32 v4, v0, 27, 1
	v_lshlrev_b32_e32 v1, 4, v0
	v_lshrrev_b32_e32 v4, 22, v4
	v_add_u32_e32 v4, v1, v4
	v_and_b32_e32 v4, 0xfffffc00, v4
	v_sub_u32_e32 v4, v1, v4
	v_ashrrev_i32_e32 v2, 31, v0
	v_lshrrev_b32_e32 v5, 4, v4
	v_lshrrev_b32_e32 v2, 26, v2
	v_bitop3_b32 v4, v5, v4, 32 bitop3:0x6c
	v_add_u32_e32 v2, v0, v2
	v_ashrrev_i32_e32 v6, 31, v4
	s_add_u32 s0, s20, 0x4861e000
	v_ashrrev_i32_e32 v2, 6, v2
	v_lshrrev_b32_e32 v6, 26, v6
	s_addc_u32 s24, s21, 0
	s_lshl_b32 s4, s27, 19
	v_lshlrev_b32_e32 v5, 3, v2
	v_add_u32_e32 v6, v4, v6
	s_add_u32 s4, s20, s4
	v_and_b32_e32 v5, -16, v5
	v_ashrrev_i32_e32 v7, 6, v6
	v_and_b32_e32 v6, 0xc0, v6
	s_addc_u32 s5, s21, 0
	v_add_u32_e32 v5, v7, v5
	v_sub_u32_e32 v4, v4, v6
	s_add_u32 s25, s4, 0x3d00000
	v_lshlrev_b32_e32 v2, 5, v2
	v_ashrrev_i16_sdwa v4, v188, sext(v4) dst_sel:DWORD dst_unused:UNUSED_PAD src0_sel:DWORD src1_sel:BYTE_0
	v_lshlrev_b32_e32 v6, 1, v5
	v_lshrrev_b32_e32 v8, 2, v5
	v_and_b32_e32 v7, 3, v7
	s_mov_b32 s4, 0x3fffe0
	v_and_b32_e32 v2, 32, v2
	v_bfe_i32 v4, v4, 0, 16
	v_and_b32_e32 v6, 24, v6
	v_and_b32_e32 v8, 4, v8
	v_and_or_b32 v7, v5, s4, v7
	v_or3_b32 v6, v7, v8, v6
	v_add_lshl_u32 v4, v2, v4, 1
	v_add_u32_e32 v1, 0x2000, v1
	v_lshl_add_u32 v2, v5, 10, v4
	s_waitcnt vmcnt(0)
	v_lshl_add_u32 v132, v6, 10, v4
	v_ashrrev_i32_e32 v4, 31, v1
	v_lshrrev_b32_e32 v4, 22, v4
	v_add_u32_e32 v4, v1, v4
	v_ashrrev_i32_e32 v4, 10, v4
	v_mul_i32_i24_e32 v5, 0x400, v4
	v_sub_u32_e32 v1, v1, v5
	v_lshrrev_b32_e32 v5, 4, v1
	v_bitop3_b32 v1, v5, v1, 32 bitop3:0x6c
	v_ashrrev_i32_e32 v6, 31, v1
	v_lshrrev_b32_e32 v6, 26, v6
	v_lshlrev_b32_e32 v5, 3, v4
	v_add_u32_e32 v6, v1, v6
	v_and_b32_e32 v5, -16, v5
	v_ashrrev_i32_e32 v7, 6, v6
	s_addc_u32 s26, s5, 0
	v_add_u32_e32 v5, v7, v5
	v_and_b32_e32 v7, 3, v7
	s_ashr_i32 s10, s8, 6
	s_ashr_i32 s9, s8, 8
	v_and_or_b32 v7, v5, s4, v7
	s_lshl_b32 s6, s10, 10
	v_readlane_b32 s4, v253, 12
	v_readlane_b32 s5, v253, 13
	s_add_u32 s16, s25, s4
	s_addc_u32 s17, s26, s5
	v_readlane_b32 s4, v253, 14
	v_readlane_b32 s5, v253, 15
	v_and_b32_e32 v6, 0xc0, v6
	s_and_b64 s[4:5], s[4:5], exec
	v_sub_u32_e32 v1, v1, v6
	s_cselect_b32 s5, s2, s0
	v_readlane_b32 s7, v253, 19
	v_lshlrev_b32_e32 v4, 5, v4
	v_ashrrev_i16_sdwa v1, v188, sext(v1) dst_sel:DWORD dst_unused:UNUSED_PAD src0_sel:DWORD src1_sel:BYTE_0
	v_lshlrev_b32_e32 v6, 1, v5
	v_lshrrev_b32_e32 v8, 2, v5
	s_cselect_b32 s4, s3, s24
	s_add_u32 s18, s5, s7
	v_and_b32_e32 v4, 32, v4
	v_bfe_i32 v1, v1, 0, 16
	v_and_b32_e32 v6, 24, v6
	v_and_b32_e32 v8, 4, v8
	s_addc_u32 s19, s4, 0
	s_add_i32 s27, s6, 0
	v_or3_b32 v6, v7, v8, v6
	v_add_lshl_u32 v1, v4, v1, 1
	s_add_i32 s28, s27, 0x10000
	s_nop 0
	v_readlane_b32 s70, v250, 60
	v_mbcnt_lo_u32_b32 v246, -1, 0
	v_mbcnt_hi_u32_b32 v246, -1, v246
	v_add_u32_e32 v246, s70, v246
	v_bfe_u32 v247, v246, 4, 2
	v_bfe_u32 v248, v246, 6, 1
	v_lshl_or_b32 v247, v248, 2, v247
	v_and_b32_e32 v248, 7, v246
	v_xor_b32_e32 v247, v247, v248
	v_lshlrev_b32_e32 v247, 4, v247
	v_lshrrev_b32_e32 v248, 3, v246
	v_lshl_add_u32 v238, v248, 10, v247
	v_add_u32_e32 v239, 0x10000, v238
	v_and_b32_e32 v249, 0x23, v248
	v_and_b32_e32 v244, 12, v248
	v_lshl_or_b32 v249, v244, 1, v249
	v_bfe_u32 v244, v248, 4, 1
	v_lshl_or_b32 v249, v244, 2, v249
	v_lshl_add_u32 v240, v249, 10, v247
	v_add_u32_e32 v241, 0x10000, v240
	v_bfe_u32 v247, v246, 4, 2
	v_bfe_u32 v248, v246, 1, 3
	v_xor_b32_e32 v247, v247, v248
	v_lshlrev_b32_e32 v247, 4, v247
	v_and_b32_e32 v248, 7, v246
	v_lshl_or_b32 v247, v248, 7, v247
	v_bfe_u32 v248, v246, 3, 1
	v_lshl_or_b32 v247, v248, 10, v247
	v_bfe_u32 v248, v246, 8, 1
	v_lshl_or_b32 v242, v248, 13, v247
	v_xor_b32_e32 v243, 64, v242
	v_bfe_u32 v248, v246, 6, 2
	v_lshl_or_b32 v244, v248, 12, v247
	v_xor_b32_e32 v245, 64, v244
	s_mov_b32 m0, s28
	s_nop 0
	global_load_lds_dwordx4 v240, s[16:17]
	v_lshl_add_u32 v134, v6, 10, v1
	s_add_i32 s29, s27, 0x12000
	s_mov_b32 m0, s29
	s_nop 0
	global_load_lds_dwordx4 v241, s[16:17]
	s_add_u32 s4, s16, 0x20000
	s_addc_u32 s5, s17, 0
	s_add_i32 s30, s27, 0x14000
	s_mov_b32 m0, s30
	s_nop 0
	global_load_lds_dwordx4 v240, s[4:5]
	s_add_i32 s31, s27, 0x16000
	s_mov_b32 m0, s31
	s_nop 0
	global_load_lds_dwordx4 v241, s[4:5]
	s_mov_b32 m0, s27
	s_nop 0
	global_load_lds_dwordx4 v238, s[18:19]
	v_lshl_add_u32 v133, v5, 10, v1
	s_add_i32 s34, s27, 0x2000
	s_mov_b32 m0, s34
	s_nop 0
	global_load_lds_dwordx4 v239, s[18:19]
	s_add_u32 s4, s18, 0x20000
	s_addc_u32 s5, s19, 0
	s_add_i32 s35, s27, 0x4000
	s_mov_b32 m0, s35
	s_nop 0
	global_load_lds_dwordx4 v238, s[4:5]
	s_add_i32 s36, s27, 0x6000
	s_mov_b32 m0, s36
	s_nop 0
	global_load_lds_dwordx4 v239, s[4:5]
	s_cmp_eq_u32 s9, 1
	s_cselect_b64 s[4:5], -1, 0
	s_cmp_lg_u32 s9, 1
	s_cbranch_scc1 .LBB0_2266
	s_barrier
.LBB0_2266:
	v_lshrrev_b32_e32 v4, 1, v0
	v_and_b32_e32 v4, 24, v4
	s_add_u32 s6, s20, 0x4881e000
	v_and_b32_e32 v1, 15, v0
	v_lshlrev_b32_e32 v5, 1, v4
	v_lshlrev_b32_e32 v0, 2, v0
	s_addc_u32 s7, s21, 0
	v_lshl_or_b32 v135, s9, 6, v1
	v_lshl_or_b32 v1, v1, 6, v5
	s_lshl_b32 s9, s9, 13
	v_and_b32_e32 v0, 32, v0
	v_bitop3_b32 v5, v1, s9, v0 bitop3:0xde
	s_lshl_b32 s9, s10, 5
	s_and_b32 s12, s9, 0x60
	s_lshl_b32 s9, s12, 7
	s_add_u32 s10, s16, 0x80
	v_bitop3_b32 v0, v1, s9, v0 bitop3:0xde
	s_waitcnt vmcnt(2)
	s_barrier
	s_addc_u32 s11, s17, 0
	s_add_i32 s37, s27, 0x18000
	s_mov_b32 m0, s37
	s_nop 0
	global_load_lds_dwordx4 v240, s[10:11]
	s_add_i32 s38, s27, 0x1a000
	s_mov_b32 m0, s38
	s_nop 0
	global_load_lds_dwordx4 v241, s[10:11]
	s_add_u32 s10, s18, 0x80
	s_addc_u32 s11, s19, 0
	s_add_i32 s39, s27, 0x8000
	s_mov_b32 m0, s39
	s_nop 0
	global_load_lds_dwordx4 v238, s[10:11]
	s_add_i32 s40, s27, 0xa000
	s_mov_b32 m0, s40
	s_nop 0
	global_load_lds_dwordx4 v239, s[10:11]
	s_add_u32 s10, s16, 0x20080
	s_addc_u32 s11, s17, 0
	s_add_i32 s41, s27, 0x1c000
	s_mov_b32 m0, s41
	s_nop 0
	global_load_lds_dwordx4 v240, s[10:11]
	s_add_i32 s42, s27, 0x1e000
	s_mov_b32 m0, s42
	s_nop 0
	global_load_lds_dwordx4 v241, s[10:11]
	s_waitcnt vmcnt(6)
	s_add_i32 s43, s27, 0xc000
	s_cmpk_lt_u32 s8, 0x100
	s_cselect_b64 s[8:9], -1, 0
	s_add_i32 s44, s27, 0xe000
	v_or_b32_e32 v136, s12, v4
	s_mov_b32 s48, 0
	v_add_u32_e32 v137, 0, v0
	v_add_u32_e32 v138, 0, v5
	v_readlane_b32 s49, v253, 18
	s_mov_b32 s45, 0
	s_mov_b64 s[12:13], s[18:19]
	s_mov_b64 s[14:15], s[16:17]
	s_barrier
	s_branch .LBB0_2269

; #define PG8_STAGE(bufoff, gbase, voff) do { _Pragma("unroll") for (int _i = 0; _i < 2; ++_i) \
;         glds16((const void*)(gbase), (voff)[_i], ldsbase + (unsigned)(bufoff) + ldsw + (unsigned)_i * 8192u); } while (0)
; #define PG8_LDA(dst, b, h) do { _Pragma("unroll") for (int m = 0; m < 4; ++m) _Pragma("unroll") for (int k = 0; k < 2; ++k) dst[m][k] = *(const LAS bf16x8*)(lds + PG8_SA(b, h) + aoff + m * 2048 + k * 1024); } while (0)
; #define PG8_LDB(dst, b, h) do { _Pragma("unroll") for (int n = 0; n < 2; ++n) _Pragma("unroll") for (int k = 0; k < 2; ++k) dst[n][k] = *(const LAS bf16x8*)(lds + PG8_SB(b, h) + boff + n * 2048 + k * 1024); } while (0)
; #define PG8_WAIT_V(n) asm volatile("s_waitcnt vmcnt(" #n ")" ::: "memory")
; #define PG8_WAIT_L(n) asm volatile("s_waitcnt lgkmcnt(" #n ")" ::: "memory")
; #define PG8_BAR __builtin_amdgcn_s_barrier()
; #define PG8_SCHED __builtin_amdgcn_sched_barrier(0)
;     ...
;         for (int t = 0; t < nt; t += 2) {
;             const bool last = (t == nt - 2);
;             const char* a1 = cA + (size_t)(t + 1) * kstep;
;             const char* a2 = last ? nA : cA + (size_t)(t + 2) * kstep; const char* b2 = last ? nB : cB + (size_t)(t + 2) * kstep;
;             const char* a3 = a2 + kstep; const char* b3 = b2 + kstep;
;             PG8_LDB(B0, 0, 0); PG8_LDB(B1, 0, 1); PG8_SCHED; PG8_LDA(At, 0, 0); PG8_STAGE(PG8_SA(1, 1), a1 + hstepA, voffA);
;             PG8_WAIT_V(8); PG8_WAIT_L(0); PG8_BAR; PG8_MMA(0, 0, At, B0); PG8_MMA(0, 1, At, B1); PG8_BAR; PG8_SCHED;
;             PG8_LDA(At, 0, 1); PG8_STAGE(PG8_SB(0, 0), b2, voffB); PG8_STAGE(PG8_SB(0, 1), b2 + hstepB, voffB); PG8_STAGE(PG8_SA(0, 0), a2, voffA);
;             PG8_WAIT_V(8); PG8_WAIT_L(0); PG8_BAR; PG8_MMA(1, 0, At, B0); PG8_MMA(1, 1, At, B1); PG8_BAR; PG8_SCHED;
;             PG8_LDB(B0, 1, 0); PG8_LDB(B1, 1, 1); PG8_SCHED; PG8_LDA(At, 1, 0); PG8_STAGE(PG8_SA(0, 1), a2 + hstepA, voffA);
;             PG8_WAIT_V(8); PG8_WAIT_L(0); PG8_BAR; PG8_MMA(0, 0, At, B0); PG8_MMA(0, 1, At, B1); PG8_BAR; PG8_SCHED;
;             PG8_LDA(At, 1, 1); PG8_STAGE(PG8_SB(1, 0), b3, voffB); PG8_STAGE(PG8_SB(1, 1), b3 + hstepB, voffB); PG8_STAGE(PG8_SA(1, 0), a3, voffA);
;             PG8_WAIT_V(8); PG8_WAIT_L(0); PG8_BAR; PG8_MMA(1, 0, At, B0); PG8_MMA(1, 1, At, B1); PG8_BAR; PG8_SCHED;
;         }
.LBB0_2276:
	v_add_u32_e32 v0, 0x10000, v244
	v_add_u32_e32 v246, 0x10000, v245
	ds_read_b128 v[140:143], v0
	ds_read_b128 v[144:147], v246
	ds_read_b128 v[148:151], v0 offset:2048
	ds_read_b128 v[152:155], v246 offset:2048
	v_add_u32_e32 v0, 0x14000, v244
	v_add_u32_e32 v246, 0x14000, v245
	ds_read_b128 v[156:159], v0
	ds_read_b128 v[160:163], v246
	ds_read_b128 v[164:167], v0 offset:2048
	ds_read_b128 v[168:171], v246 offset:2048
	s_add_u32 s18, s16, 0xfffe0080
	s_addc_u32 s19, s17, -1
	s_cmp_eq_u32 s52, 4
	s_cselect_b32 s22, s12, s18
	s_cselect_b32 s23, s13, s19
	s_cselect_b32 s20, s14, s50
	s_cselect_b32 s21, s15, s51
	s_add_u32 s18, s22, 0x80
	s_addc_u32 s19, s23, 0
	ds_read_b128 v[176:179], v242
	ds_read_b128 v[180:183], v243
	ds_read_b128 v[206:209], v242 offset:2048
	ds_read_b128 v[210:213], v243 offset:2048
	ds_read_b128 v[214:217], v242 offset:4096
	ds_read_b128 v[218:221], v243 offset:4096
	ds_read_b128 v[222:225], v242 offset:6144
	ds_read_b128 v[226:229], v243 offset:6144
	s_mov_b32 m0, s43
	s_nop 0
	global_load_lds_dwordx4 v238, s[16:17]
	s_nop 0
	s_mov_b32 m0, s44
	s_nop 0
	global_load_lds_dwordx4 v239, s[16:17]
	s_waitcnt vmcnt(8)
	s_waitcnt lgkmcnt(0)
	s_barrier
	s_setprio 1
	s_waitcnt lgkmcnt(7)
	v_mfma_f32_16x16x32_bf16 v[128:131], v[140:143], v[176:179], v[128:131]
	v_mfma_f32_16x16x32_bf16 v[124:127], v[148:151], v[176:179], v[124:127]
	s_waitcnt lgkmcnt(5)
	v_mfma_f32_16x16x32_bf16 v[120:123], v[140:143], v[206:209], v[120:123]
	v_mfma_f32_16x16x32_bf16 v[112:115], v[148:151], v[206:209], v[112:115]
	s_waitcnt lgkmcnt(3)
	v_mfma_f32_16x16x32_bf16 v[104:107], v[140:143], v[214:217], v[104:107]
	v_mfma_f32_16x16x32_bf16 v[96:99], v[148:151], v[214:217], v[96:99]
	s_waitcnt lgkmcnt(1)
	v_mfma_f32_16x16x32_bf16 v[88:91], v[140:143], v[222:225], v[88:91]
	v_mfma_f32_16x16x32_bf16 v[80:83], v[148:151], v[222:225], v[80:83]
	v_mfma_f32_16x16x32_bf16 v[128:131], v[144:147], v[180:183], v[128:131]
	v_mfma_f32_16x16x32_bf16 v[124:127], v[152:155], v[180:183], v[124:127]
	v_mfma_f32_16x16x32_bf16 v[120:123], v[144:147], v[210:213], v[120:123]
	v_mfma_f32_16x16x32_bf16 v[112:115], v[152:155], v[210:213], v[112:115]
	v_mfma_f32_16x16x32_bf16 v[104:107], v[144:147], v[218:221], v[104:107]
	v_mfma_f32_16x16x32_bf16 v[96:99], v[152:155], v[218:221], v[96:99]
	s_waitcnt lgkmcnt(0)
	v_mfma_f32_16x16x32_bf16 v[88:91], v[144:147], v[226:229], v[88:91]
	v_mfma_f32_16x16x32_bf16 v[80:83], v[152:155], v[226:229], v[80:83]
	s_setprio 0
	s_setprio 1
	v_mfma_f32_16x16x32_bf16 v[116:119], v[156:159], v[176:179], v[116:119]
	v_mfma_f32_16x16x32_bf16 v[108:111], v[164:167], v[176:179], v[108:111]
	v_mfma_f32_16x16x32_bf16 v[100:103], v[156:159], v[206:209], v[100:103]
	v_mfma_f32_16x16x32_bf16 v[92:95], v[164:167], v[206:209], v[92:95]
	v_mfma_f32_16x16x32_bf16 v[84:87], v[156:159], v[214:217], v[84:87]
	v_mfma_f32_16x16x32_bf16 v[76:79], v[164:167], v[214:217], v[76:79]
	v_mfma_f32_16x16x32_bf16 v[72:75], v[156:159], v[222:225], v[72:75]
	v_mfma_f32_16x16x32_bf16 v[68:71], v[164:167], v[222:225], v[68:71]
	v_mfma_f32_16x16x32_bf16 v[116:119], v[160:163], v[180:183], v[116:119]
	v_mfma_f32_16x16x32_bf16 v[108:111], v[168:171], v[180:183], v[108:111]
	v_mfma_f32_16x16x32_bf16 v[100:103], v[160:163], v[210:213], v[100:103]
	v_mfma_f32_16x16x32_bf16 v[92:95], v[168:171], v[210:213], v[92:95]
	v_mfma_f32_16x16x32_bf16 v[84:87], v[160:163], v[218:221], v[84:87]
	v_mfma_f32_16x16x32_bf16 v[76:79], v[168:171], v[218:221], v[76:79]
	v_mfma_f32_16x16x32_bf16 v[72:75], v[160:163], v[226:229], v[72:75]
	v_mfma_f32_16x16x32_bf16 v[68:71], v[168:171], v[226:229], v[68:71]
	s_setprio 0
	s_barrier
	ds_read_b128 v[176:179], v242 offset:16384
	ds_read_b128 v[180:183], v243 offset:16384
	ds_read_b128 v[206:209], v242 offset:18432
	ds_read_b128 v[210:213], v243 offset:18432
	ds_read_b128 v[214:217], v242 offset:20480
	ds_read_b128 v[218:221], v243 offset:20480
	ds_read_b128 v[222:225], v242 offset:22528
	ds_read_b128 v[226:229], v243 offset:22528
	s_mov_b32 m0, s28
	s_nop 0
	global_load_lds_dwordx4 v240, s[20:21]
	s_add_u32 s54, s20, 0x20000
	s_mov_b32 m0, s29
	s_nop 0
	global_load_lds_dwordx4 v241, s[20:21]
	s_addc_u32 s55, s21, 0
	s_mov_b32 m0, s30
	s_nop 0
	global_load_lds_dwordx4 v240, s[54:55]
	s_nop 0
	s_mov_b32 m0, s31
	s_nop 0
	global_load_lds_dwordx4 v241, s[54:55]
	s_nop 0
	s_mov_b32 m0, s27
	s_nop 0
	global_load_lds_dwordx4 v238, s[22:23]
	s_nop 0
	s_mov_b32 m0, s34
	s_nop 0
	global_load_lds_dwordx4 v239, s[22:23]
	s_waitcnt vmcnt(8)
	s_waitcnt lgkmcnt(0)
	s_barrier
; #define PG8_STAGE(bufoff, gbase, voff) do { _Pragma("unroll") for (int _i = 0; _i < 2; ++_i) \
;         glds16((const void*)(gbase), (voff)[_i], ldsbase + (unsigned)(bufoff) + ldsw + (unsigned)_i * 8192u); } while (0)
; #define PG8_LDA(dst, b, h) do { _Pragma("unroll") for (int m = 0; m < 4; ++m) _Pragma("unroll") for (int k = 0; k < 2; ++k) dst[m][k] = *(const LAS bf16x8*)(lds + PG8_SA(b, h) + aoff + m * 2048 + k * 1024); } while (0)
; #define PG8_LDB(dst, b, h) do { _Pragma("unroll") for (int n = 0; n < 2; ++n) _Pragma("unroll") for (int k = 0; k < 2; ++k) dst[n][k] = *(const LAS bf16x8*)(lds + PG8_SB(b, h) + boff + n * 2048 + k * 1024); } while (0)
; #define PG8_WAIT_V(n) asm volatile("s_waitcnt vmcnt(" #n ")" ::: "memory")
; #define PG8_WAIT_L(n) asm volatile("s_waitcnt lgkmcnt(" #n ")" ::: "memory")
; #define PG8_BAR __builtin_amdgcn_s_barrier()
; #define PG8_SCHED __builtin_amdgcn_sched_barrier(0)
;     ...
;         for (int t = 0; t < nt; t += 2) {
;             const bool last = (t == nt - 2);
;             const char* a1 = cA + (size_t)(t + 1) * kstep;
;             const char* a2 = last ? nA : cA + (size_t)(t + 2) * kstep; const char* b2 = last ? nB : cB + (size_t)(t + 2) * kstep;
;             const char* a3 = a2 + kstep; const char* b3 = b2 + kstep;
;             PG8_LDB(B0, 0, 0); PG8_LDB(B1, 0, 1); PG8_SCHED; PG8_LDA(At, 0, 0); PG8_STAGE(PG8_SA(1, 1), a1 + hstepA, voffA);
;             PG8_WAIT_V(8); PG8_WAIT_L(0); PG8_BAR; PG8_MMA(0, 0, At, B0); PG8_MMA(0, 1, At, B1); PG8_BAR; PG8_SCHED;
;             PG8_LDA(At, 0, 1); PG8_STAGE(PG8_SB(0, 0), b2, voffB); PG8_STAGE(PG8_SB(0, 1), b2 + hstepB, voffB); PG8_STAGE(PG8_SA(0, 0), a2, voffA);
;             PG8_WAIT_V(8); PG8_WAIT_L(0); PG8_BAR; PG8_MMA(1, 0, At, B0); PG8_MMA(1, 1, At, B1); PG8_BAR; PG8_SCHED;
;             PG8_LDB(B0, 1, 0); PG8_LDB(B1, 1, 1); PG8_SCHED; PG8_LDA(At, 1, 0); PG8_STAGE(PG8_SA(0, 1), a2 + hstepA, voffA);
;             PG8_WAIT_V(8); PG8_WAIT_L(0); PG8_BAR; PG8_MMA(0, 0, At, B0); PG8_MMA(0, 1, At, B1); PG8_BAR; PG8_SCHED;
;             PG8_LDA(At, 1, 1); PG8_STAGE(PG8_SB(1, 0), b3, voffB); PG8_STAGE(PG8_SB(1, 1), b3 + hstepB, voffB); PG8_STAGE(PG8_SA(1, 0), a3, voffA);
;             PG8_WAIT_V(8); PG8_WAIT_L(0); PG8_BAR; PG8_MMA(1, 0, At, B0); PG8_MMA(1, 1, At, B1); PG8_BAR; PG8_SCHED;
;         }
	s_setprio 1
	s_waitcnt lgkmcnt(7)
	v_mfma_f32_16x16x32_bf16 v[64:67], v[140:143], v[176:179], v[64:67]
	v_mfma_f32_16x16x32_bf16 v[60:63], v[148:151], v[176:179], v[60:63]
	s_waitcnt lgkmcnt(5)
	v_mfma_f32_16x16x32_bf16 v[56:59], v[140:143], v[206:209], v[56:59]
	v_mfma_f32_16x16x32_bf16 v[48:51], v[148:151], v[206:209], v[48:51]
	s_waitcnt lgkmcnt(3)
	v_mfma_f32_16x16x32_bf16 v[40:43], v[140:143], v[214:217], v[40:43]
	v_mfma_f32_16x16x32_bf16 v[32:35], v[148:151], v[214:217], v[32:35]
	s_waitcnt lgkmcnt(1)
	v_mfma_f32_16x16x32_bf16 v[24:27], v[140:143], v[222:225], v[24:27]
	v_mfma_f32_16x16x32_bf16 v[16:19], v[148:151], v[222:225], v[16:19]
	v_mfma_f32_16x16x32_bf16 v[64:67], v[144:147], v[180:183], v[64:67]
	v_mfma_f32_16x16x32_bf16 v[60:63], v[152:155], v[180:183], v[60:63]
	v_mfma_f32_16x16x32_bf16 v[56:59], v[144:147], v[210:213], v[56:59]
	v_mfma_f32_16x16x32_bf16 v[48:51], v[152:155], v[210:213], v[48:51]
	v_mfma_f32_16x16x32_bf16 v[40:43], v[144:147], v[218:221], v[40:43]
	v_mfma_f32_16x16x32_bf16 v[32:35], v[152:155], v[218:221], v[32:35]
	s_waitcnt lgkmcnt(0)
	v_mfma_f32_16x16x32_bf16 v[24:27], v[144:147], v[226:229], v[24:27]
	v_mfma_f32_16x16x32_bf16 v[16:19], v[152:155], v[226:229], v[16:19]
	s_setprio 0
	s_setprio 1
	v_mfma_f32_16x16x32_bf16 v[52:55], v[156:159], v[176:179], v[52:55]
	v_mfma_f32_16x16x32_bf16 v[44:47], v[164:167], v[176:179], v[44:47]
	v_mfma_f32_16x16x32_bf16 v[36:39], v[156:159], v[206:209], v[36:39]
	v_mfma_f32_16x16x32_bf16 v[28:31], v[164:167], v[206:209], v[28:31]
	v_mfma_f32_16x16x32_bf16 v[20:23], v[156:159], v[214:217], v[20:23]
	v_mfma_f32_16x16x32_bf16 v[12:15], v[164:167], v[214:217], v[12:15]
	v_mfma_f32_16x16x32_bf16 v[8:11], v[156:159], v[222:225], v[8:11]
	v_mfma_f32_16x16x32_bf16 v[4:7], v[164:167], v[222:225], v[4:7]
	v_mfma_f32_16x16x32_bf16 v[52:55], v[160:163], v[180:183], v[52:55]
	v_mfma_f32_16x16x32_bf16 v[44:47], v[168:171], v[180:183], v[44:47]
	v_mfma_f32_16x16x32_bf16 v[36:39], v[160:163], v[210:213], v[36:39]
	v_mfma_f32_16x16x32_bf16 v[28:31], v[168:171], v[210:213], v[28:31]
	v_mfma_f32_16x16x32_bf16 v[20:23], v[160:163], v[218:221], v[20:23]
	v_mfma_f32_16x16x32_bf16 v[12:15], v[168:171], v[218:221], v[12:15]
	v_mfma_f32_16x16x32_bf16 v[8:11], v[160:163], v[226:229], v[8:11]
	v_mfma_f32_16x16x32_bf16 v[4:7], v[168:171], v[226:229], v[4:7]
	s_setprio 0
	s_barrier
	v_add_u32_e32 v0, 0x18000, v244
	v_add_u32_e32 v246, 0x18000, v245
	ds_read_b128 v[140:143], v0
	ds_read_b128 v[144:147], v246
	ds_read_b128 v[148:151], v0 offset:2048
	ds_read_b128 v[152:155], v246 offset:2048
	v_add_u32_e32 v0, 0x1c000, v244
	v_add_u32_e32 v246, 0x1c000, v245
	ds_read_b128 v[156:159], v0
	ds_read_b128 v[160:163], v246
	ds_read_b128 v[164:167], v0 offset:2048
	ds_read_b128 v[168:171], v246 offset:2048
	ds_read_b128 v[176:179], v242 offset:32768
	ds_read_b128 v[180:183], v243 offset:32768
	ds_read_b128 v[206:209], v242 offset:34816
	ds_read_b128 v[210:213], v243 offset:34816
	ds_read_b128 v[214:217], v242 offset:36864
	ds_read_b128 v[218:221], v243 offset:36864
	ds_read_b128 v[222:225], v242 offset:38912
	ds_read_b128 v[226:229], v243 offset:38912
	s_add_u32 s22, s22, 0x20000
	s_addc_u32 s23, s23, 0
	s_mov_b32 m0, s35
	s_nop 0
	global_load_lds_dwordx4 v238, s[22:23]
	s_nop 0
	s_mov_b32 m0, s36
	s_nop 0
	global_load_lds_dwordx4 v239, s[22:23]
	s_waitcnt vmcnt(8)
	s_waitcnt lgkmcnt(0)
	s_barrier
	s_setprio 1
	s_waitcnt lgkmcnt(7)
	v_mfma_f32_16x16x32_bf16 v[128:131], v[140:143], v[176:179], v[128:131]
	v_mfma_f32_16x16x32_bf16 v[124:127], v[148:151], v[176:179], v[124:127]
	s_waitcnt lgkmcnt(5)
	v_mfma_f32_16x16x32_bf16 v[120:123], v[140:143], v[206:209], v[120:123]
	v_mfma_f32_16x16x32_bf16 v[112:115], v[148:151], v[206:209], v[112:115]
	s_waitcnt lgkmcnt(3)
	v_mfma_f32_16x16x32_bf16 v[104:107], v[140:143], v[214:217], v[104:107]
	v_mfma_f32_16x16x32_bf16 v[96:99], v[148:151], v[214:217], v[96:99]
	s_waitcnt lgkmcnt(1)
	v_mfma_f32_16x16x32_bf16 v[88:91], v[140:143], v[222:225], v[88:91]
	v_mfma_f32_16x16x32_bf16 v[80:83], v[148:151], v[222:225], v[80:83]
	v_mfma_f32_16x16x32_bf16 v[128:131], v[144:147], v[180:183], v[128:131]
	v_mfma_f32_16x16x32_bf16 v[124:127], v[152:155], v[180:183], v[124:127]
	v_mfma_f32_16x16x32_bf16 v[120:123], v[144:147], v[210:213], v[120:123]
	v_mfma_f32_16x16x32_bf16 v[112:115], v[152:155], v[210:213], v[112:115]
	v_mfma_f32_16x16x32_bf16 v[104:107], v[144:147], v[218:221], v[104:107]
	v_mfma_f32_16x16x32_bf16 v[96:99], v[152:155], v[218:221], v[96:99]
	s_waitcnt lgkmcnt(0)
	v_mfma_f32_16x16x32_bf16 v[88:91], v[144:147], v[226:229], v[88:91]
	v_mfma_f32_16x16x32_bf16 v[80:83], v[152:155], v[226:229], v[80:83]
	s_setprio 0
	s_setprio 1
	v_mfma_f32_16x16x32_bf16 v[116:119], v[156:159], v[176:179], v[116:119]
	v_mfma_f32_16x16x32_bf16 v[108:111], v[164:167], v[176:179], v[108:111]
	v_mfma_f32_16x16x32_bf16 v[100:103], v[156:159], v[206:209], v[100:103]
	v_mfma_f32_16x16x32_bf16 v[92:95], v[164:167], v[206:209], v[92:95]
	v_mfma_f32_16x16x32_bf16 v[84:87], v[156:159], v[214:217], v[84:87]
	v_mfma_f32_16x16x32_bf16 v[76:79], v[164:167], v[214:217], v[76:79]
	v_mfma_f32_16x16x32_bf16 v[72:75], v[156:159], v[222:225], v[72:75]
	v_mfma_f32_16x16x32_bf16 v[68:71], v[164:167], v[222:225], v[68:71]
	v_mfma_f32_16x16x32_bf16 v[116:119], v[160:163], v[180:183], v[116:119]
	v_mfma_f32_16x16x32_bf16 v[108:111], v[168:171], v[180:183], v[108:111]
	v_mfma_f32_16x16x32_bf16 v[100:103], v[160:163], v[210:213], v[100:103]
	v_mfma_f32_16x16x32_bf16 v[92:95], v[168:171], v[210:213], v[92:95]
	v_mfma_f32_16x16x32_bf16 v[84:87], v[160:163], v[218:221], v[84:87]
	v_mfma_f32_16x16x32_bf16 v[76:79], v[168:171], v[218:221], v[76:79]
	v_mfma_f32_16x16x32_bf16 v[72:75], v[160:163], v[226:229], v[72:75]
	v_mfma_f32_16x16x32_bf16 v[68:71], v[168:171], v[226:229], v[68:71]
	s_setprio 0
	s_barrier
; #define PG8_STAGE(bufoff, gbase, voff) do { _Pragma("unroll") for (int _i = 0; _i < 2; ++_i) \
;         glds16((const void*)(gbase), (voff)[_i], ldsbase + (unsigned)(bufoff) + ldsw + (unsigned)_i * 8192u); } while (0)
; #define PG8_LDA(dst, b, h) do { _Pragma("unroll") for (int m = 0; m < 4; ++m) _Pragma("unroll") for (int k = 0; k < 2; ++k) dst[m][k] = *(const LAS bf16x8*)(lds + PG8_SA(b, h) + aoff + m * 2048 + k * 1024); } while (0)
; #define PG8_LDB(dst, b, h) do { _Pragma("unroll") for (int n = 0; n < 2; ++n) _Pragma("unroll") for (int k = 0; k < 2; ++k) dst[n][k] = *(const LAS bf16x8*)(lds + PG8_SB(b, h) + boff + n * 2048 + k * 1024); } while (0)
; #define PG8_WAIT_V(n) asm volatile("s_waitcnt vmcnt(" #n ")" ::: "memory")
; #define PG8_WAIT_L(n) asm volatile("s_waitcnt lgkmcnt(" #n ")" ::: "memory")
; #define PG8_BAR __builtin_amdgcn_s_barrier()
; #define PG8_SCHED __builtin_amdgcn_sched_barrier(0)
;     ...
;         for (int t = 0; t < nt; t += 2) {
;             const bool last = (t == nt - 2);
;             const char* a1 = cA + (size_t)(t + 1) * kstep;
;             const char* a2 = last ? nA : cA + (size_t)(t + 2) * kstep; const char* b2 = last ? nB : cB + (size_t)(t + 2) * kstep;
;             const char* a3 = a2 + kstep; const char* b3 = b2 + kstep;
;             PG8_LDB(B0, 0, 0); PG8_LDB(B1, 0, 1); PG8_SCHED; PG8_LDA(At, 0, 0); PG8_STAGE(PG8_SA(1, 1), a1 + hstepA, voffA);
;             PG8_WAIT_V(8); PG8_WAIT_L(0); PG8_BAR; PG8_MMA(0, 0, At, B0); PG8_MMA(0, 1, At, B1); PG8_BAR; PG8_SCHED;
;             PG8_LDA(At, 0, 1); PG8_STAGE(PG8_SB(0, 0), b2, voffB); PG8_STAGE(PG8_SB(0, 1), b2 + hstepB, voffB); PG8_STAGE(PG8_SA(0, 0), a2, voffA);
;             PG8_WAIT_V(8); PG8_WAIT_L(0); PG8_BAR; PG8_MMA(1, 0, At, B0); PG8_MMA(1, 1, At, B1); PG8_BAR; PG8_SCHED;
;             PG8_LDB(B0, 1, 0); PG8_LDB(B1, 1, 1); PG8_SCHED; PG8_LDA(At, 1, 0); PG8_STAGE(PG8_SA(0, 1), a2 + hstepA, voffA);
;             PG8_WAIT_V(8); PG8_WAIT_L(0); PG8_BAR; PG8_MMA(0, 0, At, B0); PG8_MMA(0, 1, At, B1); PG8_BAR; PG8_SCHED;
;             PG8_LDA(At, 1, 1); PG8_STAGE(PG8_SB(1, 0), b3, voffB); PG8_STAGE(PG8_SB(1, 1), b3 + hstepB, voffB); PG8_STAGE(PG8_SA(1, 0), a3, voffA);
;             PG8_WAIT_V(8); PG8_WAIT_L(0); PG8_BAR; PG8_MMA(1, 0, At, B0); PG8_MMA(1, 1, At, B1); PG8_BAR; PG8_SCHED;
;         }
	ds_read_b128 v[176:179], v242 offset:49152
	ds_read_b128 v[180:183], v243 offset:49152
	ds_read_b128 v[206:209], v242 offset:51200
	ds_read_b128 v[210:213], v243 offset:51200
	ds_read_b128 v[214:217], v242 offset:53248
	ds_read_b128 v[218:221], v243 offset:53248
	ds_read_b128 v[222:225], v242 offset:55296
	ds_read_b128 v[226:229], v243 offset:55296
	s_add_u32 s22, s20, 0x80
	s_addc_u32 s23, s21, 0
	s_mov_b32 m0, s37
	s_nop 0
	global_load_lds_dwordx4 v240, s[22:23]
	s_add_u32 s20, s20, 0x20080
	s_mov_b32 m0, s38
	s_nop 0
	global_load_lds_dwordx4 v241, s[22:23]
	s_addc_u32 s21, s21, 0
	s_mov_b32 m0, s41
	s_nop 0
	global_load_lds_dwordx4 v240, s[20:21]
	s_nop 0
	s_mov_b32 m0, s42
	s_nop 0
	global_load_lds_dwordx4 v241, s[20:21]
	s_mov_b32 m0, s39
	s_nop 0
	global_load_lds_dwordx4 v238, s[18:19]
	s_nop 0
	s_mov_b32 m0, s40
	s_nop 0
	global_load_lds_dwordx4 v239, s[18:19]
	s_waitcnt vmcnt(8)
	s_waitcnt lgkmcnt(0)
	s_barrier
	s_setprio 1
	s_waitcnt lgkmcnt(7)
	v_mfma_f32_16x16x32_bf16 v[64:67], v[140:143], v[176:179], v[64:67]
	v_mfma_f32_16x16x32_bf16 v[60:63], v[148:151], v[176:179], v[60:63]
	s_waitcnt lgkmcnt(5)
	v_mfma_f32_16x16x32_bf16 v[56:59], v[140:143], v[206:209], v[56:59]
	v_mfma_f32_16x16x32_bf16 v[48:51], v[148:151], v[206:209], v[48:51]
	s_waitcnt lgkmcnt(3)
	v_mfma_f32_16x16x32_bf16 v[40:43], v[140:143], v[214:217], v[40:43]
	v_mfma_f32_16x16x32_bf16 v[32:35], v[148:151], v[214:217], v[32:35]
	s_waitcnt lgkmcnt(1)
	v_mfma_f32_16x16x32_bf16 v[24:27], v[140:143], v[222:225], v[24:27]
	v_mfma_f32_16x16x32_bf16 v[16:19], v[148:151], v[222:225], v[16:19]
	v_mfma_f32_16x16x32_bf16 v[64:67], v[144:147], v[180:183], v[64:67]
	v_mfma_f32_16x16x32_bf16 v[60:63], v[152:155], v[180:183], v[60:63]
	v_mfma_f32_16x16x32_bf16 v[56:59], v[144:147], v[210:213], v[56:59]
	v_mfma_f32_16x16x32_bf16 v[48:51], v[152:155], v[210:213], v[48:51]
	v_mfma_f32_16x16x32_bf16 v[40:43], v[144:147], v[218:221], v[40:43]
	v_mfma_f32_16x16x32_bf16 v[32:35], v[152:155], v[218:221], v[32:35]
	s_waitcnt lgkmcnt(0)
	v_mfma_f32_16x16x32_bf16 v[24:27], v[144:147], v[226:229], v[24:27]
	v_mfma_f32_16x16x32_bf16 v[16:19], v[152:155], v[226:229], v[16:19]
	s_setprio 0
	s_setprio 1
	v_mfma_f32_16x16x32_bf16 v[52:55], v[156:159], v[176:179], v[52:55]
	v_mfma_f32_16x16x32_bf16 v[44:47], v[164:167], v[176:179], v[44:47]
	v_mfma_f32_16x16x32_bf16 v[36:39], v[156:159], v[206:209], v[36:39]
	v_mfma_f32_16x16x32_bf16 v[28:31], v[164:167], v[206:209], v[28:31]
	v_mfma_f32_16x16x32_bf16 v[20:23], v[156:159], v[214:217], v[20:23]
	v_mfma_f32_16x16x32_bf16 v[12:15], v[164:167], v[214:217], v[12:15]
	v_mfma_f32_16x16x32_bf16 v[8:11], v[156:159], v[222:225], v[8:11]
	v_mfma_f32_16x16x32_bf16 v[4:7], v[164:167], v[222:225], v[4:7]
	v_mfma_f32_16x16x32_bf16 v[52:55], v[160:163], v[180:183], v[52:55]
	v_mfma_f32_16x16x32_bf16 v[44:47], v[168:171], v[180:183], v[44:47]
	v_mfma_f32_16x16x32_bf16 v[36:39], v[160:163], v[210:213], v[36:39]
	v_mfma_f32_16x16x32_bf16 v[28:31], v[168:171], v[210:213], v[28:31]
	v_mfma_f32_16x16x32_bf16 v[20:23], v[160:163], v[218:221], v[20:23]
	v_mfma_f32_16x16x32_bf16 v[12:15], v[168:171], v[218:221], v[12:15]
	v_mfma_f32_16x16x32_bf16 v[8:11], v[160:163], v[226:229], v[8:11]
	v_mfma_f32_16x16x32_bf16 v[4:7], v[168:171], v[226:229], v[4:7]
	s_setprio 0
	s_barrier
	s_add_i32 s52, s52, 2
	s_add_u32 s50, s50, 0x100
	s_addc_u32 s51, s51, 0
	s_add_u32 s16, s16, 0x100
	s_addc_u32 s17, s17, 0
	s_cmp_gt_u32 s52, 5
	s_cbranch_scc0 .LBB0_2276
	s_and_b64 vcc, exec, s[8:9]
	s_cbranch_vccz .LBB0_2279
	s_barrier

; #define PG8_WAIT_V(n) asm volatile("s_waitcnt vmcnt(" #n ")" ::: "memory")
; #define PG8_BAR __builtin_amdgcn_s_barrier()
;     ...
;     int tid = w0_ * 64 + lane_id(); asm volatile("" : "+v"(tid));
;     const int wid = __builtin_amdgcn_readfirstlane(tid >> 6), lane = tid & 63, wr = wid >> 2, wc = wid & 3, fr = lane & 15, fq = lane >> 4;
;     const int nt = nt_ ? nt_ : Kb / 128;
;     unsigned voffA[2], voffB[2];
; #pragma unroll
;     for (int i = 0; i < 2; ++i) { int R, C; stage_rc(tid * 16 + i * 8192, R, C); const int Rb = Epi::PERM ? ((R & ~31) + perm32(R & 31)) : R;
;         voffA[i] = (unsigned)(R * ldab + C * 2); voffB[i] = (unsigned)(Rb * Kb + C * 2); }
;     const size_t kstep = (size_t)(BK * 2);
;     const size_t hstepA = (size_t)HALF * ldab, hstepB = (size_t)HALF * Kb;
;     const unsigned ldsw = (unsigned)wid * 1024u, ldsbase = (unsigned)(size_t)lds;
;     const int aoff = lds_byte(wr * 64 + fr, fq * 8), boff = lds_byte(wc * 32 + fr, fq * 8);
;     ...
;     Unit cur, nxt; int ui = 0;
;     if (!S.next(0, cur)) return;
;     f32x4 acc[2][2][4][2];
; #pragma unroll
;     for (int a = 0; a < 2; ++a)
; #pragma unroll
;         for (int b = 0; b < 2; ++b)
; #pragma unroll
;             for (int m = 0; m < 4; ++m)
; #pragma unroll
;                 for (int n = 0; n < 2; ++n) acc[a][b][m][n] = (f32x4){0.f, 0.f, 0.f, 0.f};
;     bf16x8 At[4][2], B0[2][2], B1[2][2];
;     const char* cA = uniform_ptr(cur.a); const char* cB = uniform_ptr(cur.b);
;     PG8_STAGE(PG8_SB(0, 0), cB, voffB); PG8_STAGE(PG8_SB(0, 1), cB + hstepB, voffB); PG8_STAGE(PG8_SA(0, 0), cA, voffA); PG8_STAGE(PG8_SA(0, 1), cA + hstepA, voffA);
;     if (wr == 1) PG8_BAR;
;     PG8_WAIT_V(2); PG8_BAR;
;     PG8_STAGE(PG8_SB(1, 0), cB + kstep, voffB); PG8_STAGE(PG8_SA(1, 0), cA + kstep, voffA); PG8_STAGE(PG8_SB(1, 1), cB + hstepB + kstep, voffB);
;     PG8_WAIT_V(6); PG8_BAR;
; __global__ void __launch_bounds__(512, 2) fwd(Args args) {
;     ...
;         if (IN(pb + 6)) { PHASE_LOCALS();
;             pg8::SimpleSched S; S.o.init(T / 256, 8, G, bx); S.A = (const char*)(act + A_AO); S.Bt = (const char*)(ws + WS_WOUT + l * SZ_WOUT); S.astep = (size_t)256 * 2048 * 2; S.bstep = (size_t)256 * 2048;
;             if (l == 0) { pg8::EpiResBf16<true> E{(const void*)args.in[I_X], (bf16_t*)(ws + WS_XA), D, (float*)(ws + WS_SS)}; pg8::gemm_phase<true>(lds, 2048, 4096, S, E, w0, 123, 121); }
.LBB0_2571:
	s_cmp_gt_i32 s82, s0
	s_cselect_b64 s[2:3], -1, 0
	s_cmp_ge_i32 s0, s83
	s_cselect_b64 s[4:5], -1, 0
	s_or_b64 s[2:3], s[2:3], s[4:5]
	s_and_b64 vcc, exec, s[2:3]
	s_cbranch_vccnz .LBB0_2685
	s_mov_b64 s[2:3], 0
	s_add_u32 s0, s80, s2
	s_addc_u32 s26, s81, s3
	v_mbcnt_lo_u32_b32 v0, -1, 0
	v_mbcnt_hi_u32_b32 v0, -1, v0
	v_readlane_b32 s2, v250, 60
	s_add_u32 s30, s0, 0x4fa1e000
	s_addc_u32 s31, s26, 0
	v_add_u32_e32 v0, s2, v0
	s_lshl_b32 s2, s27, 23
	s_add_u32 s2, s0, s2
	s_addc_u32 s3, s26, 0
	s_add_u32 s34, s2, 0x1d00000
	s_addc_u32 s35, s3, 0
	v_readlane_b32 s4, v254, 44
	s_add_u32 s6, s0, 0x32892000
	v_readlane_b32 s5, v254, 45
	s_addc_u32 s7, s26, 0
	s_mov_b64 s[2:3], -1
	s_and_b64 vcc, exec, s[4:5]
	s_cbranch_vccz .LBB0_2594
	v_mbcnt_lo_u32_b32 v0, -1, 0
	v_mbcnt_hi_u32_b32 v0, -1, v0
	v_readlane_b32 s2, v250, 60
	s_nop 1
	v_add_u32_e32 v0, s2, v0
	v_readlane_b32 s2, v252, 42
	v_readlane_b32 s3, v252, 43
	s_andn2_b64 vcc, exec, s[2:3]
	v_readfirstlane_b32 s2, v0
	s_cbranch_vccnz .LBB0_2593
	v_bfe_i32 v4, v0, 27, 1
	s_waitcnt lgkmcnt(0)
	v_lshlrev_b32_e32 v1, 4, v0
	v_lshrrev_b32_e32 v4, 22, v4
	v_add_u32_e32 v4, v1, v4
	v_and_b32_e32 v4, 0xfffffc00, v4
	v_sub_u32_e32 v4, v1, v4
	v_ashrrev_i32_e32 v2, 31, v0
	v_lshrrev_b32_e32 v5, 4, v4
	v_lshrrev_b32_e32 v2, 26, v2
	v_bitop3_b32 v4, v5, v4, 32 bitop3:0x6c
	v_add_u32_e32 v2, v0, v2
	v_ashrrev_i32_e32 v6, 31, v4
	v_ashrrev_i32_e32 v2, 6, v2
	v_lshrrev_b32_e32 v6, 26, v6
	v_lshlrev_b32_e32 v5, 3, v2
	v_add_u32_e32 v6, v4, v6
	v_and_b32_e32 v5, -16, v5
	v_ashrrev_i32_e32 v7, 6, v6
	v_and_b32_e32 v6, 0xc0, v6
	v_add_u32_e32 v5, v7, v5
	v_sub_u32_e32 v4, v4, v6
	v_lshlrev_b32_e32 v2, 5, v2
	v_ashrrev_i16_sdwa v4, v188, sext(v4) dst_sel:DWORD dst_unused:UNUSED_PAD src0_sel:DWORD src1_sel:BYTE_0
	v_lshlrev_b32_e32 v6, 1, v5
	v_lshrrev_b32_e32 v8, 2, v5
	v_and_b32_e32 v7, 3, v7
	s_mov_b32 s4, 0x1fffe0
	v_and_b32_e32 v2, 32, v2
	v_bfe_i32 v4, v4, 0, 16
	v_and_b32_e32 v6, 24, v6
	v_and_b32_e32 v8, 4, v8
	v_and_or_b32 v7, v5, s4, v7
	v_or3_b32 v6, v7, v8, v6
	v_add_lshl_u32 v4, v2, v4, 1
	v_add_u32_e32 v1, 0x2000, v1
	v_lshl_add_u32 v2, v5, 12, v4
	v_lshl_add_u32 v164, v6, 11, v4
	v_ashrrev_i32_e32 v4, 31, v1
	v_lshrrev_b32_e32 v4, 22, v4
	v_add_u32_e32 v4, v1, v4
	v_ashrrev_i32_e32 v4, 10, v4
	v_mul_i32_i24_e32 v5, 0x400, v4
	v_sub_u32_e32 v1, v1, v5
	v_lshrrev_b32_e32 v5, 4, v1
	v_bitop3_b32 v1, v5, v1, 32 bitop3:0x6c
	v_ashrrev_i32_e32 v6, 31, v1
	v_lshrrev_b32_e32 v6, 26, v6
	v_lshlrev_b32_e32 v5, 3, v4
	v_add_u32_e32 v6, v1, v6
	v_and_b32_e32 v5, -16, v5
	v_ashrrev_i32_e32 v7, 6, v6
	v_add_u32_e32 v5, v7, v5
	v_and_b32_e32 v7, 3, v7
	s_ashr_i32 s8, s2, 6
	s_ashr_i32 s3, s2, 8
	v_and_or_b32 v7, v5, s4, v7
	s_lshl_b32 s27, s8, 10
	v_readlane_b32 s4, v253, 21
	v_and_b32_e32 v6, 0xc0, v6
	v_readlane_b32 s5, v253, 22
	s_add_u32 s20, s34, s4
	v_sub_u32_e32 v1, v1, v6
	s_addc_u32 s21, s35, s5
	v_readlane_b32 s4, v253, 28
	v_lshlrev_b32_e32 v4, 5, v4
	v_ashrrev_i16_sdwa v1, v188, sext(v1) dst_sel:DWORD dst_unused:UNUSED_PAD src0_sel:DWORD src1_sel:BYTE_0
	v_lshlrev_b32_e32 v6, 1, v5
	v_lshrrev_b32_e32 v8, 2, v5
	v_readlane_b32 s5, v253, 29
	s_add_u32 s18, s30, s4
	v_and_b32_e32 v4, 32, v4
	v_bfe_i32 v1, v1, 0, 16
	v_and_b32_e32 v6, 24, v6
	v_and_b32_e32 v8, 4, v8
	s_addc_u32 s19, s31, s5
	s_add_i32 s27, s27, 0
	v_or3_b32 v6, v7, v8, v6
	v_add_lshl_u32 v1, v4, v1, 1
	s_add_i32 s28, s27, 0x10000
	s_nop 0
	v_readlane_b32 s70, v250, 60
	v_mbcnt_lo_u32_b32 v246, -1, 0
	v_mbcnt_hi_u32_b32 v246, -1, v246
	v_add_u32_e32 v246, s70, v246
	v_bfe_u32 v247, v246, 4, 2
	v_bfe_u32 v248, v246, 6, 1
	v_lshl_or_b32 v247, v248, 2, v247
	v_and_b32_e32 v248, 7, v246
	v_xor_b32_e32 v247, v247, v248
	v_lshlrev_b32_e32 v247, 4, v247
	v_lshrrev_b32_e32 v248, 3, v246
	v_lshl_add_u32 v238, v248, 12, v247
	v_add_u32_e32 v239, 0x40000, v238
	v_and_b32_e32 v249, 0x23, v248
	v_and_b32_e32 v244, 12, v248
	v_lshl_or_b32 v249, v244, 1, v249
	v_bfe_u32 v244, v248, 4, 1
	v_lshl_or_b32 v249, v244, 2, v249
	v_lshl_add_u32 v240, v249, 11, v247
	v_add_u32_e32 v241, 0x20000, v240
	v_bfe_u32 v247, v246, 4, 2
	v_bfe_u32 v248, v246, 1, 3
	v_xor_b32_e32 v247, v247, v248
	v_lshlrev_b32_e32 v247, 4, v247
	v_and_b32_e32 v248, 7, v246
	v_lshl_or_b32 v247, v248, 7, v247
	v_bfe_u32 v248, v246, 3, 1
	v_lshl_or_b32 v247, v248, 10, v247
	v_bfe_u32 v248, v246, 8, 1
	v_lshl_or_b32 v242, v248, 13, v247
	v_xor_b32_e32 v243, 64, v242
	v_bfe_u32 v248, v246, 6, 2
	v_lshl_or_b32 v244, v248, 12, v247
	v_xor_b32_e32 v245, 64, v244
	s_mov_b32 m0, s28
	s_nop 0
	global_load_lds_dwordx4 v240, s[20:21]
	v_lshl_add_u32 v166, v6, 11, v1
	s_add_i32 s29, s27, 0x12000
	s_mov_b32 m0, s29
	s_nop 0
	global_load_lds_dwordx4 v241, s[20:21]
	s_add_u32 s4, s20, 0x40000
	s_addc_u32 s5, s21, 0
	s_add_i32 s36, s27, 0x14000
	s_mov_b32 m0, s36
	s_nop 0
	global_load_lds_dwordx4 v240, s[4:5]
	s_add_i32 s37, s27, 0x16000
	s_mov_b32 m0, s37
	s_nop 0
	global_load_lds_dwordx4 v241, s[4:5]
	s_mov_b32 m0, s27
	s_nop 0
	global_load_lds_dwordx4 v238, s[18:19]
	v_lshl_add_u32 v165, v5, 12, v1
	s_add_i32 s38, s27, 0x2000
	s_mov_b32 m0, s38
	s_nop 0
	global_load_lds_dwordx4 v239, s[18:19]
	s_add_u32 s4, s18, 0x80000
	s_addc_u32 s5, s19, 0
	s_add_i32 s39, s27, 0x4000
	s_mov_b32 m0, s39
	s_nop 0
	global_load_lds_dwordx4 v238, s[4:5]
	s_add_i32 s40, s27, 0x6000
	s_mov_b32 m0, s40
	s_nop 0
	global_load_lds_dwordx4 v239, s[4:5]
	s_cmp_eq_u32 s3, 1
	s_cselect_b64 s[4:5], -1, 0
	s_cmp_lg_u32 s3, 1
	s_cbranch_scc1 .LBB0_2576
	s_barrier
; #define PG8_STAGE(bufoff, gbase, voff) do { _Pragma("unroll") for (int _i = 0; _i < 2; ++_i) \
;         glds16((const void*)(gbase), (voff)[_i], ldsbase + (unsigned)(bufoff) + ldsw + (unsigned)_i * 8192u); } while (0)
; #define PG8_WAIT_V(n) asm volatile("s_waitcnt vmcnt(" #n ")" ::: "memory")
; #define PG8_BAR __builtin_amdgcn_s_barrier()
;     ...
;     PG8_STAGE(PG8_SB(0, 0), cB, voffB); PG8_STAGE(PG8_SB(0, 1), cB + hstepB, voffB); PG8_STAGE(PG8_SA(0, 0), cA, voffA); PG8_STAGE(PG8_SA(0, 1), cA + hstepA, voffA);
;     if (wr == 1) PG8_BAR;
;     PG8_WAIT_V(2); PG8_BAR;
;     PG8_STAGE(PG8_SB(1, 0), cB + kstep, voffB); PG8_STAGE(PG8_SA(1, 0), cA + kstep, voffA); PG8_STAGE(PG8_SB(1, 1), cB + hstepB + kstep, voffB);
;     PG8_WAIT_V(6); PG8_BAR;
.LBB0_2576:
	v_lshrrev_b32_e32 v4, 1, v0
	v_and_b32_e32 v4, 24, v4
	v_and_b32_e32 v1, 15, v0
	v_lshlrev_b32_e32 v5, 1, v4
	v_lshlrev_b32_e32 v0, 2, v0
	v_lshl_or_b32 v167, s3, 6, v1
	v_lshl_or_b32 v1, v1, 6, v5
	s_lshl_b32 s3, s3, 13
	v_and_b32_e32 v0, 32, v0
	v_bitop3_b32 v5, v1, s3, v0 bitop3:0xde
	s_lshl_b32 s3, s8, 5
	s_and_b32 s3, s3, 0x60
	s_lshl_b32 s8, s3, 7
	v_bitop3_b32 v0, v1, s8, v0 bitop3:0xde
	s_add_u32 s8, s20, 0x80
	s_waitcnt vmcnt(2)
	s_barrier
	s_addc_u32 s9, s21, 0
	s_add_i32 s41, s27, 0x18000
	s_mov_b32 m0, s41
	s_nop 0
	global_load_lds_dwordx4 v240, s[8:9]
	s_add_i32 s42, s27, 0x1a000
	s_mov_b32 m0, s42
	s_nop 0
	global_load_lds_dwordx4 v241, s[8:9]
	s_add_u32 s8, s18, 0x80
	s_addc_u32 s9, s19, 0
	s_add_i32 s43, s27, 0x8000
	s_mov_b32 m0, s43
	s_nop 0
	global_load_lds_dwordx4 v238, s[8:9]
	s_add_i32 s44, s27, 0xa000
	s_mov_b32 m0, s44
	s_nop 0
	global_load_lds_dwordx4 v239, s[8:9]
	s_add_u32 s8, s20, 0x40080
	s_addc_u32 s9, s21, 0
	s_add_i32 s45, s27, 0x1c000
	s_mov_b32 m0, s45
	s_nop 0
	global_load_lds_dwordx4 v240, s[8:9]
	s_add_i32 s46, s27, 0x1e000
	s_mov_b32 m0, s46
	s_nop 0
	global_load_lds_dwordx4 v241, s[8:9]
	s_waitcnt vmcnt(6)
	s_add_i32 s47, s27, 0xc000
	s_cmpk_lt_u32 s2, 0x100
	v_or_b32_e32 v168, s3, v4
	v_readlane_b32 s2, v253, 26
	s_cselect_b64 s[8:9], -1, 0
	s_add_i32 s48, s27, 0xe000
	s_mov_b32 s49, 0
	v_add_u32_e32 v169, 0, v0
	v_add_u32_e32 v170, 0, v5
	v_readlane_b32 s50, v253, 20
	s_mov_b32 s51, s2
	s_mov_b64 s[14:15], s[18:19]
	s_mov_b64 s[16:17], s[20:21]
	s_barrier
	v_readlane_b32 s3, v253, 27
	s_branch .LBB0_2579

; #define PG8_STAGE(bufoff, gbase, voff) do { _Pragma("unroll") for (int _i = 0; _i < 2; ++_i) \
;         glds16((const void*)(gbase), (voff)[_i], ldsbase + (unsigned)(bufoff) + ldsw + (unsigned)_i * 8192u); } while (0)
; #define PG8_LDA(dst, b, h) do { _Pragma("unroll") for (int m = 0; m < 4; ++m) _Pragma("unroll") for (int k = 0; k < 2; ++k) dst[m][k] = *(const LAS bf16x8*)(lds + PG8_SA(b, h) + aoff + m * 2048 + k * 1024); } while (0)
; #define PG8_LDB(dst, b, h) do { _Pragma("unroll") for (int n = 0; n < 2; ++n) _Pragma("unroll") for (int k = 0; k < 2; ++k) dst[n][k] = *(const LAS bf16x8*)(lds + PG8_SB(b, h) + boff + n * 2048 + k * 1024); } while (0)
; #define PG8_WAIT_V(n) asm volatile("s_waitcnt vmcnt(" #n ")" ::: "memory")
; #define PG8_WAIT_L(n) asm volatile("s_waitcnt lgkmcnt(" #n ")" ::: "memory")
; #define PG8_BAR __builtin_amdgcn_s_barrier()
; #define PG8_SCHED __builtin_amdgcn_sched_barrier(0)
;     ...
;         for (int t = 0; t < nt; t += 2) {
;             const bool last = (t == nt - 2);
;             const char* a1 = cA + (size_t)(t + 1) * kstep;
;             const char* a2 = last ? nA : cA + (size_t)(t + 2) * kstep; const char* b2 = last ? nB : cB + (size_t)(t + 2) * kstep;
;             const char* a3 = a2 + kstep; const char* b3 = b2 + kstep;
;             PG8_LDB(B0, 0, 0); PG8_LDB(B1, 0, 1); PG8_SCHED; PG8_LDA(At, 0, 0); PG8_STAGE(PG8_SA(1, 1), a1 + hstepA, voffA);
;             PG8_WAIT_V(8); PG8_WAIT_L(0); PG8_BAR; PG8_MMA(0, 0, At, B0); PG8_MMA(0, 1, At, B1); PG8_BAR; PG8_SCHED;
;             PG8_LDA(At, 0, 1); PG8_STAGE(PG8_SB(0, 0), b2, voffB); PG8_STAGE(PG8_SB(0, 1), b2 + hstepB, voffB); PG8_STAGE(PG8_SA(0, 0), a2, voffA);
;             PG8_WAIT_V(8); PG8_WAIT_L(0); PG8_BAR; PG8_MMA(1, 0, At, B0); PG8_MMA(1, 1, At, B1); PG8_BAR; PG8_SCHED;
;             PG8_LDB(B0, 1, 0); PG8_LDB(B1, 1, 1); PG8_SCHED; PG8_LDA(At, 1, 0); PG8_STAGE(PG8_SA(0, 1), a2 + hstepA, voffA);
;             PG8_WAIT_V(8); PG8_WAIT_L(0); PG8_BAR; PG8_MMA(0, 0, At, B0); PG8_MMA(0, 1, At, B1); PG8_BAR; PG8_SCHED;
;             PG8_LDA(At, 1, 1); PG8_STAGE(PG8_SB(1, 0), b3, voffB); PG8_STAGE(PG8_SB(1, 1), b3 + hstepB, voffB); PG8_STAGE(PG8_SA(1, 0), a3, voffA);
;             PG8_WAIT_V(8); PG8_WAIT_L(0); PG8_BAR; PG8_MMA(1, 0, At, B0); PG8_MMA(1, 1, At, B1); PG8_BAR; PG8_SCHED;
;         }
.LBB0_2586:
	v_add_u32_e32 v0, 0x10000, v244
	v_add_u32_e32 v246, 0x10000, v245
	ds_read_b128 v[28:31], v0
	ds_read_b128 v[32:35], v246
	ds_read_b128 v[20:23], v0 offset:2048
	ds_read_b128 v[24:27], v246 offset:2048
	v_add_u32_e32 v0, 0x14000, v244
	v_add_u32_e32 v246, 0x14000, v245
	s_waitcnt lgkmcnt(4)
	ds_read_b128 v[12:15], v0
	ds_read_b128 v[16:19], v246
	ds_read_b128 v[4:7], v0 offset:2048
	ds_read_b128 v[8:11], v246 offset:2048
	s_add_u32 s20, s18, 0xfff80080
	s_addc_u32 s21, s19, -1
	s_cmp_eq_u32 s52, 12
	s_cselect_b32 s24, s14, s20
	s_cselect_b32 s25, s15, s21
	s_cselect_b32 s22, s16, s11
	s_cselect_b32 s23, s17, s13
	s_add_u32 s20, s24, 0x80
	s_addc_u32 s21, s25, 0
	ds_read_b128 v[176:179], v242
	ds_read_b128 v[180:183], v243
	ds_read_b128 v[206:209], v242 offset:2048
	ds_read_b128 v[210:213], v243 offset:2048
	ds_read_b128 v[214:217], v242 offset:4096
	ds_read_b128 v[218:221], v243 offset:4096
	ds_read_b128 v[222:225], v242 offset:6144
	ds_read_b128 v[226:229], v243 offset:6144
	s_mov_b32 m0, s47
	s_nop 0
	global_load_lds_dwordx4 v238, s[18:19]
	s_nop 0
	s_mov_b32 m0, s48
	s_nop 0
	global_load_lds_dwordx4 v239, s[18:19]
	s_waitcnt vmcnt(8)
	s_waitcnt lgkmcnt(0)
	s_barrier
	s_setprio 1
	s_waitcnt lgkmcnt(6)
	v_mfma_scale_f32_16x16x128_f8f6f4 v[160:163], v[28:35], v[176:183], v[160:163], v189, v190 op_sel_hi:[0,0,0]
	v_mfma_scale_f32_16x16x128_f8f6f4 v[156:159], v[20:27], v[176:183], v[156:159], v189, v190 op_sel_hi:[0,0,0]
	s_waitcnt lgkmcnt(4)
	v_mfma_scale_f32_16x16x128_f8f6f4 v[144:147], v[28:35], v[206:213], v[144:147], v189, v190 op_sel_hi:[0,0,0]
	v_mfma_scale_f32_16x16x128_f8f6f4 v[140:143], v[20:27], v[206:213], v[140:143], v189, v190 op_sel_hi:[0,0,0]
	s_waitcnt lgkmcnt(2)
	v_mfma_scale_f32_16x16x128_f8f6f4 v[128:131], v[28:35], v[214:221], v[128:131], v189, v190 op_sel_hi:[0,0,0]
	v_mfma_scale_f32_16x16x128_f8f6f4 v[124:127], v[20:27], v[214:221], v[124:127], v189, v190 op_sel_hi:[0,0,0]
	s_waitcnt lgkmcnt(0)
	v_mfma_scale_f32_16x16x128_f8f6f4 v[112:115], v[28:35], v[222:229], v[112:115], v189, v190 op_sel_hi:[0,0,0]
	v_mfma_scale_f32_16x16x128_f8f6f4 v[108:111], v[20:27], v[222:229], v[108:111], v189, v190 op_sel_hi:[0,0,0]
	s_setprio 0
	s_setprio 1
	v_mfma_scale_f32_16x16x128_f8f6f4 v[152:155], v[12:19], v[176:183], v[152:155], v189, v190 op_sel_hi:[0,0,0]
	v_mfma_scale_f32_16x16x128_f8f6f4 v[148:151], v[4:11], v[176:183], v[148:151], v189, v190 op_sel_hi:[0,0,0]
	v_mfma_scale_f32_16x16x128_f8f6f4 v[136:139], v[12:19], v[206:213], v[136:139], v189, v190 op_sel_hi:[0,0,0]
	v_mfma_scale_f32_16x16x128_f8f6f4 v[132:135], v[4:11], v[206:213], v[132:135], v189, v190 op_sel_hi:[0,0,0]
	v_mfma_scale_f32_16x16x128_f8f6f4 v[120:123], v[12:19], v[214:221], v[120:123], v189, v190 op_sel_hi:[0,0,0]
	v_mfma_scale_f32_16x16x128_f8f6f4 v[116:119], v[4:11], v[214:221], v[116:119], v189, v190 op_sel_hi:[0,0,0]
	v_mfma_scale_f32_16x16x128_f8f6f4 v[104:107], v[12:19], v[222:229], v[104:107], v189, v190 op_sel_hi:[0,0,0]
	v_mfma_scale_f32_16x16x128_f8f6f4 v[100:103], v[4:11], v[222:229], v[100:103], v189, v190 op_sel_hi:[0,0,0]
	s_setprio 0
	s_barrier
	ds_read_b128 v[176:179], v242 offset:16384
	ds_read_b128 v[180:183], v243 offset:16384
	ds_read_b128 v[206:209], v242 offset:18432
	ds_read_b128 v[210:213], v243 offset:18432
	ds_read_b128 v[214:217], v242 offset:20480
	ds_read_b128 v[218:221], v243 offset:20480
	ds_read_b128 v[222:225], v242 offset:22528
	ds_read_b128 v[226:229], v243 offset:22528
	s_mov_b32 m0, s28
	s_nop 0
	global_load_lds_dwordx4 v240, s[22:23]
	s_add_u32 s54, s22, 0x40000
	s_mov_b32 m0, s29
	s_nop 0
	global_load_lds_dwordx4 v241, s[22:23]
	s_addc_u32 s55, s23, 0
	s_mov_b32 m0, s36
	s_nop 0
	global_load_lds_dwordx4 v240, s[54:55]
	s_nop 0
	s_mov_b32 m0, s37
	s_nop 0
	global_load_lds_dwordx4 v241, s[54:55]
	s_nop 0
	s_mov_b32 m0, s27
	s_nop 0
	global_load_lds_dwordx4 v238, s[24:25]
	s_nop 0
	s_mov_b32 m0, s38
	s_nop 0
	global_load_lds_dwordx4 v239, s[24:25]
	s_waitcnt vmcnt(8)
	s_waitcnt lgkmcnt(0)
	s_barrier
	s_setprio 1
	s_waitcnt lgkmcnt(6)
	v_mfma_scale_f32_16x16x128_f8f6f4 v[96:99], v[28:35], v[176:183], v[96:99], v189, v190 op_sel_hi:[0,0,0]
	v_mfma_scale_f32_16x16x128_f8f6f4 v[92:95], v[20:27], v[176:183], v[92:95], v189, v190 op_sel_hi:[0,0,0]
	s_waitcnt lgkmcnt(4)
	v_mfma_scale_f32_16x16x128_f8f6f4 v[80:83], v[28:35], v[206:213], v[80:83], v189, v190 op_sel_hi:[0,0,0]
	v_mfma_scale_f32_16x16x128_f8f6f4 v[76:79], v[20:27], v[206:213], v[76:79], v189, v190 op_sel_hi:[0,0,0]
	s_waitcnt lgkmcnt(2)
	v_mfma_scale_f32_16x16x128_f8f6f4 v[64:67], v[28:35], v[214:221], v[64:67], v189, v190 op_sel_hi:[0,0,0]
	v_mfma_scale_f32_16x16x128_f8f6f4 v[60:63], v[20:27], v[214:221], v[60:63], v189, v190 op_sel_hi:[0,0,0]
	s_waitcnt lgkmcnt(0)
	v_mfma_scale_f32_16x16x128_f8f6f4 v[48:51], v[28:35], v[222:229], v[48:51], v189, v190 op_sel_hi:[0,0,0]
	v_mfma_scale_f32_16x16x128_f8f6f4 v[44:47], v[20:27], v[222:229], v[44:47], v189, v190 op_sel_hi:[0,0,0]
	s_setprio 0
	s_setprio 1
	v_mfma_scale_f32_16x16x128_f8f6f4 v[88:91], v[12:19], v[176:183], v[88:91], v189, v190 op_sel_hi:[0,0,0]
	v_mfma_scale_f32_16x16x128_f8f6f4 v[84:87], v[4:11], v[176:183], v[84:87], v189, v190 op_sel_hi:[0,0,0]
	v_mfma_scale_f32_16x16x128_f8f6f4 v[72:75], v[12:19], v[206:213], v[72:75], v189, v190 op_sel_hi:[0,0,0]
	v_mfma_scale_f32_16x16x128_f8f6f4 v[68:71], v[4:11], v[206:213], v[68:71], v189, v190 op_sel_hi:[0,0,0]
	v_mfma_scale_f32_16x16x128_f8f6f4 v[56:59], v[12:19], v[214:221], v[56:59], v189, v190 op_sel_hi:[0,0,0]
	v_mfma_scale_f32_16x16x128_f8f6f4 v[52:55], v[4:11], v[214:221], v[52:55], v189, v190 op_sel_hi:[0,0,0]
	v_mfma_scale_f32_16x16x128_f8f6f4 v[40:43], v[12:19], v[222:229], v[40:43], v189, v190 op_sel_hi:[0,0,0]
	v_mfma_scale_f32_16x16x128_f8f6f4 v[36:39], v[4:11], v[222:229], v[36:39], v189, v190 op_sel_hi:[0,0,0]
	s_setprio 0
	s_barrier
; #define PG8_STAGE(bufoff, gbase, voff) do { _Pragma("unroll") for (int _i = 0; _i < 2; ++_i) \
;         glds16((const void*)(gbase), (voff)[_i], ldsbase + (unsigned)(bufoff) + ldsw + (unsigned)_i * 8192u); } while (0)
; #define PG8_LDA(dst, b, h) do { _Pragma("unroll") for (int m = 0; m < 4; ++m) _Pragma("unroll") for (int k = 0; k < 2; ++k) dst[m][k] = *(const LAS bf16x8*)(lds + PG8_SA(b, h) + aoff + m * 2048 + k * 1024); } while (0)
; #define PG8_LDB(dst, b, h) do { _Pragma("unroll") for (int n = 0; n < 2; ++n) _Pragma("unroll") for (int k = 0; k < 2; ++k) dst[n][k] = *(const LAS bf16x8*)(lds + PG8_SB(b, h) + boff + n * 2048 + k * 1024); } while (0)
; #define PG8_WAIT_V(n) asm volatile("s_waitcnt vmcnt(" #n ")" ::: "memory")
; #define PG8_WAIT_L(n) asm volatile("s_waitcnt lgkmcnt(" #n ")" ::: "memory")
; #define PG8_BAR __builtin_amdgcn_s_barrier()
; #define PG8_SCHED __builtin_amdgcn_sched_barrier(0)
;     ...
;         for (int t = 0; t < nt; t += 2) {
;             const bool last = (t == nt - 2);
;             const char* a1 = cA + (size_t)(t + 1) * kstep;
;             const char* a2 = last ? nA : cA + (size_t)(t + 2) * kstep; const char* b2 = last ? nB : cB + (size_t)(t + 2) * kstep;
;             const char* a3 = a2 + kstep; const char* b3 = b2 + kstep;
;             PG8_LDB(B0, 0, 0); PG8_LDB(B1, 0, 1); PG8_SCHED; PG8_LDA(At, 0, 0); PG8_STAGE(PG8_SA(1, 1), a1 + hstepA, voffA);
;             PG8_WAIT_V(8); PG8_WAIT_L(0); PG8_BAR; PG8_MMA(0, 0, At, B0); PG8_MMA(0, 1, At, B1); PG8_BAR; PG8_SCHED;
;             PG8_LDA(At, 0, 1); PG8_STAGE(PG8_SB(0, 0), b2, voffB); PG8_STAGE(PG8_SB(0, 1), b2 + hstepB, voffB); PG8_STAGE(PG8_SA(0, 0), a2, voffA);
;             PG8_WAIT_V(8); PG8_WAIT_L(0); PG8_BAR; PG8_MMA(1, 0, At, B0); PG8_MMA(1, 1, At, B1); PG8_BAR; PG8_SCHED;
;             PG8_LDB(B0, 1, 0); PG8_LDB(B1, 1, 1); PG8_SCHED; PG8_LDA(At, 1, 0); PG8_STAGE(PG8_SA(0, 1), a2 + hstepA, voffA);
;             PG8_WAIT_V(8); PG8_WAIT_L(0); PG8_BAR; PG8_MMA(0, 0, At, B0); PG8_MMA(0, 1, At, B1); PG8_BAR; PG8_SCHED;
;             PG8_LDA(At, 1, 1); PG8_STAGE(PG8_SB(1, 0), b3, voffB); PG8_STAGE(PG8_SB(1, 1), b3 + hstepB, voffB); PG8_STAGE(PG8_SA(1, 0), a3, voffA);
;             PG8_WAIT_V(8); PG8_WAIT_L(0); PG8_BAR; PG8_MMA(1, 0, At, B0); PG8_MMA(1, 1, At, B1); PG8_BAR; PG8_SCHED;
;         }
	v_add_u32_e32 v0, 0x18000, v244
	v_add_u32_e32 v246, 0x18000, v245
	ds_read_b128 v[20:23], v0
	ds_read_b128 v[24:27], v246
	ds_read_b128 v[28:31], v0 offset:2048
	ds_read_b128 v[32:35], v246 offset:2048
	v_add_u32_e32 v0, 0x1c000, v244
	v_add_u32_e32 v246, 0x1c000, v245
	ds_read_b128 v[12:15], v0
	ds_read_b128 v[16:19], v246
	ds_read_b128 v[4:7], v0 offset:2048
	ds_read_b128 v[8:11], v246 offset:2048
	ds_read_b128 v[176:179], v242 offset:32768
	ds_read_b128 v[180:183], v243 offset:32768
	ds_read_b128 v[206:209], v242 offset:34816
	ds_read_b128 v[210:213], v243 offset:34816
	ds_read_b128 v[214:217], v242 offset:36864
	ds_read_b128 v[218:221], v243 offset:36864
	ds_read_b128 v[222:225], v242 offset:38912
	ds_read_b128 v[226:229], v243 offset:38912
	s_add_u32 s24, s24, 0x80000
	s_addc_u32 s25, s25, 0
	s_mov_b32 m0, s39
	s_nop 0
	global_load_lds_dwordx4 v238, s[24:25]
	s_nop 0
	s_mov_b32 m0, s40
	s_nop 0
	global_load_lds_dwordx4 v239, s[24:25]
	s_waitcnt vmcnt(8)
	s_waitcnt lgkmcnt(0)
	s_barrier
	s_setprio 1
	s_waitcnt lgkmcnt(6)
	v_mfma_scale_f32_16x16x128_f8f6f4 v[160:163], v[20:27], v[176:183], v[160:163], v189, v190 op_sel_hi:[0,0,0]
	v_mfma_scale_f32_16x16x128_f8f6f4 v[156:159], v[28:35], v[176:183], v[156:159], v189, v190 op_sel_hi:[0,0,0]
	s_waitcnt lgkmcnt(4)
	v_mfma_scale_f32_16x16x128_f8f6f4 v[144:147], v[20:27], v[206:213], v[144:147], v189, v190 op_sel_hi:[0,0,0]
	v_mfma_scale_f32_16x16x128_f8f6f4 v[140:143], v[28:35], v[206:213], v[140:143], v189, v190 op_sel_hi:[0,0,0]
	s_waitcnt lgkmcnt(2)
	v_mfma_scale_f32_16x16x128_f8f6f4 v[128:131], v[20:27], v[214:221], v[128:131], v189, v190 op_sel_hi:[0,0,0]
	v_mfma_scale_f32_16x16x128_f8f6f4 v[124:127], v[28:35], v[214:221], v[124:127], v189, v190 op_sel_hi:[0,0,0]
	s_waitcnt lgkmcnt(0)
	v_mfma_scale_f32_16x16x128_f8f6f4 v[112:115], v[20:27], v[222:229], v[112:115], v189, v190 op_sel_hi:[0,0,0]
	v_mfma_scale_f32_16x16x128_f8f6f4 v[108:111], v[28:35], v[222:229], v[108:111], v189, v190 op_sel_hi:[0,0,0]
	s_setprio 0
	s_setprio 1
	v_mfma_scale_f32_16x16x128_f8f6f4 v[152:155], v[12:19], v[176:183], v[152:155], v189, v190 op_sel_hi:[0,0,0]
	v_mfma_scale_f32_16x16x128_f8f6f4 v[148:151], v[4:11], v[176:183], v[148:151], v189, v190 op_sel_hi:[0,0,0]
	v_mfma_scale_f32_16x16x128_f8f6f4 v[136:139], v[12:19], v[206:213], v[136:139], v189, v190 op_sel_hi:[0,0,0]
	v_mfma_scale_f32_16x16x128_f8f6f4 v[132:135], v[4:11], v[206:213], v[132:135], v189, v190 op_sel_hi:[0,0,0]
	v_mfma_scale_f32_16x16x128_f8f6f4 v[120:123], v[12:19], v[214:221], v[120:123], v189, v190 op_sel_hi:[0,0,0]
	v_mfma_scale_f32_16x16x128_f8f6f4 v[116:119], v[4:11], v[214:221], v[116:119], v189, v190 op_sel_hi:[0,0,0]
	v_mfma_scale_f32_16x16x128_f8f6f4 v[104:107], v[12:19], v[222:229], v[104:107], v189, v190 op_sel_hi:[0,0,0]
	v_mfma_scale_f32_16x16x128_f8f6f4 v[100:103], v[4:11], v[222:229], v[100:103], v189, v190 op_sel_hi:[0,0,0]
	s_setprio 0
	s_barrier
	ds_read_b128 v[176:179], v242 offset:49152
	ds_read_b128 v[180:183], v243 offset:49152
	ds_read_b128 v[206:209], v242 offset:51200
	ds_read_b128 v[210:213], v243 offset:51200
	ds_read_b128 v[214:217], v242 offset:53248
	ds_read_b128 v[218:221], v243 offset:53248
	ds_read_b128 v[222:225], v242 offset:55296
	ds_read_b128 v[226:229], v243 offset:55296
	s_add_u32 s24, s22, 0x80
	s_addc_u32 s25, s23, 0
	s_mov_b32 m0, s41
	s_nop 0
	global_load_lds_dwordx4 v240, s[24:25]
	s_add_u32 s22, s22, 0x40080
	s_mov_b32 m0, s42
	s_nop 0
	global_load_lds_dwordx4 v241, s[24:25]
	s_addc_u32 s23, s23, 0
	s_mov_b32 m0, s45
	s_nop 0
	global_load_lds_dwordx4 v240, s[22:23]
	s_nop 0
	s_mov_b32 m0, s46
	s_nop 0
	global_load_lds_dwordx4 v241, s[22:23]
	s_mov_b32 m0, s43
	s_nop 0
	global_load_lds_dwordx4 v238, s[20:21]
	s_nop 0
	s_mov_b32 m0, s44
	s_nop 0
	global_load_lds_dwordx4 v239, s[20:21]
	s_waitcnt vmcnt(8)
	s_waitcnt lgkmcnt(0)
	s_barrier
	s_setprio 1
	s_waitcnt lgkmcnt(6)
	v_mfma_scale_f32_16x16x128_f8f6f4 v[96:99], v[20:27], v[176:183], v[96:99], v189, v190 op_sel_hi:[0,0,0]
	v_mfma_scale_f32_16x16x128_f8f6f4 v[92:95], v[28:35], v[176:183], v[92:95], v189, v190 op_sel_hi:[0,0,0]
	s_waitcnt lgkmcnt(4)
	v_mfma_scale_f32_16x16x128_f8f6f4 v[80:83], v[20:27], v[206:213], v[80:83], v189, v190 op_sel_hi:[0,0,0]
	v_mfma_scale_f32_16x16x128_f8f6f4 v[76:79], v[28:35], v[206:213], v[76:79], v189, v190 op_sel_hi:[0,0,0]
	s_waitcnt lgkmcnt(2)
	v_mfma_scale_f32_16x16x128_f8f6f4 v[64:67], v[20:27], v[214:221], v[64:67], v189, v190 op_sel_hi:[0,0,0]
	v_mfma_scale_f32_16x16x128_f8f6f4 v[60:63], v[28:35], v[214:221], v[60:63], v189, v190 op_sel_hi:[0,0,0]
	s_waitcnt lgkmcnt(0)
	v_mfma_scale_f32_16x16x128_f8f6f4 v[48:51], v[20:27], v[222:229], v[48:51], v189, v190 op_sel_hi:[0,0,0]
	v_mfma_scale_f32_16x16x128_f8f6f4 v[44:47], v[28:35], v[222:229], v[44:47], v189, v190 op_sel_hi:[0,0,0]
	s_setprio 0
	s_setprio 1
	v_mfma_scale_f32_16x16x128_f8f6f4 v[88:91], v[12:19], v[176:183], v[88:91], v189, v190 op_sel_hi:[0,0,0]
	v_mfma_scale_f32_16x16x128_f8f6f4 v[84:87], v[4:11], v[176:183], v[84:87], v189, v190 op_sel_hi:[0,0,0]
	v_mfma_scale_f32_16x16x128_f8f6f4 v[72:75], v[12:19], v[206:213], v[72:75], v189, v190 op_sel_hi:[0,0,0]
	v_mfma_scale_f32_16x16x128_f8f6f4 v[68:71], v[4:11], v[206:213], v[68:71], v189, v190 op_sel_hi:[0,0,0]
	v_mfma_scale_f32_16x16x128_f8f6f4 v[56:59], v[12:19], v[214:221], v[56:59], v189, v190 op_sel_hi:[0,0,0]
	v_mfma_scale_f32_16x16x128_f8f6f4 v[52:55], v[4:11], v[214:221], v[52:55], v189, v190 op_sel_hi:[0,0,0]
	v_mfma_scale_f32_16x16x128_f8f6f4 v[40:43], v[12:19], v[222:229], v[40:43], v189, v190 op_sel_hi:[0,0,0]
	v_mfma_scale_f32_16x16x128_f8f6f4 v[36:39], v[4:11], v[222:229], v[36:39], v189, v190 op_sel_hi:[0,0,0]
	s_setprio 0
	s_barrier
	s_add_i32 s52, s52, 2
	s_add_u32 s11, s11, 0x100
	s_addc_u32 s13, s13, 0
	s_add_u32 s18, s18, 0x100
	s_addc_u32 s19, s19, 0
	s_cmp_gt_u32 s52, 13
	s_cbranch_scc0 .LBB0_2586
	s_and_b64 vcc, exec, s[8:9]
	s_cbranch_vccz .LBB0_2589
	s_barrier

; __device__ __forceinline__ int lane_id() { int l_; asm volatile("v_mbcnt_lo_u32_b32 %0, -1, 0\n\tv_mbcnt_hi_u32_b32 %0, -1, %0" : "=v"(l_)); return l_; }
; #define PG8_STAGE(bufoff, gbase, voff) do { _Pragma("unroll") for (int _i = 0; _i < 2; ++_i) \
;         glds16((const void*)(gbase), (voff)[_i], ldsbase + (unsigned)(bufoff) + ldsw + (unsigned)_i * 8192u); } while (0)
;     ...
;     int tid = w0_ * 64 + lane_id(); asm volatile("" : "+v"(tid));
;     const int wid = __builtin_amdgcn_readfirstlane(tid >> 6), lane = tid & 63, wr = wid >> 2, wc = wid & 3, fr = lane & 15, fq = lane >> 4;
;     const int nt = nt_ ? nt_ : Kb / 128;
;     unsigned voffA[2], voffB[2];
; #pragma unroll
;     for (int i = 0; i < 2; ++i) { int R, C; stage_rc(tid * 16 + i * 8192, R, C); const int Rb = Epi::PERM ? ((R & ~31) + perm32(R & 31)) : R;
;         voffA[i] = (unsigned)(R * ldab + C * 2); voffB[i] = (unsigned)(Rb * Kb + C * 2); }
;     const size_t kstep = (size_t)(BK * 2);
;     const size_t hstepA = (size_t)HALF * ldab, hstepB = (size_t)HALF * Kb;
;     const unsigned ldsw = (unsigned)wid * 1024u, ldsbase = (unsigned)(size_t)lds;
;     const int aoff = lds_byte(wr * 64 + fr, fq * 8), boff = lds_byte(wc * 32 + fr, fq * 8);
;     ...
;     Unit cur, nxt; int ui = 0;
;     if (!S.next(0, cur)) return;
;     f32x4 acc[2][2][4][2];
; #pragma unroll
;     for (int a = 0; a < 2; ++a)
; #pragma unroll
;         for (int b = 0; b < 2; ++b)
; #pragma unroll
;             for (int m = 0; m < 4; ++m)
; #pragma unroll
;                 for (int n = 0; n < 2; ++n) acc[a][b][m][n] = (f32x4){0.f, 0.f, 0.f, 0.f};
;     bf16x8 At[4][2], B0[2][2], B1[2][2];
;     const char* cA = uniform_ptr(cur.a); const char* cB = uniform_ptr(cur.b);
;     PG8_STAGE(PG8_SB(0, 0), cB, voffB); PG8_STAGE(PG8_SB(0, 1), cB + hstepB, voffB); PG8_STAGE(PG8_SA(0, 0), cA, voffA); PG8_STAGE(PG8_SA(0, 1), cA + hstepA, voffA);
;     if (wr == 1) PG8_BAR;
;     PG8_WAIT_V(2); PG8_BAR;
;     PG8_STAGE(PG8_SB(1, 0), cB + kstep, voffB); PG8_STAGE(PG8_SA(1, 0), cA + kstep, voffA); PG8_STAGE(PG8_SB(1, 1), cB + hstepB + kstep, voffB);
;     PG8_WAIT_V(6); PG8_BAR;
; __global__ void __launch_bounds__(512, 2) fwd(Args args) {
;     ...
;             else { pg8::EpiResBf16<false, true> E{(const void*)args.out, (bf16_t*)(ws + WS_XA), D, (float*)nullptr};
;                    pg8::gemm_phase<true>(lds, 2048, 4096, S, E, w0, 123, 121); }
.LBB0_2597:
	s_and_b64 vcc, exec, s[2:3]
	s_cbranch_vccnz .LBB0_2633
	v_bfe_i32 v4, v0, 27, 1
	v_lshlrev_b32_e32 v1, 4, v0
	v_lshrrev_b32_e32 v4, 22, v4
	v_add_u32_e32 v4, v1, v4
	v_and_b32_e32 v4, 0xfffffc00, v4
	v_sub_u32_e32 v4, v1, v4
	v_ashrrev_i32_e32 v2, 31, v0
	v_lshrrev_b32_e32 v5, 4, v4
	v_lshrrev_b32_e32 v2, 26, v2
	v_bitop3_b32 v4, v5, v4, 32 bitop3:0x6c
	v_add_u32_e32 v2, v0, v2
	v_ashrrev_i32_e32 v6, 31, v4
	v_ashrrev_i32_e32 v2, 6, v2
	v_lshrrev_b32_e32 v6, 26, v6
	v_lshlrev_b32_e32 v5, 3, v2
	v_add_u32_e32 v6, v4, v6
	v_and_b32_e32 v5, -16, v5
	v_ashrrev_i32_e32 v7, 6, v6
	v_and_b32_e32 v6, 0xc0, v6
	v_add_u32_e32 v5, v7, v5
	v_sub_u32_e32 v4, v4, v6
	v_lshlrev_b32_e32 v2, 5, v2
	v_ashrrev_i16_sdwa v4, v188, sext(v4) dst_sel:DWORD dst_unused:UNUSED_PAD src0_sel:DWORD src1_sel:BYTE_0
	v_lshlrev_b32_e32 v6, 1, v5
	v_lshrrev_b32_e32 v8, 2, v5
	v_and_b32_e32 v7, 3, v7
	s_mov_b32 s3, 0x1fffe0
	v_and_b32_e32 v2, 32, v2
	v_bfe_i32 v4, v4, 0, 16
	v_and_b32_e32 v6, 24, v6
	v_and_b32_e32 v8, 4, v8
	v_and_or_b32 v7, v5, s3, v7
	v_or3_b32 v6, v7, v8, v6
	v_add_lshl_u32 v4, v2, v4, 1
	v_add_u32_e32 v1, 0x2000, v1
	v_lshl_add_u32 v2, v5, 12, v4
	v_lshl_add_u32 v164, v6, 11, v4
	v_ashrrev_i32_e32 v4, 31, v1
	v_lshrrev_b32_e32 v4, 22, v4
	v_add_u32_e32 v4, v1, v4
	v_ashrrev_i32_e32 v4, 10, v4
	v_mul_i32_i24_e32 v5, 0x400, v4
	v_sub_u32_e32 v1, v1, v5
	v_lshrrev_b32_e32 v5, 4, v1
	v_bitop3_b32 v1, v5, v1, 32 bitop3:0x6c
	v_ashrrev_i32_e32 v6, 31, v1
	v_lshrrev_b32_e32 v6, 26, v6
	v_lshlrev_b32_e32 v5, 3, v4
	v_add_u32_e32 v6, v1, v6
	v_and_b32_e32 v5, -16, v5
	v_ashrrev_i32_e32 v7, 6, v6
	v_and_b32_e32 v6, 0xc0, v6
	s_ashr_i32 s2, s4, 6
	v_add_u32_e32 v5, v7, v5
	v_sub_u32_e32 v1, v1, v6
	v_lshlrev_b32_e32 v4, 5, v4
	v_ashrrev_i16_sdwa v1, v188, sext(v1) dst_sel:DWORD dst_unused:UNUSED_PAD src0_sel:DWORD src1_sel:BYTE_0
	v_lshlrev_b32_e32 v6, 1, v5
	v_lshrrev_b32_e32 v8, 2, v5
	v_and_b32_e32 v7, 3, v7
	s_lshl_b32 s5, s2, 10
	v_and_b32_e32 v4, 32, v4
	v_bfe_i32 v1, v1, 0, 16
	v_and_b32_e32 v6, 24, v6
	v_and_b32_e32 v8, 4, v8
	v_and_or_b32 v7, v5, s3, v7
	s_add_i32 s36, s5, 0
	v_or3_b32 v6, v7, v8, v6
	v_add_lshl_u32 v1, v4, v1, 1
	s_ashr_i32 s3, s4, 8
	s_add_i32 s37, s36, 0x10000
	s_nop 0
	v_readlane_b32 s70, v250, 60
	v_mbcnt_lo_u32_b32 v246, -1, 0
	v_mbcnt_hi_u32_b32 v246, -1, v246
	v_add_u32_e32 v246, s70, v246
	v_bfe_u32 v247, v246, 4, 2
	v_bfe_u32 v248, v246, 6, 1
	v_lshl_or_b32 v247, v248, 2, v247
	v_and_b32_e32 v248, 7, v246
	v_xor_b32_e32 v247, v247, v248
	v_lshlrev_b32_e32 v247, 4, v247
	v_lshrrev_b32_e32 v248, 3, v246
	v_lshl_add_u32 v238, v248, 12, v247
	v_add_u32_e32 v239, 0x40000, v238
	v_and_b32_e32 v249, 0x23, v248
	v_and_b32_e32 v244, 12, v248
	v_lshl_or_b32 v249, v244, 1, v249
	v_bfe_u32 v244, v248, 4, 1
	v_lshl_or_b32 v249, v244, 2, v249
	v_lshl_add_u32 v240, v249, 11, v247
	v_add_u32_e32 v241, 0x20000, v240
	v_bfe_u32 v247, v246, 4, 2
	v_bfe_u32 v248, v246, 1, 3
	v_xor_b32_e32 v247, v247, v248
	v_lshlrev_b32_e32 v247, 4, v247
	v_and_b32_e32 v248, 7, v246
	v_lshl_or_b32 v247, v248, 7, v247
	v_bfe_u32 v248, v246, 3, 1
	v_lshl_or_b32 v247, v248, 10, v247
	v_bfe_u32 v248, v246, 8, 1
	v_lshl_or_b32 v242, v248, 13, v247
	v_xor_b32_e32 v243, 64, v242
	v_bfe_u32 v248, v246, 6, 2
	v_lshl_or_b32 v244, v248, 12, v247
	v_xor_b32_e32 v245, 64, v244
	s_mov_b32 m0, s37
	s_nop 0
	global_load_lds_dwordx4 v240, s[24:25]
	s_add_i32 s38, s36, 0x12000
	v_lshl_add_u32 v166, v6, 11, v1
	s_mov_b32 m0, s38
	s_nop 0
	global_load_lds_dwordx4 v241, s[24:25]
	s_add_u32 s8, s24, 0x40000
	s_addc_u32 s9, s25, 0
	s_add_i32 s39, s36, 0x14000
	s_mov_b32 m0, s39
	s_nop 0
	global_load_lds_dwordx4 v240, s[8:9]
	s_add_i32 s40, s36, 0x16000
	s_mov_b32 m0, s40
	s_nop 0
	global_load_lds_dwordx4 v241, s[8:9]
	s_add_i32 s41, s36, 0x2000
	s_mov_b32 m0, s36
	s_nop 0
	global_load_lds_dwordx4 v238, s[22:23]
	v_lshl_add_u32 v165, v5, 12, v1
	s_mov_b32 m0, s41
	s_nop 0
	global_load_lds_dwordx4 v239, s[22:23]
	s_add_u32 s8, s22, 0x80000
	s_addc_u32 s9, s23, 0
	s_add_i32 s42, s36, 0x4000
	s_mov_b32 m0, s42
	s_nop 0
	global_load_lds_dwordx4 v238, s[8:9]
	s_add_i32 s43, s36, 0x6000
	s_mov_b32 m0, s43
	s_nop 0
	global_load_lds_dwordx4 v239, s[8:9]
	s_cmp_eq_u32 s3, 1
	s_cselect_b64 s[8:9], -1, 0
	s_cmp_lg_u32 s3, 1
	s_cbranch_scc1 .LBB0_2600
	s_barrier
.LBB0_2600:
	v_bfe_u32 v4, v0, 4, 2
	s_add_u32 s10, s0, 0x32682000
	v_and_b32_e32 v1, 15, v0
	v_lshlrev_b32_e32 v6, 4, v4
	v_lshlrev_b32_e32 v0, 2, v0
	s_addc_u32 s11, s26, 0
	s_and_b32 s44, s2, 3
	v_lshl_or_b32 v167, s3, 6, v1
	v_lshl_or_b32 v1, v1, 6, v6
	s_lshl_b32 s0, s3, 13
	v_and_b32_e32 v0, 32, v0
	v_bitop3_b32 v6, v1, s0, v0 bitop3:0xde
	s_lshl_b32 s0, s44, 12
	s_add_u32 s2, s24, 0x80
	v_bitop3_b32 v0, v1, s0, v0 bitop3:0xde
	s_waitcnt vmcnt(2)
	s_barrier
	s_addc_u32 s3, s25, 0
	s_add_i32 s45, s36, 0x18000
	s_mov_b32 m0, s45
	s_nop 0
	global_load_lds_dwordx4 v240, s[2:3]
	s_add_i32 s46, s36, 0x1a000
	s_mov_b32 m0, s46
	s_nop 0
	global_load_lds_dwordx4 v241, s[2:3]
	s_add_u32 s2, s22, 0x80
	s_addc_u32 s3, s23, 0
	s_add_i32 s47, s36, 0x8000
	s_mov_b32 m0, s47
	s_nop 0
	global_load_lds_dwordx4 v238, s[2:3]
	s_add_i32 s48, s36, 0xa000
	s_mov_b32 m0, s48
	s_nop 0
	global_load_lds_dwordx4 v239, s[2:3]
	s_add_u32 s2, s24, 0x40080
	s_addc_u32 s3, s25, 0
	s_add_i32 s49, s36, 0x1c000
	s_mov_b32 m0, s49
	s_nop 0
	global_load_lds_dwordx4 v240, s[2:3]
	s_add_i32 s50, s36, 0x1e000
	s_mov_b32 m0, s50
	s_nop 0
	global_load_lds_dwordx4 v241, s[2:3]
	s_waitcnt vmcnt(6)
	s_add_i32 s51, s36, 0xc000
	v_lshlrev_b32_e32 v5, 3, v4
	s_cmpk_lt_u32 s4, 0x100
	v_lshl_or_b32 v168, s44, 5, v5
	s_cselect_b64 s[12:13], -1, 0
	s_mov_b32 s52, 0
	v_cmp_eq_u32_e64 s[2:3], 0, v4
	s_add_i32 s53, s36, 0xe000
	v_add_u32_e32 v169, 0, v0
	v_add_u32_e32 v170, 0, v6
	s_mov_b64 s[18:19], s[22:23]
	s_mov_b64 s[20:21], s[24:25]
	s_barrier
	s_branch .LBB0_2603

; #define PG8_STAGE(bufoff, gbase, voff) do { _Pragma("unroll") for (int _i = 0; _i < 2; ++_i) \
;         glds16((const void*)(gbase), (voff)[_i], ldsbase + (unsigned)(bufoff) + ldsw + (unsigned)_i * 8192u); } while (0)
; #define PG8_LDA(dst, b, h) do { _Pragma("unroll") for (int m = 0; m < 4; ++m) _Pragma("unroll") for (int k = 0; k < 2; ++k) dst[m][k] = *(const LAS bf16x8*)(lds + PG8_SA(b, h) + aoff + m * 2048 + k * 1024); } while (0)
; #define PG8_LDB(dst, b, h) do { _Pragma("unroll") for (int n = 0; n < 2; ++n) _Pragma("unroll") for (int k = 0; k < 2; ++k) dst[n][k] = *(const LAS bf16x8*)(lds + PG8_SB(b, h) + boff + n * 2048 + k * 1024); } while (0)
; #define PG8_WAIT_V(n) asm volatile("s_waitcnt vmcnt(" #n ")" ::: "memory")
; #define PG8_WAIT_L(n) asm volatile("s_waitcnt lgkmcnt(" #n ")" ::: "memory")
; #define PG8_BAR __builtin_amdgcn_s_barrier()
; #define PG8_SCHED __builtin_amdgcn_sched_barrier(0)
;     ...
;         for (int t = 0; t < nt; t += 2) {
;             const bool last = (t == nt - 2);
;             const char* a1 = cA + (size_t)(t + 1) * kstep;
;             const char* a2 = last ? nA : cA + (size_t)(t + 2) * kstep; const char* b2 = last ? nB : cB + (size_t)(t + 2) * kstep;
;             const char* a3 = a2 + kstep; const char* b3 = b2 + kstep;
;             PG8_LDB(B0, 0, 0); PG8_LDB(B1, 0, 1); PG8_SCHED; PG8_LDA(At, 0, 0); PG8_STAGE(PG8_SA(1, 1), a1 + hstepA, voffA);
;             PG8_WAIT_V(8); PG8_WAIT_L(0); PG8_BAR; PG8_MMA(0, 0, At, B0); PG8_MMA(0, 1, At, B1); PG8_BAR; PG8_SCHED;
;             PG8_LDA(At, 0, 1); PG8_STAGE(PG8_SB(0, 0), b2, voffB); PG8_STAGE(PG8_SB(0, 1), b2 + hstepB, voffB); PG8_STAGE(PG8_SA(0, 0), a2, voffA);
;             PG8_WAIT_V(8); PG8_WAIT_L(0); PG8_BAR; PG8_MMA(1, 0, At, B0); PG8_MMA(1, 1, At, B1); PG8_BAR; PG8_SCHED;
;             PG8_LDB(B0, 1, 0); PG8_LDB(B1, 1, 1); PG8_SCHED; PG8_LDA(At, 1, 0); PG8_STAGE(PG8_SA(0, 1), a2 + hstepA, voffA);
;             PG8_WAIT_V(8); PG8_WAIT_L(0); PG8_BAR; PG8_MMA(0, 0, At, B0); PG8_MMA(0, 1, At, B1); PG8_BAR; PG8_SCHED;
;             PG8_LDA(At, 1, 1); PG8_STAGE(PG8_SB(1, 0), b3, voffB); PG8_STAGE(PG8_SB(1, 1), b3 + hstepB, voffB); PG8_STAGE(PG8_SA(1, 0), a3, voffA);
;             PG8_WAIT_V(8); PG8_WAIT_L(0); PG8_BAR; PG8_MMA(1, 0, At, B0); PG8_MMA(1, 1, At, B1); PG8_BAR; PG8_SCHED;
;         }
.LBB0_2610:
	v_add_u32_e32 v0, 0x10000, v244
	v_add_u32_e32 v246, 0x10000, v245
	ds_read_b128 v[28:31], v0
	ds_read_b128 v[32:35], v246
	ds_read_b128 v[20:23], v0 offset:2048
	ds_read_b128 v[24:27], v246 offset:2048
	v_add_u32_e32 v0, 0x14000, v244
	v_add_u32_e32 v246, 0x14000, v245
	s_waitcnt lgkmcnt(4)
	ds_read_b128 v[12:15], v0
	ds_read_b128 v[16:19], v246
	ds_read_b128 v[4:7], v0 offset:2048
	ds_read_b128 v[8:11], v246 offset:2048
	s_add_u32 s24, s22, 0xfff80080
	s_addc_u32 s25, s23, -1
	s_cmp_eq_u32 s17, 12
	s_cselect_b32 s28, s18, s24
	s_cselect_b32 s29, s19, s25
	s_cselect_b32 s26, s20, s0
	s_cselect_b32 s27, s21, s15
	s_add_u32 s24, s28, 0x80
	s_addc_u32 s25, s29, 0
	ds_read_b128 v[176:179], v242
	ds_read_b128 v[180:183], v243
	ds_read_b128 v[206:209], v242 offset:2048
	ds_read_b128 v[210:213], v243 offset:2048
	ds_read_b128 v[214:217], v242 offset:4096
	ds_read_b128 v[218:221], v243 offset:4096
	ds_read_b128 v[222:225], v242 offset:6144
	ds_read_b128 v[226:229], v243 offset:6144
	s_mov_b32 m0, s51
	s_nop 0
	global_load_lds_dwordx4 v238, s[22:23]
	s_nop 0
	s_mov_b32 m0, s53
	s_nop 0
	global_load_lds_dwordx4 v239, s[22:23]
	s_waitcnt vmcnt(8)
	s_waitcnt lgkmcnt(0)
	s_barrier
	s_setprio 1
	s_waitcnt lgkmcnt(6)
	v_mfma_scale_f32_16x16x128_f8f6f4 v[160:163], v[28:35], v[176:183], v[160:163], v189, v190 op_sel_hi:[0,0,0]
	v_mfma_scale_f32_16x16x128_f8f6f4 v[156:159], v[20:27], v[176:183], v[156:159], v189, v190 op_sel_hi:[0,0,0]
	s_waitcnt lgkmcnt(4)
	v_mfma_scale_f32_16x16x128_f8f6f4 v[144:147], v[28:35], v[206:213], v[144:147], v189, v190 op_sel_hi:[0,0,0]
	v_mfma_scale_f32_16x16x128_f8f6f4 v[140:143], v[20:27], v[206:213], v[140:143], v189, v190 op_sel_hi:[0,0,0]
	s_waitcnt lgkmcnt(2)
	v_mfma_scale_f32_16x16x128_f8f6f4 v[128:131], v[28:35], v[214:221], v[128:131], v189, v190 op_sel_hi:[0,0,0]
	v_mfma_scale_f32_16x16x128_f8f6f4 v[124:127], v[20:27], v[214:221], v[124:127], v189, v190 op_sel_hi:[0,0,0]
	s_waitcnt lgkmcnt(0)
	v_mfma_scale_f32_16x16x128_f8f6f4 v[112:115], v[28:35], v[222:229], v[112:115], v189, v190 op_sel_hi:[0,0,0]
	v_mfma_scale_f32_16x16x128_f8f6f4 v[108:111], v[20:27], v[222:229], v[108:111], v189, v190 op_sel_hi:[0,0,0]
	s_setprio 0
	s_setprio 1
	v_mfma_scale_f32_16x16x128_f8f6f4 v[152:155], v[12:19], v[176:183], v[152:155], v189, v190 op_sel_hi:[0,0,0]
	v_mfma_scale_f32_16x16x128_f8f6f4 v[148:151], v[4:11], v[176:183], v[148:151], v189, v190 op_sel_hi:[0,0,0]
	v_mfma_scale_f32_16x16x128_f8f6f4 v[136:139], v[12:19], v[206:213], v[136:139], v189, v190 op_sel_hi:[0,0,0]
	v_mfma_scale_f32_16x16x128_f8f6f4 v[132:135], v[4:11], v[206:213], v[132:135], v189, v190 op_sel_hi:[0,0,0]
	v_mfma_scale_f32_16x16x128_f8f6f4 v[120:123], v[12:19], v[214:221], v[120:123], v189, v190 op_sel_hi:[0,0,0]
	v_mfma_scale_f32_16x16x128_f8f6f4 v[116:119], v[4:11], v[214:221], v[116:119], v189, v190 op_sel_hi:[0,0,0]
	v_mfma_scale_f32_16x16x128_f8f6f4 v[104:107], v[12:19], v[222:229], v[104:107], v189, v190 op_sel_hi:[0,0,0]
	v_mfma_scale_f32_16x16x128_f8f6f4 v[100:103], v[4:11], v[222:229], v[100:103], v189, v190 op_sel_hi:[0,0,0]
	s_setprio 0
	s_barrier
	ds_read_b128 v[176:179], v242 offset:16384
	ds_read_b128 v[180:183], v243 offset:16384
	ds_read_b128 v[206:209], v242 offset:18432
	ds_read_b128 v[210:213], v243 offset:18432
	ds_read_b128 v[214:217], v242 offset:20480
	ds_read_b128 v[218:221], v243 offset:20480
	ds_read_b128 v[222:225], v242 offset:22528
	ds_read_b128 v[226:229], v243 offset:22528
	s_mov_b32 m0, s37
	s_nop 0
	global_load_lds_dwordx4 v240, s[26:27]
	s_nop 0
	s_mov_b32 m0, s38
	s_nop 0
	global_load_lds_dwordx4 v241, s[26:27]
	s_add_u32 s56, s26, 0x40000
	s_addc_u32 s57, s27, 0
	s_mov_b32 m0, s39
	s_nop 0
	global_load_lds_dwordx4 v240, s[56:57]
	s_nop 0
	s_mov_b32 m0, s40
	s_nop 0
	global_load_lds_dwordx4 v241, s[56:57]
	s_mov_b32 m0, s36
	s_nop 0
	global_load_lds_dwordx4 v238, s[28:29]
	s_nop 0
	s_mov_b32 m0, s41
	s_nop 0
	global_load_lds_dwordx4 v239, s[28:29]
	s_waitcnt vmcnt(8)
	s_waitcnt lgkmcnt(0)
	s_barrier
	s_setprio 1
	s_waitcnt lgkmcnt(6)
	v_mfma_scale_f32_16x16x128_f8f6f4 v[96:99], v[28:35], v[176:183], v[96:99], v189, v190 op_sel_hi:[0,0,0]
	v_mfma_scale_f32_16x16x128_f8f6f4 v[92:95], v[20:27], v[176:183], v[92:95], v189, v190 op_sel_hi:[0,0,0]
	s_waitcnt lgkmcnt(4)
	v_mfma_scale_f32_16x16x128_f8f6f4 v[80:83], v[28:35], v[206:213], v[80:83], v189, v190 op_sel_hi:[0,0,0]
	v_mfma_scale_f32_16x16x128_f8f6f4 v[76:79], v[20:27], v[206:213], v[76:79], v189, v190 op_sel_hi:[0,0,0]
	s_waitcnt lgkmcnt(2)
	v_mfma_scale_f32_16x16x128_f8f6f4 v[64:67], v[28:35], v[214:221], v[64:67], v189, v190 op_sel_hi:[0,0,0]
	v_mfma_scale_f32_16x16x128_f8f6f4 v[60:63], v[20:27], v[214:221], v[60:63], v189, v190 op_sel_hi:[0,0,0]
	s_waitcnt lgkmcnt(0)
	v_mfma_scale_f32_16x16x128_f8f6f4 v[48:51], v[28:35], v[222:229], v[48:51], v189, v190 op_sel_hi:[0,0,0]
	v_mfma_scale_f32_16x16x128_f8f6f4 v[44:47], v[20:27], v[222:229], v[44:47], v189, v190 op_sel_hi:[0,0,0]
	s_setprio 0
	s_setprio 1
	v_mfma_scale_f32_16x16x128_f8f6f4 v[88:91], v[12:19], v[176:183], v[88:91], v189, v190 op_sel_hi:[0,0,0]
	v_mfma_scale_f32_16x16x128_f8f6f4 v[84:87], v[4:11], v[176:183], v[84:87], v189, v190 op_sel_hi:[0,0,0]
	v_mfma_scale_f32_16x16x128_f8f6f4 v[72:75], v[12:19], v[206:213], v[72:75], v189, v190 op_sel_hi:[0,0,0]
	v_mfma_scale_f32_16x16x128_f8f6f4 v[68:71], v[4:11], v[206:213], v[68:71], v189, v190 op_sel_hi:[0,0,0]
	v_mfma_scale_f32_16x16x128_f8f6f4 v[56:59], v[12:19], v[214:221], v[56:59], v189, v190 op_sel_hi:[0,0,0]
	v_mfma_scale_f32_16x16x128_f8f6f4 v[52:55], v[4:11], v[214:221], v[52:55], v189, v190 op_sel_hi:[0,0,0]
	v_mfma_scale_f32_16x16x128_f8f6f4 v[40:43], v[12:19], v[222:229], v[40:43], v189, v190 op_sel_hi:[0,0,0]
	v_mfma_scale_f32_16x16x128_f8f6f4 v[36:39], v[4:11], v[222:229], v[36:39], v189, v190 op_sel_hi:[0,0,0]
	s_setprio 0
	s_barrier
; #define PG8_STAGE(bufoff, gbase, voff) do { _Pragma("unroll") for (int _i = 0; _i < 2; ++_i) \
;         glds16((const void*)(gbase), (voff)[_i], ldsbase + (unsigned)(bufoff) + ldsw + (unsigned)_i * 8192u); } while (0)
; #define PG8_LDA(dst, b, h) do { _Pragma("unroll") for (int m = 0; m < 4; ++m) _Pragma("unroll") for (int k = 0; k < 2; ++k) dst[m][k] = *(const LAS bf16x8*)(lds + PG8_SA(b, h) + aoff + m * 2048 + k * 1024); } while (0)
; #define PG8_LDB(dst, b, h) do { _Pragma("unroll") for (int n = 0; n < 2; ++n) _Pragma("unroll") for (int k = 0; k < 2; ++k) dst[n][k] = *(const LAS bf16x8*)(lds + PG8_SB(b, h) + boff + n * 2048 + k * 1024); } while (0)
; #define PG8_WAIT_V(n) asm volatile("s_waitcnt vmcnt(" #n ")" ::: "memory")
; #define PG8_WAIT_L(n) asm volatile("s_waitcnt lgkmcnt(" #n ")" ::: "memory")
; #define PG8_BAR __builtin_amdgcn_s_barrier()
; #define PG8_SCHED __builtin_amdgcn_sched_barrier(0)
;     ...
;         for (int t = 0; t < nt; t += 2) {
;             const bool last = (t == nt - 2);
;             const char* a1 = cA + (size_t)(t + 1) * kstep;
;             const char* a2 = last ? nA : cA + (size_t)(t + 2) * kstep; const char* b2 = last ? nB : cB + (size_t)(t + 2) * kstep;
;             const char* a3 = a2 + kstep; const char* b3 = b2 + kstep;
;             PG8_LDB(B0, 0, 0); PG8_LDB(B1, 0, 1); PG8_SCHED; PG8_LDA(At, 0, 0); PG8_STAGE(PG8_SA(1, 1), a1 + hstepA, voffA);
;             PG8_WAIT_V(8); PG8_WAIT_L(0); PG8_BAR; PG8_MMA(0, 0, At, B0); PG8_MMA(0, 1, At, B1); PG8_BAR; PG8_SCHED;
;             PG8_LDA(At, 0, 1); PG8_STAGE(PG8_SB(0, 0), b2, voffB); PG8_STAGE(PG8_SB(0, 1), b2 + hstepB, voffB); PG8_STAGE(PG8_SA(0, 0), a2, voffA);
;             PG8_WAIT_V(8); PG8_WAIT_L(0); PG8_BAR; PG8_MMA(1, 0, At, B0); PG8_MMA(1, 1, At, B1); PG8_BAR; PG8_SCHED;
;             PG8_LDB(B0, 1, 0); PG8_LDB(B1, 1, 1); PG8_SCHED; PG8_LDA(At, 1, 0); PG8_STAGE(PG8_SA(0, 1), a2 + hstepA, voffA);
;             PG8_WAIT_V(8); PG8_WAIT_L(0); PG8_BAR; PG8_MMA(0, 0, At, B0); PG8_MMA(0, 1, At, B1); PG8_BAR; PG8_SCHED;
;             PG8_LDA(At, 1, 1); PG8_STAGE(PG8_SB(1, 0), b3, voffB); PG8_STAGE(PG8_SB(1, 1), b3 + hstepB, voffB); PG8_STAGE(PG8_SA(1, 0), a3, voffA);
;             PG8_WAIT_V(8); PG8_WAIT_L(0); PG8_BAR; PG8_MMA(1, 0, At, B0); PG8_MMA(1, 1, At, B1); PG8_BAR; PG8_SCHED;
;         }
	v_add_u32_e32 v0, 0x18000, v244
	v_add_u32_e32 v246, 0x18000, v245
	ds_read_b128 v[20:23], v0
	ds_read_b128 v[24:27], v246
	ds_read_b128 v[28:31], v0 offset:2048
	ds_read_b128 v[32:35], v246 offset:2048
	v_add_u32_e32 v0, 0x1c000, v244
	v_add_u32_e32 v246, 0x1c000, v245
	ds_read_b128 v[12:15], v0
	ds_read_b128 v[16:19], v246
	ds_read_b128 v[4:7], v0 offset:2048
	ds_read_b128 v[8:11], v246 offset:2048
	ds_read_b128 v[176:179], v242 offset:32768
	ds_read_b128 v[180:183], v243 offset:32768
	ds_read_b128 v[206:209], v242 offset:34816
	ds_read_b128 v[210:213], v243 offset:34816
	ds_read_b128 v[214:217], v242 offset:36864
	ds_read_b128 v[218:221], v243 offset:36864
	ds_read_b128 v[222:225], v242 offset:38912
	ds_read_b128 v[226:229], v243 offset:38912
	s_add_u32 s28, s28, 0x80000
	s_addc_u32 s29, s29, 0
	s_mov_b32 m0, s42
	s_nop 0
	global_load_lds_dwordx4 v238, s[28:29]
	s_nop 0
	s_mov_b32 m0, s43
	s_nop 0
	global_load_lds_dwordx4 v239, s[28:29]
	s_waitcnt vmcnt(8)
	s_waitcnt lgkmcnt(0)
	s_barrier
	s_setprio 1
	s_waitcnt lgkmcnt(6)
	v_mfma_scale_f32_16x16x128_f8f6f4 v[160:163], v[20:27], v[176:183], v[160:163], v189, v190 op_sel_hi:[0,0,0]
	v_mfma_scale_f32_16x16x128_f8f6f4 v[156:159], v[28:35], v[176:183], v[156:159], v189, v190 op_sel_hi:[0,0,0]
	s_waitcnt lgkmcnt(4)
	v_mfma_scale_f32_16x16x128_f8f6f4 v[144:147], v[20:27], v[206:213], v[144:147], v189, v190 op_sel_hi:[0,0,0]
	v_mfma_scale_f32_16x16x128_f8f6f4 v[140:143], v[28:35], v[206:213], v[140:143], v189, v190 op_sel_hi:[0,0,0]
	s_waitcnt lgkmcnt(2)
	v_mfma_scale_f32_16x16x128_f8f6f4 v[128:131], v[20:27], v[214:221], v[128:131], v189, v190 op_sel_hi:[0,0,0]
	v_mfma_scale_f32_16x16x128_f8f6f4 v[124:127], v[28:35], v[214:221], v[124:127], v189, v190 op_sel_hi:[0,0,0]
	s_waitcnt lgkmcnt(0)
	v_mfma_scale_f32_16x16x128_f8f6f4 v[112:115], v[20:27], v[222:229], v[112:115], v189, v190 op_sel_hi:[0,0,0]
	v_mfma_scale_f32_16x16x128_f8f6f4 v[108:111], v[28:35], v[222:229], v[108:111], v189, v190 op_sel_hi:[0,0,0]
	s_setprio 0
	s_setprio 1
	v_mfma_scale_f32_16x16x128_f8f6f4 v[152:155], v[12:19], v[176:183], v[152:155], v189, v190 op_sel_hi:[0,0,0]
	v_mfma_scale_f32_16x16x128_f8f6f4 v[148:151], v[4:11], v[176:183], v[148:151], v189, v190 op_sel_hi:[0,0,0]
	v_mfma_scale_f32_16x16x128_f8f6f4 v[136:139], v[12:19], v[206:213], v[136:139], v189, v190 op_sel_hi:[0,0,0]
	v_mfma_scale_f32_16x16x128_f8f6f4 v[132:135], v[4:11], v[206:213], v[132:135], v189, v190 op_sel_hi:[0,0,0]
	v_mfma_scale_f32_16x16x128_f8f6f4 v[120:123], v[12:19], v[214:221], v[120:123], v189, v190 op_sel_hi:[0,0,0]
	v_mfma_scale_f32_16x16x128_f8f6f4 v[116:119], v[4:11], v[214:221], v[116:119], v189, v190 op_sel_hi:[0,0,0]
	v_mfma_scale_f32_16x16x128_f8f6f4 v[104:107], v[12:19], v[222:229], v[104:107], v189, v190 op_sel_hi:[0,0,0]
	v_mfma_scale_f32_16x16x128_f8f6f4 v[100:103], v[4:11], v[222:229], v[100:103], v189, v190 op_sel_hi:[0,0,0]
	s_setprio 0
	s_barrier
	ds_read_b128 v[176:179], v242 offset:49152
	ds_read_b128 v[180:183], v243 offset:49152
	ds_read_b128 v[206:209], v242 offset:51200
	ds_read_b128 v[210:213], v243 offset:51200
	ds_read_b128 v[214:217], v242 offset:53248
	ds_read_b128 v[218:221], v243 offset:53248
	ds_read_b128 v[222:225], v242 offset:55296
	ds_read_b128 v[226:229], v243 offset:55296
	s_add_u32 s28, s26, 0x80
	s_addc_u32 s29, s27, 0
	s_mov_b32 m0, s45
	s_nop 0
	global_load_lds_dwordx4 v240, s[28:29]
	s_add_u32 s26, s26, 0x40080
	s_mov_b32 m0, s46
	s_nop 0
	global_load_lds_dwordx4 v241, s[28:29]
	s_addc_u32 s27, s27, 0
	s_mov_b32 m0, s49
	s_nop 0
	global_load_lds_dwordx4 v240, s[26:27]
	s_nop 0
	s_mov_b32 m0, s50
	s_nop 0
	global_load_lds_dwordx4 v241, s[26:27]
	s_mov_b32 m0, s47
	s_nop 0
	global_load_lds_dwordx4 v238, s[24:25]
	s_nop 0
	s_mov_b32 m0, s48
	s_nop 0
	global_load_lds_dwordx4 v239, s[24:25]
	s_waitcnt vmcnt(8)
	s_waitcnt lgkmcnt(0)
	s_barrier
	s_setprio 1
	s_waitcnt lgkmcnt(6)
	v_mfma_scale_f32_16x16x128_f8f6f4 v[96:99], v[20:27], v[176:183], v[96:99], v189, v190 op_sel_hi:[0,0,0]
	v_mfma_scale_f32_16x16x128_f8f6f4 v[92:95], v[28:35], v[176:183], v[92:95], v189, v190 op_sel_hi:[0,0,0]
	s_waitcnt lgkmcnt(4)
	v_mfma_scale_f32_16x16x128_f8f6f4 v[80:83], v[20:27], v[206:213], v[80:83], v189, v190 op_sel_hi:[0,0,0]
	v_mfma_scale_f32_16x16x128_f8f6f4 v[76:79], v[28:35], v[206:213], v[76:79], v189, v190 op_sel_hi:[0,0,0]
	s_waitcnt lgkmcnt(2)
	v_mfma_scale_f32_16x16x128_f8f6f4 v[64:67], v[20:27], v[214:221], v[64:67], v189, v190 op_sel_hi:[0,0,0]
	v_mfma_scale_f32_16x16x128_f8f6f4 v[60:63], v[28:35], v[214:221], v[60:63], v189, v190 op_sel_hi:[0,0,0]
	s_waitcnt lgkmcnt(0)
	v_mfma_scale_f32_16x16x128_f8f6f4 v[48:51], v[20:27], v[222:229], v[48:51], v189, v190 op_sel_hi:[0,0,0]
	v_mfma_scale_f32_16x16x128_f8f6f4 v[44:47], v[28:35], v[222:229], v[44:47], v189, v190 op_sel_hi:[0,0,0]
	s_setprio 0
	s_setprio 1
	v_mfma_scale_f32_16x16x128_f8f6f4 v[88:91], v[12:19], v[176:183], v[88:91], v189, v190 op_sel_hi:[0,0,0]
	v_mfma_scale_f32_16x16x128_f8f6f4 v[84:87], v[4:11], v[176:183], v[84:87], v189, v190 op_sel_hi:[0,0,0]
	v_mfma_scale_f32_16x16x128_f8f6f4 v[72:75], v[12:19], v[206:213], v[72:75], v189, v190 op_sel_hi:[0,0,0]
	v_mfma_scale_f32_16x16x128_f8f6f4 v[68:71], v[4:11], v[206:213], v[68:71], v189, v190 op_sel_hi:[0,0,0]
	v_mfma_scale_f32_16x16x128_f8f6f4 v[56:59], v[12:19], v[214:221], v[56:59], v189, v190 op_sel_hi:[0,0,0]
	v_mfma_scale_f32_16x16x128_f8f6f4 v[52:55], v[4:11], v[214:221], v[52:55], v189, v190 op_sel_hi:[0,0,0]
	v_mfma_scale_f32_16x16x128_f8f6f4 v[40:43], v[12:19], v[222:229], v[40:43], v189, v190 op_sel_hi:[0,0,0]
	v_mfma_scale_f32_16x16x128_f8f6f4 v[36:39], v[4:11], v[222:229], v[36:39], v189, v190 op_sel_hi:[0,0,0]
	s_setprio 0
	s_barrier
	s_add_i32 s17, s17, 2
	s_add_u32 s0, s0, 0x100
	s_addc_u32 s15, s15, 0
	s_add_u32 s22, s22, 0x100
	s_addc_u32 s23, s23, 0
	s_cmp_gt_u32 s17, 13
	s_cbranch_scc0 .LBB0_2610
	s_and_b64 vcc, exec, s[12:13]
	s_cbranch_vccz .LBB0_2613
	s_barrier

; __device__ __forceinline__ int lane_id() { int l_; asm volatile("v_mbcnt_lo_u32_b32 %0, -1, 0\n\tv_mbcnt_hi_u32_b32 %0, -1, %0" : "=v"(l_)); return l_; }
;     __device__ __forceinline__ bool idx(int i, int& pm, int& pn) const {
;         const long L = (long)i * G + c; if (L >= nwg) return false;
;         int wgid = (int)L; { const int q = nwg / 8, r = nwg % 8, xcd = wgid % 8, off = wgid / 8; wgid = (xcd < r ? xcd * (q + 1) : r * (q + 1) + (xcd - r) * q) + off; }
;         const int nig = 8 * nN, gid = wgid / nig, fm = gid * 8, gsz = (nM - fm) < 8 ? (nM - fm) : 8;
;         pm = fm + ((wgid % nig) % gsz); pn = (wgid % nig) / gsz; return true;
;     ...
;     int tid = w0_ * 64 + lane_id(); asm volatile("" : "+v"(tid));
;     const int wid = __builtin_amdgcn_readfirstlane(tid >> 6), lane = tid & 63, wr = wid >> 2, wc = wid & 3, fr = lane & 15, fq = lane >> 4;
;     const int nt = nt_ ? nt_ : Kb / 128;
;     unsigned voffA[2], voffB[2];
; #pragma unroll
;     for (int i = 0; i < 2; ++i) { int R, C; stage_rc(tid * 16 + i * 8192, R, C); const int Rb = Epi::PERM ? ((R & ~31) + perm32(R & 31)) : R;
;         voffA[i] = (unsigned)(R * ldab + C * 2); voffB[i] = (unsigned)(Rb * Kb + C * 2); }
;     const size_t kstep = (size_t)(BK * 2);
;     const size_t hstepA = (size_t)HALF * ldab, hstepB = (size_t)HALF * Kb;
;     const unsigned ldsw = (unsigned)wid * 1024u, ldsbase = (unsigned)(size_t)lds;
;     const int aoff = lds_byte(wr * 64 + fr, fq * 8), boff = lds_byte(wc * 32 + fr, fq * 8);
.LBB0_2837:
	s_or_b64 exec, exec, s[4:5]
	s_waitcnt lgkmcnt(0)
	s_barrier
	v_mbcnt_lo_u32_b32 v0, -1, 0
	v_mbcnt_hi_u32_b32 v0, -1, v0
	v_readlane_b32 s5, v250, 60
	s_mul_i32 s4, s0, 56
	s_cmp_ge_i32 s78, s4
	v_add_u32_e32 v0, s5, v0
	s_nop 0
	v_readfirstlane_b32 s12, v0
	s_cbranch_scc1 .LBB0_2853
	v_bfe_i32 v4, v0, 27, 1
	v_lshlrev_b32_e32 v1, 4, v0
	v_lshrrev_b32_e32 v4, 22, v4
	v_add_u32_e32 v4, v1, v4
	v_and_b32_e32 v4, 0xfffffc00, v4
	v_sub_u32_e32 v4, v1, v4
	v_ashrrev_i32_e32 v2, 31, v0
	v_lshrrev_b32_e32 v5, 4, v4
	v_lshrrev_b32_e32 v2, 26, v2
	v_bitop3_b32 v4, v5, v4, 32 bitop3:0x6c
	v_add_u32_e32 v2, v0, v2
	v_ashrrev_i32_e32 v6, 31, v4
	v_ashrrev_i32_e32 v2, 6, v2
	v_lshrrev_b32_e32 v6, 26, v6
	v_lshlrev_b32_e32 v5, 3, v2
	v_add_u32_e32 v6, v4, v6
	v_and_b32_e32 v5, -16, v5
	v_ashrrev_i32_e32 v7, 6, v6
	v_and_b32_e32 v6, 0xc0, v6
	v_add_u32_e32 v5, v7, v5
	v_sub_u32_e32 v4, v4, v6
	v_lshlrev_b32_e32 v2, 5, v2
	v_ashrrev_i16_sdwa v4, v188, sext(v4) dst_sel:DWORD dst_unused:UNUSED_PAD src0_sel:DWORD src1_sel:BYTE_0
	v_lshlrev_b32_e32 v6, 1, v5
	v_lshrrev_b32_e32 v8, 2, v5
	v_and_b32_e32 v7, 3, v7
	s_mov_b32 s5, 0x1fffe0
	v_and_b32_e32 v2, 32, v2
	v_bfe_i32 v4, v4, 0, 16
	v_and_b32_e32 v6, 24, v6
	v_and_b32_e32 v8, 4, v8
	v_and_or_b32 v7, v5, s5, v7
	v_or3_b32 v6, v7, v8, v6
	v_add_lshl_u32 v2, v2, v4, 1
	v_add_u32_e32 v1, 0x2000, v1
	v_lshl_add_u32 v176, v5, 11, v2
	v_lshl_add_u32 v177, v6, 11, v2
	v_ashrrev_i32_e32 v2, 31, v1
	v_lshrrev_b32_e32 v2, 22, v2
	v_add_u32_e32 v2, v1, v2
	v_ashrrev_i32_e32 v2, 10, v2
	v_mul_i32_i24_e32 v4, 0x400, v2
	v_sub_u32_e32 v1, v1, v4
	v_lshrrev_b32_e32 v4, 4, v1
	v_bitop3_b32 v1, v4, v1, 32 bitop3:0x6c
	v_ashrrev_i32_e32 v5, 31, v1
	s_add_u32 s36, s2, 0x58492000
	v_lshrrev_b32_e32 v5, 26, v5
	s_addc_u32 s37, s3, 0
	v_lshlrev_b32_e32 v4, 3, v2
	v_add_u32_e32 v5, v1, v5
	s_add_u32 s6, s2, 0x8500000
	v_and_b32_e32 v4, -16, v4
	v_ashrrev_i32_e32 v6, 6, v5
	s_addc_u32 s7, s3, 0
	s_mul_i32 s38, s0, 7
	v_add_u32_e32 v4, v6, v4
	v_and_b32_e32 v6, 3, v6
	s_ashr_i32 s11, s12, 6
	v_readlane_b32 s8, v252, 62
	s_add_i32 s39, s38, 1
	s_ashr_i32 s10, s12, 8
	v_and_or_b32 v6, v4, s5, v6
	s_lshl_b32 s5, s11, 10
	v_readlane_b32 s9, v252, 63
	s_and_b64 s[8:9], s[8:9], exec
	s_cselect_b32 s8, s39, s38
	v_readlane_b32 s9, v253, 16
	s_mul_i32 s8, s8, s9
	v_readlane_b32 s9, v253, 17
	s_add_i32 s8, s8, s9
	s_mul_hi_i32 s9, s8, 0x92492493
	s_add_i32 s9, s9, s8
	s_lshr_b32 s13, s9, 31
	s_ashr_i32 s9, s9, 8
	v_and_b32_e32 v5, 0xc0, v5
	s_add_i32 s9, s9, s13
	v_sub_u32_e32 v1, v1, v5
	s_lshl_b32 s13, s9, 3
	v_lshlrev_b32_e32 v2, 5, v2
	v_ashrrev_i16_sdwa v1, v188, sext(v1) dst_sel:DWORD dst_unused:UNUSED_PAD src0_sel:DWORD src1_sel:BYTE_0
	v_lshlrev_b32_e32 v5, 1, v4
	v_lshrrev_b32_e32 v7, 2, v4
	s_sub_i32 s14, s0, s13
	v_and_b32_e32 v2, 32, v2
	v_bfe_i32 v1, v1, 0, 16
	v_and_b32_e32 v5, 24, v5
	v_and_b32_e32 v7, 4, v7
	s_min_i32 s14, s14, 8
	v_or3_b32 v5, v6, v7, v5
	v_add_lshl_u32 v1, v2, v1, 1
	s_abs_i32 s16, s14
	v_lshl_add_u32 v178, v4, 11, v1
	v_lshl_add_u32 v179, v5, 11, v1
	v_cvt_f32_u32_e32 v1, s16
	s_sub_i32 s17, 0, s16
	s_mulk_i32 s9, 0x1c0
	s_sub_i32 s8, s8, s9
	v_rcp_iflag_f32_e32 v1, v1
	s_abs_i32 s15, s8
	s_xor_b32 s9, s8, s14
	s_ashr_i32 s9, s9, 31
	v_mul_f32_e32 v1, 0x4f7ffffe, v1
	v_cvt_u32_f32_e32 v1, v1
	v_mov_b32_e32 v7, s1
	v_readfirstlane_b32 s18, v1
	s_mul_i32 s17, s17, s18
	s_mul_hi_u32 s17, s18, s17
	s_add_i32 s18, s18, s17
	s_mul_hi_u32 s17, s15, s18
	s_mul_i32 s18, s17, s16
	s_sub_i32 s15, s15, s18
	s_add_i32 s18, s17, 1
	s_sub_i32 s19, s15, s16
	s_cmp_ge_u32 s15, s16
	s_cselect_b32 s17, s18, s17
	s_cselect_b32 s15, s19, s15
	s_add_i32 s18, s17, 1
	s_cmp_ge_u32 s15, s16
	s_cselect_b32 s15, s18, s17
	s_xor_b32 s15, s15, s9
	s_sub_i32 s20, s15, s9
	s_mul_i32 s9, s20, s14
	s_sub_i32 s8, s8, s9
	s_add_i32 s22, s13, s8
	v_readlane_b32 s8, v254, 29
	v_readlane_b32 s9, v254, 30
	s_nop 0
	v_mov_b32_e32 v1, s8
	ds_read2_b32 v[4:5], v1 offset1:1
	v_mov_b32_e32 v1, s9
	v_readlane_b32 s9, v254, 31
	s_waitcnt lgkmcnt(0)
	v_readfirstlane_b32 s13, v4
	v_readfirstlane_b32 s8, v5
	ds_read2_b32 v[4:5], v1 offset1:1
	v_mov_b32_e32 v1, s9
	v_readlane_b32 s9, v254, 32
	s_cmp_ge_i32 s22, s8
	s_waitcnt lgkmcnt(0)
	v_readfirstlane_b32 s16, v4
	v_readfirstlane_b32 s17, v5
	ds_read2_b32 v[4:5], v1 offset1:1
	v_mov_b32_e32 v1, s9
	ds_read_b32 v1, v1
	s_cselect_b64 s[8:9], -1, 0
	s_cmp_ge_i32 s22, s13
	s_cselect_b64 s[14:15], -1, 0
	s_cmp_ge_i32 s22, s16
	s_waitcnt lgkmcnt(1)
	v_readfirstlane_b32 s18, v4
	s_cselect_b64 vcc, -1, 0
	s_cmp_ge_i32 s22, s17
	v_readfirstlane_b32 s19, v5
	s_waitcnt lgkmcnt(0)
; #define PG8_STAGE(bufoff, gbase, voff) do { _Pragma("unroll") for (int _i = 0; _i < 2; ++_i) \
;         glds16((const void*)(gbase), (voff)[_i], ldsbase + (unsigned)(bufoff) + ldsw + (unsigned)_i * 8192u); } while (0)
; #define PG8_WAIT_V(n) asm volatile("s_waitcnt vmcnt(" #n ")" ::: "memory")
; #define PG8_BAR __builtin_amdgcn_s_barrier()
;     ...
;     const char* cA = uniform_ptr(cur.a); const char* cB = uniform_ptr(cur.b);
;     PG8_STAGE(PG8_SB(0, 0), cB, voffB); PG8_STAGE(PG8_SB(0, 1), cB + hstepB, voffB); PG8_STAGE(PG8_SA(0, 0), cA, voffA); PG8_STAGE(PG8_SA(0, 1), cA + hstepA, voffA);
;     if (wr == 1) PG8_BAR;
;     PG8_WAIT_V(2); PG8_BAR;
;     PG8_STAGE(PG8_SB(1, 0), cB + kstep, voffB); PG8_STAGE(PG8_SA(1, 0), cA + kstep, voffA); PG8_STAGE(PG8_SB(1, 1), cB + hstepB + kstep, voffB);
;     PG8_WAIT_V(6); PG8_BAR;
;     ...
;         for (int k = 1; k < 8; ++k) e += (u.pm >= __builtin_amdgcn_readfirstlane(toff[k])) ? 1 : 0;
;         u.tag = e; u.a = A + (size_t)u.pm * astep; u.b = Bt + (size_t)e * estride + (size_t)u.pn * bstep; return true; }
	v_readfirstlane_b32 s21, v1
	v_cndmask_b32_e64 v1, 0, 1, s[8:9]
	v_cndmask_b32_e64 v2, 0, 1, s[14:15]
	s_cselect_b64 s[8:9], -1, 0
	s_cmp_ge_i32 s22, s18
	v_addc_co_u32_e32 v2, vcc, v1, v2, vcc
	v_cndmask_b32_e64 v4, 0, 1, s[8:9]
	v_mov_b32_e32 v5, s1
	s_cselect_b64 s[8:9], -1, 0
	s_cmp_ge_i32 s22, s19
	v_lshl_add_u64 v[4:5], v[2:3], 0, v[4:5]
	v_cndmask_b32_e64 v6, 0, 1, s[8:9]
	s_cselect_b64 s[8:9], -1, 0
	s_cmp_ge_i32 s22, s21
	v_lshl_add_u64 v[4:5], v[4:5], 0, v[6:7]
	v_cndmask_b32_e64 v6, 0, 1, s[8:9]
	s_cselect_b64 s[8:9], -1, 0
	v_lshl_add_u64 v[4:5], v[4:5], 0, v[6:7]
	v_cndmask_b32_e64 v6, 0, 1, s[8:9]
	v_lshl_add_u64 v[4:5], v[4:5], 0, v[6:7]
	s_mov_b32 s8, 0x3800000
	v_mul_lo_u32 v1, v5, s8
	v_mul_hi_u32 v2, v4, s8
	v_add_u32_e32 v5, v2, v1
	v_mul_lo_u32 v4, v4, s8
	s_ashr_i32 s21, s20, 31
	v_lshl_add_u64 v[4:5], s[6:7], 0, v[4:5]
	s_lshl_b64 s[8:9], s[20:21], 19
	s_ashr_i32 s23, s22, 31
	v_lshl_add_u64 v[4:5], v[4:5], 0, s[8:9]
	s_lshl_b64 s[8:9], s[22:23], 19
	s_add_u32 s26, s36, s8
	s_addc_u32 s27, s37, s9
	s_add_i32 s21, s5, 0
	v_readfirstlane_b32 s29, v5
	v_readfirstlane_b32 s28, v4
	s_add_i32 s23, s21, 0x10000
	s_nop 0
	v_readlane_b32 s70, v250, 60
	v_mbcnt_lo_u32_b32 v246, -1, 0
	v_mbcnt_hi_u32_b32 v246, -1, v246
	v_add_u32_e32 v246, s70, v246
	v_bfe_u32 v247, v246, 4, 2
	v_bfe_u32 v248, v246, 6, 1
	v_lshl_or_b32 v247, v248, 2, v247
	v_and_b32_e32 v248, 7, v246
	v_xor_b32_e32 v247, v247, v248
	v_lshlrev_b32_e32 v247, 4, v247
	v_lshrrev_b32_e32 v248, 3, v246
	v_lshl_add_u32 v238, v248, 11, v247
	v_add_u32_e32 v239, 0x20000, v238
	v_and_b32_e32 v249, 0x23, v248
	v_and_b32_e32 v244, 12, v248
	v_lshl_or_b32 v249, v244, 1, v249
	v_bfe_u32 v244, v248, 4, 1
	v_lshl_or_b32 v249, v244, 2, v249
	v_lshl_add_u32 v240, v249, 11, v247
	v_add_u32_e32 v241, 0x20000, v240
	v_bfe_u32 v247, v246, 4, 2
	v_bfe_u32 v248, v246, 1, 3
	v_xor_b32_e32 v247, v247, v248
	v_lshlrev_b32_e32 v247, 4, v247
	v_and_b32_e32 v248, 7, v246
	v_lshl_or_b32 v247, v248, 7, v247
	v_bfe_u32 v248, v246, 3, 1
	v_lshl_or_b32 v247, v248, 10, v247
	v_bfe_u32 v248, v246, 8, 1
	v_lshl_or_b32 v242, v248, 13, v247
	v_xor_b32_e32 v243, 64, v242
	v_bfe_u32 v248, v246, 6, 2
	v_lshl_or_b32 v244, v248, 12, v247
	v_xor_b32_e32 v245, 64, v244
	s_mov_b32 m0, s23
	s_nop 0
	global_load_lds_dwordx4 v240, s[28:29]
	s_add_i32 s40, s21, 0x12000
	s_mov_b32 m0, s40
	s_nop 0
	global_load_lds_dwordx4 v241, s[28:29]
	s_add_u32 s8, s28, 0x40000
	s_addc_u32 s9, s29, 0
	s_add_i32 s41, s21, 0x14000
	s_mov_b32 m0, s41
	s_nop 0
	global_load_lds_dwordx4 v240, s[8:9]
	s_add_i32 s42, s21, 0x16000
	s_mov_b32 m0, s42
	s_nop 0
	global_load_lds_dwordx4 v241, s[8:9]
	s_add_i32 s43, s21, 0x2000
	s_mov_b32 m0, s21
	s_nop 0
	global_load_lds_dwordx4 v238, s[26:27]
	s_add_u32 s8, s26, 0x40000
	s_mov_b32 m0, s43
	s_nop 0
	global_load_lds_dwordx4 v239, s[26:27]
	s_addc_u32 s9, s27, 0
	s_add_i32 s44, s21, 0x4000
	s_mov_b32 m0, s44
	s_nop 0
	global_load_lds_dwordx4 v238, s[8:9]
	s_add_i32 s45, s21, 0x6000
	s_mov_b32 m0, s45
	s_nop 0
	global_load_lds_dwordx4 v239, s[8:9]
	s_cmp_eq_u32 s10, 1
	s_cselect_b64 s[8:9], -1, 0
	s_cmp_lg_u32 s10, 1
	s_cbranch_scc1 .LBB0_2840
	s_barrier
.LBB0_2840:
	v_lshrrev_b32_e32 v2, 1, v0
	v_and_b32_e32 v2, 24, v2
	v_and_b32_e32 v1, 15, v0
	v_lshlrev_b32_e32 v4, 1, v2
	v_lshlrev_b32_e32 v0, 2, v0
	v_lshl_or_b32 v180, s10, 6, v1
	v_lshl_or_b32 v1, v1, 6, v4
	s_lshl_b32 s10, s10, 13
	v_and_b32_e32 v0, 32, v0
	v_bitop3_b32 v4, v1, s10, v0 bitop3:0xde
	s_lshl_b32 s10, s11, 5
	s_and_b32 s14, s10, 0x60
	s_ashr_i32 s5, s4, 31
	s_lshl_b32 s10, s14, 7
	v_bitop3_b32 v0, v1, s10, v0 bitop3:0xde
	s_add_u32 s10, s2, 0x3a892000
	s_addc_u32 s11, s3, 0
	s_add_u32 s2, s28, 0x80
	s_waitcnt vmcnt(2)
	s_barrier
	s_addc_u32 s3, s29, 0
	s_add_i32 s46, s21, 0x18000
	s_mov_b32 m0, s46
	s_nop 0
	global_load_lds_dwordx4 v240, s[2:3]
	s_add_i32 s47, s21, 0x1a000
	s_mov_b32 m0, s47
	s_nop 0
	global_load_lds_dwordx4 v241, s[2:3]
	s_add_u32 s2, s26, 0x80
	s_addc_u32 s3, s27, 0
	s_add_i32 s48, s21, 0x8000
	s_mov_b32 m0, s48
	s_nop 0
	global_load_lds_dwordx4 v238, s[2:3]
	s_add_i32 s49, s21, 0xa000
	s_mov_b32 m0, s49
	s_nop 0
	global_load_lds_dwordx4 v239, s[2:3]
	s_add_u32 s2, s28, 0x40080
	s_addc_u32 s3, s29, 0
	s_add_i32 s50, s21, 0x1c000
	s_mov_b32 m0, s50
	s_nop 0
	global_load_lds_dwordx4 v240, s[2:3]
	s_add_i32 s51, s21, 0x1e000
	s_mov_b32 m0, s51
	s_nop 0
	global_load_lds_dwordx4 v241, s[2:3]
	s_waitcnt vmcnt(6)
	s_add_i32 s52, s21, 0xc000
	s_cmpk_lt_u32 s12, 0x100
	s_cselect_b64 s[12:13], -1, 0
	s_add_i32 s53, s21, 0xe000
	v_or_b32_e32 v181, s14, v2
	s_mov_b32 s54, 0
	v_add_u32_e32 v182, 0, v0
	v_add_u32_e32 v183, 0, v4
	s_mov_b64 s[18:19], s[26:27]
	s_barrier
	s_branch .LBB0_2843

; #define PG8_STAGE(bufoff, gbase, voff) do { _Pragma("unroll") for (int _i = 0; _i < 2; ++_i) \
;         glds16((const void*)(gbase), (voff)[_i], ldsbase + (unsigned)(bufoff) + ldsw + (unsigned)_i * 8192u); } while (0)
; #define PG8_LDA(dst, b, h) do { _Pragma("unroll") for (int m = 0; m < 4; ++m) _Pragma("unroll") for (int k = 0; k < 2; ++k) dst[m][k] = *(const LAS bf16x8*)(lds + PG8_SA(b, h) + aoff + m * 2048 + k * 1024); } while (0)
; #define PG8_LDB(dst, b, h) do { _Pragma("unroll") for (int n = 0; n < 2; ++n) _Pragma("unroll") for (int k = 0; k < 2; ++k) dst[n][k] = *(const LAS bf16x8*)(lds + PG8_SB(b, h) + boff + n * 2048 + k * 1024); } while (0)
; #define PG8_WAIT_V(n) asm volatile("s_waitcnt vmcnt(" #n ")" ::: "memory")
; #define PG8_WAIT_L(n) asm volatile("s_waitcnt lgkmcnt(" #n ")" ::: "memory")
; #define PG8_BAR __builtin_amdgcn_s_barrier()
; #define PG8_SCHED __builtin_amdgcn_sched_barrier(0)
;     ...
;         for (int t = 0; t < nt; t += 2) {
;             const bool last = (t == nt - 2);
;             const char* a1 = cA + (size_t)(t + 1) * kstep;
;             const char* a2 = last ? nA : cA + (size_t)(t + 2) * kstep; const char* b2 = last ? nB : cB + (size_t)(t + 2) * kstep;
;             const char* a3 = a2 + kstep; const char* b3 = b2 + kstep;
;             PG8_LDB(B0, 0, 0); PG8_LDB(B1, 0, 1); PG8_SCHED; PG8_LDA(At, 0, 0); PG8_STAGE(PG8_SA(1, 1), a1 + hstepA, voffA);
;             PG8_WAIT_V(8); PG8_WAIT_L(0); PG8_BAR; PG8_MMA(0, 0, At, B0); PG8_MMA(0, 1, At, B1); PG8_BAR; PG8_SCHED;
;             PG8_LDA(At, 0, 1); PG8_STAGE(PG8_SB(0, 0), b2, voffB); PG8_STAGE(PG8_SB(0, 1), b2 + hstepB, voffB); PG8_STAGE(PG8_SA(0, 0), a2, voffA);
;             PG8_WAIT_V(8); PG8_WAIT_L(0); PG8_BAR; PG8_MMA(1, 0, At, B0); PG8_MMA(1, 1, At, B1); PG8_BAR; PG8_SCHED;
;             PG8_LDB(B0, 1, 0); PG8_LDB(B1, 1, 1); PG8_SCHED; PG8_LDA(At, 1, 0); PG8_STAGE(PG8_SA(0, 1), a2 + hstepA, voffA);
;             PG8_WAIT_V(8); PG8_WAIT_L(0); PG8_BAR; PG8_MMA(0, 0, At, B0); PG8_MMA(0, 1, At, B1); PG8_BAR; PG8_SCHED;
;             PG8_LDA(At, 1, 1); PG8_STAGE(PG8_SB(1, 0), b3, voffB); PG8_STAGE(PG8_SB(1, 1), b3 + hstepB, voffB); PG8_STAGE(PG8_SA(1, 0), a3, voffA);
;             PG8_WAIT_V(8); PG8_WAIT_L(0); PG8_BAR; PG8_MMA(1, 0, At, B0); PG8_MMA(1, 1, At, B1); PG8_BAR; PG8_SCHED;
;         }
.LBB0_2846:
	v_add_u32_e32 v0, 0x10000, v244
	v_add_u32_e32 v246, 0x10000, v245
	ds_read_b128 v[22:25], v0
	ds_read_b128 v[168:171], v246
	ds_read_b128 v[16:19], v0 offset:2048
	ds_read_b128 v[164:167], v246 offset:2048
	v_add_u32_e32 v0, 0x14000, v244
	v_add_u32_e32 v246, 0x14000, v245
	ds_read_b128 v[10:13], v0
	ds_read_b128 v[160:163], v246
	ds_read_b128 v[4:7], v0 offset:2048
	ds_read_b128 v[156:159], v246 offset:2048
	s_add_u32 s28, s26, 0xfffc0080
	s_addc_u32 s29, s27, -1
	s_cmp_eq_u32 s55, 12
	s_cselect_b32 s34, s18, s28
	s_cselect_b32 s35, s19, s29
	s_cselect_b32 s30, s24, s15
	s_cselect_b32 s31, s25, s17
	s_add_u32 s28, s34, 0x80
	s_addc_u32 s29, s35, 0
	ds_read_b128 v[206:209], v242
	ds_read_b128 v[172:175], v243
	ds_read_b128 v[212:215], v242 offset:2048
	ds_read_b128 v[184:187], v243 offset:2048
	ds_read_b128 v[218:221], v242 offset:4096
	ds_read_b128 v[196:199], v243 offset:4096
	ds_read_b128 v[224:227], v242 offset:6144
	ds_read_b128 v[228:231], v243 offset:6144
	s_mov_b32 m0, s52
	s_nop 0
	global_load_lds_dwordx4 v238, s[26:27]
	s_nop 0
	s_mov_b32 m0, s53
	s_nop 0
	global_load_lds_dwordx4 v239, s[26:27]
	s_waitcnt vmcnt(8)
	s_waitcnt lgkmcnt(0)
	s_barrier
	s_setprio 0
	s_waitcnt lgkmcnt(6)
	v_mov_b32_e32 v210, v172
	v_mov_b32_e32 v211, v173
	v_mov_b32_e32 v26, v168
	v_mov_b32_e32 v27, v169
	s_nop 1
	v_mfma_scale_f32_16x16x128_f8f6f4 v[152:155], v[22:27], v[206:211], v[152:155], v170, v174 op_sel_hi:[0,0,0] cbsz:2 blgp:2
	v_mov_b32_e32 v20, v164
	v_mov_b32_e32 v21, v165
	s_nop 1
	v_mfma_scale_f32_16x16x128_f8f6f4 v[144:147], v[16:21], v[206:211], v[144:147], v166, v174 op_sel_hi:[0,0,0] cbsz:2 blgp:2
	s_waitcnt lgkmcnt(4)
	v_mov_b32_e32 v216, v184
	v_mov_b32_e32 v217, v185
	s_nop 1
	v_mfma_scale_f32_16x16x128_f8f6f4 v[136:139], v[22:27], v[212:217], v[136:139], v170, v186 op_sel_hi:[0,0,0] cbsz:2 blgp:2
	s_nop 1
	v_mfma_scale_f32_16x16x128_f8f6f4 v[128:131], v[16:21], v[212:217], v[128:131], v166, v186 op_sel_hi:[0,0,0] cbsz:2 blgp:2
	s_waitcnt lgkmcnt(2)
	v_mov_b32_e32 v222, v196
	v_mov_b32_e32 v223, v197
	s_nop 1
	v_mfma_scale_f32_16x16x128_f8f6f4 v[120:123], v[22:27], v[218:223], v[120:123], v170, v198 op_sel_hi:[0,0,0] cbsz:2 blgp:2
	s_nop 1
	v_mfma_scale_f32_16x16x128_f8f6f4 v[112:115], v[16:21], v[218:223], v[112:115], v166, v198 op_sel_hi:[0,0,0] cbsz:2 blgp:2
	s_waitcnt lgkmcnt(0)
	s_nop 1
	v_mfma_scale_f32_16x16x128_f8f6f4 v[104:107], v[22:27], v[224:229], v[104:107], v170, v230 op_sel_hi:[0,0,0] cbsz:2 blgp:2
	s_nop 1
	v_mfma_scale_f32_16x16x128_f8f6f4 v[96:99], v[16:21], v[224:229], v[96:99], v166, v230 op_sel_hi:[0,0,0] cbsz:2 blgp:2
	s_setprio 0
	s_setprio 0
	v_mov_b32_e32 v14, v160
	v_mov_b32_e32 v15, v161
	s_nop 1
	v_mfma_scale_f32_16x16x128_f8f6f4 v[148:151], v[10:15], v[206:211], v[148:151], v162, v174 op_sel_hi:[0,0,0] cbsz:2 blgp:2
	v_mov_b32_e32 v8, v156
	v_mov_b32_e32 v9, v157
	s_nop 1
	v_mfma_scale_f32_16x16x128_f8f6f4 v[140:143], v[4:9], v[206:211], v[140:143], v158, v174 op_sel_hi:[0,0,0] cbsz:2 blgp:2
	s_nop 1
	v_mfma_scale_f32_16x16x128_f8f6f4 v[132:135], v[10:15], v[212:217], v[132:135], v162, v186 op_sel_hi:[0,0,0] cbsz:2 blgp:2
	s_nop 1
	v_mfma_scale_f32_16x16x128_f8f6f4 v[124:127], v[4:9], v[212:217], v[124:127], v158, v186 op_sel_hi:[0,0,0] cbsz:2 blgp:2
	s_nop 1
	v_mfma_scale_f32_16x16x128_f8f6f4 v[116:119], v[10:15], v[218:223], v[116:119], v162, v198 op_sel_hi:[0,0,0] cbsz:2 blgp:2
	s_nop 1
	v_mfma_scale_f32_16x16x128_f8f6f4 v[108:111], v[4:9], v[218:223], v[108:111], v158, v198 op_sel_hi:[0,0,0] cbsz:2 blgp:2
	s_nop 1
	v_mfma_scale_f32_16x16x128_f8f6f4 v[100:103], v[10:15], v[224:229], v[100:103], v162, v230 op_sel_hi:[0,0,0] cbsz:2 blgp:2
	s_nop 1
	v_mfma_scale_f32_16x16x128_f8f6f4 v[92:95], v[4:9], v[224:229], v[92:95], v158, v230 op_sel_hi:[0,0,0] cbsz:2 blgp:2
	s_setprio 0
	s_barrier
	ds_read_b128 v[206:209], v242 offset:16384
	ds_read_b128 v[172:175], v243 offset:16384
	ds_read_b128 v[212:215], v242 offset:18432
	ds_read_b128 v[184:187], v243 offset:18432
	ds_read_b128 v[218:221], v242 offset:20480
	ds_read_b128 v[196:199], v243 offset:20480
	ds_read_b128 v[224:227], v242 offset:22528
	ds_read_b128 v[228:231], v243 offset:22528
	s_mov_b32 m0, s23
	s_nop 0
	global_load_lds_dwordx4 v240, s[30:31]
	s_nop 0
	s_mov_b32 m0, s40
	s_nop 0
	global_load_lds_dwordx4 v241, s[30:31]
	s_add_u32 s56, s30, 0x40000
	s_addc_u32 s57, s31, 0
	s_mov_b32 m0, s41
	s_nop 0
	global_load_lds_dwordx4 v240, s[56:57]
	s_nop 0
	s_mov_b32 m0, s42
	s_nop 0
	global_load_lds_dwordx4 v241, s[56:57]
	s_mov_b32 m0, s21
	s_nop 0
	global_load_lds_dwordx4 v238, s[34:35]
	s_nop 0
	s_mov_b32 m0, s43
	s_nop 0
	global_load_lds_dwordx4 v239, s[34:35]
	s_waitcnt vmcnt(8)
	s_waitcnt lgkmcnt(0)
	s_barrier
; #define PG8_STAGE(bufoff, gbase, voff) do { _Pragma("unroll") for (int _i = 0; _i < 2; ++_i) \
;         glds16((const void*)(gbase), (voff)[_i], ldsbase + (unsigned)(bufoff) + ldsw + (unsigned)_i * 8192u); } while (0)
; #define PG8_LDA(dst, b, h) do { _Pragma("unroll") for (int m = 0; m < 4; ++m) _Pragma("unroll") for (int k = 0; k < 2; ++k) dst[m][k] = *(const LAS bf16x8*)(lds + PG8_SA(b, h) + aoff + m * 2048 + k * 1024); } while (0)
; #define PG8_LDB(dst, b, h) do { _Pragma("unroll") for (int n = 0; n < 2; ++n) _Pragma("unroll") for (int k = 0; k < 2; ++k) dst[n][k] = *(const LAS bf16x8*)(lds + PG8_SB(b, h) + boff + n * 2048 + k * 1024); } while (0)
; #define PG8_WAIT_V(n) asm volatile("s_waitcnt vmcnt(" #n ")" ::: "memory")
; #define PG8_WAIT_L(n) asm volatile("s_waitcnt lgkmcnt(" #n ")" ::: "memory")
; #define PG8_BAR __builtin_amdgcn_s_barrier()
; #define PG8_SCHED __builtin_amdgcn_sched_barrier(0)
;     ...
;         for (int t = 0; t < nt; t += 2) {
;             const bool last = (t == nt - 2);
;             const char* a1 = cA + (size_t)(t + 1) * kstep;
;             const char* a2 = last ? nA : cA + (size_t)(t + 2) * kstep; const char* b2 = last ? nB : cB + (size_t)(t + 2) * kstep;
;             const char* a3 = a2 + kstep; const char* b3 = b2 + kstep;
;             PG8_LDB(B0, 0, 0); PG8_LDB(B1, 0, 1); PG8_SCHED; PG8_LDA(At, 0, 0); PG8_STAGE(PG8_SA(1, 1), a1 + hstepA, voffA);
;             PG8_WAIT_V(8); PG8_WAIT_L(0); PG8_BAR; PG8_MMA(0, 0, At, B0); PG8_MMA(0, 1, At, B1); PG8_BAR; PG8_SCHED;
;             PG8_LDA(At, 0, 1); PG8_STAGE(PG8_SB(0, 0), b2, voffB); PG8_STAGE(PG8_SB(0, 1), b2 + hstepB, voffB); PG8_STAGE(PG8_SA(0, 0), a2, voffA);
;             PG8_WAIT_V(8); PG8_WAIT_L(0); PG8_BAR; PG8_MMA(1, 0, At, B0); PG8_MMA(1, 1, At, B1); PG8_BAR; PG8_SCHED;
;             PG8_LDB(B0, 1, 0); PG8_LDB(B1, 1, 1); PG8_SCHED; PG8_LDA(At, 1, 0); PG8_STAGE(PG8_SA(0, 1), a2 + hstepA, voffA);
;             PG8_WAIT_V(8); PG8_WAIT_L(0); PG8_BAR; PG8_MMA(0, 0, At, B0); PG8_MMA(0, 1, At, B1); PG8_BAR; PG8_SCHED;
;             PG8_LDA(At, 1, 1); PG8_STAGE(PG8_SB(1, 0), b3, voffB); PG8_STAGE(PG8_SB(1, 1), b3 + hstepB, voffB); PG8_STAGE(PG8_SA(1, 0), a3, voffA);
;             PG8_WAIT_V(8); PG8_WAIT_L(0); PG8_BAR; PG8_MMA(1, 0, At, B0); PG8_MMA(1, 1, At, B1); PG8_BAR; PG8_SCHED;
;         }
	s_setprio 0
	s_waitcnt lgkmcnt(6)
	v_mov_b32_e32 v210, v172
	v_mov_b32_e32 v211, v173
	s_nop 1
	v_mfma_scale_f32_16x16x128_f8f6f4 v[88:91], v[22:27], v[206:211], v[88:91], v170, v174 op_sel_hi:[0,0,0] cbsz:2 blgp:2
	s_nop 1
	v_mfma_scale_f32_16x16x128_f8f6f4 v[80:83], v[16:21], v[206:211], v[80:83], v166, v174 op_sel_hi:[0,0,0] cbsz:2 blgp:2
	s_waitcnt lgkmcnt(4)
	v_mov_b32_e32 v216, v184
	v_mov_b32_e32 v217, v185
	s_nop 1
	v_mfma_scale_f32_16x16x128_f8f6f4 v[72:75], v[22:27], v[212:217], v[72:75], v170, v186 op_sel_hi:[0,0,0] cbsz:2 blgp:2
	s_nop 1
	v_mfma_scale_f32_16x16x128_f8f6f4 v[64:67], v[16:21], v[212:217], v[64:67], v166, v186 op_sel_hi:[0,0,0] cbsz:2 blgp:2
	s_waitcnt lgkmcnt(2)
	v_mov_b32_e32 v222, v196
	v_mov_b32_e32 v223, v197
	s_nop 1
	v_mfma_scale_f32_16x16x128_f8f6f4 v[56:59], v[22:27], v[218:223], v[56:59], v170, v198 op_sel_hi:[0,0,0] cbsz:2 blgp:2
	s_nop 1
	v_mfma_scale_f32_16x16x128_f8f6f4 v[48:51], v[16:21], v[218:223], v[48:51], v166, v198 op_sel_hi:[0,0,0] cbsz:2 blgp:2
	s_waitcnt lgkmcnt(0)
	s_nop 1
	v_mfma_scale_f32_16x16x128_f8f6f4 v[40:43], v[22:27], v[224:229], v[40:43], v170, v230 op_sel_hi:[0,0,0] cbsz:2 blgp:2
	s_nop 1
	v_mfma_scale_f32_16x16x128_f8f6f4 v[32:35], v[16:21], v[224:229], v[32:35], v166, v230 op_sel_hi:[0,0,0] cbsz:2 blgp:2
	s_setprio 0
	s_setprio 0
	s_nop 1
	v_mfma_scale_f32_16x16x128_f8f6f4 v[84:87], v[10:15], v[206:211], v[84:87], v162, v174 op_sel_hi:[0,0,0] cbsz:2 blgp:2
	s_nop 1
	v_mfma_scale_f32_16x16x128_f8f6f4 v[76:79], v[4:9], v[206:211], v[76:79], v158, v174 op_sel_hi:[0,0,0] cbsz:2 blgp:2
	s_nop 1
	v_mfma_scale_f32_16x16x128_f8f6f4 v[68:71], v[10:15], v[212:217], v[68:71], v162, v186 op_sel_hi:[0,0,0] cbsz:2 blgp:2
	s_nop 1
	v_mfma_scale_f32_16x16x128_f8f6f4 v[60:63], v[4:9], v[212:217], v[60:63], v158, v186 op_sel_hi:[0,0,0] cbsz:2 blgp:2
	s_nop 1
	v_mfma_scale_f32_16x16x128_f8f6f4 v[52:55], v[10:15], v[218:223], v[52:55], v162, v198 op_sel_hi:[0,0,0] cbsz:2 blgp:2
	s_nop 1
	v_mfma_scale_f32_16x16x128_f8f6f4 v[44:47], v[4:9], v[218:223], v[44:47], v158, v198 op_sel_hi:[0,0,0] cbsz:2 blgp:2
	s_nop 1
	v_mfma_scale_f32_16x16x128_f8f6f4 v[36:39], v[10:15], v[224:229], v[36:39], v162, v230 op_sel_hi:[0,0,0] cbsz:2 blgp:2
	s_nop 1
	v_mfma_scale_f32_16x16x128_f8f6f4 v[28:31], v[4:9], v[224:229], v[28:31], v158, v230 op_sel_hi:[0,0,0] cbsz:2 blgp:2
	s_setprio 0
	s_barrier
	v_add_u32_e32 v0, 0x18000, v244
	v_add_u32_e32 v246, 0x18000, v245
	ds_read_b128 v[22:25], v0
	ds_read_b128 v[168:171], v246
	ds_read_b128 v[16:19], v0 offset:2048
	ds_read_b128 v[164:167], v246 offset:2048
	v_add_u32_e32 v0, 0x1c000, v244
	v_add_u32_e32 v246, 0x1c000, v245
	ds_read_b128 v[10:13], v0
	ds_read_b128 v[156:159], v246
	ds_read_b128 v[4:7], v0 offset:2048
	ds_read_b128 v[160:163], v246 offset:2048
	ds_read_b128 v[206:209], v242 offset:32768
	ds_read_b128 v[172:175], v243 offset:32768
	ds_read_b128 v[212:215], v242 offset:34816
	ds_read_b128 v[184:187], v243 offset:34816
	ds_read_b128 v[218:221], v242 offset:36864
	ds_read_b128 v[196:199], v243 offset:36864
	ds_read_b128 v[224:227], v242 offset:38912
	ds_read_b128 v[228:231], v243 offset:38912
	s_add_u32 s34, s34, 0x40000
	s_addc_u32 s35, s35, 0
	s_mov_b32 m0, s44
	s_nop 0
	global_load_lds_dwordx4 v238, s[34:35]
	s_nop 0
	s_mov_b32 m0, s45
	s_nop 0
	global_load_lds_dwordx4 v239, s[34:35]
	s_waitcnt vmcnt(8)
	s_waitcnt lgkmcnt(0)
	s_barrier
	s_setprio 0
	s_waitcnt lgkmcnt(6)
	v_mov_b32_e32 v210, v172
	v_mov_b32_e32 v211, v173
	v_mov_b32_e32 v26, v168
	v_mov_b32_e32 v27, v169
	s_nop 1
	v_mfma_scale_f32_16x16x128_f8f6f4 v[152:155], v[22:27], v[206:211], v[152:155], v170, v174 op_sel_hi:[0,0,0] cbsz:2 blgp:2
	v_mov_b32_e32 v20, v164
	v_mov_b32_e32 v21, v165
	s_nop 1
	v_mfma_scale_f32_16x16x128_f8f6f4 v[144:147], v[16:21], v[206:211], v[144:147], v166, v174 op_sel_hi:[0,0,0] cbsz:2 blgp:2
	s_waitcnt lgkmcnt(4)
	v_mov_b32_e32 v216, v184
	v_mov_b32_e32 v217, v185
	s_nop 1
	v_mfma_scale_f32_16x16x128_f8f6f4 v[136:139], v[22:27], v[212:217], v[136:139], v170, v186 op_sel_hi:[0,0,0] cbsz:2 blgp:2
	s_nop 1
	v_mfma_scale_f32_16x16x128_f8f6f4 v[128:131], v[16:21], v[212:217], v[128:131], v166, v186 op_sel_hi:[0,0,0] cbsz:2 blgp:2
	s_waitcnt lgkmcnt(2)
	v_mov_b32_e32 v222, v196
	v_mov_b32_e32 v223, v197
	s_nop 1
	v_mfma_scale_f32_16x16x128_f8f6f4 v[120:123], v[22:27], v[218:223], v[120:123], v170, v198 op_sel_hi:[0,0,0] cbsz:2 blgp:2
	s_nop 1
	v_mfma_scale_f32_16x16x128_f8f6f4 v[112:115], v[16:21], v[218:223], v[112:115], v166, v198 op_sel_hi:[0,0,0] cbsz:2 blgp:2
	s_waitcnt lgkmcnt(0)
	s_nop 1
	v_mfma_scale_f32_16x16x128_f8f6f4 v[104:107], v[22:27], v[224:229], v[104:107], v170, v230 op_sel_hi:[0,0,0] cbsz:2 blgp:2
	s_nop 1
	v_mfma_scale_f32_16x16x128_f8f6f4 v[96:99], v[16:21], v[224:229], v[96:99], v166, v230 op_sel_hi:[0,0,0] cbsz:2 blgp:2
	s_setprio 0
	s_setprio 0
	v_mov_b32_e32 v14, v156
	v_mov_b32_e32 v15, v157
	s_nop 1
	v_mfma_scale_f32_16x16x128_f8f6f4 v[148:151], v[10:15], v[206:211], v[148:151], v158, v174 op_sel_hi:[0,0,0] cbsz:2 blgp:2
	v_mov_b32_e32 v8, v160
	v_mov_b32_e32 v9, v161
	s_nop 1
	v_mfma_scale_f32_16x16x128_f8f6f4 v[140:143], v[4:9], v[206:211], v[140:143], v162, v174 op_sel_hi:[0,0,0] cbsz:2 blgp:2
	s_nop 1
	v_mfma_scale_f32_16x16x128_f8f6f4 v[132:135], v[10:15], v[212:217], v[132:135], v158, v186 op_sel_hi:[0,0,0] cbsz:2 blgp:2
	s_nop 1
	v_mfma_scale_f32_16x16x128_f8f6f4 v[124:127], v[4:9], v[212:217], v[124:127], v162, v186 op_sel_hi:[0,0,0] cbsz:2 blgp:2
	s_nop 1
	v_mfma_scale_f32_16x16x128_f8f6f4 v[116:119], v[10:15], v[218:223], v[116:119], v158, v198 op_sel_hi:[0,0,0] cbsz:2 blgp:2
	s_nop 1
	v_mfma_scale_f32_16x16x128_f8f6f4 v[108:111], v[4:9], v[218:223], v[108:111], v162, v198 op_sel_hi:[0,0,0] cbsz:2 blgp:2
	s_nop 1
	v_mfma_scale_f32_16x16x128_f8f6f4 v[100:103], v[10:15], v[224:229], v[100:103], v158, v230 op_sel_hi:[0,0,0] cbsz:2 blgp:2
	s_nop 1
	v_mfma_scale_f32_16x16x128_f8f6f4 v[92:95], v[4:9], v[224:229], v[92:95], v162, v230 op_sel_hi:[0,0,0] cbsz:2 blgp:2
	s_setprio 0
	s_barrier
; #define PG8_STAGE(bufoff, gbase, voff) do { _Pragma("unroll") for (int _i = 0; _i < 2; ++_i) \
;         glds16((const void*)(gbase), (voff)[_i], ldsbase + (unsigned)(bufoff) + ldsw + (unsigned)_i * 8192u); } while (0)
; #define PG8_LDA(dst, b, h) do { _Pragma("unroll") for (int m = 0; m < 4; ++m) _Pragma("unroll") for (int k = 0; k < 2; ++k) dst[m][k] = *(const LAS bf16x8*)(lds + PG8_SA(b, h) + aoff + m * 2048 + k * 1024); } while (0)
; #define PG8_LDB(dst, b, h) do { _Pragma("unroll") for (int n = 0; n < 2; ++n) _Pragma("unroll") for (int k = 0; k < 2; ++k) dst[n][k] = *(const LAS bf16x8*)(lds + PG8_SB(b, h) + boff + n * 2048 + k * 1024); } while (0)
; #define PG8_WAIT_V(n) asm volatile("s_waitcnt vmcnt(" #n ")" ::: "memory")
; #define PG8_WAIT_L(n) asm volatile("s_waitcnt lgkmcnt(" #n ")" ::: "memory")
; #define PG8_BAR __builtin_amdgcn_s_barrier()
; #define PG8_SCHED __builtin_amdgcn_sched_barrier(0)
;     ...
;         for (int t = 0; t < nt; t += 2) {
;             const bool last = (t == nt - 2);
;             const char* a1 = cA + (size_t)(t + 1) * kstep;
;             const char* a2 = last ? nA : cA + (size_t)(t + 2) * kstep; const char* b2 = last ? nB : cB + (size_t)(t + 2) * kstep;
;             const char* a3 = a2 + kstep; const char* b3 = b2 + kstep;
;             PG8_LDB(B0, 0, 0); PG8_LDB(B1, 0, 1); PG8_SCHED; PG8_LDA(At, 0, 0); PG8_STAGE(PG8_SA(1, 1), a1 + hstepA, voffA);
;             PG8_WAIT_V(8); PG8_WAIT_L(0); PG8_BAR; PG8_MMA(0, 0, At, B0); PG8_MMA(0, 1, At, B1); PG8_BAR; PG8_SCHED;
;             PG8_LDA(At, 0, 1); PG8_STAGE(PG8_SB(0, 0), b2, voffB); PG8_STAGE(PG8_SB(0, 1), b2 + hstepB, voffB); PG8_STAGE(PG8_SA(0, 0), a2, voffA);
;             PG8_WAIT_V(8); PG8_WAIT_L(0); PG8_BAR; PG8_MMA(1, 0, At, B0); PG8_MMA(1, 1, At, B1); PG8_BAR; PG8_SCHED;
;             PG8_LDB(B0, 1, 0); PG8_LDB(B1, 1, 1); PG8_SCHED; PG8_LDA(At, 1, 0); PG8_STAGE(PG8_SA(0, 1), a2 + hstepA, voffA);
;             PG8_WAIT_V(8); PG8_WAIT_L(0); PG8_BAR; PG8_MMA(0, 0, At, B0); PG8_MMA(0, 1, At, B1); PG8_BAR; PG8_SCHED;
;             PG8_LDA(At, 1, 1); PG8_STAGE(PG8_SB(1, 0), b3, voffB); PG8_STAGE(PG8_SB(1, 1), b3 + hstepB, voffB); PG8_STAGE(PG8_SA(1, 0), a3, voffA);
;             PG8_WAIT_V(8); PG8_WAIT_L(0); PG8_BAR; PG8_MMA(1, 0, At, B0); PG8_MMA(1, 1, At, B1); PG8_BAR; PG8_SCHED;
;         }
	ds_read_b128 v[206:209], v242 offset:49152
	ds_read_b128 v[172:175], v243 offset:49152
	ds_read_b128 v[212:215], v242 offset:51200
	ds_read_b128 v[184:187], v243 offset:51200
	ds_read_b128 v[218:221], v242 offset:53248
	ds_read_b128 v[196:199], v243 offset:53248
	ds_read_b128 v[224:227], v242 offset:55296
	ds_read_b128 v[228:231], v243 offset:55296
	s_add_u32 s34, s30, 0x80
	s_addc_u32 s35, s31, 0
	s_mov_b32 m0, s46
	s_nop 0
	global_load_lds_dwordx4 v240, s[34:35]
	s_add_u32 s30, s30, 0x40080
	s_mov_b32 m0, s47
	s_nop 0
	global_load_lds_dwordx4 v241, s[34:35]
	s_addc_u32 s31, s31, 0
	s_mov_b32 m0, s50
	s_nop 0
	global_load_lds_dwordx4 v240, s[30:31]
	s_nop 0
	s_mov_b32 m0, s51
	s_nop 0
	global_load_lds_dwordx4 v241, s[30:31]
	s_mov_b32 m0, s48
	s_nop 0
	global_load_lds_dwordx4 v238, s[28:29]
	s_nop 0
	s_mov_b32 m0, s49
	s_nop 0
	global_load_lds_dwordx4 v239, s[28:29]
	s_waitcnt vmcnt(8)
	s_waitcnt lgkmcnt(0)
	s_barrier
	s_setprio 0
	s_waitcnt lgkmcnt(6)
	v_mov_b32_e32 v210, v172
	v_mov_b32_e32 v211, v173
	s_nop 1
	v_mfma_scale_f32_16x16x128_f8f6f4 v[88:91], v[22:27], v[206:211], v[88:91], v170, v174 op_sel_hi:[0,0,0] cbsz:2 blgp:2
	s_nop 1
	v_mfma_scale_f32_16x16x128_f8f6f4 v[80:83], v[16:21], v[206:211], v[80:83], v166, v174 op_sel_hi:[0,0,0] cbsz:2 blgp:2
	s_waitcnt lgkmcnt(4)
	v_mov_b32_e32 v216, v184
	v_mov_b32_e32 v217, v185
	s_nop 1
	v_mfma_scale_f32_16x16x128_f8f6f4 v[72:75], v[22:27], v[212:217], v[72:75], v170, v186 op_sel_hi:[0,0,0] cbsz:2 blgp:2
	s_nop 1
	v_mfma_scale_f32_16x16x128_f8f6f4 v[64:67], v[16:21], v[212:217], v[64:67], v166, v186 op_sel_hi:[0,0,0] cbsz:2 blgp:2
	s_waitcnt lgkmcnt(2)
	v_mov_b32_e32 v222, v196
	v_mov_b32_e32 v223, v197
	s_nop 1
	v_mfma_scale_f32_16x16x128_f8f6f4 v[56:59], v[22:27], v[218:223], v[56:59], v170, v198 op_sel_hi:[0,0,0] cbsz:2 blgp:2
	s_nop 1
	v_mfma_scale_f32_16x16x128_f8f6f4 v[48:51], v[16:21], v[218:223], v[48:51], v166, v198 op_sel_hi:[0,0,0] cbsz:2 blgp:2
	s_waitcnt lgkmcnt(0)
	s_nop 1
	v_mfma_scale_f32_16x16x128_f8f6f4 v[40:43], v[22:27], v[224:229], v[40:43], v170, v230 op_sel_hi:[0,0,0] cbsz:2 blgp:2
	s_nop 1
	v_mfma_scale_f32_16x16x128_f8f6f4 v[32:35], v[16:21], v[224:229], v[32:35], v166, v230 op_sel_hi:[0,0,0] cbsz:2 blgp:2
	s_setprio 0
	s_setprio 0
	s_nop 1
	v_mfma_scale_f32_16x16x128_f8f6f4 v[84:87], v[10:15], v[206:211], v[84:87], v158, v174 op_sel_hi:[0,0,0] cbsz:2 blgp:2
	s_nop 1
	v_mfma_scale_f32_16x16x128_f8f6f4 v[76:79], v[4:9], v[206:211], v[76:79], v162, v174 op_sel_hi:[0,0,0] cbsz:2 blgp:2
	s_nop 1
	v_mfma_scale_f32_16x16x128_f8f6f4 v[68:71], v[10:15], v[212:217], v[68:71], v158, v186 op_sel_hi:[0,0,0] cbsz:2 blgp:2
	s_nop 1
	v_mfma_scale_f32_16x16x128_f8f6f4 v[60:63], v[4:9], v[212:217], v[60:63], v162, v186 op_sel_hi:[0,0,0] cbsz:2 blgp:2
	s_nop 1
	v_mfma_scale_f32_16x16x128_f8f6f4 v[52:55], v[10:15], v[218:223], v[52:55], v158, v198 op_sel_hi:[0,0,0] cbsz:2 blgp:2
	s_nop 1
	v_mfma_scale_f32_16x16x128_f8f6f4 v[44:47], v[4:9], v[218:223], v[44:47], v162, v198 op_sel_hi:[0,0,0] cbsz:2 blgp:2
	s_nop 1
	v_mfma_scale_f32_16x16x128_f8f6f4 v[36:39], v[10:15], v[224:229], v[36:39], v158, v230 op_sel_hi:[0,0,0] cbsz:2 blgp:2
	s_nop 1
	v_mfma_scale_f32_16x16x128_f8f6f4 v[28:31], v[4:9], v[224:229], v[28:31], v162, v230 op_sel_hi:[0,0,0] cbsz:2 blgp:2
	s_setprio 0
	s_barrier
	s_add_i32 s55, s55, 2
	s_add_u32 s15, s15, 0x100
	s_addc_u32 s17, s17, 0
	s_add_u32 s26, s26, 0x100
	s_addc_u32 s27, s27, 0
	s_cmp_gt_u32 s55, 13
	s_cbranch_scc0 .LBB0_2846
	s_and_b64 vcc, exec, s[12:13]
	s_cbranch_vccz .LBB0_2849
	s_barrier

;     __device__ __forceinline__ bool idx(int i, int& pm, int& pn) const {
;         const long L = (long)i * G + c; if (L >= nwg) return false;
;         int wgid = (int)L; { const int q = nwg / 8, r = nwg % 8, xcd = wgid % 8, off = wgid / 8; wgid = (xcd < r ? xcd * (q + 1) : r * (q + 1) + (xcd - r) * q) + off; }
;         const int nig = 8 * nN, gid = wgid / nig, fm = gid * 8, gsz = (nM - fm) < 8 ? (nM - fm) : 8;
;         pm = fm + ((wgid % nig) % gsz); pn = (wgid % nig) / gsz; return true;
;     }
; __device__ __forceinline__ const char* uniform_ptr(const char* p) { const unsigned long long v = (unsigned long long)p;
;     const unsigned lo = __builtin_amdgcn_readfirstlane((unsigned)v), hi = __builtin_amdgcn_readfirstlane((unsigned)(v >> 32)); return (const char*)(((unsigned long long)hi << 32) | lo); }
; __device__ __forceinline__ void glds16(const void* sbase, unsigned voff, unsigned lds_dst) {
;     unsigned keep;
;     asm volatile("s_mov_b32 %0, m0\n\ts_mov_b32 m0, %3\n\ts_nop 0\n\tglobal_load_lds_dwordx4 %1, %2\n\ts_mov_b32 m0, %0" : "=&s"(keep) : "v"(voff), "s"(sbase), "s"(lds_dst) : "memory");
; }
;     const int sB1 = sB1_ < 0 ? sB : sB1_;
;     int tid = w0_ * 64 + lane_id(); asm volatile("" : "+v"(tid));
;     const int wid = __builtin_amdgcn_readfirstlane(tid >> 6), lane = tid & 63, wr = wid >> 2, wc = wid & 3, fr = lane & 15, fq = lane >> 4;
;     const int nt = nt_ ? nt_ : Kb / 128;
;     unsigned voffA[2], voffB[2];
; #pragma unroll
;     for (int i = 0; i < 2; ++i) { int R, C; stage_rc(tid * 16 + i * 8192, R, C); const int Rb = Epi::PERM ? ((R & ~31) + perm32(R & 31)) : R;
;         voffA[i] = (unsigned)(R * ldab + C * 2); voffB[i] = (unsigned)(Rb * Kb + C * 2); }
;     const size_t kstep = (size_t)(BK * 2);
;     const size_t hstepA = (size_t)HALF * ldab, hstepB = (size_t)HALF * Kb;
;     const unsigned ldsw = (unsigned)wid * 1024u, ldsbase = (unsigned)(size_t)lds;
;     const int aoff = lds_byte(wr * 64 + fr, fq * 8), boff = lds_byte(wc * 32 + fr, fq * 8);
; #pragma unroll
;         for (int k = 1; k < 8; ++k) e += (u.pm >= __builtin_amdgcn_readfirstlane(toff[k])) ? 1 : 0;
;         u.tag = e; u.a = A + (size_t)u.pm * astep; u.b = Bt + (size_t)e * estride + (size_t)u.pn * bstep; return true; }
.LBB0_2910:
	s_or_b64 exec, exec, s[4:5]
	v_readlane_b32 s5, v250, 60
	s_waitcnt lgkmcnt(0)
	s_barrier
	s_lshl_b32 s4, s0, 3
	v_mbcnt_lo_u32_b32 v0, -1, 0
	v_mbcnt_hi_u32_b32 v0, -1, v0
	s_cmp_ge_i32 s78, s4
	v_add_u32_e32 v4, s5, v0
	s_nop 0
	v_readfirstlane_b32 s14, v4
	s_cbranch_scc1 .LBB0_2926
	v_bfe_i32 v1, v4, 27, 1
	v_lshlrev_b32_e32 v5, 4, v4
	v_lshrrev_b32_e32 v1, 22, v1
	v_add_u32_e32 v1, v5, v1
	v_and_b32_e32 v1, 0xfffffc00, v1
	v_sub_u32_e32 v1, v5, v1
	v_ashrrev_i32_e32 v0, 31, v4
	v_lshrrev_b32_e32 v2, 4, v1
	v_lshrrev_b32_e32 v0, 26, v0
	v_bitop3_b32 v1, v2, v1, 32 bitop3:0x6c
	v_add_u32_e32 v0, v4, v0
	v_ashrrev_i32_e32 v6, 31, v1
	v_ashrrev_i32_e32 v0, 6, v0
	v_lshrrev_b32_e32 v6, 26, v6
	v_lshlrev_b32_e32 v2, 3, v0
	v_add_u32_e32 v6, v1, v6
	v_and_b32_e32 v2, -16, v2
	v_ashrrev_i32_e32 v7, 6, v6
	v_add_u32_e32 v8, v7, v2
	v_and_b32_e32 v2, 0xc0, v6
	v_sub_u32_e32 v1, v1, v2
	v_lshlrev_b32_e32 v0, 5, v0
	v_ashrrev_i16_sdwa v1, v188, sext(v1) dst_sel:DWORD dst_unused:UNUSED_PAD src0_sel:DWORD src1_sel:BYTE_0
	v_lshlrev_b32_e32 v2, 1, v8
	v_lshrrev_b32_e32 v6, 2, v8
	v_and_b32_e32 v7, 3, v7
	s_mov_b32 s10, 0x3fffe0
	v_and_b32_e32 v0, 32, v0
	v_bfe_i32 v1, v1, 0, 16
	v_and_b32_e32 v2, 24, v2
	v_and_b32_e32 v6, 4, v6
	v_and_or_b32 v7, v8, s10, v7
	v_or3_b32 v6, v7, v6, v2
	v_add_lshl_u32 v2, v0, v1, 1
	s_movk_i32 s5, 0x1c00
	v_mad_u64_u32 v[0:1], s[8:9], v8, s5, v[2:3]
	v_mad_u32_u24 v1, v6, s5, v2
	v_add_u32_e32 v2, 0x2000, v5
	v_ashrrev_i32_e32 v5, 31, v2
	v_lshrrev_b32_e32 v5, 22, v5
	v_add_u32_e32 v5, v2, v5
	v_ashrrev_i32_e32 v5, 10, v5
	v_mul_i32_i24_e32 v6, 0x400, v5
	v_sub_u32_e32 v2, v2, v6
	v_lshrrev_b32_e32 v6, 4, v2
	v_bitop3_b32 v2, v6, v2, 32 bitop3:0x6c
	v_ashrrev_i32_e32 v7, 31, v2
	v_lshrrev_b32_e32 v7, 26, v7
	v_add_u32_e32 v7, v2, v7
	v_lshlrev_b32_e32 v6, 3, v5
	v_ashrrev_i32_e32 v8, 6, v7
	v_and_b32_e32 v7, 0xc0, v7
	v_and_b32_e32 v6, -16, v6
	v_sub_u32_e32 v2, v2, v7
	v_add_u32_e32 v6, v8, v6
	v_lshlrev_b32_e32 v5, 5, v5
	v_ashrrev_i16_sdwa v2, v188, sext(v2) dst_sel:DWORD dst_unused:UNUSED_PAD src0_sel:DWORD src1_sel:BYTE_0
	v_and_b32_e32 v5, 32, v5
	v_bfe_i32 v2, v2, 0, 16
	v_lshlrev_b32_e32 v7, 1, v6
	v_lshrrev_b32_e32 v9, 2, v6
	v_and_b32_e32 v8, 3, v8
	s_add_u32 s6, s2, 0x24500000
	v_and_b32_e32 v7, 24, v7
	v_and_b32_e32 v9, 4, v9
	v_and_or_b32 v8, v6, s10, v8
	v_add_lshl_u32 v2, v5, v2, 1
	s_addc_u32 s7, s3, 0
	v_or3_b32 v7, v8, v9, v7
	v_mad_u64_u32 v[164:165], s[8:9], v6, s5, v[2:3]
	s_ashr_i32 s16, s14, 6
	s_add_i32 s28, s0, 1
	s_ashr_i32 s15, s14, 8
	v_mad_u32_u24 v165, v7, s5, v2
	s_lshl_b32 s5, s16, 10
	s_add_u32 s29, s2, 0x3a892000
	v_readlane_b32 s8, v252, 62
	s_addc_u32 s30, s3, 0
	v_readlane_b32 s9, v252, 63
	s_and_b64 s[8:9], s[8:9], exec
	s_cselect_b32 s8, s28, s0
	v_readlane_b32 s9, v253, 16
	s_mul_i32 s8, s8, s9
	v_readlane_b32 s9, v253, 17
	s_add_i32 s8, s8, s9
	s_ashr_i32 s9, s8, 31
	s_lshr_b32 s9, s9, 26
	s_add_i32 s9, s8, s9
	s_ashr_i32 s10, s9, 6
	s_lshl_b32 s10, s10, 3
	s_sub_i32 s11, s0, s10
	s_min_i32 s11, s11, 8
	s_abs_i32 s13, s11
	v_cvt_f32_u32_e32 v2, s13
	s_sub_i32 s17, 0, s13
	s_andn2_b32 s9, s9, 63
	s_sub_i32 s8, s8, s9
	v_rcp_iflag_f32_e32 v2, v2
	s_abs_i32 s12, s8
	s_xor_b32 s9, s8, s11
	s_ashr_i32 s9, s9, 31
	v_mul_f32_e32 v2, 0x4f7ffffe, v2
	v_cvt_u32_f32_e32 v2, v2
	v_mov_b32_e32 v9, s1
	v_readfirstlane_b32 s18, v2
	s_mul_i32 s17, s17, s18
	s_mul_hi_u32 s17, s18, s17
	s_add_i32 s18, s18, s17
	s_mul_hi_u32 s17, s12, s18
	s_mul_i32 s18, s17, s13
	s_sub_i32 s12, s12, s18
	s_add_i32 s18, s17, 1
	s_sub_i32 s19, s12, s13
	s_cmp_ge_u32 s12, s13
	s_cselect_b32 s17, s18, s17
	s_cselect_b32 s12, s19, s12
	s_add_i32 s18, s17, 1
	s_cmp_ge_u32 s12, s13
	s_cselect_b32 s12, s18, s17
	s_xor_b32 s12, s12, s9
	s_sub_i32 s52, s12, s9
	s_mul_i32 s9, s52, s11
	s_sub_i32 s8, s8, s9
	s_add_i32 s53, s10, s8
	v_readlane_b32 s8, v254, 29
	v_readlane_b32 s9, v254, 30
	s_nop 0
	v_mov_b32_e32 v2, s8
	ds_read2_b32 v[6:7], v2 offset1:1
	v_mov_b32_e32 v2, s9
	v_readlane_b32 s9, v254, 31
	s_waitcnt lgkmcnt(0)
	v_readfirstlane_b32 s10, v6
	v_readfirstlane_b32 s8, v7
	ds_read2_b32 v[6:7], v2 offset1:1
	v_mov_b32_e32 v2, s9
	v_readlane_b32 s9, v254, 32
	s_cmp_ge_i32 s53, s8
	s_waitcnt lgkmcnt(0)
	v_readfirstlane_b32 s12, v6
	v_readfirstlane_b32 s13, v7
	ds_read2_b32 v[6:7], v2 offset1:1
	v_mov_b32_e32 v2, s9
	ds_read_b32 v2, v2
	s_cselect_b64 s[8:9], -1, 0
	s_cmp_ge_i32 s53, s10
	s_cselect_b64 s[10:11], -1, 0
	s_cmp_ge_i32 s53, s12
	s_waitcnt lgkmcnt(1)
	v_readfirstlane_b32 s17, v6
	s_cselect_b64 vcc, -1, 0
	s_cmp_ge_i32 s53, s13
	v_readfirstlane_b32 s18, v7
	s_waitcnt lgkmcnt(0)
; #define PG8_STAGE(bufoff, gbase, voff) do { _Pragma("unroll") for (int _i = 0; _i < 2; ++_i) \
;         glds16((const void*)(gbase), (voff)[_i], ldsbase + (unsigned)(bufoff) + ldsw + (unsigned)_i * 8192u); } while (0)
; #define PG8_WAIT_V(n) asm volatile("s_waitcnt vmcnt(" #n ")" ::: "memory")
; #define PG8_BAR __builtin_amdgcn_s_barrier()
;     ...
;     for (int i = 0; i < 2; ++i) { int R, C; stage_rc(tid * 16 + i * 8192, R, C); const int Rb = Epi::PERM ? ((R & ~31) + perm32(R & 31)) : R;
;         voffA[i] = (unsigned)(R * ldab + C * 2); voffB[i] = (unsigned)(Rb * Kb + C * 2); }
;     const size_t kstep = (size_t)(BK * 2);
;     const size_t hstepA = (size_t)HALF * ldab, hstepB = (size_t)HALF * Kb;
;     const unsigned ldsw = (unsigned)wid * 1024u, ldsbase = (unsigned)(size_t)lds;
;     const int aoff = lds_byte(wr * 64 + fr, fq * 8), boff = lds_byte(wc * 32 + fr, fq * 8);
;     ...
;     const char* cA = uniform_ptr(cur.a); const char* cB = uniform_ptr(cur.b);
;     PG8_STAGE(PG8_SB(0, 0), cB, voffB); PG8_STAGE(PG8_SB(0, 1), cB + hstepB, voffB); PG8_STAGE(PG8_SA(0, 0), cA, voffA); PG8_STAGE(PG8_SA(0, 1), cA + hstepA, voffA);
;     if (wr == 1) PG8_BAR;
;     PG8_WAIT_V(2); PG8_BAR;
;     PG8_STAGE(PG8_SB(1, 0), cB + kstep, voffB); PG8_STAGE(PG8_SA(1, 0), cA + kstep, voffA); PG8_STAGE(PG8_SB(1, 1), cB + hstepB + kstep, voffB);
;     PG8_WAIT_V(6); PG8_BAR;
	v_readfirstlane_b32 s19, v2
	v_cndmask_b32_e64 v2, 0, 1, s[8:9]
	v_cndmask_b32_e64 v5, 0, 1, s[10:11]
	s_cselect_b64 s[8:9], -1, 0
	s_cmp_ge_i32 s53, s17
	v_addc_co_u32_e32 v2, vcc, v2, v5, vcc
	v_cndmask_b32_e64 v6, 0, 1, s[8:9]
	v_mov_b32_e32 v7, s1
	s_cselect_b64 s[8:9], -1, 0
	s_cmp_ge_i32 s53, s18
	v_lshl_add_u64 v[6:7], v[2:3], 0, v[6:7]
	v_cndmask_b32_e64 v8, 0, 1, s[8:9]
	s_cselect_b64 s[8:9], -1, 0
	s_cmp_ge_i32 s53, s19
	v_lshl_add_u64 v[6:7], v[6:7], 0, v[8:9]
	v_cndmask_b32_e64 v8, 0, 1, s[8:9]
	s_cselect_b64 s[8:9], -1, 0
	v_lshl_add_u64 v[6:7], v[6:7], 0, v[8:9]
	v_cndmask_b32_e64 v8, 0, 1, s[8:9]
	v_lshl_add_u64 v[6:7], v[6:7], 0, v[8:9]
	s_mov_b32 s8, 0x1c00000
	v_mul_lo_u32 v2, v7, s8
	v_mul_hi_u32 v5, v6, s8
	v_add_u32_e32 v7, v5, v2
	v_mul_lo_u32 v6, v6, s8
	v_lshl_add_u64 v[6:7], s[6:7], 0, v[6:7]
	s_mul_hi_i32 s9, s52, 0x1c0000
	s_mul_i32 s8, s52, 0x1c0000
	v_lshl_add_u64 v[6:7], v[6:7], 0, s[8:9]
	s_mul_i32 s9, s53, 0x1c0000
	s_mul_hi_i32 s8, s53, 0x1c0000
	s_add_u32 s20, s29, s9
	s_addc_u32 s21, s30, s8
	s_add_i32 s31, s5, 0
	v_readfirstlane_b32 s23, v7
	v_readfirstlane_b32 s22, v6
	s_add_i32 s34, s31, 0x10000
	s_nop 0
	v_readlane_b32 s70, v250, 60
	v_mbcnt_lo_u32_b32 v246, -1, 0
	v_mbcnt_hi_u32_b32 v246, -1, v246
	v_add_u32_e32 v246, s70, v246
	v_bfe_u32 v247, v246, 4, 2
	v_bfe_u32 v248, v246, 6, 1
	v_lshl_or_b32 v247, v248, 2, v247
	v_and_b32_e32 v248, 7, v246
	v_xor_b32_e32 v247, v247, v248
	v_lshlrev_b32_e32 v247, 4, v247
	v_lshrrev_b32_e32 v248, 3, v246
	s_mov_b32 s71, 7168
	v_mad_u32_u24 v238, v248, s71, v247
	v_add_u32_e32 v239, 0x70000, v238
	v_and_b32_e32 v249, 0x23, v248
	v_and_b32_e32 v244, 12, v248
	v_lshl_or_b32 v249, v244, 1, v249
	v_bfe_u32 v244, v248, 4, 1
	v_lshl_or_b32 v249, v244, 2, v249
	s_mov_b32 s71, 7168
	v_mad_u32_u24 v240, v249, s71, v247
	v_add_u32_e32 v241, 0x70000, v240
	v_bfe_u32 v247, v246, 4, 2
	v_bfe_u32 v248, v246, 1, 3
	v_xor_b32_e32 v247, v247, v248
	v_lshlrev_b32_e32 v247, 4, v247
	v_and_b32_e32 v248, 7, v246
	v_lshl_or_b32 v247, v248, 7, v247
	v_bfe_u32 v248, v246, 3, 1
	v_lshl_or_b32 v247, v248, 10, v247
	v_bfe_u32 v248, v246, 8, 1
	v_lshl_or_b32 v242, v248, 13, v247
	v_xor_b32_e32 v243, 64, v242
	v_bfe_u32 v248, v246, 6, 2
	v_lshl_or_b32 v244, v248, 12, v247
	v_xor_b32_e32 v245, 64, v244
	s_mov_b32 m0, s34
	s_nop 0
	global_load_lds_dwordx4 v240, s[22:23]
	s_add_i32 s35, s31, 0x12000
	s_mov_b32 m0, s35
	s_nop 0
	global_load_lds_dwordx4 v241, s[22:23]
	s_add_u32 s8, s22, 0xe0000
	s_addc_u32 s9, s23, 0
	s_add_i32 s36, s31, 0x14000
	s_mov_b32 m0, s36
	s_nop 0
	global_load_lds_dwordx4 v240, s[8:9]
	s_add_i32 s37, s31, 0x16000
	s_mov_b32 m0, s37
	s_nop 0
	global_load_lds_dwordx4 v241, s[8:9]
	s_add_i32 s38, s31, 0x2000
	s_mov_b32 m0, s31
	s_nop 0
	global_load_lds_dwordx4 v238, s[20:21]
	s_add_u32 s8, s20, 0xe0000
	s_mov_b32 m0, s38
	s_nop 0
	global_load_lds_dwordx4 v239, s[20:21]
	s_addc_u32 s9, s21, 0
	s_add_i32 s39, s31, 0x4000
	s_mov_b32 m0, s39
	s_nop 0
	global_load_lds_dwordx4 v238, s[8:9]
	s_add_i32 s40, s31, 0x6000
	s_mov_b32 m0, s40
	s_nop 0
	global_load_lds_dwordx4 v239, s[8:9]
	s_cmp_eq_u32 s15, 1
	s_cselect_b64 s[8:9], -1, 0
	s_cmp_lg_u32 s15, 1
	s_cbranch_scc1 .LBB0_2913
	s_barrier
.LBB0_2913:
	s_add_u32 s10, s2, 0x60c92000
	v_lshrrev_b32_e32 v5, 1, v4
	s_addc_u32 s11, s3, 0
	v_and_b32_e32 v5, 24, v5
	s_add_u32 s12, s2, 0x69512000
	v_and_b32_e32 v2, 15, v4
	v_lshlrev_b32_e32 v6, 1, v5
	v_lshlrev_b32_e32 v4, 2, v4
	s_addc_u32 s13, s3, 0
	v_lshl_or_b32 v166, s15, 6, v2
	v_lshl_or_b32 v2, v2, 6, v6
	s_lshl_b32 s2, s15, 13
	v_and_b32_e32 v4, 32, v4
	v_bitop3_b32 v6, v2, s2, v4 bitop3:0xde
	s_lshl_b32 s2, s16, 5
	s_and_b32 s16, s2, 0x60
	s_ashr_i32 s5, s4, 31
	s_lshl_b32 s2, s16, 7
	v_bitop3_b32 v2, v2, s2, v4 bitop3:0xde
	s_add_u32 s2, s22, 0x80
	s_waitcnt vmcnt(2)
	s_barrier
	s_addc_u32 s3, s23, 0
	s_add_i32 s41, s31, 0x18000
	s_mov_b32 m0, s41
	s_nop 0
	global_load_lds_dwordx4 v240, s[2:3]
	s_add_i32 s42, s31, 0x1a000
	s_mov_b32 m0, s42
	s_nop 0
	global_load_lds_dwordx4 v241, s[2:3]
	s_add_u32 s2, s20, 0x80
	s_addc_u32 s3, s21, 0
	s_add_i32 s43, s31, 0x8000
	s_mov_b32 m0, s43
	s_nop 0
	global_load_lds_dwordx4 v238, s[2:3]
	s_add_i32 s44, s31, 0xa000
	s_mov_b32 m0, s44
	s_nop 0
	global_load_lds_dwordx4 v239, s[2:3]
	s_add_u32 s2, s22, 0xe0080
	s_addc_u32 s3, s23, 0
	s_add_i32 s45, s31, 0x1c000
	s_mov_b32 m0, s45
	s_nop 0
	global_load_lds_dwordx4 v240, s[2:3]
	s_add_i32 s46, s31, 0x1e000
	s_mov_b32 m0, s46
	s_nop 0
	global_load_lds_dwordx4 v241, s[2:3]
	s_waitcnt vmcnt(6)
	s_add_i32 s47, s31, 0xc000
	s_cmpk_lt_u32 s14, 0x100
	s_cselect_b64 s[14:15], -1, 0
	s_add_i32 s48, s31, 0xe000
	v_or_b32_e32 v167, s16, v5
	s_mov_b32 s49, 0
	v_add_u32_e32 v168, 0, v2
	v_add_u32_e32 v169, 0, v6
	s_mov_b64 s[16:17], s[20:21]
	s_barrier
	s_branch .LBB0_2916

; #define PG8_STAGE(bufoff, gbase, voff) do { _Pragma("unroll") for (int _i = 0; _i < 2; ++_i) \
;         glds16((const void*)(gbase), (voff)[_i], ldsbase + (unsigned)(bufoff) + ldsw + (unsigned)_i * 8192u); } while (0)
; #define PG8_LDA(dst, b, h) do { _Pragma("unroll") for (int m = 0; m < 4; ++m) _Pragma("unroll") for (int k = 0; k < 2; ++k) dst[m][k] = *(const LAS bf16x8*)(lds + PG8_SA(b, h) + aoff + m * 2048 + k * 1024); } while (0)
; #define PG8_LDB(dst, b, h) do { _Pragma("unroll") for (int n = 0; n < 2; ++n) _Pragma("unroll") for (int k = 0; k < 2; ++k) dst[n][k] = *(const LAS bf16x8*)(lds + PG8_SB(b, h) + boff + n * 2048 + k * 1024); } while (0)
; #define PG8_WAIT_V(n) asm volatile("s_waitcnt vmcnt(" #n ")" ::: "memory")
; #define PG8_WAIT_L(n) asm volatile("s_waitcnt lgkmcnt(" #n ")" ::: "memory")
; #define PG8_BAR __builtin_amdgcn_s_barrier()
; #define PG8_SCHED __builtin_amdgcn_sched_barrier(0)
;     ...
;         for (int t = 0; t < nt; t += 2) {
;             const bool last = (t == nt - 2);
;             const char* a1 = cA + (size_t)(t + 1) * kstep;
;             const char* a2 = last ? nA : cA + (size_t)(t + 2) * kstep; const char* b2 = last ? nB : cB + (size_t)(t + 2) * kstep;
;             const char* a3 = a2 + kstep; const char* b3 = b2 + kstep;
;             PG8_LDB(B0, 0, 0); PG8_LDB(B1, 0, 1); PG8_SCHED; PG8_LDA(At, 0, 0); PG8_STAGE(PG8_SA(1, 1), a1 + hstepA, voffA);
;             PG8_WAIT_V(8); PG8_WAIT_L(0); PG8_BAR; PG8_MMA(0, 0, At, B0); PG8_MMA(0, 1, At, B1); PG8_BAR; PG8_SCHED;
;             PG8_LDA(At, 0, 1); PG8_STAGE(PG8_SB(0, 0), b2, voffB); PG8_STAGE(PG8_SB(0, 1), b2 + hstepB, voffB); PG8_STAGE(PG8_SA(0, 0), a2, voffA);
;             PG8_WAIT_V(8); PG8_WAIT_L(0); PG8_BAR; PG8_MMA(1, 0, At, B0); PG8_MMA(1, 1, At, B1); PG8_BAR; PG8_SCHED;
;             PG8_LDB(B0, 1, 0); PG8_LDB(B1, 1, 1); PG8_SCHED; PG8_LDA(At, 1, 0); PG8_STAGE(PG8_SA(0, 1), a2 + hstepA, voffA);
;             PG8_WAIT_V(8); PG8_WAIT_L(0); PG8_BAR; PG8_MMA(0, 0, At, B0); PG8_MMA(0, 1, At, B1); PG8_BAR; PG8_SCHED;
;             PG8_LDA(At, 1, 1); PG8_STAGE(PG8_SB(1, 0), b3, voffB); PG8_STAGE(PG8_SB(1, 1), b3 + hstepB, voffB); PG8_STAGE(PG8_SA(1, 0), a3, voffA);
;             PG8_WAIT_V(8); PG8_WAIT_L(0); PG8_BAR; PG8_MMA(1, 0, At, B0); PG8_MMA(1, 1, At, B1); PG8_BAR; PG8_SCHED;
;         }
.LBB0_2919:
	v_add_u32_e32 v2, 0x10000, v244
	v_add_u32_e32 v246, 0x10000, v245
	ds_read_b128 v[28:31], v2
	ds_read_b128 v[32:35], v246
	ds_read_b128 v[20:23], v2 offset:2048
	ds_read_b128 v[24:27], v246 offset:2048
	v_add_u32_e32 v2, 0x14000, v244
	v_add_u32_e32 v246, 0x14000, v245
	ds_read_b128 v[12:15], v2
	ds_read_b128 v[16:19], v246
	ds_read_b128 v[4:7], v2 offset:2048
	ds_read_b128 v[8:11], v246 offset:2048
	s_add_u32 s22, s20, 0xfff20080
	s_addc_u32 s23, s21, -1
	s_cmp_eq_u32 s56, 52
	s_cselect_b32 s26, s16, s22
	s_cselect_b32 s27, s17, s23
	s_cselect_b32 s24, s18, s54
	s_cselect_b32 s25, s19, s55
	s_add_u32 s22, s26, 0x80
	s_addc_u32 s23, s27, 0
	ds_read_b128 v[176:179], v242
	ds_read_b128 v[180:183], v243
	ds_read_b128 v[206:209], v242 offset:2048
	ds_read_b128 v[210:213], v243 offset:2048
	ds_read_b128 v[214:217], v242 offset:4096
	ds_read_b128 v[218:221], v243 offset:4096
	ds_read_b128 v[222:225], v242 offset:6144
	ds_read_b128 v[226:229], v243 offset:6144
	s_mov_b32 m0, s47
	s_nop 0
	global_load_lds_dwordx4 v238, s[20:21]
	s_nop 0
	s_mov_b32 m0, s48
	s_nop 0
	global_load_lds_dwordx4 v239, s[20:21]
	s_waitcnt vmcnt(8)
	s_waitcnt lgkmcnt(0)
	s_barrier
	s_setprio 1
	s_waitcnt lgkmcnt(6)
	v_mfma_scale_f32_16x16x128_f8f6f4 v[160:163], v[28:35], v[176:183], v[160:163], v189, v193 op_sel_hi:[0,0,0]
	v_mfma_scale_f32_16x16x128_f8f6f4 v[156:159], v[20:27], v[176:183], v[156:159], v189, v193 op_sel_hi:[0,0,0]
	s_waitcnt lgkmcnt(4)
	v_mfma_scale_f32_16x16x128_f8f6f4 v[152:155], v[28:35], v[206:213], v[152:155], v189, v193 op_sel_hi:[0,0,0]
	v_mfma_scale_f32_16x16x128_f8f6f4 v[148:151], v[20:27], v[206:213], v[148:151], v189, v193 op_sel_hi:[0,0,0]
	s_waitcnt lgkmcnt(2)
	v_mfma_scale_f32_16x16x128_f8f6f4 v[132:135], v[28:35], v[214:221], v[132:135], v189, v193 op_sel_hi:[0,0,0]
	v_mfma_scale_f32_16x16x128_f8f6f4 v[124:127], v[20:27], v[214:221], v[124:127], v189, v193 op_sel_hi:[0,0,0]
	s_waitcnt lgkmcnt(0)
	v_mfma_scale_f32_16x16x128_f8f6f4 v[116:119], v[28:35], v[222:229], v[116:119], v189, v193 op_sel_hi:[0,0,0]
	v_mfma_scale_f32_16x16x128_f8f6f4 v[108:111], v[20:27], v[222:229], v[108:111], v189, v193 op_sel_hi:[0,0,0]
	s_setprio 0
	s_setprio 1
	v_mfma_scale_f32_16x16x128_f8f6f4 v[144:147], v[12:19], v[176:183], v[144:147], v189, v193 op_sel_hi:[0,0,0]
	v_mfma_scale_f32_16x16x128_f8f6f4 v[140:143], v[4:11], v[176:183], v[140:143], v189, v193 op_sel_hi:[0,0,0]
	v_mfma_scale_f32_16x16x128_f8f6f4 v[136:139], v[12:19], v[206:213], v[136:139], v189, v193 op_sel_hi:[0,0,0]
	v_mfma_scale_f32_16x16x128_f8f6f4 v[128:131], v[4:11], v[206:213], v[128:131], v189, v193 op_sel_hi:[0,0,0]
	v_mfma_scale_f32_16x16x128_f8f6f4 v[120:123], v[12:19], v[214:221], v[120:123], v189, v193 op_sel_hi:[0,0,0]
	v_mfma_scale_f32_16x16x128_f8f6f4 v[112:115], v[4:11], v[214:221], v[112:115], v189, v193 op_sel_hi:[0,0,0]
	v_mfma_scale_f32_16x16x128_f8f6f4 v[104:107], v[12:19], v[222:229], v[104:107], v189, v193 op_sel_hi:[0,0,0]
	v_mfma_scale_f32_16x16x128_f8f6f4 v[100:103], v[4:11], v[222:229], v[100:103], v189, v193 op_sel_hi:[0,0,0]
	s_setprio 0
	s_barrier
	ds_read_b128 v[176:179], v242 offset:16384
	ds_read_b128 v[180:183], v243 offset:16384
	ds_read_b128 v[206:209], v242 offset:18432
	ds_read_b128 v[210:213], v243 offset:18432
	ds_read_b128 v[214:217], v242 offset:20480
	ds_read_b128 v[218:221], v243 offset:20480
	ds_read_b128 v[222:225], v242 offset:22528
	ds_read_b128 v[226:229], v243 offset:22528
	s_mov_b32 m0, s34
	s_nop 0
	global_load_lds_dwordx4 v240, s[24:25]
	s_add_u32 s58, s24, 0xe0000
	s_mov_b32 m0, s35
	s_nop 0
	global_load_lds_dwordx4 v241, s[24:25]
	s_addc_u32 s59, s25, 0
	s_mov_b32 m0, s36
	s_nop 0
	global_load_lds_dwordx4 v240, s[58:59]
	s_nop 0
	s_mov_b32 m0, s37
	s_nop 0
	global_load_lds_dwordx4 v241, s[58:59]
	s_nop 0
	s_mov_b32 m0, s31
	s_nop 0
	global_load_lds_dwordx4 v238, s[26:27]
	s_nop 0
	s_mov_b32 m0, s38
	s_nop 0
	global_load_lds_dwordx4 v239, s[26:27]
	s_waitcnt vmcnt(8)
	s_waitcnt lgkmcnt(0)
	s_barrier
	s_setprio 1
	s_waitcnt lgkmcnt(6)
	v_mfma_scale_f32_16x16x128_f8f6f4 v[96:99], v[28:35], v[176:183], v[96:99], v189, v193 op_sel_hi:[0,0,0]
	v_mfma_scale_f32_16x16x128_f8f6f4 v[92:95], v[20:27], v[176:183], v[92:95], v189, v193 op_sel_hi:[0,0,0]
	s_waitcnt lgkmcnt(4)
	v_mfma_scale_f32_16x16x128_f8f6f4 v[84:87], v[28:35], v[206:213], v[84:87], v189, v193 op_sel_hi:[0,0,0]
	v_mfma_scale_f32_16x16x128_f8f6f4 v[76:79], v[20:27], v[206:213], v[76:79], v189, v193 op_sel_hi:[0,0,0]
	s_waitcnt lgkmcnt(2)
	v_mfma_scale_f32_16x16x128_f8f6f4 v[68:71], v[28:35], v[214:221], v[68:71], v189, v193 op_sel_hi:[0,0,0]
	v_mfma_scale_f32_16x16x128_f8f6f4 v[60:63], v[20:27], v[214:221], v[60:63], v189, v193 op_sel_hi:[0,0,0]
	s_waitcnt lgkmcnt(0)
	v_mfma_scale_f32_16x16x128_f8f6f4 v[52:55], v[28:35], v[222:229], v[52:55], v189, v193 op_sel_hi:[0,0,0]
	v_mfma_scale_f32_16x16x128_f8f6f4 v[44:47], v[20:27], v[222:229], v[44:47], v189, v193 op_sel_hi:[0,0,0]
	s_setprio 0
	s_setprio 1
	v_mfma_scale_f32_16x16x128_f8f6f4 v[88:91], v[12:19], v[176:183], v[88:91], v189, v193 op_sel_hi:[0,0,0]
	v_mfma_scale_f32_16x16x128_f8f6f4 v[80:83], v[4:11], v[176:183], v[80:83], v189, v193 op_sel_hi:[0,0,0]
	v_mfma_scale_f32_16x16x128_f8f6f4 v[72:75], v[12:19], v[206:213], v[72:75], v189, v193 op_sel_hi:[0,0,0]
	v_mfma_scale_f32_16x16x128_f8f6f4 v[64:67], v[4:11], v[206:213], v[64:67], v189, v193 op_sel_hi:[0,0,0]
	v_mfma_scale_f32_16x16x128_f8f6f4 v[56:59], v[12:19], v[214:221], v[56:59], v189, v193 op_sel_hi:[0,0,0]
	v_mfma_scale_f32_16x16x128_f8f6f4 v[48:51], v[4:11], v[214:221], v[48:51], v189, v193 op_sel_hi:[0,0,0]
	v_mfma_scale_f32_16x16x128_f8f6f4 v[40:43], v[12:19], v[222:229], v[40:43], v189, v193 op_sel_hi:[0,0,0]
	v_mfma_scale_f32_16x16x128_f8f6f4 v[36:39], v[4:11], v[222:229], v[36:39], v189, v193 op_sel_hi:[0,0,0]
	s_setprio 0
	s_barrier
; #define PG8_STAGE(bufoff, gbase, voff) do { _Pragma("unroll") for (int _i = 0; _i < 2; ++_i) \
;         glds16((const void*)(gbase), (voff)[_i], ldsbase + (unsigned)(bufoff) + ldsw + (unsigned)_i * 8192u); } while (0)
; #define PG8_LDA(dst, b, h) do { _Pragma("unroll") for (int m = 0; m < 4; ++m) _Pragma("unroll") for (int k = 0; k < 2; ++k) dst[m][k] = *(const LAS bf16x8*)(lds + PG8_SA(b, h) + aoff + m * 2048 + k * 1024); } while (0)
; #define PG8_LDB(dst, b, h) do { _Pragma("unroll") for (int n = 0; n < 2; ++n) _Pragma("unroll") for (int k = 0; k < 2; ++k) dst[n][k] = *(const LAS bf16x8*)(lds + PG8_SB(b, h) + boff + n * 2048 + k * 1024); } while (0)
; #define PG8_WAIT_V(n) asm volatile("s_waitcnt vmcnt(" #n ")" ::: "memory")
; #define PG8_WAIT_L(n) asm volatile("s_waitcnt lgkmcnt(" #n ")" ::: "memory")
; #define PG8_BAR __builtin_amdgcn_s_barrier()
; #define PG8_SCHED __builtin_amdgcn_sched_barrier(0)
;     ...
;         for (int t = 0; t < nt; t += 2) {
;             const bool last = (t == nt - 2);
;             const char* a1 = cA + (size_t)(t + 1) * kstep;
;             const char* a2 = last ? nA : cA + (size_t)(t + 2) * kstep; const char* b2 = last ? nB : cB + (size_t)(t + 2) * kstep;
;             const char* a3 = a2 + kstep; const char* b3 = b2 + kstep;
;             PG8_LDB(B0, 0, 0); PG8_LDB(B1, 0, 1); PG8_SCHED; PG8_LDA(At, 0, 0); PG8_STAGE(PG8_SA(1, 1), a1 + hstepA, voffA);
;             PG8_WAIT_V(8); PG8_WAIT_L(0); PG8_BAR; PG8_MMA(0, 0, At, B0); PG8_MMA(0, 1, At, B1); PG8_BAR; PG8_SCHED;
;             PG8_LDA(At, 0, 1); PG8_STAGE(PG8_SB(0, 0), b2, voffB); PG8_STAGE(PG8_SB(0, 1), b2 + hstepB, voffB); PG8_STAGE(PG8_SA(0, 0), a2, voffA);
;             PG8_WAIT_V(8); PG8_WAIT_L(0); PG8_BAR; PG8_MMA(1, 0, At, B0); PG8_MMA(1, 1, At, B1); PG8_BAR; PG8_SCHED;
;             PG8_LDB(B0, 1, 0); PG8_LDB(B1, 1, 1); PG8_SCHED; PG8_LDA(At, 1, 0); PG8_STAGE(PG8_SA(0, 1), a2 + hstepA, voffA);
;             PG8_WAIT_V(8); PG8_WAIT_L(0); PG8_BAR; PG8_MMA(0, 0, At, B0); PG8_MMA(0, 1, At, B1); PG8_BAR; PG8_SCHED;
;             PG8_LDA(At, 1, 1); PG8_STAGE(PG8_SB(1, 0), b3, voffB); PG8_STAGE(PG8_SB(1, 1), b3 + hstepB, voffB); PG8_STAGE(PG8_SA(1, 0), a3, voffA);
;             PG8_WAIT_V(8); PG8_WAIT_L(0); PG8_BAR; PG8_MMA(1, 0, At, B0); PG8_MMA(1, 1, At, B1); PG8_BAR; PG8_SCHED;
;         }
	v_add_u32_e32 v2, 0x18000, v244
	v_add_u32_e32 v246, 0x18000, v245
	ds_read_b128 v[20:23], v2
	ds_read_b128 v[24:27], v246
	ds_read_b128 v[28:31], v2 offset:2048
	ds_read_b128 v[32:35], v246 offset:2048
	v_add_u32_e32 v2, 0x1c000, v244
	v_add_u32_e32 v246, 0x1c000, v245
	ds_read_b128 v[12:15], v2
	ds_read_b128 v[16:19], v246
	ds_read_b128 v[4:7], v2 offset:2048
	ds_read_b128 v[8:11], v246 offset:2048
	ds_read_b128 v[176:179], v242 offset:32768
	ds_read_b128 v[180:183], v243 offset:32768
	ds_read_b128 v[206:209], v242 offset:34816
	ds_read_b128 v[210:213], v243 offset:34816
	ds_read_b128 v[214:217], v242 offset:36864
	ds_read_b128 v[218:221], v243 offset:36864
	ds_read_b128 v[222:225], v242 offset:38912
	ds_read_b128 v[226:229], v243 offset:38912
	s_add_u32 s26, s26, 0xe0000
	s_addc_u32 s27, s27, 0
	s_mov_b32 m0, s39
	s_nop 0
	global_load_lds_dwordx4 v238, s[26:27]
	s_nop 0
	s_mov_b32 m0, s40
	s_nop 0
	global_load_lds_dwordx4 v239, s[26:27]
	s_waitcnt vmcnt(8)
	s_waitcnt lgkmcnt(0)
	s_barrier
	s_setprio 1
	s_waitcnt lgkmcnt(6)
	v_mfma_scale_f32_16x16x128_f8f6f4 v[160:163], v[20:27], v[176:183], v[160:163], v189, v193 op_sel_hi:[0,0,0]
	v_mfma_scale_f32_16x16x128_f8f6f4 v[156:159], v[28:35], v[176:183], v[156:159], v189, v193 op_sel_hi:[0,0,0]
	s_waitcnt lgkmcnt(4)
	v_mfma_scale_f32_16x16x128_f8f6f4 v[152:155], v[20:27], v[206:213], v[152:155], v189, v193 op_sel_hi:[0,0,0]
	v_mfma_scale_f32_16x16x128_f8f6f4 v[148:151], v[28:35], v[206:213], v[148:151], v189, v193 op_sel_hi:[0,0,0]
	s_waitcnt lgkmcnt(2)
	v_mfma_scale_f32_16x16x128_f8f6f4 v[132:135], v[20:27], v[214:221], v[132:135], v189, v193 op_sel_hi:[0,0,0]
	v_mfma_scale_f32_16x16x128_f8f6f4 v[124:127], v[28:35], v[214:221], v[124:127], v189, v193 op_sel_hi:[0,0,0]
	s_waitcnt lgkmcnt(0)
	v_mfma_scale_f32_16x16x128_f8f6f4 v[116:119], v[20:27], v[222:229], v[116:119], v189, v193 op_sel_hi:[0,0,0]
	v_mfma_scale_f32_16x16x128_f8f6f4 v[108:111], v[28:35], v[222:229], v[108:111], v189, v193 op_sel_hi:[0,0,0]
	s_setprio 0
	s_setprio 1
	v_mfma_scale_f32_16x16x128_f8f6f4 v[144:147], v[12:19], v[176:183], v[144:147], v189, v193 op_sel_hi:[0,0,0]
	v_mfma_scale_f32_16x16x128_f8f6f4 v[140:143], v[4:11], v[176:183], v[140:143], v189, v193 op_sel_hi:[0,0,0]
	v_mfma_scale_f32_16x16x128_f8f6f4 v[136:139], v[12:19], v[206:213], v[136:139], v189, v193 op_sel_hi:[0,0,0]
	v_mfma_scale_f32_16x16x128_f8f6f4 v[128:131], v[4:11], v[206:213], v[128:131], v189, v193 op_sel_hi:[0,0,0]
	v_mfma_scale_f32_16x16x128_f8f6f4 v[120:123], v[12:19], v[214:221], v[120:123], v189, v193 op_sel_hi:[0,0,0]
	v_mfma_scale_f32_16x16x128_f8f6f4 v[112:115], v[4:11], v[214:221], v[112:115], v189, v193 op_sel_hi:[0,0,0]
	v_mfma_scale_f32_16x16x128_f8f6f4 v[104:107], v[12:19], v[222:229], v[104:107], v189, v193 op_sel_hi:[0,0,0]
	v_mfma_scale_f32_16x16x128_f8f6f4 v[100:103], v[4:11], v[222:229], v[100:103], v189, v193 op_sel_hi:[0,0,0]
	s_setprio 0
	s_barrier
	ds_read_b128 v[176:179], v242 offset:49152
	ds_read_b128 v[180:183], v243 offset:49152
	ds_read_b128 v[206:209], v242 offset:51200
	ds_read_b128 v[210:213], v243 offset:51200
	ds_read_b128 v[214:217], v242 offset:53248
	ds_read_b128 v[218:221], v243 offset:53248
	ds_read_b128 v[222:225], v242 offset:55296
	ds_read_b128 v[226:229], v243 offset:55296
	s_add_u32 s26, s24, 0x80
	s_addc_u32 s27, s25, 0
	s_mov_b32 m0, s41
	s_nop 0
	global_load_lds_dwordx4 v240, s[26:27]
	s_add_u32 s24, s24, 0xe0080
	s_mov_b32 m0, s42
	s_nop 0
	global_load_lds_dwordx4 v241, s[26:27]
	s_addc_u32 s25, s25, 0
	s_mov_b32 m0, s45
	s_nop 0
	global_load_lds_dwordx4 v240, s[24:25]
	s_nop 0
	s_mov_b32 m0, s46
	s_nop 0
	global_load_lds_dwordx4 v241, s[24:25]
	s_mov_b32 m0, s43
	s_nop 0
	global_load_lds_dwordx4 v238, s[22:23]
	s_nop 0
	s_mov_b32 m0, s44
	s_nop 0
	global_load_lds_dwordx4 v239, s[22:23]
	s_waitcnt vmcnt(8)
	s_waitcnt lgkmcnt(0)
	s_barrier
	s_setprio 1
	s_waitcnt lgkmcnt(6)
	v_mfma_scale_f32_16x16x128_f8f6f4 v[96:99], v[20:27], v[176:183], v[96:99], v189, v193 op_sel_hi:[0,0,0]
	v_mfma_scale_f32_16x16x128_f8f6f4 v[92:95], v[28:35], v[176:183], v[92:95], v189, v193 op_sel_hi:[0,0,0]
	s_waitcnt lgkmcnt(4)
	v_mfma_scale_f32_16x16x128_f8f6f4 v[84:87], v[20:27], v[206:213], v[84:87], v189, v193 op_sel_hi:[0,0,0]
	v_mfma_scale_f32_16x16x128_f8f6f4 v[76:79], v[28:35], v[206:213], v[76:79], v189, v193 op_sel_hi:[0,0,0]
	s_waitcnt lgkmcnt(2)
	v_mfma_scale_f32_16x16x128_f8f6f4 v[68:71], v[20:27], v[214:221], v[68:71], v189, v193 op_sel_hi:[0,0,0]
	v_mfma_scale_f32_16x16x128_f8f6f4 v[60:63], v[28:35], v[214:221], v[60:63], v189, v193 op_sel_hi:[0,0,0]
	s_waitcnt lgkmcnt(0)
	v_mfma_scale_f32_16x16x128_f8f6f4 v[52:55], v[20:27], v[222:229], v[52:55], v189, v193 op_sel_hi:[0,0,0]
	v_mfma_scale_f32_16x16x128_f8f6f4 v[44:47], v[28:35], v[222:229], v[44:47], v189, v193 op_sel_hi:[0,0,0]
	s_setprio 0
	s_setprio 1
	v_mfma_scale_f32_16x16x128_f8f6f4 v[88:91], v[12:19], v[176:183], v[88:91], v189, v193 op_sel_hi:[0,0,0]
	v_mfma_scale_f32_16x16x128_f8f6f4 v[80:83], v[4:11], v[176:183], v[80:83], v189, v193 op_sel_hi:[0,0,0]
	v_mfma_scale_f32_16x16x128_f8f6f4 v[72:75], v[12:19], v[206:213], v[72:75], v189, v193 op_sel_hi:[0,0,0]
	v_mfma_scale_f32_16x16x128_f8f6f4 v[64:67], v[4:11], v[206:213], v[64:67], v189, v193 op_sel_hi:[0,0,0]
	v_mfma_scale_f32_16x16x128_f8f6f4 v[56:59], v[12:19], v[214:221], v[56:59], v189, v193 op_sel_hi:[0,0,0]
	v_mfma_scale_f32_16x16x128_f8f6f4 v[48:51], v[4:11], v[214:221], v[48:51], v189, v193 op_sel_hi:[0,0,0]
	v_mfma_scale_f32_16x16x128_f8f6f4 v[40:43], v[12:19], v[222:229], v[40:43], v189, v193 op_sel_hi:[0,0,0]
	v_mfma_scale_f32_16x16x128_f8f6f4 v[36:39], v[4:11], v[222:229], v[36:39], v189, v193 op_sel_hi:[0,0,0]
	s_setprio 0
	s_barrier
	s_add_i32 s56, s56, 2
	s_add_u32 s54, s54, 0x100
	s_addc_u32 s55, s55, 0
	s_add_u32 s20, s20, 0x100
	s_addc_u32 s21, s21, 0
	s_cmp_gt_u32 s56, 53
	s_cbranch_scc0 .LBB0_2919
	s_and_b64 vcc, exec, s[14:15]
	s_cbranch_vccz .LBB0_2922
	s_barrier

; __device__ __forceinline__ int lane_id() { int l_; asm volatile("v_mbcnt_lo_u32_b32 %0, -1, 0\n\tv_mbcnt_hi_u32_b32 %0, -1, %0" : "=v"(l_)); return l_; }
; #define PG8_STAGE(bufoff, gbase, voff) do { _Pragma("unroll") for (int _i = 0; _i < 2; ++_i) \
;         glds16((const void*)(gbase), (voff)[_i], ldsbase + (unsigned)(bufoff) + ldsw + (unsigned)_i * 8192u); } while (0)
; #define PG8_WAIT_V(n) asm volatile("s_waitcnt vmcnt(" #n ")" ::: "memory")
; #define PG8_BAR __builtin_amdgcn_s_barrier()
;     const int sB1 = sB1_ < 0 ? sB : sB1_;
;     int tid = w0_ * 64 + lane_id(); asm volatile("" : "+v"(tid));
;     const int wid = __builtin_amdgcn_readfirstlane(tid >> 6), lane = tid & 63, wr = wid >> 2, wc = wid & 3, fr = lane & 15, fq = lane >> 4;
;     const int nt = nt_ ? nt_ : Kb / 128;
;     unsigned voffA[2], voffB[2];
; #pragma unroll
;     for (int i = 0; i < 2; ++i) { int R, C; stage_rc(tid * 16 + i * 8192, R, C); const int Rb = Epi::PERM ? ((R & ~31) + perm32(R & 31)) : R;
;         voffA[i] = (unsigned)(R * ldab + C * 2); voffB[i] = (unsigned)(Rb * Kb + C * 2); }
;     const size_t kstep = (size_t)(BK * 2);
;     const size_t hstepA = (size_t)HALF * ldab, hstepB = (size_t)HALF * Kb;
;     const unsigned ldsw = (unsigned)wid * 1024u, ldsbase = (unsigned)(size_t)lds;
;     const int aoff = lds_byte(wr * 64 + fr, fq * 8), boff = lds_byte(wc * 32 + fr, fq * 8);
;     ...
;     const char* cA = uniform_ptr(cur.a); const char* cB = uniform_ptr(cur.b);
;     PG8_STAGE(PG8_SB(0, 0), cB, voffB); PG8_STAGE(PG8_SB(0, 1), cB + hstepB, voffB); PG8_STAGE(PG8_SA(0, 0), cA, voffA); PG8_STAGE(PG8_SA(0, 1), cA + hstepA, voffA);
;     if (wr == 1) PG8_BAR;
;     PG8_WAIT_V(2); PG8_BAR;
;     PG8_STAGE(PG8_SB(1, 0), cB + kstep, voffB); PG8_STAGE(PG8_SA(1, 0), cA + kstep, voffA); PG8_STAGE(PG8_SB(1, 1), cB + hstepB + kstep, voffB);
;     PG8_WAIT_V(6); PG8_BAR;
.LBB0_3046:
	v_readlane_b32 s2, v252, 50
	v_readlane_b32 s3, v252, 51
	s_andn2_b64 vcc, exec, s[2:3]
	s_cbranch_vccnz .LBB0_3115
	s_mov_b64 s[2:3], 0
	v_mbcnt_lo_u32_b32 v0, -1, 0
	v_mbcnt_hi_u32_b32 v0, -1, v0
	v_readlane_b32 s0, v250, 60
	v_readlane_b32 s4, v252, 52
	v_readlane_b32 s5, v252, 53
	v_add_u32_e32 v0, s0, v0
	s_andn2_b64 vcc, exec, s[4:5]
	v_mbcnt_lo_u32_b32 v0, -1, 0
	v_mbcnt_hi_u32_b32 v0, -1, v0
	s_nop 0
	v_add_u32_e32 v0, s0, v0
	s_nop 0
	v_readfirstlane_b32 s10, v0
	s_cbranch_vccnz .LBB0_3063
	v_bfe_i32 v4, v0, 27, 1
	v_lshlrev_b32_e32 v2, 4, v0
	v_lshrrev_b32_e32 v4, 22, v4
	v_add_u32_e32 v4, v2, v4
	v_and_b32_e32 v4, 0xfffffc00, v4
	v_sub_u32_e32 v4, v2, v4
	s_waitcnt lgkmcnt(0)
	v_ashrrev_i32_e32 v1, 31, v0
	v_lshrrev_b32_e32 v5, 4, v4
	v_lshrrev_b32_e32 v1, 26, v1
	v_bitop3_b32 v4, v5, v4, 32 bitop3:0x6c
	v_add_u32_e32 v1, v0, v1
	v_ashrrev_i32_e32 v6, 31, v4
	v_ashrrev_i32_e32 v1, 6, v1
	v_lshrrev_b32_e32 v6, 26, v6
	v_lshlrev_b32_e32 v5, 3, v1
	v_add_u32_e32 v6, v4, v6
	v_and_b32_e32 v5, -16, v5
	v_ashrrev_i32_e32 v7, 6, v6
	v_and_b32_e32 v6, 0xc0, v6
	v_add_u32_e32 v5, v7, v5
	v_sub_u32_e32 v4, v4, v6
	v_lshlrev_b32_e32 v1, 5, v1
	v_ashrrev_i16_sdwa v4, v188, sext(v4) dst_sel:DWORD dst_unused:UNUSED_PAD src0_sel:DWORD src1_sel:BYTE_0
	v_lshlrev_b32_e32 v6, 1, v5
	v_lshrrev_b32_e32 v8, 2, v5
	v_and_b32_e32 v7, 3, v7
	s_mov_b32 s4, 0xfffe0
	v_and_b32_e32 v1, 32, v1
	v_bfe_i32 v4, v4, 0, 16
	v_and_b32_e32 v6, 24, v6
	v_and_b32_e32 v8, 4, v8
	v_and_or_b32 v7, v5, s4, v7
	v_or3_b32 v6, v7, v8, v6
	v_add_lshl_u32 v4, v1, v4, 1
	v_add_u32_e32 v2, 0x2000, v2
	v_lshl_add_u32 v1, v5, 12, v4
	s_waitcnt vmcnt(0)
	v_lshl_add_u32 v137, v6, 12, v4
	v_ashrrev_i32_e32 v4, 31, v2
	v_lshrrev_b32_e32 v4, 22, v4
	v_add_u32_e32 v4, v2, v4
	v_ashrrev_i32_e32 v4, 10, v4
	v_mul_i32_i24_e32 v5, 0x400, v4
	v_sub_u32_e32 v2, v2, v5
	v_lshrrev_b32_e32 v5, 4, v2
	s_add_u32 s8, s80, s2
	v_bitop3_b32 v2, v5, v2, 32 bitop3:0x6c
	s_addc_u32 s3, s81, s3
	v_ashrrev_i32_e32 v6, 31, v2
	s_add_u32 s0, s8, 0x32892000
	v_lshrrev_b32_e32 v6, 26, v6
	s_addc_u32 s28, s3, 0
	v_lshlrev_b32_e32 v5, 3, v4
	v_add_u32_e32 v6, v2, v6
	s_add_u32 s29, s8, 0x4300000
	v_and_b32_e32 v5, -16, v5
	v_ashrrev_i32_e32 v7, 6, v6
	s_addc_u32 s30, s3, 0
	v_add_u32_e32 v5, v7, v5
	v_and_b32_e32 v7, 3, v7
	s_ashr_i32 s11, s10, 6
	s_ashr_i32 s2, s10, 8
	v_and_or_b32 v7, v5, s4, v7
	s_lshl_b32 s4, s11, 10
	v_readlane_b32 s6, v253, 24
	v_and_b32_e32 v6, 0xc0, v6
	v_readlane_b32 s7, v253, 25
	s_add_u32 s22, s29, s6
	v_sub_u32_e32 v2, v2, v6
	s_addc_u32 s23, s30, s7
	v_readlane_b32 s6, v253, 32
	v_lshlrev_b32_e32 v4, 5, v4
	v_ashrrev_i16_sdwa v2, v188, sext(v2) dst_sel:DWORD dst_unused:UNUSED_PAD src0_sel:DWORD src1_sel:BYTE_0
	v_lshlrev_b32_e32 v6, 1, v5
	v_lshrrev_b32_e32 v8, 2, v5
	v_readlane_b32 s7, v253, 33
	s_add_u32 s20, s0, s6
	v_and_b32_e32 v4, 32, v4
	v_bfe_i32 v2, v2, 0, 16
	v_and_b32_e32 v6, 24, v6
	v_and_b32_e32 v8, 4, v8
	s_addc_u32 s21, s28, s7
	s_add_i32 s31, s4, 0
	v_or3_b32 v6, v7, v8, v6
	v_add_lshl_u32 v2, v4, v2, 1
	s_add_i32 s34, s31, 0x10000
	s_nop 0
	v_readlane_b32 s70, v250, 60
	v_mbcnt_lo_u32_b32 v246, -1, 0
	v_mbcnt_hi_u32_b32 v246, -1, v246
	v_add_u32_e32 v246, s70, v246
	v_bfe_u32 v247, v246, 4, 2
	v_bfe_u32 v248, v246, 6, 1
	v_lshl_or_b32 v247, v248, 2, v247
	v_and_b32_e32 v248, 7, v246
	v_xor_b32_e32 v247, v247, v248
	v_lshlrev_b32_e32 v247, 4, v247
	v_lshrrev_b32_e32 v248, 3, v246
	v_lshl_add_u32 v238, v248, 12, v247
	v_add_u32_e32 v239, 0x40000, v238
	v_and_b32_e32 v249, 0x23, v248
	v_and_b32_e32 v244, 12, v248
	v_lshl_or_b32 v249, v244, 1, v249
	v_bfe_u32 v244, v248, 4, 1
	v_lshl_or_b32 v249, v244, 2, v249
	v_lshl_add_u32 v240, v249, 12, v247
	v_add_u32_e32 v241, 0x40000, v240
	v_bfe_u32 v247, v246, 4, 2
	v_bfe_u32 v248, v246, 1, 3
	v_xor_b32_e32 v247, v247, v248
	v_lshlrev_b32_e32 v247, 4, v247
	v_and_b32_e32 v248, 7, v246
	v_lshl_or_b32 v247, v248, 7, v247
	v_bfe_u32 v248, v246, 3, 1
	v_lshl_or_b32 v247, v248, 10, v247
	v_bfe_u32 v248, v246, 8, 1
	v_lshl_or_b32 v242, v248, 13, v247
	v_xor_b32_e32 v243, 64, v242
	v_bfe_u32 v248, v246, 6, 2
	v_lshl_or_b32 v244, v248, 12, v247
	v_xor_b32_e32 v245, 64, v244
	s_mov_b32 m0, s34
	s_nop 0
	global_load_lds_dwordx4 v240, s[22:23]
	v_lshl_add_u32 v141, v6, 12, v2
	s_add_i32 s35, s31, 0x12000
	s_mov_b32 m0, s35
	s_nop 0
	global_load_lds_dwordx4 v241, s[22:23]
	s_add_u32 s4, s22, 0x80000
	s_addc_u32 s5, s23, 0
	s_add_i32 s36, s31, 0x14000
	s_mov_b32 m0, s36
	s_nop 0
	global_load_lds_dwordx4 v240, s[4:5]
	s_add_i32 s37, s31, 0x16000
	s_mov_b32 m0, s37
	s_nop 0
	global_load_lds_dwordx4 v241, s[4:5]
	s_mov_b32 m0, s31
	s_nop 0
	global_load_lds_dwordx4 v238, s[20:21]
	v_lshl_add_u32 v139, v5, 12, v2
	s_add_i32 s38, s31, 0x2000
	s_mov_b32 m0, s38
	s_nop 0
	global_load_lds_dwordx4 v239, s[20:21]
	s_add_u32 s4, s20, 0x80000
	s_addc_u32 s5, s21, 0
	s_add_i32 s39, s31, 0x4000
	s_mov_b32 m0, s39
	s_nop 0
	global_load_lds_dwordx4 v238, s[4:5]
	s_add_i32 s40, s31, 0x6000
	s_mov_b32 m0, s40
	s_nop 0
	global_load_lds_dwordx4 v239, s[4:5]
	s_cmp_eq_u32 s2, 1
	s_cselect_b64 s[4:5], -1, 0
	s_cmp_lg_u32 s2, 1
	s_cbranch_scc1 .LBB0_3050
	s_barrier
.LBB0_3050:
	s_add_u32 s6, s8, 0x3a892000
	v_lshrrev_b32_e32 v4, 1, v0
	s_addc_u32 s7, s3, 0
	v_and_b32_e32 v4, 24, v4
	s_add_u32 s8, s8, 0x32882000
	v_and_b32_e32 v2, 15, v0
	v_lshlrev_b32_e32 v5, 1, v4
	v_lshlrev_b32_e32 v0, 2, v0
	s_addc_u32 s9, s3, 0
	v_lshl_or_b32 v145, s2, 6, v2
	v_lshl_or_b32 v2, v2, 6, v5
	s_lshl_b32 s2, s2, 13
	v_and_b32_e32 v0, 32, v0
	v_bitop3_b32 v5, v2, s2, v0 bitop3:0xde
	s_lshl_b32 s2, s11, 5
	s_and_b32 s12, s2, 0x60
	s_lshl_b32 s2, s12, 7
	v_bitop3_b32 v0, v2, s2, v0 bitop3:0xde
	s_add_u32 s2, s22, 0x80
	s_waitcnt vmcnt(2)
	s_barrier
	s_addc_u32 s3, s23, 0
	s_add_i32 s41, s31, 0x18000
	s_mov_b32 m0, s41
	s_nop 0
	global_load_lds_dwordx4 v240, s[2:3]
	s_add_i32 s42, s31, 0x1a000
	s_mov_b32 m0, s42
	s_nop 0
	global_load_lds_dwordx4 v241, s[2:3]
	s_add_u32 s2, s20, 0x80
	s_addc_u32 s3, s21, 0
	s_add_i32 s43, s31, 0x8000
	s_mov_b32 m0, s43
	s_nop 0
	global_load_lds_dwordx4 v238, s[2:3]
	s_add_i32 s44, s31, 0xa000
	s_mov_b32 m0, s44
	s_nop 0
	global_load_lds_dwordx4 v239, s[2:3]
	s_add_u32 s2, s22, 0x80080
	s_addc_u32 s3, s23, 0
	s_add_i32 s45, s31, 0x1c000
	s_mov_b32 m0, s45
	s_nop 0
	global_load_lds_dwordx4 v240, s[2:3]
	s_add_i32 s46, s31, 0x1e000
	s_mov_b32 m0, s46
	s_nop 0
	global_load_lds_dwordx4 v241, s[2:3]
	s_waitcnt vmcnt(6)
	s_add_i32 s47, s31, 0xc000
	s_cmpk_lt_u32 s10, 0x100
	v_readlane_b32 s2, v253, 30
	s_cselect_b64 s[10:11], -1, 0
	s_add_i32 s48, s31, 0xe000
	v_or_b32_e32 v149, s12, v4
	s_mov_b32 s49, 0
	v_add_u32_e32 v152, 0, v0
	v_add_u32_e32 v153, 0, v5
	v_readlane_b32 s50, v253, 23
	s_mov_b32 s51, s2
	s_mov_b64 s[18:19], s[22:23]
	s_mov_b64 s[16:17], s[20:21]
	s_barrier
	v_readlane_b32 s3, v253, 31
	s_branch .LBB0_3053

; #define PG8_STAGE(bufoff, gbase, voff) do { _Pragma("unroll") for (int _i = 0; _i < 2; ++_i) \
;         glds16((const void*)(gbase), (voff)[_i], ldsbase + (unsigned)(bufoff) + ldsw + (unsigned)_i * 8192u); } while (0)
; #define PG8_LDA(dst, b, h) do { _Pragma("unroll") for (int m = 0; m < 4; ++m) _Pragma("unroll") for (int k = 0; k < 2; ++k) dst[m][k] = *(const LAS bf16x8*)(lds + PG8_SA(b, h) + aoff + m * 2048 + k * 1024); } while (0)
; #define PG8_LDB(dst, b, h) do { _Pragma("unroll") for (int n = 0; n < 2; ++n) _Pragma("unroll") for (int k = 0; k < 2; ++k) dst[n][k] = *(const LAS bf16x8*)(lds + PG8_SB(b, h) + boff + n * 2048 + k * 1024); } while (0)
; #define PG8_WAIT_V(n) asm volatile("s_waitcnt vmcnt(" #n ")" ::: "memory")
; #define PG8_WAIT_L(n) asm volatile("s_waitcnt lgkmcnt(" #n ")" ::: "memory")
; #define PG8_BAR __builtin_amdgcn_s_barrier()
; #define PG8_SCHED __builtin_amdgcn_sched_barrier(0)
;     ...
;         for (int t = 0; t < nt; t += 2) {
;             const bool last = (t == nt - 2);
;             const char* a1 = cA + (size_t)(t + 1) * kstep;
;             const char* a2 = last ? nA : cA + (size_t)(t + 2) * kstep; const char* b2 = last ? nB : cB + (size_t)(t + 2) * kstep;
;             const char* a3 = a2 + kstep; const char* b3 = b2 + kstep;
;             PG8_LDB(B0, 0, 0); PG8_LDB(B1, 0, 1); PG8_SCHED; PG8_LDA(At, 0, 0); PG8_STAGE(PG8_SA(1, 1), a1 + hstepA, voffA);
;             PG8_WAIT_V(8); PG8_WAIT_L(0); PG8_BAR; PG8_MMA(0, 0, At, B0); PG8_MMA(0, 1, At, B1); PG8_BAR; PG8_SCHED;
;             PG8_LDA(At, 0, 1); PG8_STAGE(PG8_SB(0, 0), b2, voffB); PG8_STAGE(PG8_SB(0, 1), b2 + hstepB, voffB); PG8_STAGE(PG8_SA(0, 0), a2, voffA);
;             PG8_WAIT_V(8); PG8_WAIT_L(0); PG8_BAR; PG8_MMA(1, 0, At, B0); PG8_MMA(1, 1, At, B1); PG8_BAR; PG8_SCHED;
;             PG8_LDB(B0, 1, 0); PG8_LDB(B1, 1, 1); PG8_SCHED; PG8_LDA(At, 1, 0); PG8_STAGE(PG8_SA(0, 1), a2 + hstepA, voffA);
;             PG8_WAIT_V(8); PG8_WAIT_L(0); PG8_BAR; PG8_MMA(0, 0, At, B0); PG8_MMA(0, 1, At, B1); PG8_BAR; PG8_SCHED;
;             PG8_LDA(At, 1, 1); PG8_STAGE(PG8_SB(1, 0), b3, voffB); PG8_STAGE(PG8_SB(1, 1), b3 + hstepB, voffB); PG8_STAGE(PG8_SA(1, 0), a3, voffA);
;             PG8_WAIT_V(8); PG8_WAIT_L(0); PG8_BAR; PG8_MMA(1, 0, At, B0); PG8_MMA(1, 1, At, B1); PG8_BAR; PG8_SCHED;
;         }
.LBB0_3056:
	v_add_u32_e32 v0, 0x10000, v244
	v_add_u32_e32 v246, 0x10000, v245
	ds_read_b128 v[132:135], v0
	ds_read_b128 v[154:157], v246
	ds_read_b128 v[158:161], v0 offset:2048
	ds_read_b128 v[162:165], v246 offset:2048
	v_add_u32_e32 v0, 0x14000, v244
	v_add_u32_e32 v246, 0x14000, v245
	ds_read_b128 v[166:169], v0
	ds_read_b128 v[170:173], v246
	ds_read_b128 v[174:177], v0 offset:2048
	ds_read_b128 v[178:181], v246 offset:2048
	s_add_u32 s22, s20, 0xfff80080
	s_addc_u32 s23, s21, -1
	s_cmp_eq_u32 s52, 28
	s_cselect_b32 s26, s16, s22
	s_cselect_b32 s27, s17, s23
	s_cselect_b32 s24, s18, s13
	s_cselect_b32 s25, s19, s15
	s_add_u32 s22, s26, 0x80
	s_addc_u32 s23, s27, 0
	ds_read_b128 v[182:185], v242
	ds_read_b128 v[196:199], v243
	ds_read_b128 v[206:209], v242 offset:2048
	ds_read_b128 v[210:213], v243 offset:2048
	ds_read_b128 v[214:217], v242 offset:4096
	ds_read_b128 v[218:221], v243 offset:4096
	ds_read_b128 v[222:225], v242 offset:6144
	ds_read_b128 v[226:229], v243 offset:6144
	s_mov_b32 m0, s47
	s_nop 0
	global_load_lds_dwordx4 v238, s[20:21]
	s_nop 0
	s_mov_b32 m0, s48
	s_nop 0
	global_load_lds_dwordx4 v239, s[20:21]
	s_waitcnt vmcnt(8)
	s_waitcnt lgkmcnt(0)
	s_barrier
	s_setprio 1
	s_waitcnt lgkmcnt(7)
	v_mfma_f32_16x16x32_bf16 v[128:131], v[132:135], v[182:185], v[128:131]
	v_mfma_f32_16x16x32_bf16 v[124:127], v[158:161], v[182:185], v[124:127]
	s_waitcnt lgkmcnt(5)
	v_mfma_f32_16x16x32_bf16 v[112:115], v[132:135], v[206:209], v[112:115]
	v_mfma_f32_16x16x32_bf16 v[108:111], v[158:161], v[206:209], v[108:111]
	s_waitcnt lgkmcnt(3)
	v_mfma_f32_16x16x32_bf16 v[96:99], v[132:135], v[214:217], v[96:99]
	v_mfma_f32_16x16x32_bf16 v[92:95], v[158:161], v[214:217], v[92:95]
	s_waitcnt lgkmcnt(1)
	v_mfma_f32_16x16x32_bf16 v[80:83], v[132:135], v[222:225], v[80:83]
	v_mfma_f32_16x16x32_bf16 v[76:79], v[158:161], v[222:225], v[76:79]
	v_mfma_f32_16x16x32_bf16 v[128:131], v[154:157], v[196:199], v[128:131]
	v_mfma_f32_16x16x32_bf16 v[124:127], v[162:165], v[196:199], v[124:127]
	v_mfma_f32_16x16x32_bf16 v[112:115], v[154:157], v[210:213], v[112:115]
	v_mfma_f32_16x16x32_bf16 v[108:111], v[162:165], v[210:213], v[108:111]
	v_mfma_f32_16x16x32_bf16 v[96:99], v[154:157], v[218:221], v[96:99]
	v_mfma_f32_16x16x32_bf16 v[92:95], v[162:165], v[218:221], v[92:95]
	s_waitcnt lgkmcnt(0)
	v_mfma_f32_16x16x32_bf16 v[80:83], v[154:157], v[226:229], v[80:83]
	v_mfma_f32_16x16x32_bf16 v[76:79], v[162:165], v[226:229], v[76:79]
	s_setprio 0
	s_setprio 1
	v_mfma_f32_16x16x32_bf16 v[120:123], v[166:169], v[182:185], v[120:123]
	v_mfma_f32_16x16x32_bf16 v[116:119], v[174:177], v[182:185], v[116:119]
	v_mfma_f32_16x16x32_bf16 v[104:107], v[166:169], v[206:209], v[104:107]
	v_mfma_f32_16x16x32_bf16 v[100:103], v[174:177], v[206:209], v[100:103]
	v_mfma_f32_16x16x32_bf16 v[88:91], v[166:169], v[214:217], v[88:91]
	v_mfma_f32_16x16x32_bf16 v[84:87], v[174:177], v[214:217], v[84:87]
	v_mfma_f32_16x16x32_bf16 v[72:75], v[166:169], v[222:225], v[72:75]
	v_mfma_f32_16x16x32_bf16 v[68:71], v[174:177], v[222:225], v[68:71]
	v_mfma_f32_16x16x32_bf16 v[120:123], v[170:173], v[196:199], v[120:123]
	v_mfma_f32_16x16x32_bf16 v[116:119], v[178:181], v[196:199], v[116:119]
	v_mfma_f32_16x16x32_bf16 v[104:107], v[170:173], v[210:213], v[104:107]
	v_mfma_f32_16x16x32_bf16 v[100:103], v[178:181], v[210:213], v[100:103]
	v_mfma_f32_16x16x32_bf16 v[88:91], v[170:173], v[218:221], v[88:91]
	v_mfma_f32_16x16x32_bf16 v[84:87], v[178:181], v[218:221], v[84:87]
	v_mfma_f32_16x16x32_bf16 v[72:75], v[170:173], v[226:229], v[72:75]
	v_mfma_f32_16x16x32_bf16 v[68:71], v[178:181], v[226:229], v[68:71]
	s_setprio 0
	s_barrier
	ds_read_b128 v[182:185], v242 offset:16384
	ds_read_b128 v[196:199], v243 offset:16384
	ds_read_b128 v[206:209], v242 offset:18432
	ds_read_b128 v[210:213], v243 offset:18432
	ds_read_b128 v[214:217], v242 offset:20480
	ds_read_b128 v[218:221], v243 offset:20480
	ds_read_b128 v[222:225], v242 offset:22528
	ds_read_b128 v[226:229], v243 offset:22528
	s_mov_b32 m0, s34
	s_nop 0
	global_load_lds_dwordx4 v240, s[24:25]
	s_add_u32 s54, s24, 0x80000
	s_mov_b32 m0, s35
	s_nop 0
	global_load_lds_dwordx4 v241, s[24:25]
	s_addc_u32 s55, s25, 0
	s_mov_b32 m0, s36
	s_nop 0
	global_load_lds_dwordx4 v240, s[54:55]
	s_nop 0
	s_mov_b32 m0, s37
	s_nop 0
	global_load_lds_dwordx4 v241, s[54:55]
	s_nop 0
	s_mov_b32 m0, s31
	s_nop 0
	global_load_lds_dwordx4 v238, s[26:27]
	s_nop 0
	s_mov_b32 m0, s38
	s_nop 0
	global_load_lds_dwordx4 v239, s[26:27]
	s_waitcnt vmcnt(8)
	s_waitcnt lgkmcnt(0)
	s_barrier
; #define PG8_STAGE(bufoff, gbase, voff) do { _Pragma("unroll") for (int _i = 0; _i < 2; ++_i) \
;         glds16((const void*)(gbase), (voff)[_i], ldsbase + (unsigned)(bufoff) + ldsw + (unsigned)_i * 8192u); } while (0)
; #define PG8_LDA(dst, b, h) do { _Pragma("unroll") for (int m = 0; m < 4; ++m) _Pragma("unroll") for (int k = 0; k < 2; ++k) dst[m][k] = *(const LAS bf16x8*)(lds + PG8_SA(b, h) + aoff + m * 2048 + k * 1024); } while (0)
; #define PG8_LDB(dst, b, h) do { _Pragma("unroll") for (int n = 0; n < 2; ++n) _Pragma("unroll") for (int k = 0; k < 2; ++k) dst[n][k] = *(const LAS bf16x8*)(lds + PG8_SB(b, h) + boff + n * 2048 + k * 1024); } while (0)
; #define PG8_WAIT_V(n) asm volatile("s_waitcnt vmcnt(" #n ")" ::: "memory")
; #define PG8_WAIT_L(n) asm volatile("s_waitcnt lgkmcnt(" #n ")" ::: "memory")
; #define PG8_BAR __builtin_amdgcn_s_barrier()
; #define PG8_SCHED __builtin_amdgcn_sched_barrier(0)
;     ...
;         for (int t = 0; t < nt; t += 2) {
;             const bool last = (t == nt - 2);
;             const char* a1 = cA + (size_t)(t + 1) * kstep;
;             const char* a2 = last ? nA : cA + (size_t)(t + 2) * kstep; const char* b2 = last ? nB : cB + (size_t)(t + 2) * kstep;
;             const char* a3 = a2 + kstep; const char* b3 = b2 + kstep;
;             PG8_LDB(B0, 0, 0); PG8_LDB(B1, 0, 1); PG8_SCHED; PG8_LDA(At, 0, 0); PG8_STAGE(PG8_SA(1, 1), a1 + hstepA, voffA);
;             PG8_WAIT_V(8); PG8_WAIT_L(0); PG8_BAR; PG8_MMA(0, 0, At, B0); PG8_MMA(0, 1, At, B1); PG8_BAR; PG8_SCHED;
;             PG8_LDA(At, 0, 1); PG8_STAGE(PG8_SB(0, 0), b2, voffB); PG8_STAGE(PG8_SB(0, 1), b2 + hstepB, voffB); PG8_STAGE(PG8_SA(0, 0), a2, voffA);
;             PG8_WAIT_V(8); PG8_WAIT_L(0); PG8_BAR; PG8_MMA(1, 0, At, B0); PG8_MMA(1, 1, At, B1); PG8_BAR; PG8_SCHED;
;             PG8_LDB(B0, 1, 0); PG8_LDB(B1, 1, 1); PG8_SCHED; PG8_LDA(At, 1, 0); PG8_STAGE(PG8_SA(0, 1), a2 + hstepA, voffA);
;             PG8_WAIT_V(8); PG8_WAIT_L(0); PG8_BAR; PG8_MMA(0, 0, At, B0); PG8_MMA(0, 1, At, B1); PG8_BAR; PG8_SCHED;
;             PG8_LDA(At, 1, 1); PG8_STAGE(PG8_SB(1, 0), b3, voffB); PG8_STAGE(PG8_SB(1, 1), b3 + hstepB, voffB); PG8_STAGE(PG8_SA(1, 0), a3, voffA);
;             PG8_WAIT_V(8); PG8_WAIT_L(0); PG8_BAR; PG8_MMA(1, 0, At, B0); PG8_MMA(1, 1, At, B1); PG8_BAR; PG8_SCHED;
;         }
	s_setprio 1
	s_waitcnt lgkmcnt(7)
	v_mfma_f32_16x16x32_bf16 v[64:67], v[132:135], v[182:185], v[64:67]
	v_mfma_f32_16x16x32_bf16 v[60:63], v[158:161], v[182:185], v[60:63]
	s_waitcnt lgkmcnt(5)
	v_mfma_f32_16x16x32_bf16 v[48:51], v[132:135], v[206:209], v[48:51]
	v_mfma_f32_16x16x32_bf16 v[44:47], v[158:161], v[206:209], v[44:47]
	s_waitcnt lgkmcnt(3)
	v_mfma_f32_16x16x32_bf16 v[32:35], v[132:135], v[214:217], v[32:35]
	v_mfma_f32_16x16x32_bf16 v[28:31], v[158:161], v[214:217], v[28:31]
	s_waitcnt lgkmcnt(1)
	v_mfma_f32_16x16x32_bf16 v[16:19], v[132:135], v[222:225], v[16:19]
	v_mfma_f32_16x16x32_bf16 v[12:15], v[158:161], v[222:225], v[12:15]
	v_mfma_f32_16x16x32_bf16 v[64:67], v[154:157], v[196:199], v[64:67]
	v_mfma_f32_16x16x32_bf16 v[60:63], v[162:165], v[196:199], v[60:63]
	v_mfma_f32_16x16x32_bf16 v[48:51], v[154:157], v[210:213], v[48:51]
	v_mfma_f32_16x16x32_bf16 v[44:47], v[162:165], v[210:213], v[44:47]
	v_mfma_f32_16x16x32_bf16 v[32:35], v[154:157], v[218:221], v[32:35]
	v_mfma_f32_16x16x32_bf16 v[28:31], v[162:165], v[218:221], v[28:31]
	s_waitcnt lgkmcnt(0)
	v_mfma_f32_16x16x32_bf16 v[16:19], v[154:157], v[226:229], v[16:19]
	v_mfma_f32_16x16x32_bf16 v[12:15], v[162:165], v[226:229], v[12:15]
	s_setprio 0
	s_setprio 1
	v_mfma_f32_16x16x32_bf16 v[56:59], v[166:169], v[182:185], v[56:59]
	v_mfma_f32_16x16x32_bf16 v[52:55], v[174:177], v[182:185], v[52:55]
	v_mfma_f32_16x16x32_bf16 v[40:43], v[166:169], v[206:209], v[40:43]
	v_mfma_f32_16x16x32_bf16 v[36:39], v[174:177], v[206:209], v[36:39]
	v_mfma_f32_16x16x32_bf16 v[24:27], v[166:169], v[214:217], v[24:27]
	v_mfma_f32_16x16x32_bf16 v[20:23], v[174:177], v[214:217], v[20:23]
	v_mfma_f32_16x16x32_bf16 v[8:11], v[166:169], v[222:225], v[8:11]
	v_mfma_f32_16x16x32_bf16 v[4:7], v[174:177], v[222:225], v[4:7]
	v_mfma_f32_16x16x32_bf16 v[56:59], v[170:173], v[196:199], v[56:59]
	v_mfma_f32_16x16x32_bf16 v[52:55], v[178:181], v[196:199], v[52:55]
	v_mfma_f32_16x16x32_bf16 v[40:43], v[170:173], v[210:213], v[40:43]
	v_mfma_f32_16x16x32_bf16 v[36:39], v[178:181], v[210:213], v[36:39]
	v_mfma_f32_16x16x32_bf16 v[24:27], v[170:173], v[218:221], v[24:27]
	v_mfma_f32_16x16x32_bf16 v[20:23], v[178:181], v[218:221], v[20:23]
	v_mfma_f32_16x16x32_bf16 v[8:11], v[170:173], v[226:229], v[8:11]
	v_mfma_f32_16x16x32_bf16 v[4:7], v[178:181], v[226:229], v[4:7]
	s_setprio 0
	s_barrier
	v_add_u32_e32 v0, 0x18000, v244
	v_add_u32_e32 v246, 0x18000, v245
	ds_read_b128 v[132:135], v0
	ds_read_b128 v[154:157], v246
	ds_read_b128 v[158:161], v0 offset:2048
	ds_read_b128 v[162:165], v246 offset:2048
	v_add_u32_e32 v0, 0x1c000, v244
	v_add_u32_e32 v246, 0x1c000, v245
	ds_read_b128 v[166:169], v0
	ds_read_b128 v[170:173], v246
	ds_read_b128 v[174:177], v0 offset:2048
	ds_read_b128 v[178:181], v246 offset:2048
	ds_read_b128 v[182:185], v242 offset:32768
	ds_read_b128 v[196:199], v243 offset:32768
	ds_read_b128 v[206:209], v242 offset:34816
	ds_read_b128 v[210:213], v243 offset:34816
	ds_read_b128 v[214:217], v242 offset:36864
	ds_read_b128 v[218:221], v243 offset:36864
	ds_read_b128 v[222:225], v242 offset:38912
	ds_read_b128 v[226:229], v243 offset:38912
	s_add_u32 s26, s26, 0x80000
	s_addc_u32 s27, s27, 0
	s_mov_b32 m0, s39
	s_nop 0
	global_load_lds_dwordx4 v238, s[26:27]
	s_nop 0
	s_mov_b32 m0, s40
	s_nop 0
	global_load_lds_dwordx4 v239, s[26:27]
	s_waitcnt vmcnt(8)
	s_waitcnt lgkmcnt(0)
	s_barrier
	s_setprio 1
	s_waitcnt lgkmcnt(7)
	v_mfma_f32_16x16x32_bf16 v[128:131], v[132:135], v[182:185], v[128:131]
	v_mfma_f32_16x16x32_bf16 v[124:127], v[158:161], v[182:185], v[124:127]
	s_waitcnt lgkmcnt(5)
	v_mfma_f32_16x16x32_bf16 v[112:115], v[132:135], v[206:209], v[112:115]
	v_mfma_f32_16x16x32_bf16 v[108:111], v[158:161], v[206:209], v[108:111]
	s_waitcnt lgkmcnt(3)
	v_mfma_f32_16x16x32_bf16 v[96:99], v[132:135], v[214:217], v[96:99]
	v_mfma_f32_16x16x32_bf16 v[92:95], v[158:161], v[214:217], v[92:95]
	s_waitcnt lgkmcnt(1)
	v_mfma_f32_16x16x32_bf16 v[80:83], v[132:135], v[222:225], v[80:83]
	v_mfma_f32_16x16x32_bf16 v[76:79], v[158:161], v[222:225], v[76:79]
	v_mfma_f32_16x16x32_bf16 v[128:131], v[154:157], v[196:199], v[128:131]
	v_mfma_f32_16x16x32_bf16 v[124:127], v[162:165], v[196:199], v[124:127]
	v_mfma_f32_16x16x32_bf16 v[112:115], v[154:157], v[210:213], v[112:115]
	v_mfma_f32_16x16x32_bf16 v[108:111], v[162:165], v[210:213], v[108:111]
	v_mfma_f32_16x16x32_bf16 v[96:99], v[154:157], v[218:221], v[96:99]
	v_mfma_f32_16x16x32_bf16 v[92:95], v[162:165], v[218:221], v[92:95]
	s_waitcnt lgkmcnt(0)
	v_mfma_f32_16x16x32_bf16 v[80:83], v[154:157], v[226:229], v[80:83]
	v_mfma_f32_16x16x32_bf16 v[76:79], v[162:165], v[226:229], v[76:79]
	s_setprio 0
	s_setprio 1
	v_mfma_f32_16x16x32_bf16 v[120:123], v[166:169], v[182:185], v[120:123]
	v_mfma_f32_16x16x32_bf16 v[116:119], v[174:177], v[182:185], v[116:119]
	v_mfma_f32_16x16x32_bf16 v[104:107], v[166:169], v[206:209], v[104:107]
	v_mfma_f32_16x16x32_bf16 v[100:103], v[174:177], v[206:209], v[100:103]
	v_mfma_f32_16x16x32_bf16 v[88:91], v[166:169], v[214:217], v[88:91]
	v_mfma_f32_16x16x32_bf16 v[84:87], v[174:177], v[214:217], v[84:87]
	v_mfma_f32_16x16x32_bf16 v[72:75], v[166:169], v[222:225], v[72:75]
	v_mfma_f32_16x16x32_bf16 v[68:71], v[174:177], v[222:225], v[68:71]
	v_mfma_f32_16x16x32_bf16 v[120:123], v[170:173], v[196:199], v[120:123]
	v_mfma_f32_16x16x32_bf16 v[116:119], v[178:181], v[196:199], v[116:119]
	v_mfma_f32_16x16x32_bf16 v[104:107], v[170:173], v[210:213], v[104:107]
	v_mfma_f32_16x16x32_bf16 v[100:103], v[178:181], v[210:213], v[100:103]
	v_mfma_f32_16x16x32_bf16 v[88:91], v[170:173], v[218:221], v[88:91]
	v_mfma_f32_16x16x32_bf16 v[84:87], v[178:181], v[218:221], v[84:87]
	v_mfma_f32_16x16x32_bf16 v[72:75], v[170:173], v[226:229], v[72:75]
	v_mfma_f32_16x16x32_bf16 v[68:71], v[178:181], v[226:229], v[68:71]
	s_setprio 0
	s_barrier
; #define PG8_STAGE(bufoff, gbase, voff) do { _Pragma("unroll") for (int _i = 0; _i < 2; ++_i) \
;         glds16((const void*)(gbase), (voff)[_i], ldsbase + (unsigned)(bufoff) + ldsw + (unsigned)_i * 8192u); } while (0)
; #define PG8_LDA(dst, b, h) do { _Pragma("unroll") for (int m = 0; m < 4; ++m) _Pragma("unroll") for (int k = 0; k < 2; ++k) dst[m][k] = *(const LAS bf16x8*)(lds + PG8_SA(b, h) + aoff + m * 2048 + k * 1024); } while (0)
; #define PG8_LDB(dst, b, h) do { _Pragma("unroll") for (int n = 0; n < 2; ++n) _Pragma("unroll") for (int k = 0; k < 2; ++k) dst[n][k] = *(const LAS bf16x8*)(lds + PG8_SB(b, h) + boff + n * 2048 + k * 1024); } while (0)
; #define PG8_WAIT_V(n) asm volatile("s_waitcnt vmcnt(" #n ")" ::: "memory")
; #define PG8_WAIT_L(n) asm volatile("s_waitcnt lgkmcnt(" #n ")" ::: "memory")
; #define PG8_BAR __builtin_amdgcn_s_barrier()
; #define PG8_SCHED __builtin_amdgcn_sched_barrier(0)
;     ...
;         for (int t = 0; t < nt; t += 2) {
;             const bool last = (t == nt - 2);
;             const char* a1 = cA + (size_t)(t + 1) * kstep;
;             const char* a2 = last ? nA : cA + (size_t)(t + 2) * kstep; const char* b2 = last ? nB : cB + (size_t)(t + 2) * kstep;
;             const char* a3 = a2 + kstep; const char* b3 = b2 + kstep;
;             PG8_LDB(B0, 0, 0); PG8_LDB(B1, 0, 1); PG8_SCHED; PG8_LDA(At, 0, 0); PG8_STAGE(PG8_SA(1, 1), a1 + hstepA, voffA);
;             PG8_WAIT_V(8); PG8_WAIT_L(0); PG8_BAR; PG8_MMA(0, 0, At, B0); PG8_MMA(0, 1, At, B1); PG8_BAR; PG8_SCHED;
;             PG8_LDA(At, 0, 1); PG8_STAGE(PG8_SB(0, 0), b2, voffB); PG8_STAGE(PG8_SB(0, 1), b2 + hstepB, voffB); PG8_STAGE(PG8_SA(0, 0), a2, voffA);
;             PG8_WAIT_V(8); PG8_WAIT_L(0); PG8_BAR; PG8_MMA(1, 0, At, B0); PG8_MMA(1, 1, At, B1); PG8_BAR; PG8_SCHED;
;             PG8_LDB(B0, 1, 0); PG8_LDB(B1, 1, 1); PG8_SCHED; PG8_LDA(At, 1, 0); PG8_STAGE(PG8_SA(0, 1), a2 + hstepA, voffA);
;             PG8_WAIT_V(8); PG8_WAIT_L(0); PG8_BAR; PG8_MMA(0, 0, At, B0); PG8_MMA(0, 1, At, B1); PG8_BAR; PG8_SCHED;
;             PG8_LDA(At, 1, 1); PG8_STAGE(PG8_SB(1, 0), b3, voffB); PG8_STAGE(PG8_SB(1, 1), b3 + hstepB, voffB); PG8_STAGE(PG8_SA(1, 0), a3, voffA);
;             PG8_WAIT_V(8); PG8_WAIT_L(0); PG8_BAR; PG8_MMA(1, 0, At, B0); PG8_MMA(1, 1, At, B1); PG8_BAR; PG8_SCHED;
;         }
	ds_read_b128 v[182:185], v242 offset:49152
	ds_read_b128 v[196:199], v243 offset:49152
	ds_read_b128 v[206:209], v242 offset:51200
	ds_read_b128 v[210:213], v243 offset:51200
	ds_read_b128 v[214:217], v242 offset:53248
	ds_read_b128 v[218:221], v243 offset:53248
	ds_read_b128 v[222:225], v242 offset:55296
	ds_read_b128 v[226:229], v243 offset:55296
	s_add_u32 s26, s24, 0x80
	s_addc_u32 s27, s25, 0
	s_mov_b32 m0, s41
	s_nop 0
	global_load_lds_dwordx4 v240, s[26:27]
	s_add_u32 s24, s24, 0x80080
	s_mov_b32 m0, s42
	s_nop 0
	global_load_lds_dwordx4 v241, s[26:27]
	s_addc_u32 s25, s25, 0
	s_mov_b32 m0, s45
	s_nop 0
	global_load_lds_dwordx4 v240, s[24:25]
	s_nop 0
	s_mov_b32 m0, s46
	s_nop 0
	global_load_lds_dwordx4 v241, s[24:25]
	s_mov_b32 m0, s43
	s_nop 0
	global_load_lds_dwordx4 v238, s[22:23]
	s_nop 0
	s_mov_b32 m0, s44
	s_nop 0
	global_load_lds_dwordx4 v239, s[22:23]
	s_waitcnt vmcnt(8)
	s_waitcnt lgkmcnt(0)
	s_barrier
	s_setprio 1
	s_waitcnt lgkmcnt(7)
	v_mfma_f32_16x16x32_bf16 v[64:67], v[132:135], v[182:185], v[64:67]
	v_mfma_f32_16x16x32_bf16 v[60:63], v[158:161], v[182:185], v[60:63]
	s_waitcnt lgkmcnt(5)
	v_mfma_f32_16x16x32_bf16 v[48:51], v[132:135], v[206:209], v[48:51]
	v_mfma_f32_16x16x32_bf16 v[44:47], v[158:161], v[206:209], v[44:47]
	s_waitcnt lgkmcnt(3)
	v_mfma_f32_16x16x32_bf16 v[32:35], v[132:135], v[214:217], v[32:35]
	v_mfma_f32_16x16x32_bf16 v[28:31], v[158:161], v[214:217], v[28:31]
	s_waitcnt lgkmcnt(1)
	v_mfma_f32_16x16x32_bf16 v[16:19], v[132:135], v[222:225], v[16:19]
	v_mfma_f32_16x16x32_bf16 v[12:15], v[158:161], v[222:225], v[12:15]
	v_mfma_f32_16x16x32_bf16 v[64:67], v[154:157], v[196:199], v[64:67]
	v_mfma_f32_16x16x32_bf16 v[60:63], v[162:165], v[196:199], v[60:63]
	v_mfma_f32_16x16x32_bf16 v[48:51], v[154:157], v[210:213], v[48:51]
	v_mfma_f32_16x16x32_bf16 v[44:47], v[162:165], v[210:213], v[44:47]
	v_mfma_f32_16x16x32_bf16 v[32:35], v[154:157], v[218:221], v[32:35]
	v_mfma_f32_16x16x32_bf16 v[28:31], v[162:165], v[218:221], v[28:31]
	s_waitcnt lgkmcnt(0)
	v_mfma_f32_16x16x32_bf16 v[16:19], v[154:157], v[226:229], v[16:19]
	v_mfma_f32_16x16x32_bf16 v[12:15], v[162:165], v[226:229], v[12:15]
	s_setprio 0
	s_setprio 1
	v_mfma_f32_16x16x32_bf16 v[56:59], v[166:169], v[182:185], v[56:59]
	v_mfma_f32_16x16x32_bf16 v[52:55], v[174:177], v[182:185], v[52:55]
	v_mfma_f32_16x16x32_bf16 v[40:43], v[166:169], v[206:209], v[40:43]
	v_mfma_f32_16x16x32_bf16 v[36:39], v[174:177], v[206:209], v[36:39]
	v_mfma_f32_16x16x32_bf16 v[24:27], v[166:169], v[214:217], v[24:27]
	v_mfma_f32_16x16x32_bf16 v[20:23], v[174:177], v[214:217], v[20:23]
	v_mfma_f32_16x16x32_bf16 v[8:11], v[166:169], v[222:225], v[8:11]
	v_mfma_f32_16x16x32_bf16 v[4:7], v[174:177], v[222:225], v[4:7]
	v_mfma_f32_16x16x32_bf16 v[56:59], v[170:173], v[196:199], v[56:59]
	v_mfma_f32_16x16x32_bf16 v[52:55], v[178:181], v[196:199], v[52:55]
	v_mfma_f32_16x16x32_bf16 v[40:43], v[170:173], v[210:213], v[40:43]
	v_mfma_f32_16x16x32_bf16 v[36:39], v[178:181], v[210:213], v[36:39]
	v_mfma_f32_16x16x32_bf16 v[24:27], v[170:173], v[218:221], v[24:27]
	v_mfma_f32_16x16x32_bf16 v[20:23], v[178:181], v[218:221], v[20:23]
	v_mfma_f32_16x16x32_bf16 v[8:11], v[170:173], v[226:229], v[8:11]
	v_mfma_f32_16x16x32_bf16 v[4:7], v[178:181], v[226:229], v[4:7]
	s_setprio 0
	s_barrier
	s_add_i32 s52, s52, 2
	s_add_u32 s13, s13, 0x100
	s_addc_u32 s15, s15, 0
	s_add_u32 s20, s20, 0x100
	s_addc_u32 s21, s21, 0
	s_cmp_gt_u32 s52, 29
	s_cbranch_scc0 .LBB0_3056
	s_and_b64 vcc, exec, s[10:11]
	s_cbranch_vccz .LBB0_3059
	s_barrier

; __device__ __forceinline__ int lane_id() { int l_; asm volatile("v_mbcnt_lo_u32_b32 %0, -1, 0\n\tv_mbcnt_hi_u32_b32 %0, -1, %0" : "=v"(l_)); return l_; }
; #define PG8_STAGE(bufoff, gbase, voff) do { _Pragma("unroll") for (int _i = 0; _i < 2; ++_i) \
;         glds16((const void*)(gbase), (voff)[_i], ldsbase + (unsigned)(bufoff) + ldsw + (unsigned)_i * 8192u); } while (0)
; #define PG8_WAIT_V(n) asm volatile("s_waitcnt vmcnt(" #n ")" ::: "memory")
; #define PG8_BAR __builtin_amdgcn_s_barrier()
;     const int sB1 = sB1_ < 0 ? sB : sB1_;
;     int tid = w0_ * 64 + lane_id(); asm volatile("" : "+v"(tid));
;     const int wid = __builtin_amdgcn_readfirstlane(tid >> 6), lane = tid & 63, wr = wid >> 2, wc = wid & 3, fr = lane & 15, fq = lane >> 4;
;     const int nt = nt_ ? nt_ : Kb / 128;
;     unsigned voffA[2], voffB[2];
; #pragma unroll
;     for (int i = 0; i < 2; ++i) { int R, C; stage_rc(tid * 16 + i * 8192, R, C); const int Rb = Epi::PERM ? ((R & ~31) + perm32(R & 31)) : R;
;         voffA[i] = (unsigned)(R * ldab + C * 2); voffB[i] = (unsigned)(Rb * Kb + C * 2); }
;     const size_t kstep = (size_t)(BK * 2);
;     const size_t hstepA = (size_t)HALF * ldab, hstepB = (size_t)HALF * Kb;
;     const unsigned ldsw = (unsigned)wid * 1024u, ldsbase = (unsigned)(size_t)lds;
;     const int aoff = lds_byte(wr * 64 + fr, fq * 8), boff = lds_byte(wc * 32 + fr, fq * 8);
;     ...
;     const char* cA = uniform_ptr(cur.a); const char* cB = uniform_ptr(cur.b);
;     PG8_STAGE(PG8_SB(0, 0), cB, voffB); PG8_STAGE(PG8_SB(0, 1), cB + hstepB, voffB); PG8_STAGE(PG8_SA(0, 0), cA, voffA); PG8_STAGE(PG8_SA(0, 1), cA + hstepA, voffA);
;     if (wr == 1) PG8_BAR;
;     PG8_WAIT_V(2); PG8_BAR;
;     PG8_STAGE(PG8_SB(1, 0), cB + kstep, voffB); PG8_STAGE(PG8_SA(1, 0), cA + kstep, voffA); PG8_STAGE(PG8_SB(1, 1), cB + hstepB + kstep, voffB);
;     PG8_WAIT_V(6); PG8_BAR;
.LBB0_3118:
	s_and_b64 vcc, exec, s[2:3]
	s_cbranch_vccnz .LBB0_3154
	s_waitcnt lgkmcnt(0)
	v_bfe_i32 v1, v4, 27, 1
	v_lshlrev_b32_e32 v5, 4, v4
	v_lshrrev_b32_e32 v1, 22, v1
	v_add_u32_e32 v1, v5, v1
	v_and_b32_e32 v1, 0xfffffc00, v1
	v_sub_u32_e32 v1, v5, v1
	v_ashrrev_i32_e32 v0, 31, v4
	v_lshrrev_b32_e32 v2, 4, v1
	v_lshrrev_b32_e32 v0, 26, v0
	v_bitop3_b32 v1, v2, v1, 32 bitop3:0x6c
	v_add_u32_e32 v0, v4, v0
	v_ashrrev_i32_e32 v6, 31, v1
	v_ashrrev_i32_e32 v0, 6, v0
	v_lshrrev_b32_e32 v6, 26, v6
	v_lshlrev_b32_e32 v2, 3, v0
	v_add_u32_e32 v6, v1, v6
	v_and_b32_e32 v2, -16, v2
	v_ashrrev_i32_e32 v7, 6, v6
	v_add_u32_e32 v8, v7, v2
	v_and_b32_e32 v2, 0xc0, v6
	v_sub_u32_e32 v1, v1, v2
	v_lshlrev_b32_e32 v0, 5, v0
	v_ashrrev_i16_sdwa v1, v188, sext(v1) dst_sel:DWORD dst_unused:UNUSED_PAD src0_sel:DWORD src1_sel:BYTE_0
	v_lshlrev_b32_e32 v2, 1, v8
	v_lshrrev_b32_e32 v6, 2, v8
	v_and_b32_e32 v7, 3, v7
	s_mov_b32 s3, 0x3fffe0
	v_and_b32_e32 v0, 32, v0
	v_bfe_i32 v1, v1, 0, 16
	v_and_b32_e32 v2, 24, v2
	v_and_b32_e32 v6, 4, v6
	v_and_or_b32 v7, v8, s3, v7
	v_or3_b32 v6, v7, v6, v2
	v_add_lshl_u32 v2, v0, v1, 1
	s_movk_i32 s8, 0x2c00
	v_mad_u64_u32 v[0:1], s[6:7], v8, s8, v[2:3]
	v_mad_u32_u24 v1, v6, s8, v2
	v_add_u32_e32 v2, 0x2000, v5
	v_ashrrev_i32_e32 v5, 31, v2
	v_lshrrev_b32_e32 v5, 22, v5
	v_add_u32_e32 v5, v2, v5
	v_ashrrev_i32_e32 v5, 10, v5
	v_mul_i32_i24_e32 v6, 0x400, v5
	v_sub_u32_e32 v2, v2, v6
	v_lshrrev_b32_e32 v6, 4, v2
	v_bitop3_b32 v2, v6, v2, 32 bitop3:0x6c
	v_ashrrev_i32_e32 v7, 31, v2
	v_lshrrev_b32_e32 v7, 26, v7
	v_add_u32_e32 v7, v2, v7
	v_ashrrev_i32_e32 v8, 6, v7
	v_and_b32_e32 v7, 0xc0, v7
	v_sub_u32_e32 v2, v2, v7
	v_lshlrev_b32_e32 v6, 3, v5
	v_lshlrev_b32_e32 v5, 5, v5
	v_ashrrev_i16_sdwa v2, v188, sext(v2) dst_sel:DWORD dst_unused:UNUSED_PAD src0_sel:DWORD src1_sel:BYTE_0
	v_and_b32_e32 v6, -16, v6
	v_and_b32_e32 v5, 32, v5
	v_bfe_i32 v2, v2, 0, 16
	v_add_u32_e32 v6, v8, v6
	v_add_lshl_u32 v2, v5, v2, 1
	s_ashr_i32 s2, s4, 6
	s_waitcnt vmcnt(0)
	v_mad_u64_u32 v[140:141], s[6:7], v6, s8, v[2:3]
	v_lshlrev_b32_e32 v7, 1, v6
	v_lshrrev_b32_e32 v9, 2, v6
	v_and_b32_e32 v8, 3, v8
	s_lshl_b32 s6, s2, 10
	v_and_b32_e32 v7, 24, v7
	v_and_b32_e32 v9, 4, v9
	v_and_or_b32 v8, v6, s3, v8
	s_add_i32 s34, s6, 0
	v_or3_b32 v7, v8, v9, v7
	s_add_i32 s35, s34, 0x10000
	s_nop 0
	v_readlane_b32 s70, v250, 60
	v_mbcnt_lo_u32_b32 v246, -1, 0
	v_mbcnt_hi_u32_b32 v246, -1, v246
	v_add_u32_e32 v246, s70, v246
	v_bfe_u32 v247, v246, 4, 2
	v_bfe_u32 v248, v246, 6, 1
	v_lshl_or_b32 v247, v248, 2, v247
	v_and_b32_e32 v248, 7, v246
	v_xor_b32_e32 v247, v247, v248
	v_lshlrev_b32_e32 v247, 4, v247
	v_lshrrev_b32_e32 v248, 3, v246
	s_mov_b32 s71, 11264
	v_mad_u32_u24 v238, v248, s71, v247
	v_add_u32_e32 v239, 0xb0000, v238
	v_and_b32_e32 v249, 0x23, v248
	v_and_b32_e32 v244, 12, v248
	v_lshl_or_b32 v249, v244, 1, v249
	v_bfe_u32 v244, v248, 4, 1
	v_lshl_or_b32 v249, v244, 2, v249
	s_mov_b32 s71, 11264
	v_mad_u32_u24 v240, v249, s71, v247
	v_add_u32_e32 v241, 0xb0000, v240
	v_bfe_u32 v247, v246, 4, 2
	v_bfe_u32 v248, v246, 1, 3
	v_xor_b32_e32 v247, v247, v248
	v_lshlrev_b32_e32 v247, 4, v247
	v_and_b32_e32 v248, 7, v246
	v_lshl_or_b32 v247, v248, 7, v247
	v_bfe_u32 v248, v246, 3, 1
	v_lshl_or_b32 v247, v248, 10, v247
	v_bfe_u32 v248, v246, 8, 1
	v_lshl_or_b32 v242, v248, 13, v247
	v_xor_b32_e32 v243, 64, v242
	v_bfe_u32 v248, v246, 6, 2
	v_lshl_or_b32 v244, v248, 12, v247
	v_xor_b32_e32 v245, 64, v244
	s_mov_b32 m0, s35
	s_nop 0
	global_load_lds_dwordx4 v240, s[22:23]
	v_mad_u32_u24 v2, v7, s8, v2
	s_ashr_i32 s3, s4, 8
	s_add_i32 s36, s34, 0x12000
	s_mov_b32 m0, s36
	s_nop 0
	global_load_lds_dwordx4 v241, s[22:23]
	s_add_u32 s6, s22, 0x160000
	s_addc_u32 s7, s23, 0
	s_add_i32 s37, s34, 0x14000
	s_mov_b32 m0, s37
	s_nop 0
	global_load_lds_dwordx4 v240, s[6:7]
	s_add_i32 s38, s34, 0x16000
	s_mov_b32 m0, s38
	s_nop 0
	global_load_lds_dwordx4 v241, s[6:7]
	s_mov_b32 m0, s34
	s_nop 0
	global_load_lds_dwordx4 v238, s[20:21]
	s_add_i32 s39, s34, 0x2000
	s_mov_b32 m0, s39
	s_nop 0
	global_load_lds_dwordx4 v239, s[20:21]
	s_add_u32 s6, s20, 0x160000
	s_addc_u32 s7, s21, 0
	s_add_i32 s40, s34, 0x4000
	s_mov_b32 m0, s40
	s_nop 0
	global_load_lds_dwordx4 v238, s[6:7]
	s_add_i32 s41, s34, 0x6000
	s_mov_b32 m0, s41
	s_nop 0
	global_load_lds_dwordx4 v239, s[6:7]
	s_cmp_eq_u32 s3, 1
	s_cselect_b64 s[6:7], -1, 0
	s_cmp_lg_u32 s3, 1
	s_cbranch_scc1 .LBB0_3121
	s_barrier
.LBB0_3121:
	s_add_u32 s8, s5, 0x32892000
	s_addc_u32 s9, s13, 0
	s_add_u32 s10, s5, 0x32682000
	s_addc_u32 s11, s13, 0
	v_bfe_u32 v6, v4, 4, 2
	s_add_u32 s12, s5, 0x36892000
	v_and_b32_e32 v5, 15, v4
	v_lshlrev_b32_e32 v8, 4, v6
	v_lshlrev_b32_e32 v4, 2, v4
	s_addc_u32 s13, s13, 0
	s_and_b32 s42, s2, 3
	v_lshl_or_b32 v141, s3, 6, v5
	v_lshl_or_b32 v5, v5, 6, v8
	s_lshl_b32 s2, s3, 13
	v_and_b32_e32 v4, 32, v4
	v_bitop3_b32 v8, v5, s2, v4 bitop3:0xde
	s_lshl_b32 s2, s42, 12
	v_bitop3_b32 v4, v5, s2, v4 bitop3:0xde
	s_add_u32 s2, s22, 0x80
	s_waitcnt vmcnt(2)
	s_barrier
	s_addc_u32 s3, s23, 0
	s_add_i32 s43, s34, 0x18000
	s_mov_b32 m0, s43
	s_nop 0
	global_load_lds_dwordx4 v240, s[2:3]
	s_add_i32 s44, s34, 0x1a000
	s_mov_b32 m0, s44
	s_nop 0
	global_load_lds_dwordx4 v241, s[2:3]
	s_add_u32 s2, s20, 0x80
	s_addc_u32 s3, s21, 0
	s_add_i32 s45, s34, 0x8000
	s_mov_b32 m0, s45
	s_nop 0
	global_load_lds_dwordx4 v238, s[2:3]
	s_add_i32 s46, s34, 0xa000
	s_mov_b32 m0, s46
	s_nop 0
	global_load_lds_dwordx4 v239, s[2:3]
	s_add_u32 s2, s22, 0x160080
	s_addc_u32 s3, s23, 0
	s_add_i32 s47, s34, 0x1c000
	s_mov_b32 m0, s47
	s_nop 0
	global_load_lds_dwordx4 v240, s[2:3]
	s_add_i32 s48, s34, 0x1e000
	s_mov_b32 m0, s48
	s_nop 0
	global_load_lds_dwordx4 v241, s[2:3]
	s_waitcnt vmcnt(6)
	s_add_i32 s49, s34, 0xc000
	v_lshlrev_b32_e32 v7, 3, v6
	s_cmpk_lt_u32 s4, 0x100
	v_lshl_or_b32 v150, s42, 5, v7
	s_cselect_b64 s[14:15], -1, 0
	s_mov_b32 s50, 0
	v_cmp_eq_u32_e64 s[2:3], 0, v6
	s_add_i32 s51, s34, 0xe000
	v_add_u32_e32 v151, 0, v4
	v_add_u32_e32 v152, 0, v8
	s_mov_b64 s[16:17], s[20:21]
	s_mov_b64 s[18:19], s[22:23]
	s_barrier
	s_branch .LBB0_3124

; #define PG8_STAGE(bufoff, gbase, voff) do { _Pragma("unroll") for (int _i = 0; _i < 2; ++_i) \
;         glds16((const void*)(gbase), (voff)[_i], ldsbase + (unsigned)(bufoff) + ldsw + (unsigned)_i * 8192u); } while (0)
; #define PG8_LDA(dst, b, h) do { _Pragma("unroll") for (int m = 0; m < 4; ++m) _Pragma("unroll") for (int k = 0; k < 2; ++k) dst[m][k] = *(const LAS bf16x8*)(lds + PG8_SA(b, h) + aoff + m * 2048 + k * 1024); } while (0)
; #define PG8_LDB(dst, b, h) do { _Pragma("unroll") for (int n = 0; n < 2; ++n) _Pragma("unroll") for (int k = 0; k < 2; ++k) dst[n][k] = *(const LAS bf16x8*)(lds + PG8_SB(b, h) + boff + n * 2048 + k * 1024); } while (0)
; #define PG8_WAIT_V(n) asm volatile("s_waitcnt vmcnt(" #n ")" ::: "memory")
; #define PG8_WAIT_L(n) asm volatile("s_waitcnt lgkmcnt(" #n ")" ::: "memory")
; #define PG8_BAR __builtin_amdgcn_s_barrier()
; #define PG8_SCHED __builtin_amdgcn_sched_barrier(0)
;     ...
;         for (int t = 0; t < nt; t += 2) {
;             const bool last = (t == nt - 2);
;             const char* a1 = cA + (size_t)(t + 1) * kstep;
;             const char* a2 = last ? nA : cA + (size_t)(t + 2) * kstep; const char* b2 = last ? nB : cB + (size_t)(t + 2) * kstep;
;             const char* a3 = a2 + kstep; const char* b3 = b2 + kstep;
;             PG8_LDB(B0, 0, 0); PG8_LDB(B1, 0, 1); PG8_SCHED; PG8_LDA(At, 0, 0); PG8_STAGE(PG8_SA(1, 1), a1 + hstepA, voffA);
;             PG8_WAIT_V(8); PG8_WAIT_L(0); PG8_BAR; PG8_MMA(0, 0, At, B0); PG8_MMA(0, 1, At, B1); PG8_BAR; PG8_SCHED;
;             PG8_LDA(At, 0, 1); PG8_STAGE(PG8_SB(0, 0), b2, voffB); PG8_STAGE(PG8_SB(0, 1), b2 + hstepB, voffB); PG8_STAGE(PG8_SA(0, 0), a2, voffA);
;             PG8_WAIT_V(8); PG8_WAIT_L(0); PG8_BAR; PG8_MMA(1, 0, At, B0); PG8_MMA(1, 1, At, B1); PG8_BAR; PG8_SCHED;
;             PG8_LDB(B0, 1, 0); PG8_LDB(B1, 1, 1); PG8_SCHED; PG8_LDA(At, 1, 0); PG8_STAGE(PG8_SA(0, 1), a2 + hstepA, voffA);
;             PG8_WAIT_V(8); PG8_WAIT_L(0); PG8_BAR; PG8_MMA(0, 0, At, B0); PG8_MMA(0, 1, At, B1); PG8_BAR; PG8_SCHED;
;             PG8_LDA(At, 1, 1); PG8_STAGE(PG8_SB(1, 0), b3, voffB); PG8_STAGE(PG8_SB(1, 1), b3 + hstepB, voffB); PG8_STAGE(PG8_SA(1, 0), a3, voffA);
;             PG8_WAIT_V(8); PG8_WAIT_L(0); PG8_BAR; PG8_MMA(1, 0, At, B0); PG8_MMA(1, 1, At, B1); PG8_BAR; PG8_SCHED;
;         }
.LBB0_3131:
	v_add_u32_e32 v146, 0x10000, v244
	v_add_u32_e32 v246, 0x10000, v245
	v_add_u32_e32 v153, 0x14000, v244
	v_add_u32_e32 v247, 0x14000, v245
	ds_read_b128 v[132:135], v146
	ds_read_b128 v[136:139], v246
	ds_read_b128 v[142:145], v146 offset:2048
	ds_read_b128 v[146:149], v246 offset:2048
	ds_read_b128 v[154:157], v153
	ds_read_b128 v[158:161], v247
	ds_read_b128 v[162:165], v153 offset:2048
	ds_read_b128 v[166:169], v247 offset:2048
	s_add_u32 s22, s20, 0xffea0080
	s_addc_u32 s23, s21, -1
	s_cmpk_eq_i32 s57, 0x54
	s_cselect_b32 s26, s16, s22
	s_cselect_b32 s27, s17, s23
	s_cselect_b32 s24, s18, s55
	s_cselect_b32 s25, s19, s56
	s_add_u32 s22, s26, 0x80
	s_addc_u32 s23, s27, 0
	ds_read_b128 v[170:173], v242
	ds_read_b128 v[174:177], v243
	ds_read_b128 v[178:181], v242 offset:2048
	ds_read_b128 v[182:185], v243 offset:2048
	ds_read_b128 v[196:199], v242 offset:4096
	ds_read_b128 v[206:209], v243 offset:4096
	ds_read_b128 v[210:213], v242 offset:6144
	ds_read_b128 v[214:217], v243 offset:6144
	s_mov_b32 m0, s49
	s_nop 0
	global_load_lds_dwordx4 v238, s[20:21]
	s_nop 0
	s_mov_b32 m0, s51
	s_nop 0
	global_load_lds_dwordx4 v239, s[20:21]
	s_waitcnt vmcnt(8)
	s_waitcnt lgkmcnt(0)
	s_barrier
	s_setprio 1
	s_waitcnt lgkmcnt(7)
	v_mfma_f32_16x16x32_bf16 v[128:131], v[132:135], v[170:173], v[128:131]
	v_mfma_f32_16x16x32_bf16 v[124:127], v[142:145], v[170:173], v[124:127]
	s_waitcnt lgkmcnt(5)
	v_mfma_f32_16x16x32_bf16 v[112:115], v[132:135], v[178:181], v[112:115]
	v_mfma_f32_16x16x32_bf16 v[108:111], v[142:145], v[178:181], v[108:111]
	s_waitcnt lgkmcnt(3)
	v_mfma_f32_16x16x32_bf16 v[96:99], v[132:135], v[196:199], v[96:99]
	v_mfma_f32_16x16x32_bf16 v[92:95], v[142:145], v[196:199], v[92:95]
	s_waitcnt lgkmcnt(1)
	v_mfma_f32_16x16x32_bf16 v[80:83], v[132:135], v[210:213], v[80:83]
	v_mfma_f32_16x16x32_bf16 v[76:79], v[142:145], v[210:213], v[76:79]
	v_mfma_f32_16x16x32_bf16 v[128:131], v[136:139], v[174:177], v[128:131]
	v_mfma_f32_16x16x32_bf16 v[124:127], v[146:149], v[174:177], v[124:127]
	v_mfma_f32_16x16x32_bf16 v[112:115], v[136:139], v[182:185], v[112:115]
	v_mfma_f32_16x16x32_bf16 v[108:111], v[146:149], v[182:185], v[108:111]
	v_mfma_f32_16x16x32_bf16 v[96:99], v[136:139], v[206:209], v[96:99]
	v_mfma_f32_16x16x32_bf16 v[92:95], v[146:149], v[206:209], v[92:95]
	s_waitcnt lgkmcnt(0)
	v_mfma_f32_16x16x32_bf16 v[80:83], v[136:139], v[214:217], v[80:83]
	v_mfma_f32_16x16x32_bf16 v[76:79], v[146:149], v[214:217], v[76:79]
	s_setprio 0
	s_setprio 1
	v_mfma_f32_16x16x32_bf16 v[120:123], v[154:157], v[170:173], v[120:123]
	v_mfma_f32_16x16x32_bf16 v[116:119], v[162:165], v[170:173], v[116:119]
	v_mfma_f32_16x16x32_bf16 v[104:107], v[154:157], v[178:181], v[104:107]
	v_mfma_f32_16x16x32_bf16 v[100:103], v[162:165], v[178:181], v[100:103]
	v_mfma_f32_16x16x32_bf16 v[88:91], v[154:157], v[196:199], v[88:91]
	v_mfma_f32_16x16x32_bf16 v[84:87], v[162:165], v[196:199], v[84:87]
	v_mfma_f32_16x16x32_bf16 v[72:75], v[154:157], v[210:213], v[72:75]
	v_mfma_f32_16x16x32_bf16 v[68:71], v[162:165], v[210:213], v[68:71]
	v_mfma_f32_16x16x32_bf16 v[120:123], v[158:161], v[174:177], v[120:123]
	v_mfma_f32_16x16x32_bf16 v[116:119], v[166:169], v[174:177], v[116:119]
	v_mfma_f32_16x16x32_bf16 v[104:107], v[158:161], v[182:185], v[104:107]
	v_mfma_f32_16x16x32_bf16 v[100:103], v[166:169], v[182:185], v[100:103]
	v_mfma_f32_16x16x32_bf16 v[88:91], v[158:161], v[206:209], v[88:91]
	v_mfma_f32_16x16x32_bf16 v[84:87], v[166:169], v[206:209], v[84:87]
	v_mfma_f32_16x16x32_bf16 v[72:75], v[158:161], v[214:217], v[72:75]
	v_mfma_f32_16x16x32_bf16 v[68:71], v[166:169], v[214:217], v[68:71]
	s_setprio 0
	s_barrier
	ds_read_b128 v[170:173], v242 offset:16384
	ds_read_b128 v[174:177], v243 offset:16384
	ds_read_b128 v[178:181], v242 offset:18432
	ds_read_b128 v[182:185], v243 offset:18432
	ds_read_b128 v[196:199], v242 offset:20480
	ds_read_b128 v[206:209], v243 offset:20480
	ds_read_b128 v[210:213], v242 offset:22528
	ds_read_b128 v[214:217], v243 offset:22528
	s_mov_b32 m0, s35
	s_nop 0
	global_load_lds_dwordx4 v240, s[24:25]
	s_nop 0
	s_mov_b32 m0, s36
	s_nop 0
	global_load_lds_dwordx4 v241, s[24:25]
	s_add_u32 s58, s24, 0x160000
	s_addc_u32 s59, s25, 0
	s_mov_b32 m0, s37
	s_nop 0
	global_load_lds_dwordx4 v240, s[58:59]
	s_nop 0
	s_mov_b32 m0, s38
	s_nop 0
	global_load_lds_dwordx4 v241, s[58:59]
	s_mov_b32 m0, s34
	s_nop 0
	global_load_lds_dwordx4 v238, s[26:27]
	s_nop 0
	s_mov_b32 m0, s39
	s_nop 0
	global_load_lds_dwordx4 v239, s[26:27]
	s_waitcnt vmcnt(8)
	s_waitcnt lgkmcnt(0)
	s_barrier
; #define PG8_STAGE(bufoff, gbase, voff) do { _Pragma("unroll") for (int _i = 0; _i < 2; ++_i) \
;         glds16((const void*)(gbase), (voff)[_i], ldsbase + (unsigned)(bufoff) + ldsw + (unsigned)_i * 8192u); } while (0)
; #define PG8_LDA(dst, b, h) do { _Pragma("unroll") for (int m = 0; m < 4; ++m) _Pragma("unroll") for (int k = 0; k < 2; ++k) dst[m][k] = *(const LAS bf16x8*)(lds + PG8_SA(b, h) + aoff + m * 2048 + k * 1024); } while (0)
; #define PG8_LDB(dst, b, h) do { _Pragma("unroll") for (int n = 0; n < 2; ++n) _Pragma("unroll") for (int k = 0; k < 2; ++k) dst[n][k] = *(const LAS bf16x8*)(lds + PG8_SB(b, h) + boff + n * 2048 + k * 1024); } while (0)
; #define PG8_WAIT_V(n) asm volatile("s_waitcnt vmcnt(" #n ")" ::: "memory")
; #define PG8_WAIT_L(n) asm volatile("s_waitcnt lgkmcnt(" #n ")" ::: "memory")
; #define PG8_BAR __builtin_amdgcn_s_barrier()
; #define PG8_SCHED __builtin_amdgcn_sched_barrier(0)
;     ...
;         for (int t = 0; t < nt; t += 2) {
;             const bool last = (t == nt - 2);
;             const char* a1 = cA + (size_t)(t + 1) * kstep;
;             const char* a2 = last ? nA : cA + (size_t)(t + 2) * kstep; const char* b2 = last ? nB : cB + (size_t)(t + 2) * kstep;
;             const char* a3 = a2 + kstep; const char* b3 = b2 + kstep;
;             PG8_LDB(B0, 0, 0); PG8_LDB(B1, 0, 1); PG8_SCHED; PG8_LDA(At, 0, 0); PG8_STAGE(PG8_SA(1, 1), a1 + hstepA, voffA);
;             PG8_WAIT_V(8); PG8_WAIT_L(0); PG8_BAR; PG8_MMA(0, 0, At, B0); PG8_MMA(0, 1, At, B1); PG8_BAR; PG8_SCHED;
;             PG8_LDA(At, 0, 1); PG8_STAGE(PG8_SB(0, 0), b2, voffB); PG8_STAGE(PG8_SB(0, 1), b2 + hstepB, voffB); PG8_STAGE(PG8_SA(0, 0), a2, voffA);
;             PG8_WAIT_V(8); PG8_WAIT_L(0); PG8_BAR; PG8_MMA(1, 0, At, B0); PG8_MMA(1, 1, At, B1); PG8_BAR; PG8_SCHED;
;             PG8_LDB(B0, 1, 0); PG8_LDB(B1, 1, 1); PG8_SCHED; PG8_LDA(At, 1, 0); PG8_STAGE(PG8_SA(0, 1), a2 + hstepA, voffA);
;             PG8_WAIT_V(8); PG8_WAIT_L(0); PG8_BAR; PG8_MMA(0, 0, At, B0); PG8_MMA(0, 1, At, B1); PG8_BAR; PG8_SCHED;
;             PG8_LDA(At, 1, 1); PG8_STAGE(PG8_SB(1, 0), b3, voffB); PG8_STAGE(PG8_SB(1, 1), b3 + hstepB, voffB); PG8_STAGE(PG8_SA(1, 0), a3, voffA);
;             PG8_WAIT_V(8); PG8_WAIT_L(0); PG8_BAR; PG8_MMA(1, 0, At, B0); PG8_MMA(1, 1, At, B1); PG8_BAR; PG8_SCHED;
;         }
	s_setprio 1
	s_waitcnt lgkmcnt(7)
	v_mfma_f32_16x16x32_bf16 v[64:67], v[132:135], v[170:173], v[64:67]
	v_mfma_f32_16x16x32_bf16 v[60:63], v[142:145], v[170:173], v[60:63]
	s_waitcnt lgkmcnt(5)
	v_mfma_f32_16x16x32_bf16 v[48:51], v[132:135], v[178:181], v[48:51]
	v_mfma_f32_16x16x32_bf16 v[44:47], v[142:145], v[178:181], v[44:47]
	s_waitcnt lgkmcnt(3)
	v_mfma_f32_16x16x32_bf16 v[32:35], v[132:135], v[196:199], v[32:35]
	v_mfma_f32_16x16x32_bf16 v[28:31], v[142:145], v[196:199], v[28:31]
	s_waitcnt lgkmcnt(1)
	v_mfma_f32_16x16x32_bf16 v[16:19], v[132:135], v[210:213], v[16:19]
	v_mfma_f32_16x16x32_bf16 v[12:15], v[142:145], v[210:213], v[12:15]
	v_mfma_f32_16x16x32_bf16 v[64:67], v[136:139], v[174:177], v[64:67]
	v_mfma_f32_16x16x32_bf16 v[60:63], v[146:149], v[174:177], v[60:63]
	v_mfma_f32_16x16x32_bf16 v[48:51], v[136:139], v[182:185], v[48:51]
	v_mfma_f32_16x16x32_bf16 v[44:47], v[146:149], v[182:185], v[44:47]
	v_mfma_f32_16x16x32_bf16 v[32:35], v[136:139], v[206:209], v[32:35]
	v_mfma_f32_16x16x32_bf16 v[28:31], v[146:149], v[206:209], v[28:31]
	s_waitcnt lgkmcnt(0)
	v_mfma_f32_16x16x32_bf16 v[16:19], v[136:139], v[214:217], v[16:19]
	v_mfma_f32_16x16x32_bf16 v[12:15], v[146:149], v[214:217], v[12:15]
	s_setprio 0
	s_setprio 1
	v_mfma_f32_16x16x32_bf16 v[56:59], v[154:157], v[170:173], v[56:59]
	v_mfma_f32_16x16x32_bf16 v[52:55], v[162:165], v[170:173], v[52:55]
	v_mfma_f32_16x16x32_bf16 v[40:43], v[154:157], v[178:181], v[40:43]
	v_mfma_f32_16x16x32_bf16 v[36:39], v[162:165], v[178:181], v[36:39]
	v_mfma_f32_16x16x32_bf16 v[24:27], v[154:157], v[196:199], v[24:27]
	v_mfma_f32_16x16x32_bf16 v[20:23], v[162:165], v[196:199], v[20:23]
	v_mfma_f32_16x16x32_bf16 v[8:11], v[154:157], v[210:213], v[8:11]
	v_mfma_f32_16x16x32_bf16 v[4:7], v[162:165], v[210:213], v[4:7]
	v_mfma_f32_16x16x32_bf16 v[56:59], v[158:161], v[174:177], v[56:59]
	v_mfma_f32_16x16x32_bf16 v[52:55], v[166:169], v[174:177], v[52:55]
	v_mfma_f32_16x16x32_bf16 v[40:43], v[158:161], v[182:185], v[40:43]
	v_mfma_f32_16x16x32_bf16 v[36:39], v[166:169], v[182:185], v[36:39]
	v_mfma_f32_16x16x32_bf16 v[24:27], v[158:161], v[206:209], v[24:27]
	v_mfma_f32_16x16x32_bf16 v[20:23], v[166:169], v[206:209], v[20:23]
	v_mfma_f32_16x16x32_bf16 v[8:11], v[158:161], v[214:217], v[8:11]
	v_mfma_f32_16x16x32_bf16 v[4:7], v[166:169], v[214:217], v[4:7]
	s_setprio 0
	s_barrier
	v_add_u32_e32 v146, 0x18000, v244
	v_add_u32_e32 v246, 0x18000, v245
	v_add_u32_e32 v153, 0x1c000, v244
	v_add_u32_e32 v247, 0x1c000, v245
	ds_read_b128 v[132:135], v146
	ds_read_b128 v[136:139], v246
	ds_read_b128 v[142:145], v146 offset:2048
	ds_read_b128 v[146:149], v246 offset:2048
	ds_read_b128 v[154:157], v153
	ds_read_b128 v[158:161], v247
	ds_read_b128 v[162:165], v153 offset:2048
	ds_read_b128 v[166:169], v247 offset:2048
	ds_read_b128 v[170:173], v242 offset:32768
	ds_read_b128 v[174:177], v243 offset:32768
	ds_read_b128 v[178:181], v242 offset:34816
	ds_read_b128 v[182:185], v243 offset:34816
	ds_read_b128 v[196:199], v242 offset:36864
	ds_read_b128 v[206:209], v243 offset:36864
	ds_read_b128 v[210:213], v242 offset:38912
	ds_read_b128 v[214:217], v243 offset:38912
	s_add_u32 s26, s26, 0x160000
	s_addc_u32 s27, s27, 0
	s_mov_b32 m0, s40
	s_nop 0
	global_load_lds_dwordx4 v238, s[26:27]
	s_nop 0
	s_mov_b32 m0, s41
	s_nop 0
	global_load_lds_dwordx4 v239, s[26:27]
	s_waitcnt vmcnt(8)
	s_waitcnt lgkmcnt(0)
	s_barrier
	s_setprio 1
	s_waitcnt lgkmcnt(7)
	v_mfma_f32_16x16x32_bf16 v[128:131], v[132:135], v[170:173], v[128:131]
	v_mfma_f32_16x16x32_bf16 v[124:127], v[142:145], v[170:173], v[124:127]
	s_waitcnt lgkmcnt(5)
	v_mfma_f32_16x16x32_bf16 v[112:115], v[132:135], v[178:181], v[112:115]
	v_mfma_f32_16x16x32_bf16 v[108:111], v[142:145], v[178:181], v[108:111]
	s_waitcnt lgkmcnt(3)
	v_mfma_f32_16x16x32_bf16 v[96:99], v[132:135], v[196:199], v[96:99]
	v_mfma_f32_16x16x32_bf16 v[92:95], v[142:145], v[196:199], v[92:95]
	s_waitcnt lgkmcnt(1)
	v_mfma_f32_16x16x32_bf16 v[80:83], v[132:135], v[210:213], v[80:83]
	v_mfma_f32_16x16x32_bf16 v[76:79], v[142:145], v[210:213], v[76:79]
	v_mfma_f32_16x16x32_bf16 v[128:131], v[136:139], v[174:177], v[128:131]
	v_mfma_f32_16x16x32_bf16 v[124:127], v[146:149], v[174:177], v[124:127]
	v_mfma_f32_16x16x32_bf16 v[112:115], v[136:139], v[182:185], v[112:115]
	v_mfma_f32_16x16x32_bf16 v[108:111], v[146:149], v[182:185], v[108:111]
	v_mfma_f32_16x16x32_bf16 v[96:99], v[136:139], v[206:209], v[96:99]
	v_mfma_f32_16x16x32_bf16 v[92:95], v[146:149], v[206:209], v[92:95]
	s_waitcnt lgkmcnt(0)
	v_mfma_f32_16x16x32_bf16 v[80:83], v[136:139], v[214:217], v[80:83]
	v_mfma_f32_16x16x32_bf16 v[76:79], v[146:149], v[214:217], v[76:79]
	s_setprio 0
	s_setprio 1
	v_mfma_f32_16x16x32_bf16 v[120:123], v[154:157], v[170:173], v[120:123]
	v_mfma_f32_16x16x32_bf16 v[116:119], v[162:165], v[170:173], v[116:119]
	v_mfma_f32_16x16x32_bf16 v[104:107], v[154:157], v[178:181], v[104:107]
	v_mfma_f32_16x16x32_bf16 v[100:103], v[162:165], v[178:181], v[100:103]
	v_mfma_f32_16x16x32_bf16 v[88:91], v[154:157], v[196:199], v[88:91]
	v_mfma_f32_16x16x32_bf16 v[84:87], v[162:165], v[196:199], v[84:87]
	v_mfma_f32_16x16x32_bf16 v[72:75], v[154:157], v[210:213], v[72:75]
	v_mfma_f32_16x16x32_bf16 v[68:71], v[162:165], v[210:213], v[68:71]
	v_mfma_f32_16x16x32_bf16 v[120:123], v[158:161], v[174:177], v[120:123]
	v_mfma_f32_16x16x32_bf16 v[116:119], v[166:169], v[174:177], v[116:119]
	v_mfma_f32_16x16x32_bf16 v[104:107], v[158:161], v[182:185], v[104:107]
	v_mfma_f32_16x16x32_bf16 v[100:103], v[166:169], v[182:185], v[100:103]
	v_mfma_f32_16x16x32_bf16 v[88:91], v[158:161], v[206:209], v[88:91]
	v_mfma_f32_16x16x32_bf16 v[84:87], v[166:169], v[206:209], v[84:87]
	v_mfma_f32_16x16x32_bf16 v[72:75], v[158:161], v[214:217], v[72:75]
	v_mfma_f32_16x16x32_bf16 v[68:71], v[166:169], v[214:217], v[68:71]
	s_setprio 0
	s_barrier
; #define PG8_STAGE(bufoff, gbase, voff) do { _Pragma("unroll") for (int _i = 0; _i < 2; ++_i) \
;         glds16((const void*)(gbase), (voff)[_i], ldsbase + (unsigned)(bufoff) + ldsw + (unsigned)_i * 8192u); } while (0)
; #define PG8_LDA(dst, b, h) do { _Pragma("unroll") for (int m = 0; m < 4; ++m) _Pragma("unroll") for (int k = 0; k < 2; ++k) dst[m][k] = *(const LAS bf16x8*)(lds + PG8_SA(b, h) + aoff + m * 2048 + k * 1024); } while (0)
; #define PG8_LDB(dst, b, h) do { _Pragma("unroll") for (int n = 0; n < 2; ++n) _Pragma("unroll") for (int k = 0; k < 2; ++k) dst[n][k] = *(const LAS bf16x8*)(lds + PG8_SB(b, h) + boff + n * 2048 + k * 1024); } while (0)
; #define PG8_WAIT_V(n) asm volatile("s_waitcnt vmcnt(" #n ")" ::: "memory")
; #define PG8_WAIT_L(n) asm volatile("s_waitcnt lgkmcnt(" #n ")" ::: "memory")
; #define PG8_BAR __builtin_amdgcn_s_barrier()
; #define PG8_SCHED __builtin_amdgcn_sched_barrier(0)
;     ...
;         for (int t = 0; t < nt; t += 2) {
;             const bool last = (t == nt - 2);
;             const char* a1 = cA + (size_t)(t + 1) * kstep;
;             const char* a2 = last ? nA : cA + (size_t)(t + 2) * kstep; const char* b2 = last ? nB : cB + (size_t)(t + 2) * kstep;
;             const char* a3 = a2 + kstep; const char* b3 = b2 + kstep;
;             PG8_LDB(B0, 0, 0); PG8_LDB(B1, 0, 1); PG8_SCHED; PG8_LDA(At, 0, 0); PG8_STAGE(PG8_SA(1, 1), a1 + hstepA, voffA);
;             PG8_WAIT_V(8); PG8_WAIT_L(0); PG8_BAR; PG8_MMA(0, 0, At, B0); PG8_MMA(0, 1, At, B1); PG8_BAR; PG8_SCHED;
;             PG8_LDA(At, 0, 1); PG8_STAGE(PG8_SB(0, 0), b2, voffB); PG8_STAGE(PG8_SB(0, 1), b2 + hstepB, voffB); PG8_STAGE(PG8_SA(0, 0), a2, voffA);
;             PG8_WAIT_V(8); PG8_WAIT_L(0); PG8_BAR; PG8_MMA(1, 0, At, B0); PG8_MMA(1, 1, At, B1); PG8_BAR; PG8_SCHED;
;             PG8_LDB(B0, 1, 0); PG8_LDB(B1, 1, 1); PG8_SCHED; PG8_LDA(At, 1, 0); PG8_STAGE(PG8_SA(0, 1), a2 + hstepA, voffA);
;             PG8_WAIT_V(8); PG8_WAIT_L(0); PG8_BAR; PG8_MMA(0, 0, At, B0); PG8_MMA(0, 1, At, B1); PG8_BAR; PG8_SCHED;
;             PG8_LDA(At, 1, 1); PG8_STAGE(PG8_SB(1, 0), b3, voffB); PG8_STAGE(PG8_SB(1, 1), b3 + hstepB, voffB); PG8_STAGE(PG8_SA(1, 0), a3, voffA);
;             PG8_WAIT_V(8); PG8_WAIT_L(0); PG8_BAR; PG8_MMA(1, 0, At, B0); PG8_MMA(1, 1, At, B1); PG8_BAR; PG8_SCHED;
;         }
	ds_read_b128 v[170:173], v242 offset:49152
	ds_read_b128 v[174:177], v243 offset:49152
	ds_read_b128 v[178:181], v242 offset:51200
	ds_read_b128 v[182:185], v243 offset:51200
	ds_read_b128 v[196:199], v242 offset:53248
	ds_read_b128 v[206:209], v243 offset:53248
	ds_read_b128 v[210:213], v242 offset:55296
	ds_read_b128 v[214:217], v243 offset:55296
	s_add_u32 s26, s24, 0x80
	s_addc_u32 s27, s25, 0
	s_mov_b32 m0, s43
	s_nop 0
	global_load_lds_dwordx4 v240, s[26:27]
	s_add_u32 s24, s24, 0x160080
	s_mov_b32 m0, s44
	s_nop 0
	global_load_lds_dwordx4 v241, s[26:27]
	s_addc_u32 s25, s25, 0
	s_mov_b32 m0, s47
	s_nop 0
	global_load_lds_dwordx4 v240, s[24:25]
	s_nop 0
	s_mov_b32 m0, s48
	s_nop 0
	global_load_lds_dwordx4 v241, s[24:25]
	s_mov_b32 m0, s45
	s_nop 0
	global_load_lds_dwordx4 v238, s[22:23]
	s_nop 0
	s_mov_b32 m0, s46
	s_nop 0
	global_load_lds_dwordx4 v239, s[22:23]
	s_waitcnt vmcnt(8)
	s_waitcnt lgkmcnt(0)
	s_barrier
	s_setprio 1
	s_waitcnt lgkmcnt(7)
	v_mfma_f32_16x16x32_bf16 v[64:67], v[132:135], v[170:173], v[64:67]
	v_mfma_f32_16x16x32_bf16 v[60:63], v[142:145], v[170:173], v[60:63]
	s_waitcnt lgkmcnt(5)
	v_mfma_f32_16x16x32_bf16 v[48:51], v[132:135], v[178:181], v[48:51]
	v_mfma_f32_16x16x32_bf16 v[44:47], v[142:145], v[178:181], v[44:47]
	s_waitcnt lgkmcnt(3)
	v_mfma_f32_16x16x32_bf16 v[32:35], v[132:135], v[196:199], v[32:35]
	v_mfma_f32_16x16x32_bf16 v[28:31], v[142:145], v[196:199], v[28:31]
	s_waitcnt lgkmcnt(1)
	v_mfma_f32_16x16x32_bf16 v[16:19], v[132:135], v[210:213], v[16:19]
	v_mfma_f32_16x16x32_bf16 v[12:15], v[142:145], v[210:213], v[12:15]
	v_mfma_f32_16x16x32_bf16 v[64:67], v[136:139], v[174:177], v[64:67]
	v_mfma_f32_16x16x32_bf16 v[60:63], v[146:149], v[174:177], v[60:63]
	v_mfma_f32_16x16x32_bf16 v[48:51], v[136:139], v[182:185], v[48:51]
	v_mfma_f32_16x16x32_bf16 v[44:47], v[146:149], v[182:185], v[44:47]
	v_mfma_f32_16x16x32_bf16 v[32:35], v[136:139], v[206:209], v[32:35]
	v_mfma_f32_16x16x32_bf16 v[28:31], v[146:149], v[206:209], v[28:31]
	s_waitcnt lgkmcnt(0)
	v_mfma_f32_16x16x32_bf16 v[16:19], v[136:139], v[214:217], v[16:19]
	v_mfma_f32_16x16x32_bf16 v[12:15], v[146:149], v[214:217], v[12:15]
	s_setprio 0
	s_setprio 1
	v_mfma_f32_16x16x32_bf16 v[56:59], v[154:157], v[170:173], v[56:59]
	v_mfma_f32_16x16x32_bf16 v[52:55], v[162:165], v[170:173], v[52:55]
	v_mfma_f32_16x16x32_bf16 v[40:43], v[154:157], v[178:181], v[40:43]
	v_mfma_f32_16x16x32_bf16 v[36:39], v[162:165], v[178:181], v[36:39]
	v_mfma_f32_16x16x32_bf16 v[24:27], v[154:157], v[196:199], v[24:27]
	v_mfma_f32_16x16x32_bf16 v[20:23], v[162:165], v[196:199], v[20:23]
	v_mfma_f32_16x16x32_bf16 v[8:11], v[154:157], v[210:213], v[8:11]
	v_mfma_f32_16x16x32_bf16 v[4:7], v[162:165], v[210:213], v[4:7]
	v_mfma_f32_16x16x32_bf16 v[56:59], v[158:161], v[174:177], v[56:59]
	v_mfma_f32_16x16x32_bf16 v[52:55], v[166:169], v[174:177], v[52:55]
	v_mfma_f32_16x16x32_bf16 v[40:43], v[158:161], v[182:185], v[40:43]
	v_mfma_f32_16x16x32_bf16 v[36:39], v[166:169], v[182:185], v[36:39]
	v_mfma_f32_16x16x32_bf16 v[24:27], v[158:161], v[206:209], v[24:27]
	v_mfma_f32_16x16x32_bf16 v[20:23], v[166:169], v[206:209], v[20:23]
	v_mfma_f32_16x16x32_bf16 v[8:11], v[158:161], v[214:217], v[8:11]
	v_mfma_f32_16x16x32_bf16 v[4:7], v[166:169], v[214:217], v[4:7]
	s_setprio 0
	s_barrier
	s_add_i32 s57, s57, 2
	s_add_u32 s55, s55, 0x100
	s_addc_u32 s56, s56, 0
	s_add_u32 s20, s20, 0x100
	s_addc_u32 s21, s21, 0
	s_cmpk_gt_u32 s57, 0x55
	s_cbranch_scc0 .LBB0_3131
	s_and_b64 vcc, exec, s[14:15]
	s_cbranch_vccz .LBB0_3134
	s_barrier
